# all 8-phase K loops: per-MFMA counted lgkmcnt waits instead of one lgkmcnt(0) in front of each phase's MFMA block; G1a head sums by permlane swaps
# speedup vs baseline: 1.0109x; 1.0046x over previous
.LBB0_418:
	s_add_i32 s60, 0, 0x10000
	v_add_u32_e32 v130, s60, v168
	ds_read_b128 v[2:5], v130
	ds_read_b128 v[6:9], v130 offset:1024
	ds_read_b128 v[10:13], v130 offset:2048
	ds_read_b128 v[14:17], v130 offset:3072
	s_add_u32 s58, s66, 0x20080
	s_addc_u32 s59, s67, 0
	s_add_i32 s9, s39, 0xc000
	v_lshl_add_u64 v[50:51], s[58:59], 0, v[152:153]
	s_mov_b32 m0, s9
	s_add_i32 s51, s39, 0xe000
	ds_read_b128 v[18:21], v170
	ds_read_b128 v[22:25], v170 offset:1024
	ds_read_b128 v[26:29], v170 offset:2048
	ds_read_b128 v[30:33], v170 offset:3072
	ds_read_b128 v[34:37], v170 offset:4096
	ds_read_b128 v[38:41], v170 offset:5120
	ds_read_b128 v[42:45], v170 offset:6144
	ds_read_b128 v[46:49], v170 offset:7168
	global_load_lds_dwordx4 v[50:51], off
	v_lshl_add_u64 v[50:51], s[58:59], 0, v[148:149]
	s_mov_b32 m0, s51
	s_nop 0
	global_load_lds_dwordx4 v[50:51], off
	s_waitcnt lgkmcnt(8)
	s_waitcnt vmcnt(10)
	s_barrier
	s_setprio 1
	s_waitcnt lgkmcnt(6)
	v_mfma_scale_f32_16x16x128_f8f6f4 v[136:139], v[2:9], v[18:25], 0, v205, v205 op_sel_hi:[0,0,0]
	v_mfma_scale_f32_16x16x128_f8f6f4 v[132:135], v[10:17], v[18:25], 0, v205, v205 op_sel_hi:[0,0,0]
	s_waitcnt lgkmcnt(4)
	v_mfma_scale_f32_16x16x128_f8f6f4 v[118:121], v[2:9], v[26:33], 0, v205, v205 op_sel_hi:[0,0,0]
	v_mfma_scale_f32_16x16x128_f8f6f4 v[114:117], v[10:17], v[26:33], 0, v205, v205 op_sel_hi:[0,0,0]
	s_waitcnt lgkmcnt(2)
	v_mfma_scale_f32_16x16x128_f8f6f4 v[106:109], v[2:9], v[34:41], 0, v205, v205 op_sel_hi:[0,0,0]
	v_mfma_scale_f32_16x16x128_f8f6f4 v[98:101], v[10:17], v[34:41], 0, v205, v205 op_sel_hi:[0,0,0]
	s_waitcnt lgkmcnt(0)
	v_mfma_scale_f32_16x16x128_f8f6f4 v[86:89], v[2:9], v[42:49], 0, v205, v205 op_sel_hi:[0,0,0]
	v_mfma_scale_f32_16x16x128_f8f6f4 v[70:73], v[10:17], v[42:49], 0, v205, v205 op_sel_hi:[0,0,0]
	s_setprio 0
	s_barrier
	s_add_i32 s61, 0, 0x14000
	v_lshl_add_u64 v[164:165], s[68:69], 0, v[154:155]
	s_mov_b64 s[62:63], 0x100
	s_add_i32 s58, s60, s37
	v_add_u32_e32 v171, s61, v168
	v_lshl_add_u64 v[50:51], v[164:165], 0, s[62:63]
	s_mov_b32 m0, s58
	v_lshl_add_u64 v[166:167], s[68:69], 0, v[150:151]
	s_add_i32 s59, s58, 0x2000
	ds_read_b128 v[178:181], v171
	ds_read_b128 v[182:185], v171 offset:1024
	ds_read_b128 v[186:189], v171 offset:2048
	ds_read_b128 v[190:193], v171 offset:3072
	global_load_lds_dwordx4 v[50:51], off
	v_lshl_add_u64 v[50:51], v[166:167], 0, s[62:63]
	s_mov_b32 m0, s59
	s_nop 0
	global_load_lds_dwordx4 v[50:51], off
	s_waitcnt vmcnt(10)
	s_barrier
	s_setprio 1
	s_waitcnt lgkmcnt(2)
	v_mfma_scale_f32_16x16x128_f8f6f4 v[144:147], v[178:185], v[18:25], 0, v205, v205 op_sel_hi:[0,0,0]
	s_waitcnt lgkmcnt(0)
	v_mfma_scale_f32_16x16x128_f8f6f4 v[140:143], v[186:193], v[18:25], 0, v205, v205 op_sel_hi:[0,0,0]
	v_mfma_scale_f32_16x16x128_f8f6f4 v[126:129], v[178:185], v[26:33], 0, v205, v205 op_sel_hi:[0,0,0]
	v_mfma_scale_f32_16x16x128_f8f6f4 v[122:125], v[186:193], v[26:33], 0, v205, v205 op_sel_hi:[0,0,0]
	v_mfma_scale_f32_16x16x128_f8f6f4 v[110:113], v[178:185], v[34:41], 0, v205, v205 op_sel_hi:[0,0,0]
	v_mfma_scale_f32_16x16x128_f8f6f4 v[102:105], v[186:193], v[34:41], 0, v205, v205 op_sel_hi:[0,0,0]
	v_mfma_scale_f32_16x16x128_f8f6f4 v[94:97], v[178:185], v[42:49], 0, v205, v205 op_sel_hi:[0,0,0]
	v_mfma_scale_f32_16x16x128_f8f6f4 v[78:81], v[186:193], v[42:49], 0, v205, v205 op_sel_hi:[0,0,0]
	s_setprio 0
	v_lshl_add_u64 v[160:161], s[66:67], 0, v[152:153]
	s_mov_b32 m0, s39
	v_lshl_add_u64 v[18:19], v[160:161], 0, s[62:63]
	v_lshl_add_u64 v[162:163], s[66:67], 0, v[148:149]
	s_barrier
	ds_read_b128 v[194:197], v170 offset:16384
	ds_read_b128 v[198:201], v170 offset:17408
	ds_read_b128 v[218:221], v170 offset:18432
	ds_read_b128 v[222:225], v170 offset:19456
	ds_read_b128 v[226:229], v170 offset:20480
	ds_read_b128 v[230:233], v170 offset:21504
	ds_read_b128 v[234:237], v170 offset:22528
	ds_read_b128 v[238:241], v170 offset:23552
	global_load_lds_dwordx4 v[18:19], off
	v_lshl_add_u64 v[18:19], v[162:163], 0, s[62:63]
	s_mov_b32 m0, s42
	s_nop 0
	global_load_lds_dwordx4 v[18:19], off
	s_barrier
	s_setprio 1
	s_waitcnt lgkmcnt(6)
	v_mfma_scale_f32_16x16x128_f8f6f4 v[82:85], v[2:9], v[194:201], 0, v205, v205 op_sel_hi:[0,0,0]
	v_mfma_scale_f32_16x16x128_f8f6f4 v[66:69], v[10:17], v[194:201], 0, v205, v205 op_sel_hi:[0,0,0]
	s_waitcnt lgkmcnt(4)
	v_mfma_scale_f32_16x16x128_f8f6f4 v[58:61], v[2:9], v[218:225], 0, v205, v205 op_sel_hi:[0,0,0]
	v_mfma_scale_f32_16x16x128_f8f6f4 v[50:53], v[10:17], v[218:225], 0, v205, v205 op_sel_hi:[0,0,0]
	s_waitcnt lgkmcnt(2)
	v_mfma_scale_f32_16x16x128_f8f6f4 v[46:49], v[2:9], v[226:233], 0, v205, v205 op_sel_hi:[0,0,0]
	v_mfma_scale_f32_16x16x128_f8f6f4 v[38:41], v[10:17], v[226:233], 0, v205, v205 op_sel_hi:[0,0,0]
	s_waitcnt lgkmcnt(0)
	v_mfma_scale_f32_16x16x128_f8f6f4 v[30:33], v[2:9], v[234:241], 0, v205, v205 op_sel_hi:[0,0,0]
	v_mfma_scale_f32_16x16x128_f8f6f4 v[22:25], v[10:17], v[234:241], 0, v205, v205 op_sel_hi:[0,0,0]
	s_setprio 0
	s_barrier
	s_add_u32 s62, s68, 0x2100
	s_addc_u32 s63, s69, 0
	s_add_i32 s60, s61, s37
	v_lshl_add_u64 v[2:3], s[62:63], 0, v[154:155]
	s_mov_b32 m0, s60
	s_add_i32 s61, s60, 0x2000
	global_load_lds_dwordx4 v[2:3], off
	v_lshl_add_u64 v[2:3], s[62:63], 0, v[150:151]
	s_mov_b32 m0, s61
	s_nop 0
	global_load_lds_dwordx4 v[2:3], off
	s_waitcnt vmcnt(10)
	s_barrier
	s_setprio 1
	v_mfma_scale_f32_16x16x128_f8f6f4 v[90:93], v[178:185], v[194:201], 0, v205, v205 op_sel_hi:[0,0,0]
	v_mfma_scale_f32_16x16x128_f8f6f4 v[74:77], v[186:193], v[194:201], 0, v205, v205 op_sel_hi:[0,0,0]
	v_mfma_scale_f32_16x16x128_f8f6f4 v[62:65], v[178:185], v[218:225], 0, v205, v205 op_sel_hi:[0,0,0]
	v_mfma_scale_f32_16x16x128_f8f6f4 v[54:57], v[186:193], v[218:225], 0, v205, v205 op_sel_hi:[0,0,0]
	v_mfma_scale_f32_16x16x128_f8f6f4 v[42:45], v[178:185], v[226:233], 0, v205, v205 op_sel_hi:[0,0,0]
	v_mfma_scale_f32_16x16x128_f8f6f4 v[34:37], v[186:193], v[226:233], 0, v205, v205 op_sel_hi:[0,0,0]
	v_mfma_scale_f32_16x16x128_f8f6f4 v[26:29], v[178:185], v[234:241], 0, v205, v205 op_sel_hi:[0,0,0]
	v_mfma_scale_f32_16x16x128_f8f6f4 v[18:21], v[186:193], v[234:241], 0, v205, v205 op_sel_hi:[0,0,0]
	s_setprio 0
	s_add_i32 s70, 0, 0x18000
	v_add_u32_e32 v172, s70, v168
	s_barrier
	ds_read_b128 v[10:13], v172
	ds_read_b128 v[14:17], v172 offset:1024
	ds_read_b128 v[2:5], v172 offset:2048
	ds_read_b128 v[6:9], v172 offset:3072
	s_add_u32 s62, s66, 0x20100
	s_addc_u32 s63, s67, 0
	s_mov_b32 m0, s43
	v_lshl_add_u64 v[174:175], s[62:63], 0, v[152:153]
	ds_read_b128 v[178:181], v170 offset:32768
	ds_read_b128 v[182:185], v170 offset:33792
	ds_read_b128 v[186:189], v170 offset:34816
	ds_read_b128 v[190:193], v170 offset:35840
	ds_read_b128 v[194:197], v170 offset:36864
	ds_read_b128 v[198:201], v170 offset:37888
	ds_read_b128 v[218:221], v170 offset:38912
	ds_read_b128 v[222:225], v170 offset:39936
	global_load_lds_dwordx4 v[174:175], off
	v_lshl_add_u64 v[174:175], s[62:63], 0, v[148:149]
	s_mov_b32 m0, s44
	s_nop 0
	global_load_lds_dwordx4 v[174:175], off
	s_waitcnt lgkmcnt(8)
	s_waitcnt vmcnt(10)
	s_barrier
	s_setprio 1
	s_waitcnt lgkmcnt(6)
	v_mfma_scale_f32_16x16x128_f8f6f4 v[136:139], v[10:17], v[178:185], v[136:139], v205, v205 op_sel_hi:[0,0,0]
	v_mfma_scale_f32_16x16x128_f8f6f4 v[132:135], v[2:9], v[178:185], v[132:135], v205, v205 op_sel_hi:[0,0,0]
	s_waitcnt lgkmcnt(4)
	v_mfma_scale_f32_16x16x128_f8f6f4 v[118:121], v[10:17], v[186:193], v[118:121], v205, v205 op_sel_hi:[0,0,0]
	v_mfma_scale_f32_16x16x128_f8f6f4 v[114:117], v[2:9], v[186:193], v[114:117], v205, v205 op_sel_hi:[0,0,0]
	s_waitcnt lgkmcnt(2)
	v_mfma_scale_f32_16x16x128_f8f6f4 v[106:109], v[10:17], v[194:201], v[106:109], v205, v205 op_sel_hi:[0,0,0]
	v_mfma_scale_f32_16x16x128_f8f6f4 v[98:101], v[2:9], v[194:201], v[98:101], v205, v205 op_sel_hi:[0,0,0]
	s_waitcnt lgkmcnt(0)
	v_mfma_scale_f32_16x16x128_f8f6f4 v[86:89], v[10:17], v[218:225], v[86:89], v205, v205 op_sel_hi:[0,0,0]
	v_mfma_scale_f32_16x16x128_f8f6f4 v[70:73], v[2:9], v[218:225], v[70:73], v205, v205 op_sel_hi:[0,0,0]
	s_setprio 0
	s_barrier
	s_add_i32 s72, 0, 0x1c000
	s_mov_b64 s[74:75], 0x180
	s_add_i32 s62, s70, s37
	v_add_u32_e32 v173, s72, v168
	v_lshl_add_u64 v[164:165], v[164:165], 0, s[74:75]
	s_mov_b32 m0, s62
	s_add_i32 s63, s62, 0x2000
	ds_read_b128 v[226:229], v173
	ds_read_b128 v[230:233], v173 offset:1024
	ds_read_b128 v[234:237], v173 offset:2048
	ds_read_b128 v[238:241], v173 offset:3072
	global_load_lds_dwordx4 v[164:165], off
	v_lshl_add_u64 v[164:165], v[166:167], 0, s[74:75]
	s_mov_b32 m0, s63
	s_nop 0
	global_load_lds_dwordx4 v[164:165], off
	s_waitcnt vmcnt(10)
	s_barrier
	s_setprio 1
	s_waitcnt lgkmcnt(2)
	v_mfma_scale_f32_16x16x128_f8f6f4 v[144:147], v[226:233], v[178:185], v[144:147], v205, v205 op_sel_hi:[0,0,0]
	s_waitcnt lgkmcnt(0)
	v_mfma_scale_f32_16x16x128_f8f6f4 v[140:143], v[234:241], v[178:185], v[140:143], v205, v205 op_sel_hi:[0,0,0]
	v_mfma_scale_f32_16x16x128_f8f6f4 v[126:129], v[226:233], v[186:193], v[126:129], v205, v205 op_sel_hi:[0,0,0]
	v_mfma_scale_f32_16x16x128_f8f6f4 v[122:125], v[234:241], v[186:193], v[122:125], v205, v205 op_sel_hi:[0,0,0]
	v_mfma_scale_f32_16x16x128_f8f6f4 v[110:113], v[226:233], v[194:201], v[110:113], v205, v205 op_sel_hi:[0,0,0]
	v_mfma_scale_f32_16x16x128_f8f6f4 v[102:105], v[234:241], v[194:201], v[102:105], v205, v205 op_sel_hi:[0,0,0]
	v_mfma_scale_f32_16x16x128_f8f6f4 v[94:97], v[226:233], v[218:225], v[94:97], v205, v205 op_sel_hi:[0,0,0]
	v_mfma_scale_f32_16x16x128_f8f6f4 v[78:81], v[234:241], v[218:225], v[78:81], v205, v205 op_sel_hi:[0,0,0]
	s_setprio 0
	s_mov_b32 m0, s45
	v_lshl_add_u64 v[160:161], v[160:161], 0, s[74:75]
	s_barrier
	ds_read_b128 v[178:181], v170 offset:49152
	ds_read_b128 v[182:185], v170 offset:50176
	ds_read_b128 v[186:189], v170 offset:51200
	ds_read_b128 v[190:193], v170 offset:52224
	ds_read_b128 v[194:197], v170 offset:53248
	ds_read_b128 v[198:201], v170 offset:54272
	ds_read_b128 v[218:221], v170 offset:55296
	ds_read_b128 v[222:225], v170 offset:56320
	global_load_lds_dwordx4 v[160:161], off
	v_lshl_add_u64 v[160:161], v[162:163], 0, s[74:75]
	s_mov_b32 m0, s46
	s_nop 0
	global_load_lds_dwordx4 v[160:161], off
	s_barrier
	s_setprio 1
	s_waitcnt lgkmcnt(6)
	v_mfma_scale_f32_16x16x128_f8f6f4 v[82:85], v[10:17], v[178:185], v[82:85], v205, v205 op_sel_hi:[0,0,0]
	v_mfma_scale_f32_16x16x128_f8f6f4 v[66:69], v[2:9], v[178:185], v[66:69], v205, v205 op_sel_hi:[0,0,0]
	s_waitcnt lgkmcnt(4)
	v_mfma_scale_f32_16x16x128_f8f6f4 v[58:61], v[10:17], v[186:193], v[58:61], v205, v205 op_sel_hi:[0,0,0]
	v_mfma_scale_f32_16x16x128_f8f6f4 v[50:53], v[2:9], v[186:193], v[50:53], v205, v205 op_sel_hi:[0,0,0]
	s_waitcnt lgkmcnt(2)
	v_mfma_scale_f32_16x16x128_f8f6f4 v[46:49], v[10:17], v[194:201], v[46:49], v205, v205 op_sel_hi:[0,0,0]
	v_mfma_scale_f32_16x16x128_f8f6f4 v[38:41], v[2:9], v[194:201], v[38:41], v205, v205 op_sel_hi:[0,0,0]
	s_waitcnt lgkmcnt(0)
	v_mfma_scale_f32_16x16x128_f8f6f4 v[30:33], v[10:17], v[218:225], v[30:33], v205, v205 op_sel_hi:[0,0,0]
	v_mfma_scale_f32_16x16x128_f8f6f4 v[22:25], v[2:9], v[218:225], v[22:25], v205, v205 op_sel_hi:[0,0,0]
	s_setprio 0
	s_barrier
	s_add_u32 s70, s68, 0x2180
	s_addc_u32 s71, s69, 0
	s_add_i32 s72, s72, s37
	v_lshl_add_u64 v[2:3], s[70:71], 0, v[154:155]
	s_mov_b32 m0, s72
	s_add_i32 s73, s72, 0x2000
	global_load_lds_dwordx4 v[2:3], off
	v_lshl_add_u64 v[2:3], s[70:71], 0, v[150:151]
	s_mov_b32 m0, s73
	s_nop 0
	global_load_lds_dwordx4 v[2:3], off
	s_waitcnt vmcnt(10)
	s_barrier
	s_setprio 1
	v_mfma_scale_f32_16x16x128_f8f6f4 v[90:93], v[226:233], v[178:185], v[90:93], v205, v205 op_sel_hi:[0,0,0]
	v_mfma_scale_f32_16x16x128_f8f6f4 v[74:77], v[234:241], v[178:185], v[74:77], v205, v205 op_sel_hi:[0,0,0]
	v_mfma_scale_f32_16x16x128_f8f6f4 v[62:65], v[226:233], v[186:193], v[62:65], v205, v205 op_sel_hi:[0,0,0]
	v_mfma_scale_f32_16x16x128_f8f6f4 v[54:57], v[234:241], v[186:193], v[54:57], v205, v205 op_sel_hi:[0,0,0]
	v_mfma_scale_f32_16x16x128_f8f6f4 v[42:45], v[226:233], v[194:201], v[42:45], v205, v205 op_sel_hi:[0,0,0]
	v_mfma_scale_f32_16x16x128_f8f6f4 v[34:37], v[234:241], v[194:201], v[34:37], v205, v205 op_sel_hi:[0,0,0]
	v_mfma_scale_f32_16x16x128_f8f6f4 v[26:29], v[226:233], v[218:225], v[26:29], v205, v205 op_sel_hi:[0,0,0]
	v_mfma_scale_f32_16x16x128_f8f6f4 v[18:21], v[234:241], v[218:225], v[18:21], v205, v205 op_sel_hi:[0,0,0]
	s_setprio 0
	s_add_u32 s66, s66, 0x20180
	s_addc_u32 s67, s67, 0
	s_add_u32 s74, s68, 0x200
	s_addc_u32 s75, s69, 0
	s_mov_b32 s76, 0
	s_barrier
.LBB0_419:
	ds_read_b128 v[10:13], v130
	ds_read_b128 v[14:17], v130 offset:1024
	ds_read_b128 v[160:163], v130 offset:2048
	ds_read_b128 v[164:167], v130 offset:3072
	s_add_u32 s68, s66, 0xfffe0080
	s_addc_u32 s69, s67, -1
	s_cmp_eq_u32 s76, 4
	s_cselect_b32 s71, s19, s69
	s_cselect_b32 s70, s18, s68
	s_cselect_b32 s69, s65, s75
	s_cselect_b32 s68, s64, s74
	s_mov_b32 m0, s9
	v_lshl_add_u64 v[2:3], s[66:67], 0, v[156:157]
	ds_read_b128 v[178:181], v170
	ds_read_b128 v[182:185], v170 offset:1024
	ds_read_b128 v[186:189], v170 offset:2048
	ds_read_b128 v[190:193], v170 offset:3072
	ds_read_b128 v[194:197], v170 offset:4096
	ds_read_b128 v[198:201], v170 offset:5120
	ds_read_b128 v[218:221], v170 offset:6144
	ds_read_b128 v[222:225], v170 offset:7168
	global_load_lds_dwordx4 v[2:3], off
	v_lshl_add_u64 v[2:3], s[66:67], 0, v[158:159]
	s_mov_b32 m0, s51
	s_nop 0
	global_load_lds_dwordx4 v[2:3], off
	s_waitcnt lgkmcnt(8)
	s_waitcnt vmcnt(10)
	s_barrier
	s_setprio 1
	s_waitcnt lgkmcnt(6)
	v_mfma_scale_f32_16x16x128_f8f6f4 v[136:139], v[10:17], v[178:185], v[136:139], v205, v205 op_sel_hi:[0,0,0]
	v_mfma_scale_f32_16x16x128_f8f6f4 v[132:135], v[160:167], v[178:185], v[132:135], v205, v205 op_sel_hi:[0,0,0]
	s_waitcnt lgkmcnt(4)
	v_mfma_scale_f32_16x16x128_f8f6f4 v[118:121], v[10:17], v[186:193], v[118:121], v205, v205 op_sel_hi:[0,0,0]
	v_mfma_scale_f32_16x16x128_f8f6f4 v[114:117], v[160:167], v[186:193], v[114:117], v205, v205 op_sel_hi:[0,0,0]
	s_waitcnt lgkmcnt(2)
	v_mfma_scale_f32_16x16x128_f8f6f4 v[106:109], v[10:17], v[194:201], v[106:109], v205, v205 op_sel_hi:[0,0,0]
	v_mfma_scale_f32_16x16x128_f8f6f4 v[98:101], v[160:167], v[194:201], v[98:101], v205, v205 op_sel_hi:[0,0,0]
	s_waitcnt lgkmcnt(0)
	v_mfma_scale_f32_16x16x128_f8f6f4 v[86:89], v[10:17], v[218:225], v[86:89], v205, v205 op_sel_hi:[0,0,0]
	v_mfma_scale_f32_16x16x128_f8f6f4 v[70:73], v[160:167], v[218:225], v[70:73], v205, v205 op_sel_hi:[0,0,0]
	s_setprio 0
	s_barrier
	s_mov_b32 m0, s58
	v_lshl_add_u64 v[6:7], s[68:69], 0, v[154:155]
	ds_read_b128 v[226:229], v171
	ds_read_b128 v[230:233], v171 offset:1024
	ds_read_b128 v[234:237], v171 offset:2048
	ds_read_b128 v[238:241], v171 offset:3072
	global_load_lds_dwordx4 v[6:7], off
	v_lshl_add_u64 v[8:9], s[68:69], 0, v[150:151]
	s_mov_b32 m0, s59
	s_nop 0
	global_load_lds_dwordx4 v[8:9], off
	s_waitcnt vmcnt(10)
	s_barrier
	s_setprio 1
	s_waitcnt lgkmcnt(2)
	v_mfma_scale_f32_16x16x128_f8f6f4 v[144:147], v[226:233], v[178:185], v[144:147], v205, v205 op_sel_hi:[0,0,0]
	s_waitcnt lgkmcnt(0)
	v_mfma_scale_f32_16x16x128_f8f6f4 v[140:143], v[234:241], v[178:185], v[140:143], v205, v205 op_sel_hi:[0,0,0]
	v_mfma_scale_f32_16x16x128_f8f6f4 v[126:129], v[226:233], v[186:193], v[126:129], v205, v205 op_sel_hi:[0,0,0]
	v_mfma_scale_f32_16x16x128_f8f6f4 v[122:125], v[234:241], v[186:193], v[122:125], v205, v205 op_sel_hi:[0,0,0]
	v_mfma_scale_f32_16x16x128_f8f6f4 v[110:113], v[226:233], v[194:201], v[110:113], v205, v205 op_sel_hi:[0,0,0]
	v_mfma_scale_f32_16x16x128_f8f6f4 v[102:105], v[234:241], v[194:201], v[102:105], v205, v205 op_sel_hi:[0,0,0]
	v_mfma_scale_f32_16x16x128_f8f6f4 v[94:97], v[226:233], v[218:225], v[94:97], v205, v205 op_sel_hi:[0,0,0]
	v_mfma_scale_f32_16x16x128_f8f6f4 v[78:81], v[234:241], v[218:225], v[78:81], v205, v205 op_sel_hi:[0,0,0]
	s_setprio 0
	s_mov_b32 m0, s39
	v_lshl_add_u64 v[2:3], s[70:71], 0, v[152:153]
	s_barrier
	ds_read_b128 v[178:181], v170 offset:16384
	ds_read_b128 v[182:185], v170 offset:17408
	ds_read_b128 v[186:189], v170 offset:18432
	ds_read_b128 v[190:193], v170 offset:19456
	ds_read_b128 v[194:197], v170 offset:20480
	ds_read_b128 v[198:201], v170 offset:21504
	ds_read_b128 v[218:221], v170 offset:22528
	ds_read_b128 v[222:225], v170 offset:23552
	global_load_lds_dwordx4 v[2:3], off
	v_lshl_add_u64 v[4:5], s[70:71], 0, v[148:149]
	s_mov_b32 m0, s42
	s_nop 0
	global_load_lds_dwordx4 v[4:5], off
	s_barrier
	s_setprio 1
	s_waitcnt lgkmcnt(6)
	v_mfma_scale_f32_16x16x128_f8f6f4 v[82:85], v[10:17], v[178:185], v[82:85], v205, v205 op_sel_hi:[0,0,0]
	v_mfma_scale_f32_16x16x128_f8f6f4 v[66:69], v[160:167], v[178:185], v[66:69], v205, v205 op_sel_hi:[0,0,0]
	s_waitcnt lgkmcnt(4)
	v_mfma_scale_f32_16x16x128_f8f6f4 v[58:61], v[10:17], v[186:193], v[58:61], v205, v205 op_sel_hi:[0,0,0]
	v_mfma_scale_f32_16x16x128_f8f6f4 v[50:53], v[160:167], v[186:193], v[50:53], v205, v205 op_sel_hi:[0,0,0]
	s_waitcnt lgkmcnt(2)
	v_mfma_scale_f32_16x16x128_f8f6f4 v[46:49], v[10:17], v[194:201], v[46:49], v205, v205 op_sel_hi:[0,0,0]
	v_mfma_scale_f32_16x16x128_f8f6f4 v[38:41], v[160:167], v[194:201], v[38:41], v205, v205 op_sel_hi:[0,0,0]
	s_waitcnt lgkmcnt(0)
	v_mfma_scale_f32_16x16x128_f8f6f4 v[30:33], v[10:17], v[218:225], v[30:33], v205, v205 op_sel_hi:[0,0,0]
	v_mfma_scale_f32_16x16x128_f8f6f4 v[22:25], v[160:167], v[218:225], v[22:25], v205, v205 op_sel_hi:[0,0,0]
	s_setprio 0
	s_barrier
	s_add_u32 s78, s68, 0x2000
	s_addc_u32 s79, s69, 0
	s_mov_b32 m0, s60
	v_lshl_add_u64 v[10:11], s[78:79], 0, v[154:155]
	global_load_lds_dwordx4 v[10:11], off
	v_lshl_add_u64 v[10:11], s[78:79], 0, v[150:151]
	s_mov_b32 m0, s61
	s_nop 0
	global_load_lds_dwordx4 v[10:11], off
	s_waitcnt vmcnt(10)
	s_barrier
	s_setprio 1
	v_mfma_scale_f32_16x16x128_f8f6f4 v[90:93], v[226:233], v[178:185], v[90:93], v205, v205 op_sel_hi:[0,0,0]
	v_mfma_scale_f32_16x16x128_f8f6f4 v[74:77], v[234:241], v[178:185], v[74:77], v205, v205 op_sel_hi:[0,0,0]
	v_mfma_scale_f32_16x16x128_f8f6f4 v[62:65], v[226:233], v[186:193], v[62:65], v205, v205 op_sel_hi:[0,0,0]
	v_mfma_scale_f32_16x16x128_f8f6f4 v[54:57], v[234:241], v[186:193], v[54:57], v205, v205 op_sel_hi:[0,0,0]
	v_mfma_scale_f32_16x16x128_f8f6f4 v[42:45], v[226:233], v[194:201], v[42:45], v205, v205 op_sel_hi:[0,0,0]
	v_mfma_scale_f32_16x16x128_f8f6f4 v[34:37], v[234:241], v[194:201], v[34:37], v205, v205 op_sel_hi:[0,0,0]
	v_mfma_scale_f32_16x16x128_f8f6f4 v[26:29], v[226:233], v[218:225], v[26:29], v205, v205 op_sel_hi:[0,0,0]
	v_mfma_scale_f32_16x16x128_f8f6f4 v[18:21], v[234:241], v[218:225], v[18:21], v205, v205 op_sel_hi:[0,0,0]
	s_setprio 0
	s_barrier
	ds_read_b128 v[10:13], v172
	ds_read_b128 v[14:17], v172 offset:1024
	ds_read_b128 v[160:163], v172 offset:2048
	ds_read_b128 v[164:167], v172 offset:3072
	s_add_u32 s70, s70, 0x20000
	s_addc_u32 s71, s71, 0
	s_mov_b32 m0, s43
	v_lshl_add_u64 v[174:175], s[70:71], 0, v[152:153]
	ds_read_b128 v[178:181], v170 offset:32768
	ds_read_b128 v[182:185], v170 offset:33792
	ds_read_b128 v[186:189], v170 offset:34816
	ds_read_b128 v[190:193], v170 offset:35840
	ds_read_b128 v[194:197], v170 offset:36864
	ds_read_b128 v[198:201], v170 offset:37888
	ds_read_b128 v[218:221], v170 offset:38912
	ds_read_b128 v[222:225], v170 offset:39936
	global_load_lds_dwordx4 v[174:175], off
	v_lshl_add_u64 v[174:175], s[70:71], 0, v[148:149]
	s_mov_b32 m0, s44
	s_nop 0
	global_load_lds_dwordx4 v[174:175], off
	s_waitcnt lgkmcnt(8)
	s_waitcnt vmcnt(10)
	s_barrier
	s_setprio 1
	s_waitcnt lgkmcnt(6)
	v_mfma_scale_f32_16x16x128_f8f6f4 v[136:139], v[10:17], v[178:185], v[136:139], v205, v205 op_sel_hi:[0,0,0]
	v_mfma_scale_f32_16x16x128_f8f6f4 v[132:135], v[160:167], v[178:185], v[132:135], v205, v205 op_sel_hi:[0,0,0]
	s_waitcnt lgkmcnt(4)
	v_mfma_scale_f32_16x16x128_f8f6f4 v[118:121], v[10:17], v[186:193], v[118:121], v205, v205 op_sel_hi:[0,0,0]
	v_mfma_scale_f32_16x16x128_f8f6f4 v[114:117], v[160:167], v[186:193], v[114:117], v205, v205 op_sel_hi:[0,0,0]
	s_waitcnt lgkmcnt(2)
	v_mfma_scale_f32_16x16x128_f8f6f4 v[106:109], v[10:17], v[194:201], v[106:109], v205, v205 op_sel_hi:[0,0,0]
	v_mfma_scale_f32_16x16x128_f8f6f4 v[98:101], v[160:167], v[194:201], v[98:101], v205, v205 op_sel_hi:[0,0,0]
	s_waitcnt lgkmcnt(0)
	v_mfma_scale_f32_16x16x128_f8f6f4 v[86:89], v[10:17], v[218:225], v[86:89], v205, v205 op_sel_hi:[0,0,0]
	v_mfma_scale_f32_16x16x128_f8f6f4 v[70:73], v[160:167], v[218:225], v[70:73], v205, v205 op_sel_hi:[0,0,0]
	s_setprio 0
	s_barrier
	s_mov_b32 m0, s62
	v_lshl_add_u64 v[6:7], v[6:7], 0, s[30:31]
	ds_read_b128 v[226:229], v173
	ds_read_b128 v[230:233], v173 offset:1024
	ds_read_b128 v[234:237], v173 offset:2048
	ds_read_b128 v[238:241], v173 offset:3072
	global_load_lds_dwordx4 v[6:7], off
	v_lshl_add_u64 v[6:7], v[8:9], 0, s[30:31]
	s_mov_b32 m0, s63
	s_nop 0
	global_load_lds_dwordx4 v[6:7], off
	s_waitcnt vmcnt(10)
	s_barrier
	s_setprio 1
	s_waitcnt lgkmcnt(2)
	v_mfma_scale_f32_16x16x128_f8f6f4 v[144:147], v[226:233], v[178:185], v[144:147], v205, v205 op_sel_hi:[0,0,0]
	s_waitcnt lgkmcnt(0)
	v_mfma_scale_f32_16x16x128_f8f6f4 v[140:143], v[234:241], v[178:185], v[140:143], v205, v205 op_sel_hi:[0,0,0]
	v_mfma_scale_f32_16x16x128_f8f6f4 v[126:129], v[226:233], v[186:193], v[126:129], v205, v205 op_sel_hi:[0,0,0]
	v_mfma_scale_f32_16x16x128_f8f6f4 v[122:125], v[234:241], v[186:193], v[122:125], v205, v205 op_sel_hi:[0,0,0]
	v_mfma_scale_f32_16x16x128_f8f6f4 v[110:113], v[226:233], v[194:201], v[110:113], v205, v205 op_sel_hi:[0,0,0]
	v_mfma_scale_f32_16x16x128_f8f6f4 v[102:105], v[234:241], v[194:201], v[102:105], v205, v205 op_sel_hi:[0,0,0]
	v_mfma_scale_f32_16x16x128_f8f6f4 v[94:97], v[226:233], v[218:225], v[94:97], v205, v205 op_sel_hi:[0,0,0]
	v_mfma_scale_f32_16x16x128_f8f6f4 v[78:81], v[234:241], v[218:225], v[78:81], v205, v205 op_sel_hi:[0,0,0]
	s_setprio 0
	s_mov_b32 m0, s45
	v_lshl_add_u64 v[2:3], v[2:3], 0, s[30:31]
	s_barrier
	ds_read_b128 v[178:181], v170 offset:49152
	ds_read_b128 v[182:185], v170 offset:50176
	ds_read_b128 v[186:189], v170 offset:51200
	ds_read_b128 v[190:193], v170 offset:52224
	ds_read_b128 v[194:197], v170 offset:53248
	ds_read_b128 v[198:201], v170 offset:54272
	ds_read_b128 v[218:221], v170 offset:55296
	ds_read_b128 v[222:225], v170 offset:56320
	global_load_lds_dwordx4 v[2:3], off
	v_lshl_add_u64 v[2:3], v[4:5], 0, s[30:31]
	s_mov_b32 m0, s46
	s_nop 0
	global_load_lds_dwordx4 v[2:3], off
	s_barrier
	s_setprio 1
	s_waitcnt lgkmcnt(6)
	v_mfma_scale_f32_16x16x128_f8f6f4 v[82:85], v[10:17], v[178:185], v[82:85], v205, v205 op_sel_hi:[0,0,0]
	v_mfma_scale_f32_16x16x128_f8f6f4 v[66:69], v[160:167], v[178:185], v[66:69], v205, v205 op_sel_hi:[0,0,0]
	s_waitcnt lgkmcnt(4)
	v_mfma_scale_f32_16x16x128_f8f6f4 v[58:61], v[10:17], v[186:193], v[58:61], v205, v205 op_sel_hi:[0,0,0]
	v_mfma_scale_f32_16x16x128_f8f6f4 v[50:53], v[160:167], v[186:193], v[50:53], v205, v205 op_sel_hi:[0,0,0]
	s_waitcnt lgkmcnt(2)
	v_mfma_scale_f32_16x16x128_f8f6f4 v[46:49], v[10:17], v[194:201], v[46:49], v205, v205 op_sel_hi:[0,0,0]
	v_mfma_scale_f32_16x16x128_f8f6f4 v[38:41], v[160:167], v[194:201], v[38:41], v205, v205 op_sel_hi:[0,0,0]
	s_waitcnt lgkmcnt(0)
	v_mfma_scale_f32_16x16x128_f8f6f4 v[30:33], v[10:17], v[218:225], v[30:33], v205, v205 op_sel_hi:[0,0,0]
	v_mfma_scale_f32_16x16x128_f8f6f4 v[22:25], v[160:167], v[218:225], v[22:25], v205, v205 op_sel_hi:[0,0,0]
	s_setprio 0
	s_barrier
	s_add_u32 s68, s68, 0x2080
	s_addc_u32 s69, s69, 0
	s_mov_b32 m0, s72
	v_lshl_add_u64 v[2:3], s[68:69], 0, v[154:155]
	global_load_lds_dwordx4 v[2:3], off
	v_lshl_add_u64 v[2:3], s[68:69], 0, v[150:151]
	s_mov_b32 m0, s73
	s_nop 0
	global_load_lds_dwordx4 v[2:3], off
	s_waitcnt vmcnt(10)
	s_barrier
	s_setprio 1
	v_mfma_scale_f32_16x16x128_f8f6f4 v[90:93], v[226:233], v[178:185], v[90:93], v205, v205 op_sel_hi:[0,0,0]
	v_mfma_scale_f32_16x16x128_f8f6f4 v[74:77], v[234:241], v[178:185], v[74:77], v205, v205 op_sel_hi:[0,0,0]
	v_mfma_scale_f32_16x16x128_f8f6f4 v[62:65], v[226:233], v[186:193], v[62:65], v205, v205 op_sel_hi:[0,0,0]
	v_mfma_scale_f32_16x16x128_f8f6f4 v[54:57], v[234:241], v[186:193], v[54:57], v205, v205 op_sel_hi:[0,0,0]
	v_mfma_scale_f32_16x16x128_f8f6f4 v[42:45], v[226:233], v[194:201], v[42:45], v205, v205 op_sel_hi:[0,0,0]
	v_mfma_scale_f32_16x16x128_f8f6f4 v[34:37], v[234:241], v[194:201], v[34:37], v205, v205 op_sel_hi:[0,0,0]
	v_mfma_scale_f32_16x16x128_f8f6f4 v[26:29], v[226:233], v[218:225], v[26:29], v205, v205 op_sel_hi:[0,0,0]
	v_mfma_scale_f32_16x16x128_f8f6f4 v[18:21], v[234:241], v[218:225], v[18:21], v205, v205 op_sel_hi:[0,0,0]
	s_setprio 0
	s_add_i32 s76, s76, 2
	s_add_u32 s66, s66, 0x100
	s_addc_u32 s67, s67, 0
	s_add_u32 s74, s74, 0x100
	s_addc_u32 s75, s75, 0
	s_cmp_gt_u32 s76, 5
	s_barrier
	s_cbranch_scc0 .LBB0_419
	v_mul_f32_e32 v4, 0xbcb8aa3b, v136
	v_mul_f32_e32 v5, 0xbcb8aa3b, v137
	v_exp_f32_e32 v4, v4
	v_exp_f32_e32 v5, v5
	v_mul_f32_e32 v6, 0xbcb8aa3b, v138
	v_mul_f32_e32 v7, 0xbcb8aa3b, v139
	v_exp_f32_e32 v6, v6
	v_exp_f32_e32 v7, v7
	v_med3_f32 v8, v4, s26, v209
	v_med3_f32 v5, v5, s26, v209
	v_mov_b32_e32 v4, v131
	v_cvt_pk_fp8_f32 v4, v8, v5
	v_med3_f32 v5, v6, s26, v209
	v_med3_f32 v6, v7, s26, v209
	v_mul_f32_e32 v7, 0xbcb8aa3b, v134
	v_cvt_pk_fp8_f32 v4, v5, v6 op_sel:[0,0,1]
	v_mul_f32_e32 v5, 0xbcb8aa3b, v132
	v_mul_f32_e32 v6, 0xbcb8aa3b, v133
	v_exp_f32_e32 v5, v5
	v_exp_f32_e32 v6, v6
	v_mul_f32_e32 v8, 0xbcb8aa3b, v135
	v_exp_f32_e32 v7, v7
	v_exp_f32_e32 v8, v8
	v_med3_f32 v9, v5, s26, v209
	v_med3_f32 v6, v6, s26, v209
	v_mov_b32_e32 v5, v131
	v_cvt_pk_fp8_f32 v5, v9, v6
	v_med3_f32 v6, v7, s26, v209
	v_med3_f32 v7, v8, s26, v209
	v_mul_f32_e32 v8, 0xbcb8aa3b, v146
	v_cvt_pk_fp8_f32 v5, v6, v7 op_sel:[0,0,1]
	v_mul_f32_e32 v6, 0xbcb8aa3b, v144
	v_mul_f32_e32 v7, 0xbcb8aa3b, v145
	v_exp_f32_e32 v6, v6
	v_exp_f32_e32 v7, v7
	v_mul_f32_e32 v9, 0xbcb8aa3b, v147
	v_exp_f32_e32 v8, v8
	v_exp_f32_e32 v9, v9
	v_med3_f32 v10, v6, s26, v209
	v_med3_f32 v7, v7, s26, v209
	v_mov_b32_e32 v6, v131
	v_cvt_pk_fp8_f32 v6, v10, v7
	v_med3_f32 v7, v8, s26, v209
	v_med3_f32 v8, v9, s26, v209
	v_mul_f32_e32 v9, 0xbcb8aa3b, v142
	v_cvt_pk_fp8_f32 v6, v7, v8 op_sel:[0,0,1]
	v_mul_f32_e32 v7, 0xbcb8aa3b, v140
	v_mul_f32_e32 v8, 0xbcb8aa3b, v141
	v_exp_f32_e32 v7, v7
	v_exp_f32_e32 v8, v8
	v_mul_f32_e32 v10, 0xbcb8aa3b, v143
	v_exp_f32_e32 v9, v9
	v_exp_f32_e32 v10, v10
	v_med3_f32 v11, v7, s26, v209
	v_med3_f32 v8, v8, s26, v209
	v_mov_b32_e32 v7, v131
	v_cvt_pk_fp8_f32 v7, v11, v8
	s_lshl_b32 s9, s16, 8
	s_mul_i32 s16, s16, 0x1e0000
	s_mul_hi_i32 s9, s9, 0x1e00
	s_add_u32 s16, s53, s16
	v_med3_f32 v8, v9, s26, v209
	v_med3_f32 v9, v10, s26, v209
	s_addc_u32 s9, s57, s9
	s_lshl_b32 s17, s17, 8
	v_cvt_pk_fp8_f32 v7, v8, v9 op_sel:[0,0,1]
	s_ashr_i32 s18, s17, 31
	s_add_u32 s16, s16, s17
	s_addc_u32 s17, s9, s18
	v_mov_b32_e32 v130, v169
	s_nop 15
	s_nop 15
	global_store_dwordx4 v130, v[4:7], s[16:17] offset:1536
	v_lshl_add_u64 v[2:3], s[16:17], 0, v[130:131]
	s_mov_b32 s9, 0x1e000
	v_mul_f32_e32 v4, 0xbcb8aa3b, v118
	v_mul_f32_e32 v5, 0xbcb8aa3b, v119
	v_exp_f32_e32 v4, v4
	v_exp_f32_e32 v5, v5
	v_mul_f32_e32 v6, 0xbcb8aa3b, v120
	v_mul_f32_e32 v7, 0xbcb8aa3b, v121
	v_exp_f32_e32 v6, v6
	v_exp_f32_e32 v7, v7
	v_med3_f32 v8, v4, s26, v209
	v_med3_f32 v5, v5, s26, v209
	v_mov_b32_e32 v4, v131
	v_cvt_pk_fp8_f32 v4, v8, v5
	v_med3_f32 v5, v6, s26, v209
	v_med3_f32 v6, v7, s26, v209
	v_mul_f32_e32 v7, 0xbcb8aa3b, v116
	v_cvt_pk_fp8_f32 v4, v5, v6 op_sel:[0,0,1]
	v_mul_f32_e32 v5, 0xbcb8aa3b, v114
	v_mul_f32_e32 v6, 0xbcb8aa3b, v115
	v_exp_f32_e32 v5, v5
	v_exp_f32_e32 v6, v6
	v_mul_f32_e32 v8, 0xbcb8aa3b, v117
	v_exp_f32_e32 v7, v7
	v_exp_f32_e32 v8, v8
	v_med3_f32 v9, v5, s26, v209
	v_med3_f32 v6, v6, s26, v209
	v_mov_b32_e32 v5, v131
	v_cvt_pk_fp8_f32 v5, v9, v6
	v_med3_f32 v6, v7, s26, v209
	v_med3_f32 v7, v8, s26, v209
	v_mul_f32_e32 v8, 0xbcb8aa3b, v128
	v_cvt_pk_fp8_f32 v5, v6, v7 op_sel:[0,0,1]
	v_mul_f32_e32 v6, 0xbcb8aa3b, v126
	v_mul_f32_e32 v7, 0xbcb8aa3b, v127
	v_exp_f32_e32 v6, v6
	v_exp_f32_e32 v7, v7
	v_mul_f32_e32 v9, 0xbcb8aa3b, v129
	v_exp_f32_e32 v8, v8
	v_exp_f32_e32 v9, v9
	v_med3_f32 v10, v6, s26, v209
	v_med3_f32 v7, v7, s26, v209
	v_mov_b32_e32 v6, v131
	v_cvt_pk_fp8_f32 v6, v10, v7
	v_med3_f32 v7, v8, s26, v209
	v_med3_f32 v8, v9, s26, v209
	v_mul_f32_e32 v9, 0xbcb8aa3b, v124
	v_cvt_pk_fp8_f32 v6, v7, v8 op_sel:[0,0,1]
	v_mul_f32_e32 v7, 0xbcb8aa3b, v122
	v_mul_f32_e32 v8, 0xbcb8aa3b, v123
	v_exp_f32_e32 v7, v7
	v_exp_f32_e32 v8, v8
	v_mul_f32_e32 v10, 0xbcb8aa3b, v125
	v_exp_f32_e32 v9, v9
	v_exp_f32_e32 v10, v10
	v_med3_f32 v11, v7, s26, v209
	v_med3_f32 v8, v8, s26, v209
	v_mov_b32_e32 v7, v131
	v_cvt_pk_fp8_f32 v7, v11, v8
	v_med3_f32 v8, v9, s26, v209
	v_med3_f32 v9, v10, s26, v209
	s_mov_b32 s16, s8
	v_cvt_pk_fp8_f32 v7, v8, v9 op_sel:[0,0,1]
	v_add_co_u32_e32 v8, vcc, s9, v2
	s_mov_b32 s9, 0x3c000
	s_nop 0
	v_addc_co_u32_e32 v9, vcc, 0, v3, vcc
	global_store_dwordx4 v[8:9], v[4:7], off offset:1536
	s_mov_b32 s17, s50
	s_mov_b64 s[68:69], s[10:11]
	v_mul_f32_e32 v4, 0xbcb8aa3b, v106
	v_mul_f32_e32 v5, 0xbcb8aa3b, v107
	v_exp_f32_e32 v4, v4
	v_exp_f32_e32 v5, v5
	v_mul_f32_e32 v6, 0xbcb8aa3b, v108
	v_mul_f32_e32 v7, 0xbcb8aa3b, v109
	v_exp_f32_e32 v6, v6
	v_exp_f32_e32 v7, v7
	v_med3_f32 v8, v4, s26, v209
	v_med3_f32 v5, v5, s26, v209
	v_mov_b32_e32 v4, v131
	v_cvt_pk_fp8_f32 v4, v8, v5
	v_med3_f32 v5, v6, s26, v209
	v_med3_f32 v6, v7, s26, v209
	v_mul_f32_e32 v7, 0xbcb8aa3b, v100
	v_cvt_pk_fp8_f32 v4, v5, v6 op_sel:[0,0,1]
	v_mul_f32_e32 v5, 0xbcb8aa3b, v98
	v_mul_f32_e32 v6, 0xbcb8aa3b, v99
	v_exp_f32_e32 v5, v5
	v_exp_f32_e32 v6, v6
	v_mul_f32_e32 v8, 0xbcb8aa3b, v101
	v_exp_f32_e32 v7, v7
	v_exp_f32_e32 v8, v8
	v_med3_f32 v9, v5, s26, v209
	v_med3_f32 v6, v6, s26, v209
	v_mov_b32_e32 v5, v131
	v_cvt_pk_fp8_f32 v5, v9, v6
	v_med3_f32 v6, v7, s26, v209
	v_med3_f32 v7, v8, s26, v209
	v_mul_f32_e32 v8, 0xbcb8aa3b, v112
	v_cvt_pk_fp8_f32 v5, v6, v7 op_sel:[0,0,1]
	v_mul_f32_e32 v6, 0xbcb8aa3b, v110
	v_mul_f32_e32 v7, 0xbcb8aa3b, v111
	v_exp_f32_e32 v6, v6
	v_exp_f32_e32 v7, v7
	v_mul_f32_e32 v9, 0xbcb8aa3b, v113
	v_exp_f32_e32 v8, v8
	v_exp_f32_e32 v9, v9
	v_med3_f32 v10, v6, s26, v209
	v_med3_f32 v7, v7, s26, v209
	v_mov_b32_e32 v6, v131
	v_cvt_pk_fp8_f32 v6, v10, v7
	v_med3_f32 v7, v8, s26, v209
	v_med3_f32 v8, v9, s26, v209
	v_mul_f32_e32 v9, 0xbcb8aa3b, v104
	v_cvt_pk_fp8_f32 v6, v7, v8 op_sel:[0,0,1]
	v_mul_f32_e32 v7, 0xbcb8aa3b, v102
	v_mul_f32_e32 v8, 0xbcb8aa3b, v103
	v_exp_f32_e32 v7, v7
	v_exp_f32_e32 v8, v8
	v_mul_f32_e32 v10, 0xbcb8aa3b, v105
	v_exp_f32_e32 v9, v9
	v_exp_f32_e32 v10, v10
	v_med3_f32 v11, v7, s26, v209
	v_med3_f32 v8, v8, s26, v209
	v_mov_b32_e32 v7, v131
	v_cvt_pk_fp8_f32 v7, v11, v8
	v_med3_f32 v8, v9, s26, v209
	v_med3_f32 v9, v10, s26, v209
	s_mov_b64 s[66:67], s[14:15]
	v_cvt_pk_fp8_f32 v7, v8, v9 op_sel:[0,0,1]
	v_add_co_u32_e32 v8, vcc, s9, v2
	s_mov_b32 s9, 0x5a000
	s_nop 0
	v_addc_co_u32_e32 v9, vcc, 0, v3, vcc
	global_store_dwordx4 v[8:9], v[4:7], off offset:1536
	s_nop 1
	v_mul_f32_e32 v4, 0xbcb8aa3b, v86
	v_mul_f32_e32 v5, 0xbcb8aa3b, v87
	v_exp_f32_e32 v4, v4
	v_exp_f32_e32 v5, v5
	v_mul_f32_e32 v6, 0xbcb8aa3b, v88
	v_mul_f32_e32 v7, 0xbcb8aa3b, v89
	v_exp_f32_e32 v6, v6
	v_exp_f32_e32 v7, v7
	v_med3_f32 v8, v4, s26, v209
	v_med3_f32 v5, v5, s26, v209
	v_mov_b32_e32 v4, v131
	v_cvt_pk_fp8_f32 v4, v8, v5
	v_med3_f32 v5, v6, s26, v209
	v_med3_f32 v6, v7, s26, v209
	v_mul_f32_e32 v7, 0xbcb8aa3b, v72
	v_cvt_pk_fp8_f32 v4, v5, v6 op_sel:[0,0,1]
	v_mul_f32_e32 v5, 0xbcb8aa3b, v70
	v_mul_f32_e32 v6, 0xbcb8aa3b, v71
	v_exp_f32_e32 v5, v5
	v_exp_f32_e32 v6, v6
	v_mul_f32_e32 v8, 0xbcb8aa3b, v73
	v_exp_f32_e32 v7, v7
	v_exp_f32_e32 v8, v8
	v_med3_f32 v9, v5, s26, v209
	v_med3_f32 v6, v6, s26, v209
	v_mov_b32_e32 v5, v131
	v_cvt_pk_fp8_f32 v5, v9, v6
	v_med3_f32 v6, v7, s26, v209
	v_med3_f32 v7, v8, s26, v209
	v_mul_f32_e32 v8, 0xbcb8aa3b, v96
	v_cvt_pk_fp8_f32 v5, v6, v7 op_sel:[0,0,1]
	v_mul_f32_e32 v6, 0xbcb8aa3b, v94
	v_mul_f32_e32 v7, 0xbcb8aa3b, v95
	v_exp_f32_e32 v6, v6
	v_exp_f32_e32 v7, v7
	v_mul_f32_e32 v9, 0xbcb8aa3b, v97
	v_exp_f32_e32 v8, v8
	v_exp_f32_e32 v9, v9
	v_med3_f32 v10, v6, s26, v209
	v_med3_f32 v7, v7, s26, v209
	v_mov_b32_e32 v6, v131
	v_cvt_pk_fp8_f32 v6, v10, v7
	v_med3_f32 v7, v8, s26, v209
	v_med3_f32 v8, v9, s26, v209
	v_mul_f32_e32 v9, 0xbcb8aa3b, v80
	v_cvt_pk_fp8_f32 v6, v7, v8 op_sel:[0,0,1]
	v_mul_f32_e32 v7, 0xbcb8aa3b, v78
	v_mul_f32_e32 v8, 0xbcb8aa3b, v79
	v_exp_f32_e32 v7, v7
	v_exp_f32_e32 v8, v8
	v_mul_f32_e32 v10, 0xbcb8aa3b, v81
	v_exp_f32_e32 v9, v9
	v_exp_f32_e32 v10, v10
	v_med3_f32 v11, v7, s26, v209
	v_med3_f32 v8, v8, s26, v209
	v_mov_b32_e32 v7, v131
	v_cvt_pk_fp8_f32 v7, v11, v8
	v_med3_f32 v8, v9, s26, v209
	v_med3_f32 v9, v10, s26, v209
	v_cvt_pk_fp8_f32 v7, v8, v9 op_sel:[0,0,1]
	v_add_co_u32_e32 v8, vcc, s9, v2
	s_mov_b32 s9, 0xf0000
	s_nop 0
	v_addc_co_u32_e32 v9, vcc, 0, v3, vcc
	global_store_dwordx4 v[8:9], v[4:7], off offset:1536
	s_nop 1
	v_mul_f32_e32 v4, 0xbcb8aa3b, v82
	v_mul_f32_e32 v5, 0xbcb8aa3b, v83
	v_exp_f32_e32 v4, v4
	v_exp_f32_e32 v5, v5
	v_mul_f32_e32 v6, 0xbcb8aa3b, v84
	v_mul_f32_e32 v7, 0xbcb8aa3b, v85
	v_exp_f32_e32 v6, v6
	v_exp_f32_e32 v7, v7
	v_med3_f32 v8, v4, s26, v209
	v_med3_f32 v5, v5, s26, v209
	v_mov_b32_e32 v4, v131
	v_cvt_pk_fp8_f32 v4, v8, v5
	v_med3_f32 v5, v6, s26, v209
	v_med3_f32 v6, v7, s26, v209
	v_mul_f32_e32 v7, 0xbcb8aa3b, v68
	v_cvt_pk_fp8_f32 v4, v5, v6 op_sel:[0,0,1]
	v_mul_f32_e32 v5, 0xbcb8aa3b, v66
	v_mul_f32_e32 v6, 0xbcb8aa3b, v67
	v_exp_f32_e32 v5, v5
	v_exp_f32_e32 v6, v6
	v_mul_f32_e32 v8, 0xbcb8aa3b, v69
	v_exp_f32_e32 v7, v7
	v_exp_f32_e32 v8, v8
	v_med3_f32 v9, v5, s26, v209
	v_med3_f32 v6, v6, s26, v209
	v_mov_b32_e32 v5, v131
	v_cvt_pk_fp8_f32 v5, v9, v6
	v_med3_f32 v6, v7, s26, v209
	v_med3_f32 v7, v8, s26, v209
	v_mul_f32_e32 v8, 0xbcb8aa3b, v92
	v_cvt_pk_fp8_f32 v5, v6, v7 op_sel:[0,0,1]
	v_mul_f32_e32 v6, 0xbcb8aa3b, v90
	v_mul_f32_e32 v7, 0xbcb8aa3b, v91
	v_exp_f32_e32 v6, v6
	v_exp_f32_e32 v7, v7
	v_mul_f32_e32 v9, 0xbcb8aa3b, v93
	v_exp_f32_e32 v8, v8
	v_exp_f32_e32 v9, v9
	v_med3_f32 v10, v6, s26, v209
	v_med3_f32 v7, v7, s26, v209
	v_mov_b32_e32 v6, v131
	v_cvt_pk_fp8_f32 v6, v10, v7
	v_med3_f32 v7, v8, s26, v209
	v_med3_f32 v8, v9, s26, v209
	v_mul_f32_e32 v9, 0xbcb8aa3b, v76
	v_cvt_pk_fp8_f32 v6, v7, v8 op_sel:[0,0,1]
	v_mul_f32_e32 v7, 0xbcb8aa3b, v74
	v_mul_f32_e32 v8, 0xbcb8aa3b, v75
	v_exp_f32_e32 v7, v7
	v_exp_f32_e32 v8, v8
	v_mul_f32_e32 v10, 0xbcb8aa3b, v77
	v_exp_f32_e32 v9, v9
	v_exp_f32_e32 v10, v10
	v_med3_f32 v11, v7, s26, v209
	v_med3_f32 v8, v8, s26, v209
	v_mov_b32_e32 v7, v131
	v_cvt_pk_fp8_f32 v7, v11, v8
	v_med3_f32 v8, v9, s26, v209
	v_med3_f32 v9, v10, s26, v209
	v_cvt_pk_fp8_f32 v7, v8, v9 op_sel:[0,0,1]
	v_add_co_u32_e32 v8, vcc, s9, v2
	s_mov_b32 s9, 0x10e000
	s_nop 0
	v_addc_co_u32_e32 v9, vcc, 0, v3, vcc
	global_store_dwordx4 v[8:9], v[4:7], off offset:1536
	s_nop 1
	v_mul_f32_e32 v4, 0xbcb8aa3b, v58
	v_mul_f32_e32 v5, 0xbcb8aa3b, v59
	v_exp_f32_e32 v4, v4
	v_exp_f32_e32 v5, v5
	v_mul_f32_e32 v6, 0xbcb8aa3b, v60
	v_mul_f32_e32 v7, 0xbcb8aa3b, v61
	v_exp_f32_e32 v6, v6
	v_exp_f32_e32 v7, v7
	v_med3_f32 v8, v4, s26, v209
	v_med3_f32 v5, v5, s26, v209
	v_mov_b32_e32 v4, v131
	v_cvt_pk_fp8_f32 v4, v8, v5
	v_med3_f32 v5, v6, s26, v209
	v_med3_f32 v6, v7, s26, v209
	v_mul_f32_e32 v7, 0xbcb8aa3b, v52
	v_cvt_pk_fp8_f32 v4, v5, v6 op_sel:[0,0,1]
	v_mul_f32_e32 v5, 0xbcb8aa3b, v50
	v_mul_f32_e32 v6, 0xbcb8aa3b, v51
	v_exp_f32_e32 v5, v5
	v_exp_f32_e32 v6, v6
	v_mul_f32_e32 v8, 0xbcb8aa3b, v53
	v_exp_f32_e32 v7, v7
	v_exp_f32_e32 v8, v8
	v_med3_f32 v9, v5, s26, v209
	v_med3_f32 v6, v6, s26, v209
	v_mov_b32_e32 v5, v131
	v_cvt_pk_fp8_f32 v5, v9, v6
	v_med3_f32 v6, v7, s26, v209
	v_med3_f32 v7, v8, s26, v209
	v_mul_f32_e32 v8, 0xbcb8aa3b, v64
	v_cvt_pk_fp8_f32 v5, v6, v7 op_sel:[0,0,1]
	v_mul_f32_e32 v6, 0xbcb8aa3b, v62
	v_mul_f32_e32 v7, 0xbcb8aa3b, v63
	v_exp_f32_e32 v6, v6
	v_exp_f32_e32 v7, v7
	v_mul_f32_e32 v9, 0xbcb8aa3b, v65
	v_exp_f32_e32 v8, v8
	v_exp_f32_e32 v9, v9
	v_med3_f32 v10, v6, s26, v209
	v_med3_f32 v7, v7, s26, v209
	v_mov_b32_e32 v6, v131
	v_cvt_pk_fp8_f32 v6, v10, v7
	v_med3_f32 v7, v8, s26, v209
	v_med3_f32 v8, v9, s26, v209
	v_mul_f32_e32 v9, 0xbcb8aa3b, v56
	v_cvt_pk_fp8_f32 v6, v7, v8 op_sel:[0,0,1]
	v_mul_f32_e32 v7, 0xbcb8aa3b, v54
	v_mul_f32_e32 v8, 0xbcb8aa3b, v55
	v_exp_f32_e32 v7, v7
	v_exp_f32_e32 v8, v8
	v_mul_f32_e32 v10, 0xbcb8aa3b, v57
	v_exp_f32_e32 v9, v9
	v_exp_f32_e32 v10, v10
	v_med3_f32 v11, v7, s26, v209
	v_med3_f32 v8, v8, s26, v209
	v_mov_b32_e32 v7, v131
	v_cvt_pk_fp8_f32 v7, v11, v8
	v_med3_f32 v8, v9, s26, v209
	v_med3_f32 v9, v10, s26, v209
	v_cvt_pk_fp8_f32 v7, v8, v9 op_sel:[0,0,1]
	v_add_co_u32_e32 v8, vcc, s9, v2
	s_mov_b32 s9, 0x12c000
	s_nop 0
	v_addc_co_u32_e32 v9, vcc, 0, v3, vcc
	global_store_dwordx4 v[8:9], v[4:7], off offset:1536
	s_nop 1
	v_mul_f32_e32 v4, 0xbcb8aa3b, v46
	v_mul_f32_e32 v5, 0xbcb8aa3b, v47
	v_exp_f32_e32 v4, v4
	v_exp_f32_e32 v5, v5
	v_mul_f32_e32 v6, 0xbcb8aa3b, v48
	v_mul_f32_e32 v7, 0xbcb8aa3b, v49
	v_exp_f32_e32 v6, v6
	v_exp_f32_e32 v7, v7
	v_med3_f32 v8, v4, s26, v209
	v_med3_f32 v5, v5, s26, v209
	v_mov_b32_e32 v4, v131
	v_cvt_pk_fp8_f32 v4, v8, v5
	v_med3_f32 v5, v6, s26, v209
	v_med3_f32 v6, v7, s26, v209
	v_mul_f32_e32 v7, 0xbcb8aa3b, v40
	v_cvt_pk_fp8_f32 v4, v5, v6 op_sel:[0,0,1]
	v_mul_f32_e32 v5, 0xbcb8aa3b, v38
	v_mul_f32_e32 v6, 0xbcb8aa3b, v39
	v_exp_f32_e32 v5, v5
	v_exp_f32_e32 v6, v6
	v_mul_f32_e32 v8, 0xbcb8aa3b, v41
	v_exp_f32_e32 v7, v7
	v_exp_f32_e32 v8, v8
	v_med3_f32 v9, v5, s26, v209
	v_med3_f32 v6, v6, s26, v209
	v_mov_b32_e32 v5, v131
	v_cvt_pk_fp8_f32 v5, v9, v6
	v_med3_f32 v6, v7, s26, v209
	v_med3_f32 v7, v8, s26, v209
	v_mul_f32_e32 v8, 0xbcb8aa3b, v44
	v_cvt_pk_fp8_f32 v5, v6, v7 op_sel:[0,0,1]
	v_mul_f32_e32 v6, 0xbcb8aa3b, v42
	v_mul_f32_e32 v7, 0xbcb8aa3b, v43
	v_exp_f32_e32 v6, v6
	v_exp_f32_e32 v7, v7
	v_mul_f32_e32 v9, 0xbcb8aa3b, v45
	v_exp_f32_e32 v8, v8
	v_exp_f32_e32 v9, v9
	v_med3_f32 v10, v6, s26, v209
	v_med3_f32 v7, v7, s26, v209
	v_mov_b32_e32 v6, v131
	v_cvt_pk_fp8_f32 v6, v10, v7
	v_med3_f32 v7, v8, s26, v209
	v_med3_f32 v8, v9, s26, v209
	v_mul_f32_e32 v9, 0xbcb8aa3b, v36
	v_cvt_pk_fp8_f32 v6, v7, v8 op_sel:[0,0,1]
	v_mul_f32_e32 v7, 0xbcb8aa3b, v34
	v_mul_f32_e32 v8, 0xbcb8aa3b, v35
	v_exp_f32_e32 v7, v7
	v_exp_f32_e32 v8, v8
	v_mul_f32_e32 v10, 0xbcb8aa3b, v37
	v_exp_f32_e32 v9, v9
	v_exp_f32_e32 v10, v10
	v_med3_f32 v11, v7, s26, v209
	v_med3_f32 v8, v8, s26, v209
	v_mov_b32_e32 v7, v131
	v_cvt_pk_fp8_f32 v7, v11, v8
	v_med3_f32 v8, v9, s26, v209
	v_med3_f32 v9, v10, s26, v209
	v_cvt_pk_fp8_f32 v7, v8, v9 op_sel:[0,0,1]
	v_add_co_u32_e32 v8, vcc, s9, v2
	s_nop 1
	v_addc_co_u32_e32 v9, vcc, 0, v3, vcc
	global_store_dwordx4 v[8:9], v[4:7], off offset:1536
	v_add_co_u32_e32 v2, vcc, 0x14a000, v2
	s_nop 0
	v_mul_f32_e32 v4, 0xbcb8aa3b, v30
	v_mul_f32_e32 v5, 0xbcb8aa3b, v31
	v_exp_f32_e32 v4, v4
	v_exp_f32_e32 v5, v5
	v_mul_f32_e32 v6, 0xbcb8aa3b, v32
	v_mul_f32_e32 v7, 0xbcb8aa3b, v33
	v_exp_f32_e32 v6, v6
	v_exp_f32_e32 v7, v7
	v_med3_f32 v8, v4, s26, v209
	v_med3_f32 v5, v5, s26, v209
	v_mov_b32_e32 v4, v131
	v_cvt_pk_fp8_f32 v4, v8, v5
	v_med3_f32 v5, v6, s26, v209
	v_med3_f32 v6, v7, s26, v209
	v_mul_f32_e32 v7, 0xbcb8aa3b, v24
	v_cvt_pk_fp8_f32 v4, v5, v6 op_sel:[0,0,1]
	v_mul_f32_e32 v5, 0xbcb8aa3b, v22
	v_mul_f32_e32 v6, 0xbcb8aa3b, v23
	v_exp_f32_e32 v5, v5
	v_exp_f32_e32 v6, v6
	v_mul_f32_e32 v8, 0xbcb8aa3b, v25
	v_exp_f32_e32 v7, v7
	v_exp_f32_e32 v8, v8
	v_med3_f32 v9, v5, s26, v209
	v_med3_f32 v6, v6, s26, v209
	v_mov_b32_e32 v5, v131
	v_cvt_pk_fp8_f32 v5, v9, v6
	v_med3_f32 v6, v7, s26, v209
	v_med3_f32 v7, v8, s26, v209
	v_mul_f32_e32 v8, 0xbcb8aa3b, v28
	v_cvt_pk_fp8_f32 v5, v6, v7 op_sel:[0,0,1]
	v_mul_f32_e32 v6, 0xbcb8aa3b, v26
	v_mul_f32_e32 v7, 0xbcb8aa3b, v27
	v_exp_f32_e32 v6, v6
	v_exp_f32_e32 v7, v7
	v_mul_f32_e32 v9, 0xbcb8aa3b, v29
	v_exp_f32_e32 v8, v8
	v_exp_f32_e32 v9, v9
	v_med3_f32 v10, v6, s26, v209
	v_med3_f32 v7, v7, s26, v209
	v_mov_b32_e32 v6, v131
	v_cvt_pk_fp8_f32 v6, v10, v7
	v_med3_f32 v7, v8, s26, v209
	v_med3_f32 v8, v9, s26, v209
	v_mul_f32_e32 v9, 0xbcb8aa3b, v20
	v_cvt_pk_fp8_f32 v6, v7, v8 op_sel:[0,0,1]
	v_mul_f32_e32 v7, 0xbcb8aa3b, v18
	v_mul_f32_e32 v8, 0xbcb8aa3b, v19
	v_exp_f32_e32 v7, v7
	v_exp_f32_e32 v8, v8
	v_mul_f32_e32 v10, 0xbcb8aa3b, v21
	v_exp_f32_e32 v9, v9
	v_exp_f32_e32 v10, v10
	v_med3_f32 v11, v7, s26, v209
	v_med3_f32 v8, v8, s26, v209
	v_mov_b32_e32 v7, v131
	v_cvt_pk_fp8_f32 v7, v11, v8
	v_med3_f32 v8, v9, s26, v209
	v_med3_f32 v9, v10, s26, v209
	v_addc_co_u32_e32 v3, vcc, 0, v3, vcc
	v_cvt_pk_fp8_f32 v7, v8, v9 op_sel:[0,0,1]
	s_and_b64 vcc, exec, s[6:7]
	global_store_dwordx4 v[2:3], v[4:7], off offset:1536
	s_cbranch_vccz .LBB0_416
	s_waitcnt vmcnt(0)
	s_cmpk_gt_u32 s33, 0xff
	s_cbranch_scc1 .LBB0_423
	s_barrier

.LBB0_456:
	s_xor_b64 s[72:73], s[76:77], -1
	s_and_b64 s[60:61], s[76:77], exec
	s_cselect_b32 s59, s19, s7
	s_cselect_b32 s60, s18, s6
	s_add_i32 s69, 0, 0x10000
	v_add_u32_e32 v130, s69, v157
	ds_read_b128 v[2:5], v130
	ds_read_b128 v[6:9], v130 offset:1024
	ds_read_b128 v[10:13], v130 offset:2048
	ds_read_b128 v[14:17], v130 offset:3072
	s_and_b64 s[62:63], s[76:77], exec
	s_cselect_b32 s61, s67, s75
	s_cselect_b32 s62, s66, s74
	s_add_u32 s64, s6, 0x20080
	s_addc_u32 s65, s7, 0
	s_add_i32 s63, s37, 0xc000
	v_lshl_add_u64 v[42:43], s[64:65], 0, v[150:151]
	s_mov_b32 m0, s63
	ds_read_b128 v[18:21], v161
	ds_read_b128 v[22:25], v161 offset:1024
	ds_read_b128 v[26:29], v161 offset:2048
	ds_read_b128 v[30:33], v161 offset:3072
	ds_read_b128 v[34:37], v161 offset:4096
	ds_read_b128 v[38:41], v161 offset:5120
	ds_read_b128 v[54:57], v161 offset:6144
	ds_read_b128 v[58:61], v161 offset:7168
	global_load_lds_dwordx4 v[42:43], off
	v_lshl_add_u64 v[42:43], s[64:65], 0, v[154:155]
	s_add_i32 s64, s37, 0xe000
	s_mov_b32 m0, s64
	s_nop 0
	global_load_lds_dwordx4 v[42:43], off
	s_waitcnt lgkmcnt(8)
	s_waitcnt vmcnt(10)
	s_barrier
	s_setprio 1
	s_waitcnt lgkmcnt(6)
	v_mfma_scale_f32_16x16x128_f8f6f4 v[114:117], v[2:9], v[18:25], 0, v205, v205 op_sel_hi:[0,0,0]
	v_mfma_scale_f32_16x16x128_f8f6f4 v[126:129], v[10:17], v[18:25], 0, v205, v205 op_sel_hi:[0,0,0]
	s_waitcnt lgkmcnt(4)
	v_mfma_scale_f32_16x16x128_f8f6f4 v[102:105], v[2:9], v[26:33], 0, v205, v205 op_sel_hi:[0,0,0]
	v_mfma_scale_f32_16x16x128_f8f6f4 v[98:101], v[10:17], v[26:33], 0, v205, v205 op_sel_hi:[0,0,0]
	s_waitcnt lgkmcnt(2)
	v_mfma_scale_f32_16x16x128_f8f6f4 v[78:81], v[2:9], v[34:41], 0, v205, v205 op_sel_hi:[0,0,0]
	v_mfma_scale_f32_16x16x128_f8f6f4 v[70:73], v[10:17], v[34:41], 0, v205, v205 op_sel_hi:[0,0,0]
	s_waitcnt lgkmcnt(0)
	v_mfma_scale_f32_16x16x128_f8f6f4 v[50:53], v[2:9], v[54:61], 0, v205, v205 op_sel_hi:[0,0,0]
	v_mfma_scale_f32_16x16x128_f8f6f4 v[42:45], v[10:17], v[54:61], 0, v205, v205 op_sel_hi:[0,0,0]
	s_setprio 0
	s_barrier
	s_add_i32 s71, 0, 0x14000
	v_lshl_add_u64 v[186:187], s[74:75], 0, v[148:149]
	s_mov_b64 s[76:77], 0x100
	s_add_i32 s65, s69, s36
	v_add_u32_e32 v163, s71, v157
	v_lshl_add_u64 v[46:47], v[186:187], 0, s[76:77]
	s_mov_b32 m0, s65
	v_lshl_add_u64 v[188:189], s[74:75], 0, v[152:153]
	s_add_i32 s69, s65, 0x2000
	ds_read_b128 v[190:193], v163
	ds_read_b128 v[194:197], v163 offset:1024
	ds_read_b128 v[218:221], v163 offset:2048
	ds_read_b128 v[222:225], v163 offset:3072
	global_load_lds_dwordx4 v[46:47], off
	v_lshl_add_u64 v[46:47], v[188:189], 0, s[76:77]
	s_mov_b32 m0, s69
	s_nop 0
	global_load_lds_dwordx4 v[46:47], off
	s_waitcnt vmcnt(10)
	s_barrier
	s_setprio 1
	s_waitcnt lgkmcnt(2)
	v_mfma_scale_f32_16x16x128_f8f6f4 v[140:143], v[190:197], v[18:25], 0, v205, v205 op_sel_hi:[0,0,0]
	s_waitcnt lgkmcnt(0)
	v_mfma_scale_f32_16x16x128_f8f6f4 v[144:147], v[218:225], v[18:25], 0, v205, v205 op_sel_hi:[0,0,0]
	v_mfma_scale_f32_16x16x128_f8f6f4 v[136:139], v[190:197], v[26:33], 0, v205, v205 op_sel_hi:[0,0,0]
	v_mfma_scale_f32_16x16x128_f8f6f4 v[132:135], v[218:225], v[26:33], 0, v205, v205 op_sel_hi:[0,0,0]
	v_mfma_scale_f32_16x16x128_f8f6f4 v[110:113], v[190:197], v[34:41], 0, v205, v205 op_sel_hi:[0,0,0]
	v_mfma_scale_f32_16x16x128_f8f6f4 v[106:109], v[218:225], v[34:41], 0, v205, v205 op_sel_hi:[0,0,0]
	v_mfma_scale_f32_16x16x128_f8f6f4 v[74:77], v[190:197], v[54:61], 0, v205, v205 op_sel_hi:[0,0,0]
	v_mfma_scale_f32_16x16x128_f8f6f4 v[66:69], v[218:225], v[54:61], 0, v205, v205 op_sel_hi:[0,0,0]
	s_setprio 0
	v_lshl_add_u64 v[182:183], s[6:7], 0, v[150:151]
	s_mov_b32 m0, s37
	v_lshl_add_u64 v[18:19], v[182:183], 0, s[76:77]
	v_lshl_add_u64 v[184:185], s[6:7], 0, v[154:155]
	s_barrier
	ds_read_b128 v[26:29], v161 offset:16384
	ds_read_b128 v[30:33], v161 offset:17408
	ds_read_b128 v[226:229], v161 offset:18432
	ds_read_b128 v[230:233], v161 offset:19456
	ds_read_b128 v[234:237], v161 offset:20480
	ds_read_b128 v[238:241], v161 offset:21504
	ds_read_b128 v[242:245], v161 offset:22528
	ds_read_b128 v[246:249], v161 offset:23552
	global_load_lds_dwordx4 v[18:19], off
	v_lshl_add_u64 v[18:19], v[184:185], 0, s[76:77]
	s_mov_b32 m0, s38
	s_nop 0
	global_load_lds_dwordx4 v[18:19], off
	s_barrier
	s_setprio 1
	s_waitcnt lgkmcnt(6)
	v_mfma_scale_f32_16x16x128_f8f6f4 v[94:97], v[2:9], v[26:33], 0, v205, v205 op_sel_hi:[0,0,0]
	v_mfma_scale_f32_16x16x128_f8f6f4 v[90:93], v[10:17], v[26:33], 0, v205, v205 op_sel_hi:[0,0,0]
	s_waitcnt lgkmcnt(4)
	v_mfma_scale_f32_16x16x128_f8f6f4 v[62:65], v[2:9], v[226:233], 0, v205, v205 op_sel_hi:[0,0,0]
	v_mfma_scale_f32_16x16x128_f8f6f4 v[58:61], v[10:17], v[226:233], 0, v205, v205 op_sel_hi:[0,0,0]
	s_waitcnt lgkmcnt(2)
	v_mfma_scale_f32_16x16x128_f8f6f4 v[38:41], v[2:9], v[234:241], 0, v205, v205 op_sel_hi:[0,0,0]
	v_mfma_scale_f32_16x16x128_f8f6f4 v[34:37], v[10:17], v[234:241], 0, v205, v205 op_sel_hi:[0,0,0]
	s_waitcnt lgkmcnt(0)
	v_mfma_scale_f32_16x16x128_f8f6f4 v[22:25], v[2:9], v[242:249], 0, v205, v205 op_sel_hi:[0,0,0]
	v_mfma_scale_f32_16x16x128_f8f6f4 v[18:21], v[10:17], v[242:249], 0, v205, v205 op_sel_hi:[0,0,0]
	s_setprio 0
	s_barrier
	s_add_u32 s76, s74, 0x2100
	s_addc_u32 s77, s75, 0
	s_add_i32 s71, s71, s36
	v_lshl_add_u64 v[2:3], s[76:77], 0, v[148:149]
	s_mov_b32 m0, s71
	s_add_i32 s79, s71, 0x2000
	global_load_lds_dwordx4 v[2:3], off
	v_lshl_add_u64 v[2:3], s[76:77], 0, v[152:153]
	s_mov_b32 m0, s79
	s_nop 0
	global_load_lds_dwordx4 v[2:3], off
	s_waitcnt vmcnt(10)
	s_barrier
	s_setprio 1
	v_mfma_scale_f32_16x16x128_f8f6f4 v[122:125], v[190:197], v[26:33], 0, v205, v205 op_sel_hi:[0,0,0]
	v_mfma_scale_f32_16x16x128_f8f6f4 v[118:121], v[218:225], v[26:33], 0, v205, v205 op_sel_hi:[0,0,0]
	v_mfma_scale_f32_16x16x128_f8f6f4 v[86:89], v[190:197], v[226:233], 0, v205, v205 op_sel_hi:[0,0,0]
	v_mfma_scale_f32_16x16x128_f8f6f4 v[82:85], v[218:225], v[226:233], 0, v205, v205 op_sel_hi:[0,0,0]
	v_mfma_scale_f32_16x16x128_f8f6f4 v[54:57], v[190:197], v[234:241], 0, v205, v205 op_sel_hi:[0,0,0]
	v_mfma_scale_f32_16x16x128_f8f6f4 v[46:49], v[218:225], v[234:241], 0, v205, v205 op_sel_hi:[0,0,0]
	v_mfma_scale_f32_16x16x128_f8f6f4 v[30:33], v[190:197], v[242:249], 0, v205, v205 op_sel_hi:[0,0,0]
	v_mfma_scale_f32_16x16x128_f8f6f4 v[26:29], v[218:225], v[242:249], 0, v205, v205 op_sel_hi:[0,0,0]
	s_setprio 0
	s_add_i32 s81, 0, 0x18000
	v_add_u32_e32 v165, s81, v157
	s_barrier
	ds_read_b128 v[10:13], v165
	ds_read_b128 v[14:17], v165 offset:1024
	ds_read_b128 v[2:5], v165 offset:2048
	ds_read_b128 v[6:9], v165 offset:3072
	s_add_u32 s76, s6, 0x20100
	s_addc_u32 s77, s7, 0
	s_mov_b32 m0, s39
	v_lshl_add_u64 v[168:169], s[76:77], 0, v[150:151]
	ds_read_b128 v[190:193], v161 offset:32768
	ds_read_b128 v[194:197], v161 offset:33792
	ds_read_b128 v[218:221], v161 offset:34816
	ds_read_b128 v[222:225], v161 offset:35840
	ds_read_b128 v[226:229], v161 offset:36864
	ds_read_b128 v[230:233], v161 offset:37888
	ds_read_b128 v[234:237], v161 offset:38912
	ds_read_b128 v[238:241], v161 offset:39936
	global_load_lds_dwordx4 v[168:169], off
	v_lshl_add_u64 v[168:169], s[76:77], 0, v[154:155]
	s_mov_b32 m0, s42
	s_nop 0
	global_load_lds_dwordx4 v[168:169], off
	s_waitcnt lgkmcnt(8)
	s_waitcnt vmcnt(10)
	s_barrier
	s_setprio 1
	s_waitcnt lgkmcnt(6)
	v_mfma_scale_f32_16x16x128_f8f6f4 v[114:117], v[10:17], v[190:197], v[114:117], v205, v205 op_sel_hi:[0,0,0]
	v_mfma_scale_f32_16x16x128_f8f6f4 v[126:129], v[2:9], v[190:197], v[126:129], v205, v205 op_sel_hi:[0,0,0]
	s_waitcnt lgkmcnt(4)
	v_mfma_scale_f32_16x16x128_f8f6f4 v[102:105], v[10:17], v[218:225], v[102:105], v205, v205 op_sel_hi:[0,0,0]
	v_mfma_scale_f32_16x16x128_f8f6f4 v[98:101], v[2:9], v[218:225], v[98:101], v205, v205 op_sel_hi:[0,0,0]
	s_waitcnt lgkmcnt(2)
	v_mfma_scale_f32_16x16x128_f8f6f4 v[78:81], v[10:17], v[226:233], v[78:81], v205, v205 op_sel_hi:[0,0,0]
	v_mfma_scale_f32_16x16x128_f8f6f4 v[70:73], v[2:9], v[226:233], v[70:73], v205, v205 op_sel_hi:[0,0,0]
	s_waitcnt lgkmcnt(0)
	v_mfma_scale_f32_16x16x128_f8f6f4 v[50:53], v[10:17], v[234:241], v[50:53], v205, v205 op_sel_hi:[0,0,0]
	v_mfma_scale_f32_16x16x128_f8f6f4 v[42:45], v[2:9], v[234:241], v[42:45], v205, v205 op_sel_hi:[0,0,0]
	s_setprio 0
	s_barrier
	s_add_i32 s83, 0, 0x1c000
	s_mov_b64 s[76:77], 0x180
	s_add_i32 s81, s81, s36
	v_add_u32_e32 v167, s83, v157
	v_lshl_add_u64 v[186:187], v[186:187], 0, s[76:77]
	s_mov_b32 m0, s81
	s_add_i32 s82, s81, 0x2000
	ds_read_b128 v[242:245], v167
	ds_read_b128 v[246:249], v167 offset:1024
	ds_read_b128 v[168:171], v167 offset:2048
	ds_read_b128 v[172:175], v167 offset:3072
	global_load_lds_dwordx4 v[186:187], off
	v_lshl_add_u64 v[186:187], v[188:189], 0, s[76:77]
	s_mov_b32 m0, s82
	s_nop 0
	global_load_lds_dwordx4 v[186:187], off
	s_waitcnt vmcnt(10)
	s_barrier
	s_setprio 1
	s_waitcnt lgkmcnt(2)
	v_mfma_scale_f32_16x16x128_f8f6f4 v[140:143], v[242:249], v[190:197], v[140:143], v205, v205 op_sel_hi:[0,0,0]
	s_waitcnt lgkmcnt(0)
	v_mfma_scale_f32_16x16x128_f8f6f4 v[144:147], v[168:175], v[190:197], v[144:147], v205, v205 op_sel_hi:[0,0,0]
	v_mfma_scale_f32_16x16x128_f8f6f4 v[136:139], v[242:249], v[218:225], v[136:139], v205, v205 op_sel_hi:[0,0,0]
	v_mfma_scale_f32_16x16x128_f8f6f4 v[132:135], v[168:175], v[218:225], v[132:135], v205, v205 op_sel_hi:[0,0,0]
	v_mfma_scale_f32_16x16x128_f8f6f4 v[110:113], v[242:249], v[226:233], v[110:113], v205, v205 op_sel_hi:[0,0,0]
	v_mfma_scale_f32_16x16x128_f8f6f4 v[106:109], v[168:175], v[226:233], v[106:109], v205, v205 op_sel_hi:[0,0,0]
	v_mfma_scale_f32_16x16x128_f8f6f4 v[74:77], v[242:249], v[234:241], v[74:77], v205, v205 op_sel_hi:[0,0,0]
	v_mfma_scale_f32_16x16x128_f8f6f4 v[66:69], v[168:175], v[234:241], v[66:69], v205, v205 op_sel_hi:[0,0,0]
	s_setprio 0
	s_mov_b32 m0, s45
	v_lshl_add_u64 v[182:183], v[182:183], 0, s[76:77]
	s_barrier
	ds_read_b128 v[186:189], v161 offset:49152
	ds_read_b128 v[190:193], v161 offset:50176
	ds_read_b128 v[194:197], v161 offset:51200
	ds_read_b128 v[198:201], v161 offset:52224
	ds_read_b128 v[218:221], v161 offset:53248
	ds_read_b128 v[222:225], v161 offset:54272
	ds_read_b128 v[226:229], v161 offset:55296
	ds_read_b128 v[230:233], v161 offset:56320
	global_load_lds_dwordx4 v[182:183], off
	v_lshl_add_u64 v[182:183], v[184:185], 0, s[76:77]
	s_mov_b32 m0, s46
	s_nop 0
	global_load_lds_dwordx4 v[182:183], off
	s_barrier
	s_setprio 1
	s_waitcnt lgkmcnt(6)
	v_mfma_scale_f32_16x16x128_f8f6f4 v[94:97], v[10:17], v[186:193], v[94:97], v205, v205 op_sel_hi:[0,0,0]
	v_mfma_scale_f32_16x16x128_f8f6f4 v[90:93], v[2:9], v[186:193], v[90:93], v205, v205 op_sel_hi:[0,0,0]
	s_waitcnt lgkmcnt(4)
	v_mfma_scale_f32_16x16x128_f8f6f4 v[62:65], v[10:17], v[194:201], v[62:65], v205, v205 op_sel_hi:[0,0,0]
	v_mfma_scale_f32_16x16x128_f8f6f4 v[58:61], v[2:9], v[194:201], v[58:61], v205, v205 op_sel_hi:[0,0,0]
	s_waitcnt lgkmcnt(2)
	v_mfma_scale_f32_16x16x128_f8f6f4 v[38:41], v[10:17], v[218:225], v[38:41], v205, v205 op_sel_hi:[0,0,0]
	v_mfma_scale_f32_16x16x128_f8f6f4 v[34:37], v[2:9], v[218:225], v[34:37], v205, v205 op_sel_hi:[0,0,0]
	s_waitcnt lgkmcnt(0)
	v_mfma_scale_f32_16x16x128_f8f6f4 v[22:25], v[10:17], v[226:233], v[22:25], v205, v205 op_sel_hi:[0,0,0]
	v_mfma_scale_f32_16x16x128_f8f6f4 v[18:21], v[2:9], v[226:233], v[18:21], v205, v205 op_sel_hi:[0,0,0]
	s_setprio 0
	s_barrier
	s_add_u32 s76, s74, 0x2180
	s_addc_u32 s77, s75, 0
	s_add_i32 s83, s83, s36
	v_lshl_add_u64 v[2:3], s[76:77], 0, v[148:149]
	s_mov_b32 m0, s83
	s_add_i32 s84, s83, 0x2000
	global_load_lds_dwordx4 v[2:3], off
	v_lshl_add_u64 v[2:3], s[76:77], 0, v[152:153]
	s_mov_b32 m0, s84
	s_nop 0
	global_load_lds_dwordx4 v[2:3], off
	s_waitcnt vmcnt(10)
	s_barrier
	s_setprio 1
	v_mfma_scale_f32_16x16x128_f8f6f4 v[122:125], v[242:249], v[186:193], v[122:125], v205, v205 op_sel_hi:[0,0,0]
	v_mfma_scale_f32_16x16x128_f8f6f4 v[118:121], v[168:175], v[186:193], v[118:121], v205, v205 op_sel_hi:[0,0,0]
	v_mfma_scale_f32_16x16x128_f8f6f4 v[86:89], v[242:249], v[194:201], v[86:89], v205, v205 op_sel_hi:[0,0,0]
	v_mfma_scale_f32_16x16x128_f8f6f4 v[82:85], v[168:175], v[194:201], v[82:85], v205, v205 op_sel_hi:[0,0,0]
	v_mfma_scale_f32_16x16x128_f8f6f4 v[54:57], v[242:249], v[218:225], v[54:57], v205, v205 op_sel_hi:[0,0,0]
	v_mfma_scale_f32_16x16x128_f8f6f4 v[46:49], v[168:175], v[218:225], v[46:49], v205, v205 op_sel_hi:[0,0,0]
	v_mfma_scale_f32_16x16x128_f8f6f4 v[30:33], v[242:249], v[226:233], v[30:33], v205, v205 op_sel_hi:[0,0,0]
	v_mfma_scale_f32_16x16x128_f8f6f4 v[26:29], v[168:175], v[226:233], v[26:29], v205, v205 op_sel_hi:[0,0,0]
	s_setprio 0
	s_add_u32 s6, s6, 0x20180
	s_addc_u32 s7, s7, 0
	s_add_u32 s85, s74, 0x200
	s_addc_u32 s86, s75, 0
	s_mov_b32 s87, 0
	s_barrier
.LBB0_457:
	ds_read_b128 v[10:13], v130
	ds_read_b128 v[14:17], v130 offset:1024
	ds_read_b128 v[168:171], v130 offset:2048
	ds_read_b128 v[172:175], v130 offset:3072
	s_add_u32 s74, s6, 0xfffe0080
	s_addc_u32 s75, s7, -1
	s_cmp_eq_u32 s87, 4
	s_cselect_b32 s77, s59, s75
	s_cselect_b32 s76, s60, s74
	s_cselect_b32 s75, s61, s86
	s_cselect_b32 s74, s62, s85
	s_mov_b32 m0, s63
	v_lshl_add_u64 v[2:3], s[6:7], 0, v[178:179]
	ds_read_b128 v[182:185], v161
	ds_read_b128 v[186:189], v161 offset:1024
	ds_read_b128 v[190:193], v161 offset:2048
	ds_read_b128 v[194:197], v161 offset:3072
	ds_read_b128 v[218:221], v161 offset:4096
	ds_read_b128 v[222:225], v161 offset:5120
	ds_read_b128 v[226:229], v161 offset:6144
	ds_read_b128 v[230:233], v161 offset:7168
	global_load_lds_dwordx4 v[2:3], off
	v_lshl_add_u64 v[2:3], s[6:7], 0, v[180:181]
	s_mov_b32 m0, s64
	s_nop 0
	global_load_lds_dwordx4 v[2:3], off
	s_waitcnt lgkmcnt(8)
	s_waitcnt vmcnt(10)
	s_barrier
	s_setprio 1
	s_waitcnt lgkmcnt(6)
	v_mfma_scale_f32_16x16x128_f8f6f4 v[114:117], v[10:17], v[182:189], v[114:117], v205, v205 op_sel_hi:[0,0,0]
	v_mfma_scale_f32_16x16x128_f8f6f4 v[126:129], v[168:175], v[182:189], v[126:129], v205, v205 op_sel_hi:[0,0,0]
	s_waitcnt lgkmcnt(4)
	v_mfma_scale_f32_16x16x128_f8f6f4 v[102:105], v[10:17], v[190:197], v[102:105], v205, v205 op_sel_hi:[0,0,0]
	v_mfma_scale_f32_16x16x128_f8f6f4 v[98:101], v[168:175], v[190:197], v[98:101], v205, v205 op_sel_hi:[0,0,0]
	s_waitcnt lgkmcnt(2)
	v_mfma_scale_f32_16x16x128_f8f6f4 v[78:81], v[10:17], v[218:225], v[78:81], v205, v205 op_sel_hi:[0,0,0]
	v_mfma_scale_f32_16x16x128_f8f6f4 v[70:73], v[168:175], v[218:225], v[70:73], v205, v205 op_sel_hi:[0,0,0]
	s_waitcnt lgkmcnt(0)
	v_mfma_scale_f32_16x16x128_f8f6f4 v[50:53], v[10:17], v[226:233], v[50:53], v205, v205 op_sel_hi:[0,0,0]
	v_mfma_scale_f32_16x16x128_f8f6f4 v[42:45], v[168:175], v[226:233], v[42:45], v205, v205 op_sel_hi:[0,0,0]
	s_setprio 0
	s_barrier
	s_mov_b32 m0, s65
	v_lshl_add_u64 v[6:7], s[74:75], 0, v[148:149]
	ds_read_b128 v[234:237], v163
	ds_read_b128 v[238:241], v163 offset:1024
	ds_read_b128 v[242:245], v163 offset:2048
	ds_read_b128 v[246:249], v163 offset:3072
	global_load_lds_dwordx4 v[6:7], off
	v_lshl_add_u64 v[8:9], s[74:75], 0, v[152:153]
	s_mov_b32 m0, s69
	s_nop 0
	global_load_lds_dwordx4 v[8:9], off
	s_waitcnt vmcnt(10)
	s_barrier
	s_setprio 1
	s_waitcnt lgkmcnt(2)
	v_mfma_scale_f32_16x16x128_f8f6f4 v[140:143], v[234:241], v[182:189], v[140:143], v205, v205 op_sel_hi:[0,0,0]
	s_waitcnt lgkmcnt(0)
	v_mfma_scale_f32_16x16x128_f8f6f4 v[144:147], v[242:249], v[182:189], v[144:147], v205, v205 op_sel_hi:[0,0,0]
	v_mfma_scale_f32_16x16x128_f8f6f4 v[136:139], v[234:241], v[190:197], v[136:139], v205, v205 op_sel_hi:[0,0,0]
	v_mfma_scale_f32_16x16x128_f8f6f4 v[132:135], v[242:249], v[190:197], v[132:135], v205, v205 op_sel_hi:[0,0,0]
	v_mfma_scale_f32_16x16x128_f8f6f4 v[110:113], v[234:241], v[218:225], v[110:113], v205, v205 op_sel_hi:[0,0,0]
	v_mfma_scale_f32_16x16x128_f8f6f4 v[106:109], v[242:249], v[218:225], v[106:109], v205, v205 op_sel_hi:[0,0,0]
	v_mfma_scale_f32_16x16x128_f8f6f4 v[74:77], v[234:241], v[226:233], v[74:77], v205, v205 op_sel_hi:[0,0,0]
	v_mfma_scale_f32_16x16x128_f8f6f4 v[66:69], v[242:249], v[226:233], v[66:69], v205, v205 op_sel_hi:[0,0,0]
	s_setprio 0
	s_mov_b32 m0, s37
	v_lshl_add_u64 v[2:3], s[76:77], 0, v[150:151]
	s_barrier
	ds_read_b128 v[182:185], v161 offset:16384
	ds_read_b128 v[186:189], v161 offset:17408
	ds_read_b128 v[190:193], v161 offset:18432
	ds_read_b128 v[194:197], v161 offset:19456
	ds_read_b128 v[218:221], v161 offset:20480
	ds_read_b128 v[222:225], v161 offset:21504
	ds_read_b128 v[226:229], v161 offset:22528
	ds_read_b128 v[230:233], v161 offset:23552
	global_load_lds_dwordx4 v[2:3], off
	v_lshl_add_u64 v[4:5], s[76:77], 0, v[154:155]
	s_mov_b32 m0, s38
	s_nop 0
	global_load_lds_dwordx4 v[4:5], off
	s_barrier
	s_setprio 1
	s_waitcnt lgkmcnt(6)
	v_mfma_scale_f32_16x16x128_f8f6f4 v[94:97], v[10:17], v[182:189], v[94:97], v205, v205 op_sel_hi:[0,0,0]
	v_mfma_scale_f32_16x16x128_f8f6f4 v[90:93], v[168:175], v[182:189], v[90:93], v205, v205 op_sel_hi:[0,0,0]
	s_waitcnt lgkmcnt(4)
	v_mfma_scale_f32_16x16x128_f8f6f4 v[62:65], v[10:17], v[190:197], v[62:65], v205, v205 op_sel_hi:[0,0,0]
	v_mfma_scale_f32_16x16x128_f8f6f4 v[58:61], v[168:175], v[190:197], v[58:61], v205, v205 op_sel_hi:[0,0,0]
	s_waitcnt lgkmcnt(2)
	v_mfma_scale_f32_16x16x128_f8f6f4 v[38:41], v[10:17], v[218:225], v[38:41], v205, v205 op_sel_hi:[0,0,0]
	v_mfma_scale_f32_16x16x128_f8f6f4 v[34:37], v[168:175], v[218:225], v[34:37], v205, v205 op_sel_hi:[0,0,0]
	s_waitcnt lgkmcnt(0)
	v_mfma_scale_f32_16x16x128_f8f6f4 v[22:25], v[10:17], v[226:233], v[22:25], v205, v205 op_sel_hi:[0,0,0]
	v_mfma_scale_f32_16x16x128_f8f6f4 v[18:21], v[168:175], v[226:233], v[18:21], v205, v205 op_sel_hi:[0,0,0]
	s_setprio 0
	s_barrier
	s_add_u32 s88, s74, 0x2000
	s_addc_u32 s89, s75, 0
	s_mov_b32 m0, s71
	v_lshl_add_u64 v[10:11], s[88:89], 0, v[148:149]
	global_load_lds_dwordx4 v[10:11], off
	v_lshl_add_u64 v[10:11], s[88:89], 0, v[152:153]
	s_mov_b32 m0, s79
	s_nop 0
	global_load_lds_dwordx4 v[10:11], off
	s_waitcnt vmcnt(10)
	s_barrier
	s_setprio 1
	v_mfma_scale_f32_16x16x128_f8f6f4 v[122:125], v[234:241], v[182:189], v[122:125], v205, v205 op_sel_hi:[0,0,0]
	v_mfma_scale_f32_16x16x128_f8f6f4 v[118:121], v[242:249], v[182:189], v[118:121], v205, v205 op_sel_hi:[0,0,0]
	v_mfma_scale_f32_16x16x128_f8f6f4 v[86:89], v[234:241], v[190:197], v[86:89], v205, v205 op_sel_hi:[0,0,0]
	v_mfma_scale_f32_16x16x128_f8f6f4 v[82:85], v[242:249], v[190:197], v[82:85], v205, v205 op_sel_hi:[0,0,0]
	v_mfma_scale_f32_16x16x128_f8f6f4 v[54:57], v[234:241], v[218:225], v[54:57], v205, v205 op_sel_hi:[0,0,0]
	v_mfma_scale_f32_16x16x128_f8f6f4 v[46:49], v[242:249], v[218:225], v[46:49], v205, v205 op_sel_hi:[0,0,0]
	v_mfma_scale_f32_16x16x128_f8f6f4 v[30:33], v[234:241], v[226:233], v[30:33], v205, v205 op_sel_hi:[0,0,0]
	v_mfma_scale_f32_16x16x128_f8f6f4 v[26:29], v[242:249], v[226:233], v[26:29], v205, v205 op_sel_hi:[0,0,0]
	s_setprio 0
	s_barrier
	ds_read_b128 v[10:13], v165
	ds_read_b128 v[14:17], v165 offset:1024
	ds_read_b128 v[168:171], v165 offset:2048
	ds_read_b128 v[172:175], v165 offset:3072
	s_add_u32 s76, s76, 0x20000
	s_addc_u32 s77, s77, 0
	s_mov_b32 m0, s39
	v_lshl_add_u64 v[198:199], s[76:77], 0, v[150:151]
	ds_read_b128 v[182:185], v161 offset:32768
	ds_read_b128 v[186:189], v161 offset:33792
	ds_read_b128 v[190:193], v161 offset:34816
	ds_read_b128 v[194:197], v161 offset:35840
	ds_read_b128 v[218:221], v161 offset:36864
	ds_read_b128 v[222:225], v161 offset:37888
	ds_read_b128 v[226:229], v161 offset:38912
	ds_read_b128 v[230:233], v161 offset:39936
	global_load_lds_dwordx4 v[198:199], off
	v_lshl_add_u64 v[198:199], s[76:77], 0, v[154:155]
	s_mov_b32 m0, s42
	s_nop 0
	global_load_lds_dwordx4 v[198:199], off
	s_waitcnt lgkmcnt(8)
	s_waitcnt vmcnt(10)
	s_barrier
	s_setprio 1
	s_waitcnt lgkmcnt(6)
	v_mfma_scale_f32_16x16x128_f8f6f4 v[114:117], v[10:17], v[182:189], v[114:117], v205, v205 op_sel_hi:[0,0,0]
	v_mfma_scale_f32_16x16x128_f8f6f4 v[126:129], v[168:175], v[182:189], v[126:129], v205, v205 op_sel_hi:[0,0,0]
	s_waitcnt lgkmcnt(4)
	v_mfma_scale_f32_16x16x128_f8f6f4 v[102:105], v[10:17], v[190:197], v[102:105], v205, v205 op_sel_hi:[0,0,0]
	v_mfma_scale_f32_16x16x128_f8f6f4 v[98:101], v[168:175], v[190:197], v[98:101], v205, v205 op_sel_hi:[0,0,0]
	s_waitcnt lgkmcnt(2)
	v_mfma_scale_f32_16x16x128_f8f6f4 v[78:81], v[10:17], v[218:225], v[78:81], v205, v205 op_sel_hi:[0,0,0]
	v_mfma_scale_f32_16x16x128_f8f6f4 v[70:73], v[168:175], v[218:225], v[70:73], v205, v205 op_sel_hi:[0,0,0]
	s_waitcnt lgkmcnt(0)
	v_mfma_scale_f32_16x16x128_f8f6f4 v[50:53], v[10:17], v[226:233], v[50:53], v205, v205 op_sel_hi:[0,0,0]
	v_mfma_scale_f32_16x16x128_f8f6f4 v[42:45], v[168:175], v[226:233], v[42:45], v205, v205 op_sel_hi:[0,0,0]
	s_setprio 0
	s_barrier
	s_mov_b32 m0, s81
	v_lshl_add_u64 v[6:7], v[6:7], 0, s[30:31]
	ds_read_b128 v[234:237], v167
	ds_read_b128 v[238:241], v167 offset:1024
	ds_read_b128 v[242:245], v167 offset:2048
	ds_read_b128 v[246:249], v167 offset:3072
	global_load_lds_dwordx4 v[6:7], off
	v_lshl_add_u64 v[6:7], v[8:9], 0, s[30:31]
	s_mov_b32 m0, s82
	s_nop 0
	global_load_lds_dwordx4 v[6:7], off
	s_waitcnt vmcnt(10)
	s_barrier
	s_setprio 1
	s_waitcnt lgkmcnt(2)
	v_mfma_scale_f32_16x16x128_f8f6f4 v[140:143], v[234:241], v[182:189], v[140:143], v205, v205 op_sel_hi:[0,0,0]
	s_waitcnt lgkmcnt(0)
	v_mfma_scale_f32_16x16x128_f8f6f4 v[144:147], v[242:249], v[182:189], v[144:147], v205, v205 op_sel_hi:[0,0,0]
	v_mfma_scale_f32_16x16x128_f8f6f4 v[136:139], v[234:241], v[190:197], v[136:139], v205, v205 op_sel_hi:[0,0,0]
	v_mfma_scale_f32_16x16x128_f8f6f4 v[132:135], v[242:249], v[190:197], v[132:135], v205, v205 op_sel_hi:[0,0,0]
	v_mfma_scale_f32_16x16x128_f8f6f4 v[110:113], v[234:241], v[218:225], v[110:113], v205, v205 op_sel_hi:[0,0,0]
	v_mfma_scale_f32_16x16x128_f8f6f4 v[106:109], v[242:249], v[218:225], v[106:109], v205, v205 op_sel_hi:[0,0,0]
	v_mfma_scale_f32_16x16x128_f8f6f4 v[74:77], v[234:241], v[226:233], v[74:77], v205, v205 op_sel_hi:[0,0,0]
	v_mfma_scale_f32_16x16x128_f8f6f4 v[66:69], v[242:249], v[226:233], v[66:69], v205, v205 op_sel_hi:[0,0,0]
	s_setprio 0
	s_mov_b32 m0, s45
	v_lshl_add_u64 v[2:3], v[2:3], 0, s[30:31]
	s_barrier
	ds_read_b128 v[182:185], v161 offset:49152
	ds_read_b128 v[186:189], v161 offset:50176
	ds_read_b128 v[190:193], v161 offset:51200
	ds_read_b128 v[194:197], v161 offset:52224
	ds_read_b128 v[218:221], v161 offset:53248
	ds_read_b128 v[222:225], v161 offset:54272
	ds_read_b128 v[226:229], v161 offset:55296
	ds_read_b128 v[230:233], v161 offset:56320
	global_load_lds_dwordx4 v[2:3], off
	v_lshl_add_u64 v[2:3], v[4:5], 0, s[30:31]
	s_mov_b32 m0, s46
	s_nop 0
	global_load_lds_dwordx4 v[2:3], off
	s_barrier
	s_setprio 1
	s_waitcnt lgkmcnt(6)
	v_mfma_scale_f32_16x16x128_f8f6f4 v[94:97], v[10:17], v[182:189], v[94:97], v205, v205 op_sel_hi:[0,0,0]
	v_mfma_scale_f32_16x16x128_f8f6f4 v[90:93], v[168:175], v[182:189], v[90:93], v205, v205 op_sel_hi:[0,0,0]
	s_waitcnt lgkmcnt(4)
	v_mfma_scale_f32_16x16x128_f8f6f4 v[62:65], v[10:17], v[190:197], v[62:65], v205, v205 op_sel_hi:[0,0,0]
	v_mfma_scale_f32_16x16x128_f8f6f4 v[58:61], v[168:175], v[190:197], v[58:61], v205, v205 op_sel_hi:[0,0,0]
	s_waitcnt lgkmcnt(2)
	v_mfma_scale_f32_16x16x128_f8f6f4 v[38:41], v[10:17], v[218:225], v[38:41], v205, v205 op_sel_hi:[0,0,0]
	v_mfma_scale_f32_16x16x128_f8f6f4 v[34:37], v[168:175], v[218:225], v[34:37], v205, v205 op_sel_hi:[0,0,0]
	s_waitcnt lgkmcnt(0)
	v_mfma_scale_f32_16x16x128_f8f6f4 v[22:25], v[10:17], v[226:233], v[22:25], v205, v205 op_sel_hi:[0,0,0]
	v_mfma_scale_f32_16x16x128_f8f6f4 v[18:21], v[168:175], v[226:233], v[18:21], v205, v205 op_sel_hi:[0,0,0]
	s_setprio 0
	s_barrier
	s_add_u32 s74, s74, 0x2080
	s_addc_u32 s75, s75, 0
	s_mov_b32 m0, s83
	v_lshl_add_u64 v[2:3], s[74:75], 0, v[148:149]
	global_load_lds_dwordx4 v[2:3], off
	v_lshl_add_u64 v[2:3], s[74:75], 0, v[152:153]
	s_mov_b32 m0, s84
	s_nop 0
	global_load_lds_dwordx4 v[2:3], off
	s_waitcnt vmcnt(10)
	s_barrier
	s_setprio 1
	v_mfma_scale_f32_16x16x128_f8f6f4 v[122:125], v[234:241], v[182:189], v[122:125], v205, v205 op_sel_hi:[0,0,0]
	v_mfma_scale_f32_16x16x128_f8f6f4 v[118:121], v[242:249], v[182:189], v[118:121], v205, v205 op_sel_hi:[0,0,0]
	v_mfma_scale_f32_16x16x128_f8f6f4 v[86:89], v[234:241], v[190:197], v[86:89], v205, v205 op_sel_hi:[0,0,0]
	v_mfma_scale_f32_16x16x128_f8f6f4 v[82:85], v[242:249], v[190:197], v[82:85], v205, v205 op_sel_hi:[0,0,0]
	v_mfma_scale_f32_16x16x128_f8f6f4 v[54:57], v[234:241], v[218:225], v[54:57], v205, v205 op_sel_hi:[0,0,0]
	v_mfma_scale_f32_16x16x128_f8f6f4 v[46:49], v[242:249], v[218:225], v[46:49], v205, v205 op_sel_hi:[0,0,0]
	v_mfma_scale_f32_16x16x128_f8f6f4 v[30:33], v[234:241], v[226:233], v[30:33], v205, v205 op_sel_hi:[0,0,0]
	v_mfma_scale_f32_16x16x128_f8f6f4 v[26:29], v[242:249], v[226:233], v[26:29], v205, v205 op_sel_hi:[0,0,0]
	s_setprio 0
	s_add_i32 s87, s87, 2
	s_add_u32 s6, s6, 0x100
	s_addc_u32 s7, s7, 0
	s_add_u32 s85, s85, 0x100
	s_addc_u32 s86, s86, 0
	s_cmp_gt_u32 s87, 5
	s_barrier
	s_cbranch_scc0 .LBB0_457
	s_lshl_b32 s74, s78, 8
	s_cmp_eq_u32 s80, 2
	s_nop 15
	s_nop 15
	s_cselect_b64 s[6:7], -1, 0
	s_and_b64 s[6:7], s[6:7], s[16:17]
	s_andn2_b64 vcc, exec, s[6:7]
	s_mov_b64 s[6:7], -1
	s_cbranch_vccz .LBB0_528
	s_cmp_lt_i32 s80, 2
	s_cselect_b64 s[6:7], -1, 0
	s_and_b64 s[60:61], s[6:7], exec
	v_readlane_b32 s60, v254, 30
	v_readlane_b32 s61, v254, 31
	s_cselect_b32 s59, s9, s11
	s_cselect_b32 s62, s8, s10
	s_lshl_b64 s[60:61], s[60:61], 2
	s_add_u32 s60, s62, s60
	s_addc_u32 s61, s59, s61
	v_lshlrev_b32_e32 v14, 2, v160
	global_load_dwordx4 v[2:5], v14, s[60:61] offset:48
	global_load_dwordx4 v[6:9], v14, s[60:61] offset:32
	global_load_dwordx4 v[10:13], v14, s[60:61] offset:16
	s_nop 0
	global_load_dwordx4 v[14:17], v14, s[60:61]
	s_ashr_i32 s75, s74, 31
	s_cmp_gt_i32 s80, 1
	s_mov_b64 s[76:77], -1
	s_cbranch_scc0 .LBB0_461
	s_lshl_b64 s[60:61], s[74:75], 8
	s_add_u32 s82, s50, s60
	s_addc_u32 s83, s51, s61
	s_mov_b64 s[76:77], 0

.LBB0_463:
	v_and_b32_e32 v163, 64, v177
	v_mov_b32_e32 v170, v115
	v_mov_b32_e32 v171, v127
	v_xor_b32_e32 v130, 16, v177
	v_add_u32_e32 v163, 64, v163
	v_mov_b32_e32 v168, v114
	v_mov_b32_e32 v169, v126
	v_pk_mul_f32 v[170:171], v[170:171], v[170:171]
	v_cmp_lt_i32_e32 vcc, v130, v163
	v_pk_fma_f32 v[168:169], v[168:169], v[168:169], v[170:171]
	v_mov_b32_e32 v170, v116
	v_mov_b32_e32 v171, v128
	v_cndmask_b32_e32 v130, v177, v130, vcc
	v_pk_fma_f32 v[168:169], v[170:171], v[170:171], v[168:169]
	v_mov_b32_e32 v170, v117
	v_mov_b32_e32 v171, v129
	v_mov_b32_e32 v172, v141
	v_mov_b32_e32 v173, v145
	v_lshlrev_b32_e32 v165, 2, v130
	v_xor_b32_e32 v130, 32, v177
	v_pk_fma_f32 v[168:169], v[170:171], v[170:171], v[168:169]
	v_mov_b32_e32 v170, v140
	v_mov_b32_e32 v171, v144
	v_pk_mul_f32 v[172:173], v[172:173], v[172:173]
	v_cmp_lt_i32_e32 vcc, v130, v163
	v_pk_fma_f32 v[170:171], v[170:171], v[170:171], v[172:173]
	v_mov_b32_e32 v172, v142
	v_mov_b32_e32 v173, v146
	v_cndmask_b32_e32 v130, v177, v130, vcc
	v_pk_fma_f32 v[170:171], v[172:173], v[172:173], v[170:171]
	v_mov_b32_e32 v172, v143
	v_mov_b32_e32 v173, v147
	v_lshlrev_b32_e32 v163, 2, v130
	v_pk_fma_f32 v[170:171], v[172:173], v[172:173], v[170:171]
	v_add_f32_e32 v130, v168, v169
	v_add_f32_e32 v130, v130, v170
	v_add_f32_e32 v130, v130, v171
	v_mov_b32_e32 v167, v130
	v_mov_b32_e32 v234, v130
	s_nop 1
	v_permlane16_swap_b32_e32 v167, v234
	v_cndmask_b32_e64 v182, 1.0, v251, s[6:7]
	s_mul_hi_i32 s6, s78, 0x38e38e39
	s_lshr_b32 s7, s6, 31
	s_ashr_i32 s6, s6, 1
	s_waitcnt lgkmcnt(0)
	v_add_f32_e32 v130, v167, v234
	v_mov_b32_e32 v167, v130
	v_mov_b32_e32 v234, v130
	s_nop 1
	v_permlane32_swap_b32_e32 v167, v234
	s_add_i32 s6, s6, s7
	s_mul_i32 s6, s6, 9
	s_sub_i32 s6, s78, s6
	s_lshl_b32 s59, s6, 8
	s_waitcnt lgkmcnt(0)
	v_add_f32_e32 v130, v167, v234
	v_fmamk_f32 v130, v130, 0x36800000, v176
	v_cmp_gt_f32_e32 vcc, s25, v130
	v_mul_f32_e32 v167, 0x4b800000, v130
	v_add_u32_e32 v168, s59, v156
	v_cndmask_b32_e32 v130, v130, v167, vcc
	v_rsq_f32_e32 v130, v130
	v_ashrrev_i32_e32 v169, 31, v168
	v_lshlrev_b64 v[168:169], 5, v[168:169]
	s_waitcnt vmcnt(0)
	v_pk_mul_f32 v[16:17], v[182:183], v[16:17] op_sel_hi:[0,1]
	v_mul_f32_e32 v167, 0x45800000, v130
	v_cndmask_b32_e32 v130, v130, v167, vcc
	v_mul_f32_e32 v188, 0x3c800000, v130
	v_pk_mul_f32 v[14:15], v[182:183], v[14:15] op_sel_hi:[0,1]
	s_cmp_lt_i32 s6, 8
	v_or_b32_e32 v168, v168, v158
	v_pk_mul_f32 v[170:171], v[114:115], v[188:189] op_sel_hi:[1,0]
	v_pk_mul_f32 v[172:173], v[116:117], v[188:189] op_sel_hi:[1,0]
	s_cselect_b64 s[78:79], -1, 0
	s_cmp_gt_i32 s6, 7
	v_pk_mul_f32 v[186:187], v[16:17], v[172:173]
	v_pk_mul_f32 v[184:185], v[14:15], v[170:171]
	v_lshl_add_u64 v[190:191], v[168:169], 3, s[14:15]
	s_cbranch_scc1 .LBB0_465
	global_load_dwordx4 v[218:221], v[190:191], off
	global_load_dwordx4 v[222:225], v[190:191], off offset:16
	global_load_dwordx4 v[226:229], v[190:191], off offset:32
	global_load_dwordx4 v[230:233], v[190:191], off offset:48
	s_waitcnt vmcnt(3)
	v_mov_b64_e32 v[168:169], v[218:219]
	v_mov_b64_e32 v[170:171], v[220:221]
	v_pk_mul_f32 v[174:175], v[184:185], v[168:169] op_sel:[1,1] op_sel_hi:[1,0]
	v_mul_f32_e32 v130, v187, v171
	v_pk_mul_f32 v[172:173], v[184:185], v[168:169]
	v_pk_fma_f32 v[184:185], v[184:185], v[168:169], v[174:175] op_sel_hi:[0,1,1]
	v_pk_fma_f32 v[168:169], v[186:187], v[170:171], v[130:131] op_sel_hi:[1,1,0] neg_lo:[0,0,1] neg_hi:[0,0,1]
	v_mul_f32_e32 v130, v187, v170
	v_pk_fma_f32 v[170:171], v[186:187], v[170:171], v[130:131] op_sel:[0,1,0] op_sel_hi:[1,0,0]
	v_sub_f32_e32 v184, v172, v174
	v_mov_b32_e32 v186, v168
	v_mov_b32_e32 v187, v170

.LBB0_471:
	v_lshlrev_b32_e32 v130, 1, v160
	v_lshl_add_u64 v[182:183], s[82:83], 0, v[130:131]
	v_mad_i64_i32 v[172:173], s[60:61], s76, v156, 0
	v_cvt_pk_bf16_f32 v168, v184, v185
	v_cvt_pk_bf16_f32 v169, v186, v187
	v_cvt_pk_bf16_f32 v170, v194, v195
	v_cvt_pk_bf16_f32 v171, v192, v193
	v_lshl_add_u64 v[172:173], v[172:173], 1, v[182:183]
	global_store_dwordx4 v[172:173], v[168:171], off
	s_nop 1
	v_cvt_pk_bf16_f32 v168, v198, v199
	v_cvt_pk_bf16_f32 v169, v196, v197
	v_cvt_pk_bf16_f32 v170, v200, v201
	v_cvt_pk_bf16_f32 v171, v188, v189
	global_store_dwordx4 v[172:173], v[168:171], off offset:16
	v_mov_b32_e32 v172, v137
	v_mov_b32_e32 v173, v133
	v_mov_b32_e32 v170, v103
	v_mov_b32_e32 v171, v99
	v_mov_b32_e32 v168, v102
	v_mov_b32_e32 v169, v98
	v_pk_mul_f32 v[170:171], v[170:171], v[170:171]
	v_pk_mul_f32 v[172:173], v[172:173], v[172:173]
	v_pk_fma_f32 v[168:169], v[168:169], v[168:169], v[170:171]
	v_mov_b32_e32 v170, v104
	v_mov_b32_e32 v171, v100
	v_pk_fma_f32 v[168:169], v[170:171], v[170:171], v[168:169]
	v_mov_b32_e32 v170, v105
	v_mov_b32_e32 v171, v101
	v_pk_fma_f32 v[168:169], v[170:171], v[170:171], v[168:169]
	v_mov_b32_e32 v170, v136
	v_mov_b32_e32 v171, v132
	v_pk_fma_f32 v[170:171], v[170:171], v[170:171], v[172:173]
	v_mov_b32_e32 v172, v138
	v_mov_b32_e32 v173, v134
	v_pk_fma_f32 v[170:171], v[172:173], v[172:173], v[170:171]
	v_mov_b32_e32 v172, v139
	v_mov_b32_e32 v173, v135
	v_pk_fma_f32 v[170:171], v[172:173], v[172:173], v[170:171]
	v_add_f32_e32 v130, v168, v169
	v_add_f32_e32 v130, v130, v170
	v_add_f32_e32 v130, v130, v171
	v_mov_b32_e32 v167, v130
	v_mov_b32_e32 v234, v130
	s_nop 1
	v_permlane16_swap_b32_e32 v167, v234
	v_add_u32_e32 v168, s59, v162
	v_ashrrev_i32_e32 v169, 31, v168
	v_lshlrev_b64 v[168:169], 5, v[168:169]
	v_or_b32_e32 v168, v168, v158
	s_waitcnt lgkmcnt(0)
	v_add_f32_e32 v130, v167, v234
	v_mov_b32_e32 v167, v130
	v_mov_b32_e32 v234, v130
	s_nop 1
	v_permlane32_swap_b32_e32 v167, v234
	v_lshl_add_u64 v[190:191], v[168:169], 3, s[14:15]
	s_waitcnt lgkmcnt(0)
	v_add_f32_e32 v130, v167, v234
	v_fmamk_f32 v130, v130, 0x36800000, v176
	v_cmp_gt_f32_e32 vcc, s25, v130
	v_mul_f32_e32 v167, 0x4b800000, v130
	s_nop 0
	v_cndmask_b32_e32 v130, v130, v167, vcc
	v_rsq_f32_e32 v130, v130
	s_nop 0
	v_mul_f32_e32 v167, 0x45800000, v130
	v_cndmask_b32_e32 v130, v130, v167, vcc
	v_mul_f32_e32 v188, 0x3c800000, v130
	v_pk_mul_f32 v[170:171], v[102:103], v[188:189] op_sel_hi:[1,0]
	v_pk_mul_f32 v[172:173], v[104:105], v[188:189] op_sel_hi:[1,0]
	v_pk_mul_f32 v[184:185], v[14:15], v[170:171]
	v_pk_mul_f32 v[186:187], v[16:17], v[172:173]
	s_and_b64 vcc, exec, s[6:7]
	s_cbranch_vccnz .LBB0_473
	global_load_dwordx4 v[218:221], v[190:191], off
	global_load_dwordx4 v[222:225], v[190:191], off offset:16
	global_load_dwordx4 v[226:229], v[190:191], off offset:32
	global_load_dwordx4 v[230:233], v[190:191], off offset:48
	s_waitcnt vmcnt(3)
	v_mov_b64_e32 v[168:169], v[218:219]
	v_mov_b64_e32 v[170:171], v[220:221]
	v_pk_mul_f32 v[174:175], v[184:185], v[168:169] op_sel:[1,1] op_sel_hi:[1,0]
	v_mul_f32_e32 v130, v187, v171
	v_pk_mul_f32 v[172:173], v[184:185], v[168:169]
	v_pk_fma_f32 v[184:185], v[184:185], v[168:169], v[174:175] op_sel_hi:[0,1,1]
	v_pk_fma_f32 v[168:169], v[186:187], v[170:171], v[130:131] op_sel_hi:[1,1,0] neg_lo:[0,0,1] neg_hi:[0,0,1]
	v_mul_f32_e32 v130, v187, v170
	v_pk_fma_f32 v[170:171], v[186:187], v[170:171], v[130:131] op_sel:[0,1,0] op_sel_hi:[1,0,0]
	v_sub_f32_e32 v184, v172, v174
	v_mov_b32_e32 v186, v168
	v_mov_b32_e32 v187, v170

.LBB0_479:
	v_mad_i64_i32 v[172:173], s[60:61], s76, v162, 0
	v_cvt_pk_bf16_f32 v168, v184, v185
	v_cvt_pk_bf16_f32 v169, v186, v187
	v_cvt_pk_bf16_f32 v170, v194, v195
	v_cvt_pk_bf16_f32 v171, v192, v193
	v_lshl_add_u64 v[172:173], v[172:173], 1, v[182:183]
	global_store_dwordx4 v[172:173], v[168:171], off
	s_nop 1
	v_cvt_pk_bf16_f32 v168, v198, v199
	v_cvt_pk_bf16_f32 v169, v196, v197
	v_cvt_pk_bf16_f32 v170, v200, v201
	v_cvt_pk_bf16_f32 v171, v188, v189
	global_store_dwordx4 v[172:173], v[168:171], off offset:16
	v_mov_b32_e32 v172, v111
	v_mov_b32_e32 v173, v107
	v_mov_b32_e32 v170, v79
	v_mov_b32_e32 v171, v71
	v_mov_b32_e32 v168, v78
	v_mov_b32_e32 v169, v70
	v_pk_mul_f32 v[170:171], v[170:171], v[170:171]
	v_pk_mul_f32 v[172:173], v[172:173], v[172:173]
	v_pk_fma_f32 v[168:169], v[168:169], v[168:169], v[170:171]
	v_mov_b32_e32 v170, v80
	v_mov_b32_e32 v171, v72
	v_pk_fma_f32 v[168:169], v[170:171], v[170:171], v[168:169]
	v_mov_b32_e32 v170, v81
	v_mov_b32_e32 v171, v73
	v_pk_fma_f32 v[168:169], v[170:171], v[170:171], v[168:169]
	v_mov_b32_e32 v170, v110
	v_mov_b32_e32 v171, v106
	v_pk_fma_f32 v[170:171], v[170:171], v[170:171], v[172:173]
	v_mov_b32_e32 v172, v112
	v_mov_b32_e32 v173, v108
	v_pk_fma_f32 v[170:171], v[172:173], v[172:173], v[170:171]
	v_mov_b32_e32 v172, v113
	v_mov_b32_e32 v173, v109
	v_pk_fma_f32 v[170:171], v[172:173], v[172:173], v[170:171]
	v_add_f32_e32 v130, v168, v169
	v_add_f32_e32 v130, v130, v170
	v_add_f32_e32 v130, v130, v171
	v_mov_b32_e32 v167, v130
	v_mov_b32_e32 v234, v130
	s_nop 1
	v_permlane16_swap_b32_e32 v167, v234
	v_add_u32_e32 v168, s59, v164
	v_ashrrev_i32_e32 v169, 31, v168
	v_lshlrev_b64 v[168:169], 5, v[168:169]
	v_or_b32_e32 v168, v168, v158
	s_waitcnt lgkmcnt(0)
	v_add_f32_e32 v130, v167, v234
	v_mov_b32_e32 v167, v130
	v_mov_b32_e32 v234, v130
	s_nop 1
	v_permlane32_swap_b32_e32 v167, v234
	v_lshl_add_u64 v[190:191], v[168:169], 3, s[14:15]
	s_waitcnt lgkmcnt(0)
	v_add_f32_e32 v130, v167, v234
	v_fmamk_f32 v130, v130, 0x36800000, v176
	v_cmp_gt_f32_e32 vcc, s25, v130
	v_mul_f32_e32 v167, 0x4b800000, v130
	s_nop 0
	v_cndmask_b32_e32 v130, v130, v167, vcc
	v_rsq_f32_e32 v130, v130
	s_nop 0
	v_mul_f32_e32 v167, 0x45800000, v130
	v_cndmask_b32_e32 v130, v130, v167, vcc
	v_mul_f32_e32 v188, 0x3c800000, v130
	v_pk_mul_f32 v[170:171], v[78:79], v[188:189] op_sel_hi:[1,0]
	v_pk_mul_f32 v[172:173], v[80:81], v[188:189] op_sel_hi:[1,0]
	v_pk_mul_f32 v[184:185], v[14:15], v[170:171]
	v_pk_mul_f32 v[186:187], v[16:17], v[172:173]
	s_and_b64 vcc, exec, s[6:7]
	s_cbranch_vccnz .LBB0_481
	global_load_dwordx4 v[218:221], v[190:191], off
	global_load_dwordx4 v[222:225], v[190:191], off offset:16
	global_load_dwordx4 v[226:229], v[190:191], off offset:32
	global_load_dwordx4 v[230:233], v[190:191], off offset:48
	s_waitcnt vmcnt(3)
	v_mov_b64_e32 v[168:169], v[218:219]
	v_mov_b64_e32 v[170:171], v[220:221]
	v_pk_mul_f32 v[174:175], v[184:185], v[168:169] op_sel:[1,1] op_sel_hi:[1,0]
	v_mul_f32_e32 v130, v187, v171
	v_pk_mul_f32 v[172:173], v[184:185], v[168:169]
	v_pk_fma_f32 v[184:185], v[184:185], v[168:169], v[174:175] op_sel_hi:[0,1,1]
	v_pk_fma_f32 v[168:169], v[186:187], v[170:171], v[130:131] op_sel_hi:[1,1,0] neg_lo:[0,0,1] neg_hi:[0,0,1]
	v_mul_f32_e32 v130, v187, v170
	v_pk_fma_f32 v[170:171], v[186:187], v[170:171], v[130:131] op_sel:[0,1,0] op_sel_hi:[1,0,0]
	v_sub_f32_e32 v184, v172, v174
	v_mov_b32_e32 v186, v168
	v_mov_b32_e32 v187, v170

.LBB0_487:
	v_mad_i64_i32 v[172:173], s[60:61], s76, v164, 0
	v_cvt_pk_bf16_f32 v168, v184, v185
	v_cvt_pk_bf16_f32 v169, v186, v187
	v_cvt_pk_bf16_f32 v170, v194, v195
	v_cvt_pk_bf16_f32 v171, v192, v193
	v_lshl_add_u64 v[172:173], v[172:173], 1, v[182:183]
	global_store_dwordx4 v[172:173], v[168:171], off
	s_nop 1
	v_cvt_pk_bf16_f32 v168, v198, v199
	v_cvt_pk_bf16_f32 v169, v196, v197
	v_cvt_pk_bf16_f32 v170, v200, v201
	v_cvt_pk_bf16_f32 v171, v188, v189
	global_store_dwordx4 v[172:173], v[168:171], off offset:16
	v_mov_b32_e32 v172, v75
	v_mov_b32_e32 v173, v67
	v_mov_b32_e32 v170, v51
	v_mov_b32_e32 v171, v43
	v_mov_b32_e32 v168, v50
	v_mov_b32_e32 v169, v42
	v_pk_mul_f32 v[170:171], v[170:171], v[170:171]
	v_pk_mul_f32 v[172:173], v[172:173], v[172:173]
	v_pk_fma_f32 v[168:169], v[168:169], v[168:169], v[170:171]
	v_mov_b32_e32 v170, v52
	v_mov_b32_e32 v171, v44
	v_pk_fma_f32 v[168:169], v[170:171], v[170:171], v[168:169]
	v_mov_b32_e32 v170, v53
	v_mov_b32_e32 v171, v45
	v_pk_fma_f32 v[168:169], v[170:171], v[170:171], v[168:169]
	v_mov_b32_e32 v170, v74
	v_mov_b32_e32 v171, v66
	v_pk_fma_f32 v[170:171], v[170:171], v[170:171], v[172:173]
	v_mov_b32_e32 v172, v76
	v_mov_b32_e32 v173, v68
	v_pk_fma_f32 v[170:171], v[172:173], v[172:173], v[170:171]
	v_mov_b32_e32 v172, v77
	v_mov_b32_e32 v173, v69
	v_pk_fma_f32 v[170:171], v[172:173], v[172:173], v[170:171]
	v_add_f32_e32 v130, v168, v169
	v_add_f32_e32 v130, v130, v170
	v_add_f32_e32 v130, v130, v171
	v_mov_b32_e32 v167, v130
	v_mov_b32_e32 v234, v130
	s_nop 1
	v_permlane16_swap_b32_e32 v167, v234
	v_add_u32_e32 v168, s59, v166
	v_ashrrev_i32_e32 v169, 31, v168
	v_lshlrev_b64 v[168:169], 5, v[168:169]
	v_or_b32_e32 v168, v168, v158
	s_waitcnt lgkmcnt(0)
	v_add_f32_e32 v130, v167, v234
	v_mov_b32_e32 v167, v130
	v_mov_b32_e32 v234, v130
	s_nop 1
	v_permlane32_swap_b32_e32 v167, v234
	v_lshl_add_u64 v[190:191], v[168:169], 3, s[14:15]
	s_waitcnt lgkmcnt(0)
	v_add_f32_e32 v130, v167, v234
	v_fmamk_f32 v130, v130, 0x36800000, v176
	v_cmp_gt_f32_e32 vcc, s25, v130
	v_mul_f32_e32 v167, 0x4b800000, v130
	s_nop 0
	v_cndmask_b32_e32 v130, v130, v167, vcc
	v_rsq_f32_e32 v130, v130
	s_nop 0
	v_mul_f32_e32 v167, 0x45800000, v130
	v_cndmask_b32_e32 v130, v130, v167, vcc
	v_mul_f32_e32 v188, 0x3c800000, v130
	v_pk_mul_f32 v[170:171], v[50:51], v[188:189] op_sel_hi:[1,0]
	v_pk_mul_f32 v[172:173], v[52:53], v[188:189] op_sel_hi:[1,0]
	v_pk_mul_f32 v[184:185], v[14:15], v[170:171]
	v_pk_mul_f32 v[186:187], v[16:17], v[172:173]
	s_and_b64 vcc, exec, s[6:7]
	s_cbranch_vccnz .LBB0_489
	global_load_dwordx4 v[218:221], v[190:191], off
	global_load_dwordx4 v[222:225], v[190:191], off offset:16
	global_load_dwordx4 v[226:229], v[190:191], off offset:32
	global_load_dwordx4 v[230:233], v[190:191], off offset:48
	s_waitcnt vmcnt(3)
	v_mov_b64_e32 v[168:169], v[218:219]
	v_mov_b64_e32 v[170:171], v[220:221]
	v_pk_mul_f32 v[174:175], v[184:185], v[168:169] op_sel:[1,1] op_sel_hi:[1,0]
	v_mul_f32_e32 v130, v187, v171
	v_pk_mul_f32 v[172:173], v[184:185], v[168:169]
	v_pk_fma_f32 v[184:185], v[184:185], v[168:169], v[174:175] op_sel_hi:[0,1,1]
	v_pk_fma_f32 v[168:169], v[186:187], v[170:171], v[130:131] op_sel_hi:[1,1,0] neg_lo:[0,0,1] neg_hi:[0,0,1]
	v_mul_f32_e32 v130, v187, v170
	v_pk_fma_f32 v[170:171], v[186:187], v[170:171], v[130:131] op_sel:[0,1,0] op_sel_hi:[1,0,0]
	v_sub_f32_e32 v184, v172, v174
	v_mov_b32_e32 v186, v168
	v_mov_b32_e32 v187, v170

.LBB0_495:
	v_mad_i64_i32 v[172:173], s[60:61], s76, v166, 0
	v_cvt_pk_bf16_f32 v168, v184, v185
	v_cvt_pk_bf16_f32 v169, v186, v187
	v_cvt_pk_bf16_f32 v170, v194, v195
	v_cvt_pk_bf16_f32 v171, v192, v193
	v_lshl_add_u64 v[172:173], v[172:173], 1, v[182:183]
	global_store_dwordx4 v[172:173], v[168:171], off
	s_nop 1
	v_cvt_pk_bf16_f32 v168, v198, v199
	v_cvt_pk_bf16_f32 v169, v196, v197
	v_cvt_pk_bf16_f32 v170, v200, v201
	v_cvt_pk_bf16_f32 v171, v188, v189
	global_store_dwordx4 v[172:173], v[168:171], off offset:16
	v_mov_b32_e32 v172, v123
	v_mov_b32_e32 v173, v119
	v_mov_b32_e32 v170, v95
	v_mov_b32_e32 v171, v91
	v_mov_b32_e32 v168, v94
	v_mov_b32_e32 v169, v90
	v_pk_mul_f32 v[170:171], v[170:171], v[170:171]
	v_pk_mul_f32 v[172:173], v[172:173], v[172:173]
	v_pk_fma_f32 v[168:169], v[168:169], v[168:169], v[170:171]
	v_mov_b32_e32 v170, v96
	v_mov_b32_e32 v171, v92
	v_pk_fma_f32 v[168:169], v[170:171], v[170:171], v[168:169]
	v_mov_b32_e32 v170, v97
	v_mov_b32_e32 v171, v93
	v_pk_fma_f32 v[168:169], v[170:171], v[170:171], v[168:169]
	v_mov_b32_e32 v170, v122
	v_mov_b32_e32 v171, v118
	v_pk_fma_f32 v[170:171], v[170:171], v[170:171], v[172:173]
	v_mov_b32_e32 v172, v124
	v_mov_b32_e32 v173, v120
	v_pk_fma_f32 v[170:171], v[172:173], v[172:173], v[170:171]
	v_mov_b32_e32 v172, v125
	v_mov_b32_e32 v173, v121
	v_pk_fma_f32 v[170:171], v[172:173], v[172:173], v[170:171]
	v_add_f32_e32 v130, v168, v169
	v_add_f32_e32 v130, v130, v170
	v_add_f32_e32 v130, v130, v171
	v_mov_b32_e32 v167, v130
	v_mov_b32_e32 v234, v130
	s_nop 1
	v_permlane16_swap_b32_e32 v167, v234
	v_add_u32_e32 v168, s59, v250
	v_ashrrev_i32_e32 v169, 31, v168
	v_lshlrev_b64 v[168:169], 5, v[168:169]
	v_or_b32_e32 v168, v168, v158
	s_waitcnt lgkmcnt(0)
	v_add_f32_e32 v130, v167, v234
	v_mov_b32_e32 v167, v130
	v_mov_b32_e32 v234, v130
	s_nop 1
	v_permlane32_swap_b32_e32 v167, v234
	v_lshl_add_u64 v[190:191], v[168:169], 3, s[14:15]
	s_waitcnt lgkmcnt(0)
	v_add_f32_e32 v130, v167, v234
	v_fmamk_f32 v130, v130, 0x36800000, v176
	v_cmp_gt_f32_e32 vcc, s25, v130
	v_mul_f32_e32 v167, 0x4b800000, v130
	s_nop 0
	v_cndmask_b32_e32 v130, v130, v167, vcc
	v_rsq_f32_e32 v130, v130
	s_nop 0
	v_mul_f32_e32 v167, 0x45800000, v130
	v_cndmask_b32_e32 v130, v130, v167, vcc
	v_mul_f32_e32 v188, 0x3c800000, v130
	v_pk_mul_f32 v[170:171], v[94:95], v[188:189] op_sel_hi:[1,0]
	v_pk_mul_f32 v[172:173], v[96:97], v[188:189] op_sel_hi:[1,0]
	v_pk_mul_f32 v[184:185], v[14:15], v[170:171]
	v_pk_mul_f32 v[186:187], v[16:17], v[172:173]
	s_and_b64 vcc, exec, s[6:7]
	s_cbranch_vccnz .LBB0_497
	global_load_dwordx4 v[218:221], v[190:191], off
	global_load_dwordx4 v[222:225], v[190:191], off offset:16
	global_load_dwordx4 v[226:229], v[190:191], off offset:32
	global_load_dwordx4 v[230:233], v[190:191], off offset:48
	s_waitcnt vmcnt(3)
	v_mov_b64_e32 v[168:169], v[218:219]
	v_mov_b64_e32 v[170:171], v[220:221]
	v_pk_mul_f32 v[174:175], v[184:185], v[168:169] op_sel:[1,1] op_sel_hi:[1,0]
	v_mul_f32_e32 v130, v187, v171
	v_pk_mul_f32 v[172:173], v[184:185], v[168:169]
	v_pk_fma_f32 v[184:185], v[184:185], v[168:169], v[174:175] op_sel_hi:[0,1,1]
	v_pk_fma_f32 v[168:169], v[186:187], v[170:171], v[130:131] op_sel_hi:[1,1,0] neg_lo:[0,0,1] neg_hi:[0,0,1]
	v_mul_f32_e32 v130, v187, v170
	v_pk_fma_f32 v[170:171], v[186:187], v[170:171], v[130:131] op_sel:[0,1,0] op_sel_hi:[1,0,0]
	v_sub_f32_e32 v184, v172, v174
	v_mov_b32_e32 v186, v168
	v_mov_b32_e32 v187, v170

.LBB0_503:
	v_mad_i64_i32 v[172:173], s[60:61], s76, v250, 0
	v_cvt_pk_bf16_f32 v168, v184, v185
	v_cvt_pk_bf16_f32 v169, v186, v187
	v_cvt_pk_bf16_f32 v170, v194, v195
	v_cvt_pk_bf16_f32 v171, v192, v193
	v_lshl_add_u64 v[172:173], v[172:173], 1, v[182:183]
	global_store_dwordx4 v[172:173], v[168:171], off
	s_nop 1
	v_cvt_pk_bf16_f32 v168, v198, v199
	v_cvt_pk_bf16_f32 v169, v196, v197
	v_cvt_pk_bf16_f32 v170, v200, v201
	v_cvt_pk_bf16_f32 v171, v188, v189
	global_store_dwordx4 v[172:173], v[168:171], off offset:16
	v_mov_b32_e32 v172, v87
	v_mov_b32_e32 v173, v83
	v_mov_b32_e32 v170, v63
	v_mov_b32_e32 v171, v59
	v_mov_b32_e32 v168, v62
	v_mov_b32_e32 v169, v58
	v_pk_mul_f32 v[170:171], v[170:171], v[170:171]
	v_pk_mul_f32 v[172:173], v[172:173], v[172:173]
	v_pk_fma_f32 v[168:169], v[168:169], v[168:169], v[170:171]
	v_mov_b32_e32 v170, v64
	v_mov_b32_e32 v171, v60
	v_pk_fma_f32 v[168:169], v[170:171], v[170:171], v[168:169]
	v_mov_b32_e32 v170, v65
	v_mov_b32_e32 v171, v61
	v_pk_fma_f32 v[168:169], v[170:171], v[170:171], v[168:169]
	v_mov_b32_e32 v170, v86
	v_mov_b32_e32 v171, v82
	v_pk_fma_f32 v[170:171], v[170:171], v[170:171], v[172:173]
	v_mov_b32_e32 v172, v88
	v_mov_b32_e32 v173, v84
	v_pk_fma_f32 v[170:171], v[172:173], v[172:173], v[170:171]
	v_mov_b32_e32 v172, v89
	v_mov_b32_e32 v173, v85
	v_pk_fma_f32 v[170:171], v[172:173], v[172:173], v[170:171]
	v_add_f32_e32 v130, v168, v169
	v_add_f32_e32 v130, v130, v170
	v_add_f32_e32 v130, v130, v171
	v_mov_b32_e32 v167, v130
	v_mov_b32_e32 v234, v130
	s_nop 1
	v_permlane16_swap_b32_e32 v167, v234
	v_add_u32_e32 v168, s59, v252
	v_ashrrev_i32_e32 v169, 31, v168
	v_lshlrev_b64 v[168:169], 5, v[168:169]
	v_or_b32_e32 v168, v168, v158
	s_waitcnt lgkmcnt(0)
	v_add_f32_e32 v130, v167, v234
	v_mov_b32_e32 v167, v130
	v_mov_b32_e32 v234, v130
	s_nop 1
	v_permlane32_swap_b32_e32 v167, v234
	v_lshl_add_u64 v[190:191], v[168:169], 3, s[14:15]
	s_waitcnt lgkmcnt(0)
	v_add_f32_e32 v130, v167, v234
	v_fmamk_f32 v130, v130, 0x36800000, v176
	v_cmp_gt_f32_e32 vcc, s25, v130
	v_mul_f32_e32 v167, 0x4b800000, v130
	s_nop 0
	v_cndmask_b32_e32 v130, v130, v167, vcc
	v_rsq_f32_e32 v130, v130
	s_nop 0
	v_mul_f32_e32 v167, 0x45800000, v130
	v_cndmask_b32_e32 v130, v130, v167, vcc
	v_mul_f32_e32 v188, 0x3c800000, v130
	v_pk_mul_f32 v[170:171], v[62:63], v[188:189] op_sel_hi:[1,0]
	v_pk_mul_f32 v[172:173], v[64:65], v[188:189] op_sel_hi:[1,0]
	v_pk_mul_f32 v[184:185], v[14:15], v[170:171]
	v_pk_mul_f32 v[186:187], v[16:17], v[172:173]
	s_and_b64 vcc, exec, s[6:7]
	s_cbranch_vccnz .LBB0_505
	global_load_dwordx4 v[218:221], v[190:191], off
	global_load_dwordx4 v[222:225], v[190:191], off offset:16
	global_load_dwordx4 v[226:229], v[190:191], off offset:32
	global_load_dwordx4 v[230:233], v[190:191], off offset:48
	s_waitcnt vmcnt(3)
	v_mov_b64_e32 v[168:169], v[218:219]
	v_mov_b64_e32 v[170:171], v[220:221]
	v_pk_mul_f32 v[174:175], v[184:185], v[168:169] op_sel:[1,1] op_sel_hi:[1,0]
	v_mul_f32_e32 v130, v187, v171
	v_pk_mul_f32 v[172:173], v[184:185], v[168:169]
	v_pk_fma_f32 v[184:185], v[184:185], v[168:169], v[174:175] op_sel_hi:[0,1,1]
	v_pk_fma_f32 v[168:169], v[186:187], v[170:171], v[130:131] op_sel_hi:[1,1,0] neg_lo:[0,0,1] neg_hi:[0,0,1]
	v_mul_f32_e32 v130, v187, v170
	v_pk_fma_f32 v[170:171], v[186:187], v[170:171], v[130:131] op_sel:[0,1,0] op_sel_hi:[1,0,0]
	v_sub_f32_e32 v184, v172, v174
	v_mov_b32_e32 v186, v168
	v_mov_b32_e32 v187, v170

.LBB0_511:
	v_mad_i64_i32 v[172:173], s[60:61], s76, v252, 0
	v_cvt_pk_bf16_f32 v168, v184, v185
	v_cvt_pk_bf16_f32 v169, v186, v187
	v_cvt_pk_bf16_f32 v170, v194, v195
	v_cvt_pk_bf16_f32 v171, v192, v193
	v_lshl_add_u64 v[172:173], v[172:173], 1, v[182:183]
	global_store_dwordx4 v[172:173], v[168:171], off
	s_nop 1
	v_cvt_pk_bf16_f32 v168, v198, v199
	v_cvt_pk_bf16_f32 v169, v196, v197
	v_cvt_pk_bf16_f32 v170, v200, v201
	v_cvt_pk_bf16_f32 v171, v188, v189
	global_store_dwordx4 v[172:173], v[168:171], off offset:16
	v_mov_b32_e32 v172, v55
	v_mov_b32_e32 v173, v47
	v_mov_b32_e32 v170, v39
	v_mov_b32_e32 v171, v35
	v_mov_b32_e32 v168, v38
	v_mov_b32_e32 v169, v34
	v_pk_mul_f32 v[170:171], v[170:171], v[170:171]
	v_pk_mul_f32 v[172:173], v[172:173], v[172:173]
	v_pk_fma_f32 v[168:169], v[168:169], v[168:169], v[170:171]
	v_mov_b32_e32 v170, v40
	v_mov_b32_e32 v171, v36
	v_pk_fma_f32 v[168:169], v[170:171], v[170:171], v[168:169]
	v_mov_b32_e32 v170, v41
	v_mov_b32_e32 v171, v37
	v_pk_fma_f32 v[168:169], v[170:171], v[170:171], v[168:169]
	v_mov_b32_e32 v170, v54
	v_mov_b32_e32 v171, v46
	v_pk_fma_f32 v[170:171], v[170:171], v[170:171], v[172:173]
	v_mov_b32_e32 v172, v56
	v_mov_b32_e32 v173, v48
	v_pk_fma_f32 v[170:171], v[172:173], v[172:173], v[170:171]
	v_mov_b32_e32 v172, v57
	v_mov_b32_e32 v173, v49
	v_pk_fma_f32 v[170:171], v[172:173], v[172:173], v[170:171]
	v_add_f32_e32 v130, v168, v169
	v_add_f32_e32 v130, v130, v170
	v_add_f32_e32 v130, v130, v171
	v_mov_b32_e32 v167, v130
	v_mov_b32_e32 v234, v130
	s_nop 1
	v_permlane16_swap_b32_e32 v167, v234
	v_add_u32_e32 v168, s59, v202
	v_ashrrev_i32_e32 v169, 31, v168
	v_lshlrev_b64 v[168:169], 5, v[168:169]
	v_or_b32_e32 v168, v168, v158
	s_waitcnt lgkmcnt(0)
	v_add_f32_e32 v130, v167, v234
	v_mov_b32_e32 v167, v130
	v_mov_b32_e32 v234, v130
	s_nop 1
	v_permlane32_swap_b32_e32 v167, v234
	v_lshl_add_u64 v[190:191], v[168:169], 3, s[14:15]
	s_waitcnt lgkmcnt(0)
	v_add_f32_e32 v130, v167, v234
	v_fmamk_f32 v130, v130, 0x36800000, v176
	v_cmp_gt_f32_e32 vcc, s25, v130
	v_mul_f32_e32 v167, 0x4b800000, v130
	s_nop 0
	v_cndmask_b32_e32 v130, v130, v167, vcc
	v_rsq_f32_e32 v130, v130
	s_nop 0
	v_mul_f32_e32 v167, 0x45800000, v130
	v_cndmask_b32_e32 v130, v130, v167, vcc
	v_mul_f32_e32 v188, 0x3c800000, v130
	v_pk_mul_f32 v[170:171], v[38:39], v[188:189] op_sel_hi:[1,0]
	v_pk_mul_f32 v[172:173], v[40:41], v[188:189] op_sel_hi:[1,0]
	v_pk_mul_f32 v[184:185], v[14:15], v[170:171]
	v_pk_mul_f32 v[186:187], v[16:17], v[172:173]
	s_and_b64 vcc, exec, s[6:7]
	s_cbranch_vccnz .LBB0_513
	global_load_dwordx4 v[218:221], v[190:191], off
	global_load_dwordx4 v[222:225], v[190:191], off offset:16
	global_load_dwordx4 v[226:229], v[190:191], off offset:32
	global_load_dwordx4 v[230:233], v[190:191], off offset:48
	s_waitcnt vmcnt(3)
	v_mov_b64_e32 v[168:169], v[218:219]
	v_mov_b64_e32 v[170:171], v[220:221]
	v_pk_mul_f32 v[174:175], v[184:185], v[168:169] op_sel:[1,1] op_sel_hi:[1,0]
	v_mul_f32_e32 v130, v187, v171
	v_pk_mul_f32 v[172:173], v[184:185], v[168:169]
	v_pk_fma_f32 v[184:185], v[184:185], v[168:169], v[174:175] op_sel_hi:[0,1,1]
	v_pk_fma_f32 v[168:169], v[186:187], v[170:171], v[130:131] op_sel_hi:[1,1,0] neg_lo:[0,0,1] neg_hi:[0,0,1]
	v_mul_f32_e32 v130, v187, v170
	v_pk_fma_f32 v[170:171], v[186:187], v[170:171], v[130:131] op_sel:[0,1,0] op_sel_hi:[1,0,0]
	v_sub_f32_e32 v184, v172, v174
	v_mov_b32_e32 v186, v168
	v_mov_b32_e32 v187, v170

.LBB0_519:
	v_mad_i64_i32 v[172:173], s[60:61], s76, v202, 0
	v_cvt_pk_bf16_f32 v168, v184, v185
	v_cvt_pk_bf16_f32 v169, v186, v187
	v_cvt_pk_bf16_f32 v170, v194, v195
	v_cvt_pk_bf16_f32 v171, v192, v193
	v_lshl_add_u64 v[172:173], v[172:173], 1, v[182:183]
	global_store_dwordx4 v[172:173], v[168:171], off
	s_nop 1
	v_cvt_pk_bf16_f32 v168, v198, v199
	v_cvt_pk_bf16_f32 v169, v196, v197
	v_cvt_pk_bf16_f32 v170, v200, v201
	v_cvt_pk_bf16_f32 v171, v188, v189
	global_store_dwordx4 v[172:173], v[168:171], off offset:16
	v_mov_b32_e32 v172, v31
	v_mov_b32_e32 v173, v27
	v_mov_b32_e32 v170, v23
	v_mov_b32_e32 v171, v19
	v_mov_b32_e32 v168, v22
	v_mov_b32_e32 v169, v18
	v_pk_mul_f32 v[170:171], v[170:171], v[170:171]
	v_pk_mul_f32 v[172:173], v[172:173], v[172:173]
	v_pk_fma_f32 v[168:169], v[168:169], v[168:169], v[170:171]
	v_mov_b32_e32 v170, v24
	v_mov_b32_e32 v171, v20
	v_pk_fma_f32 v[168:169], v[170:171], v[170:171], v[168:169]
	v_mov_b32_e32 v170, v25
	v_mov_b32_e32 v171, v21
	v_pk_fma_f32 v[168:169], v[170:171], v[170:171], v[168:169]
	v_mov_b32_e32 v170, v30
	v_mov_b32_e32 v171, v26
	v_pk_fma_f32 v[170:171], v[170:171], v[170:171], v[172:173]
	v_mov_b32_e32 v172, v32
	v_mov_b32_e32 v173, v28
	v_pk_fma_f32 v[170:171], v[172:173], v[172:173], v[170:171]
	v_mov_b32_e32 v172, v33
	v_mov_b32_e32 v173, v29
	v_pk_fma_f32 v[170:171], v[172:173], v[172:173], v[170:171]
	v_add_f32_e32 v130, v168, v169
	v_add_f32_e32 v130, v130, v170
	v_add_f32_e32 v130, v130, v171
	v_mov_b32_e32 v165, v130
	v_mov_b32_e32 v234, v130
	s_nop 1
	v_permlane16_swap_b32_e32 v165, v234
	v_add_u32_e32 v168, s59, v210
	v_ashrrev_i32_e32 v169, 31, v168
	v_lshlrev_b64 v[168:169], 5, v[168:169]
	v_or_b32_e32 v168, v168, v158
	s_waitcnt lgkmcnt(0)
	v_add_f32_e32 v130, v165, v234
	v_mov_b32_e32 v163, v130
	v_mov_b32_e32 v234, v130
	s_nop 1
	v_permlane32_swap_b32_e32 v163, v234
	v_lshl_add_u64 v[186:187], v[168:169], 3, s[14:15]
	s_waitcnt lgkmcnt(0)
	v_add_f32_e32 v130, v163, v234
	v_fmamk_f32 v130, v130, 0x36800000, v176
	v_cmp_gt_f32_e32 vcc, s25, v130
	v_mul_f32_e32 v163, 0x4b800000, v130
	s_nop 0
	v_cndmask_b32_e32 v130, v130, v163, vcc
	v_rsq_f32_e32 v130, v130
	s_nop 0
	v_mul_f32_e32 v163, 0x45800000, v130
	v_cndmask_b32_e32 v130, v130, v163, vcc
	v_mul_f32_e32 v184, 0x3c800000, v130
	v_pk_mul_f32 v[170:171], v[22:23], v[184:185] op_sel_hi:[1,0]
	v_pk_mul_f32 v[172:173], v[24:25], v[184:185] op_sel_hi:[1,0]
	v_pk_mul_f32 v[14:15], v[14:15], v[170:171]
	v_pk_mul_f32 v[16:17], v[16:17], v[172:173]
	s_and_b64 vcc, exec, s[6:7]
	s_cbranch_vccnz .LBB0_521
	global_load_dwordx4 v[218:221], v[186:187], off
	global_load_dwordx4 v[222:225], v[186:187], off offset:16
	global_load_dwordx4 v[226:229], v[186:187], off offset:32
	global_load_dwordx4 v[230:233], v[186:187], off offset:48
	s_waitcnt vmcnt(3)
	v_mov_b64_e32 v[168:169], v[218:219]
	v_mov_b64_e32 v[170:171], v[220:221]
	v_pk_mul_f32 v[174:175], v[14:15], v[168:169] op_sel:[1,1] op_sel_hi:[1,0]
	v_pk_mul_f32 v[172:173], v[14:15], v[168:169]
	v_pk_fma_f32 v[14:15], v[14:15], v[168:169], v[174:175] op_sel_hi:[0,1,1]
	v_mul_f32_e32 v14, v17, v171
	v_pk_fma_f32 v[168:169], v[16:17], v[170:171], v[14:15] op_sel_hi:[1,1,0] neg_lo:[0,0,1] neg_hi:[0,0,1]
	v_mul_f32_e32 v14, v17, v170
	v_pk_fma_f32 v[170:171], v[16:17], v[170:171], v[14:15] op_sel:[0,1,0] op_sel_hi:[1,0,0]
	v_sub_f32_e32 v14, v172, v174
	v_mov_b32_e32 v16, v168
	v_mov_b32_e32 v17, v170

.LBB0_541:
	s_add_u32 s17, s18, 0xfffc0080
	s_addc_u32 s22, s19, -1
	s_cmp_eq_u32 s11, 12
	s_cselect_b32 s69, s13, s22
	s_cselect_b32 s68, s12, s17
	s_cselect_b32 s67, s15, s9
	s_cselect_b32 s66, s14, s5
	s_add_i32 s17, 0, 0x10000
	v_add_u32_e32 v130, s17, v145
	ds_read_b128 v[148:151], v130
	ds_read_b128 v[152:155], v130 offset:1024
	ds_read_b128 v[156:159], v130 offset:2048
	ds_read_b128 v[160:163], v130 offset:3072
	v_lshl_add_u64 v[198:199], s[18:19], 0, v[140:141]
	s_add_i32 m0, s43, 0xc000
	ds_read_b128 v[164:167], v147
	ds_read_b128 v[168:171], v147 offset:1024
	ds_read_b128 v[172:175], v147 offset:2048
	ds_read_b128 v[178:181], v147 offset:3072
	ds_read_b128 v[182:185], v147 offset:4096
	ds_read_b128 v[186:189], v147 offset:5120
	ds_read_b128 v[190:193], v147 offset:6144
	ds_read_b128 v[194:197], v147 offset:7168
	global_load_lds_dwordx4 v[198:199], off
	v_lshl_add_u64 v[198:199], s[18:19], 0, v[142:143]
	s_add_i32 m0, s43, 0xe000
	s_nop 0
	global_load_lds_dwordx4 v[198:199], off
	s_waitcnt lgkmcnt(8)
	s_waitcnt vmcnt(10)
	s_barrier
	s_setprio 1
	s_waitcnt lgkmcnt(7)
	v_mfma_f32_16x16x32_bf16 v[126:129], v[148:151], v[164:167], v[126:129]
	s_waitcnt lgkmcnt(5)
	v_mfma_f32_16x16x32_bf16 v[122:125], v[156:159], v[164:167], v[122:125]
	v_mfma_f32_16x16x32_bf16 v[118:121], v[148:151], v[172:175], v[118:121]
	s_waitcnt lgkmcnt(3)
	v_mfma_f32_16x16x32_bf16 v[114:117], v[156:159], v[172:175], v[114:117]
	v_mfma_f32_16x16x32_bf16 v[102:105], v[148:151], v[182:185], v[102:105]
	s_waitcnt lgkmcnt(1)
	v_mfma_f32_16x16x32_bf16 v[98:101], v[156:159], v[182:185], v[98:101]
	v_mfma_f32_16x16x32_bf16 v[86:89], v[148:151], v[190:193], v[86:89]
	v_mfma_f32_16x16x32_bf16 v[82:85], v[156:159], v[190:193], v[82:85]
	v_mfma_f32_16x16x32_bf16 v[126:129], v[152:155], v[168:171], v[126:129]
	v_mfma_f32_16x16x32_bf16 v[122:125], v[160:163], v[168:171], v[122:125]
	v_mfma_f32_16x16x32_bf16 v[118:121], v[152:155], v[178:181], v[118:121]
	v_mfma_f32_16x16x32_bf16 v[114:117], v[160:163], v[178:181], v[114:117]
	v_mfma_f32_16x16x32_bf16 v[102:105], v[152:155], v[186:189], v[102:105]
	s_waitcnt lgkmcnt(0)
	v_mfma_f32_16x16x32_bf16 v[98:101], v[160:163], v[186:189], v[98:101]
	v_mfma_f32_16x16x32_bf16 v[86:89], v[152:155], v[194:197], v[86:89]
	v_mfma_f32_16x16x32_bf16 v[82:85], v[160:163], v[194:197], v[82:85]
	s_setprio 0
	s_barrier
	s_add_i32 s22, 0, 0x14000
	s_add_i32 s17, s17, s38
	v_add_u32_e32 v130, s22, v145
	v_lshl_add_u64 v[230:231], s[66:67], 0, v[138:139]
	s_mov_b32 m0, s17
	ds_read_b128 v[198:201], v130
	ds_read_b128 v[218:221], v130 offset:1024
	ds_read_b128 v[222:225], v130 offset:2048
	ds_read_b128 v[226:229], v130 offset:3072
	global_load_lds_dwordx4 v[230:231], off
	v_lshl_add_u64 v[232:233], s[66:67], 0, v[134:135]
	s_add_i32 m0, s17, 0x2000
	s_nop 0
	global_load_lds_dwordx4 v[232:233], off
	s_waitcnt vmcnt(10)
	s_barrier
	s_setprio 1
	s_waitcnt lgkmcnt(3)
	s_waitcnt lgkmcnt(1)
	v_mfma_f32_16x16x32_bf16 v[110:113], v[198:201], v[164:167], v[110:113]
	v_mfma_f32_16x16x32_bf16 v[106:109], v[222:225], v[164:167], v[106:109]
	v_mfma_f32_16x16x32_bf16 v[94:97], v[198:201], v[172:175], v[94:97]
	v_mfma_f32_16x16x32_bf16 v[90:93], v[222:225], v[172:175], v[90:93]
	v_mfma_f32_16x16x32_bf16 v[78:81], v[198:201], v[182:185], v[78:81]
	v_mfma_f32_16x16x32_bf16 v[74:77], v[222:225], v[182:185], v[74:77]
	v_mfma_f32_16x16x32_bf16 v[70:73], v[198:201], v[190:193], v[70:73]
	v_mfma_f32_16x16x32_bf16 v[58:61], v[222:225], v[190:193], v[58:61]
	s_waitcnt lgkmcnt(0)
	v_mfma_f32_16x16x32_bf16 v[110:113], v[218:221], v[168:171], v[110:113]
	v_mfma_f32_16x16x32_bf16 v[106:109], v[226:229], v[168:171], v[106:109]
	v_mfma_f32_16x16x32_bf16 v[94:97], v[218:221], v[178:181], v[94:97]
	v_mfma_f32_16x16x32_bf16 v[90:93], v[226:229], v[178:181], v[90:93]
	v_mfma_f32_16x16x32_bf16 v[78:81], v[218:221], v[186:189], v[78:81]
	v_mfma_f32_16x16x32_bf16 v[74:77], v[226:229], v[186:189], v[74:77]
	v_mfma_f32_16x16x32_bf16 v[70:73], v[218:221], v[194:197], v[70:73]
	v_mfma_f32_16x16x32_bf16 v[58:61], v[226:229], v[194:197], v[58:61]
	s_setprio 0
	s_mov_b32 m0, s43
	v_lshl_add_u64 v[234:235], s[68:69], 0, v[136:137]
	s_barrier
	ds_read_b128 v[164:167], v147 offset:16384
	ds_read_b128 v[168:171], v147 offset:17408
	ds_read_b128 v[172:175], v147 offset:18432
	ds_read_b128 v[178:181], v147 offset:19456
	ds_read_b128 v[182:185], v147 offset:20480
	ds_read_b128 v[186:189], v147 offset:21504
	ds_read_b128 v[190:193], v147 offset:22528
	ds_read_b128 v[194:197], v147 offset:23552
	global_load_lds_dwordx4 v[234:235], off
	v_lshl_add_u64 v[236:237], s[68:69], 0, v[132:133]
	s_mov_b32 m0, s44
	s_nop 0
	global_load_lds_dwordx4 v[236:237], off
	s_barrier
	s_setprio 1
	s_waitcnt lgkmcnt(7)
	v_mfma_f32_16x16x32_bf16 v[46:49], v[148:151], v[164:167], v[46:49]
	s_waitcnt lgkmcnt(5)
	v_mfma_f32_16x16x32_bf16 v[42:45], v[156:159], v[164:167], v[42:45]
	v_mfma_f32_16x16x32_bf16 v[38:41], v[148:151], v[172:175], v[38:41]
	s_waitcnt lgkmcnt(3)
	v_mfma_f32_16x16x32_bf16 v[34:37], v[156:159], v[172:175], v[34:37]
	v_mfma_f32_16x16x32_bf16 v[22:25], v[148:151], v[182:185], v[22:25]
	s_waitcnt lgkmcnt(1)
	v_mfma_f32_16x16x32_bf16 v[18:21], v[156:159], v[182:185], v[18:21]
	v_mfma_f32_16x16x32_bf16 v[6:9], v[148:151], v[190:193], v[6:9]
	v_mfma_f32_16x16x32_bf16 v[2:5], v[156:159], v[190:193], v[2:5]
	v_mfma_f32_16x16x32_bf16 v[46:49], v[152:155], v[168:171], v[46:49]
	v_mfma_f32_16x16x32_bf16 v[42:45], v[160:163], v[168:171], v[42:45]
	v_mfma_f32_16x16x32_bf16 v[38:41], v[152:155], v[178:181], v[38:41]
	v_mfma_f32_16x16x32_bf16 v[34:37], v[160:163], v[178:181], v[34:37]
	v_mfma_f32_16x16x32_bf16 v[22:25], v[152:155], v[186:189], v[22:25]
	s_waitcnt lgkmcnt(0)
	v_mfma_f32_16x16x32_bf16 v[18:21], v[160:163], v[186:189], v[18:21]
	v_mfma_f32_16x16x32_bf16 v[6:9], v[152:155], v[194:197], v[6:9]
	v_mfma_f32_16x16x32_bf16 v[2:5], v[160:163], v[194:197], v[2:5]
	s_setprio 0
	s_barrier
	s_add_u32 s64, s66, 0x4000
	s_addc_u32 s65, s67, 0
	s_add_i32 s17, s22, s38
	v_lshl_add_u64 v[148:149], s[64:65], 0, v[138:139]
	s_mov_b32 m0, s17
	s_nop 0
	global_load_lds_dwordx4 v[148:149], off
	v_lshl_add_u64 v[148:149], s[64:65], 0, v[134:135]
	s_add_i32 m0, s17, 0x2000
	s_nop 0
	global_load_lds_dwordx4 v[148:149], off
	s_waitcnt vmcnt(10)
	s_barrier
	s_setprio 1
	v_mfma_f32_16x16x32_bf16 v[30:33], v[198:201], v[164:167], v[30:33]
	v_mfma_f32_16x16x32_bf16 v[26:29], v[222:225], v[164:167], v[26:29]
	v_mfma_f32_16x16x32_bf16 v[14:17], v[198:201], v[172:175], v[14:17]
	v_mfma_f32_16x16x32_bf16 v[10:13], v[222:225], v[172:175], v[10:13]
	v_mfma_f32_16x16x32_bf16 v[62:65], v[198:201], v[182:185], v[62:65]
	v_mfma_f32_16x16x32_bf16 v[66:69], v[222:225], v[182:185], v[66:69]
	v_mfma_f32_16x16x32_bf16 v[50:53], v[198:201], v[190:193], v[50:53]
	v_mfma_f32_16x16x32_bf16 v[54:57], v[222:225], v[190:193], v[54:57]
	v_mfma_f32_16x16x32_bf16 v[30:33], v[218:221], v[168:171], v[30:33]
	v_mfma_f32_16x16x32_bf16 v[26:29], v[226:229], v[168:171], v[26:29]
	v_mfma_f32_16x16x32_bf16 v[14:17], v[218:221], v[178:181], v[14:17]
	v_mfma_f32_16x16x32_bf16 v[10:13], v[226:229], v[178:181], v[10:13]
	v_mfma_f32_16x16x32_bf16 v[62:65], v[218:221], v[186:189], v[62:65]
	v_mfma_f32_16x16x32_bf16 v[66:69], v[226:229], v[186:189], v[66:69]
	v_mfma_f32_16x16x32_bf16 v[50:53], v[218:221], v[194:197], v[50:53]
	v_mfma_f32_16x16x32_bf16 v[54:57], v[226:229], v[194:197], v[54:57]
	s_setprio 0
	s_add_i32 s17, 0, 0x18000
	v_add_u32_e32 v130, s17, v145
	s_barrier
	ds_read_b128 v[148:151], v130
	ds_read_b128 v[152:155], v130 offset:1024
	ds_read_b128 v[156:159], v130 offset:2048
	ds_read_b128 v[160:163], v130 offset:3072
	s_add_u32 s64, s68, 0x40000
	s_addc_u32 s65, s69, 0
	s_mov_b32 m0, s45
	v_lshl_add_u64 v[198:199], s[64:65], 0, v[136:137]
	ds_read_b128 v[164:167], v147 offset:32768
	ds_read_b128 v[168:171], v147 offset:33792
	ds_read_b128 v[172:175], v147 offset:34816
	ds_read_b128 v[178:181], v147 offset:35840
	ds_read_b128 v[182:185], v147 offset:36864
	ds_read_b128 v[186:189], v147 offset:37888
	ds_read_b128 v[190:193], v147 offset:38912
	ds_read_b128 v[194:197], v147 offset:39936
	global_load_lds_dwordx4 v[198:199], off
	v_lshl_add_u64 v[198:199], s[64:65], 0, v[132:133]
	s_mov_b32 m0, s46
	s_nop 0
	global_load_lds_dwordx4 v[198:199], off
	s_waitcnt lgkmcnt(8)
	s_waitcnt vmcnt(10)
	s_barrier
	s_setprio 1
	s_waitcnt lgkmcnt(7)
	v_mfma_f32_16x16x32_bf16 v[126:129], v[148:151], v[164:167], v[126:129]
	s_waitcnt lgkmcnt(5)
	v_mfma_f32_16x16x32_bf16 v[122:125], v[156:159], v[164:167], v[122:125]
	v_mfma_f32_16x16x32_bf16 v[118:121], v[148:151], v[172:175], v[118:121]
	s_waitcnt lgkmcnt(3)
	v_mfma_f32_16x16x32_bf16 v[114:117], v[156:159], v[172:175], v[114:117]
	v_mfma_f32_16x16x32_bf16 v[102:105], v[148:151], v[182:185], v[102:105]
	s_waitcnt lgkmcnt(1)
	v_mfma_f32_16x16x32_bf16 v[98:101], v[156:159], v[182:185], v[98:101]
	v_mfma_f32_16x16x32_bf16 v[86:89], v[148:151], v[190:193], v[86:89]
	v_mfma_f32_16x16x32_bf16 v[82:85], v[156:159], v[190:193], v[82:85]
	v_mfma_f32_16x16x32_bf16 v[126:129], v[152:155], v[168:171], v[126:129]
	v_mfma_f32_16x16x32_bf16 v[122:125], v[160:163], v[168:171], v[122:125]
	v_mfma_f32_16x16x32_bf16 v[118:121], v[152:155], v[178:181], v[118:121]
	v_mfma_f32_16x16x32_bf16 v[114:117], v[160:163], v[178:181], v[114:117]
	v_mfma_f32_16x16x32_bf16 v[102:105], v[152:155], v[186:189], v[102:105]
	s_waitcnt lgkmcnt(0)
	v_mfma_f32_16x16x32_bf16 v[98:101], v[160:163], v[186:189], v[98:101]
	v_mfma_f32_16x16x32_bf16 v[86:89], v[152:155], v[194:197], v[86:89]
	v_mfma_f32_16x16x32_bf16 v[82:85], v[160:163], v[194:197], v[82:85]
	s_setprio 0
	s_barrier
	s_add_i32 s22, 0, 0x1c000
	s_add_i32 s17, s17, s38
	v_add_u32_e32 v130, s22, v145
	v_lshl_add_u64 v[230:231], v[230:231], 0, s[30:31]
	s_mov_b32 m0, s17
	ds_read_b128 v[198:201], v130
	ds_read_b128 v[218:221], v130 offset:1024
	ds_read_b128 v[222:225], v130 offset:2048
	ds_read_b128 v[226:229], v130 offset:3072
	global_load_lds_dwordx4 v[230:231], off
	v_lshl_add_u64 v[230:231], v[232:233], 0, s[30:31]
	s_add_i32 m0, s17, 0x2000
	s_nop 0
	global_load_lds_dwordx4 v[230:231], off
	s_waitcnt vmcnt(10)
	s_barrier
	s_setprio 1
	s_waitcnt lgkmcnt(3)
	s_waitcnt lgkmcnt(1)
	v_mfma_f32_16x16x32_bf16 v[110:113], v[198:201], v[164:167], v[110:113]
	v_mfma_f32_16x16x32_bf16 v[106:109], v[222:225], v[164:167], v[106:109]
	v_mfma_f32_16x16x32_bf16 v[94:97], v[198:201], v[172:175], v[94:97]
	v_mfma_f32_16x16x32_bf16 v[90:93], v[222:225], v[172:175], v[90:93]
	v_mfma_f32_16x16x32_bf16 v[78:81], v[198:201], v[182:185], v[78:81]
	v_mfma_f32_16x16x32_bf16 v[74:77], v[222:225], v[182:185], v[74:77]
	v_mfma_f32_16x16x32_bf16 v[70:73], v[198:201], v[190:193], v[70:73]
	v_mfma_f32_16x16x32_bf16 v[58:61], v[222:225], v[190:193], v[58:61]
	s_waitcnt lgkmcnt(0)
	v_mfma_f32_16x16x32_bf16 v[110:113], v[218:221], v[168:171], v[110:113]
	v_mfma_f32_16x16x32_bf16 v[106:109], v[226:229], v[168:171], v[106:109]
	v_mfma_f32_16x16x32_bf16 v[94:97], v[218:221], v[178:181], v[94:97]
	v_mfma_f32_16x16x32_bf16 v[90:93], v[226:229], v[178:181], v[90:93]
	v_mfma_f32_16x16x32_bf16 v[78:81], v[218:221], v[186:189], v[78:81]
	v_mfma_f32_16x16x32_bf16 v[74:77], v[226:229], v[186:189], v[74:77]
	v_mfma_f32_16x16x32_bf16 v[70:73], v[218:221], v[194:197], v[70:73]
	v_mfma_f32_16x16x32_bf16 v[58:61], v[226:229], v[194:197], v[58:61]
	s_setprio 0
	s_mov_b32 m0, s61
	v_lshl_add_u64 v[230:231], v[234:235], 0, s[30:31]
	s_barrier
	ds_read_b128 v[164:167], v147 offset:49152
	ds_read_b128 v[168:171], v147 offset:50176
	ds_read_b128 v[172:175], v147 offset:51200
	ds_read_b128 v[178:181], v147 offset:52224
	ds_read_b128 v[182:185], v147 offset:53248
	ds_read_b128 v[186:189], v147 offset:54272
	ds_read_b128 v[190:193], v147 offset:55296
	ds_read_b128 v[194:197], v147 offset:56320
	global_load_lds_dwordx4 v[230:231], off
	v_lshl_add_u64 v[230:231], v[236:237], 0, s[30:31]
	s_mov_b32 m0, s62
	s_nop 0
	global_load_lds_dwordx4 v[230:231], off
	s_barrier
	s_setprio 1
	s_waitcnt lgkmcnt(7)
	v_mfma_f32_16x16x32_bf16 v[46:49], v[148:151], v[164:167], v[46:49]
	s_waitcnt lgkmcnt(5)
	v_mfma_f32_16x16x32_bf16 v[42:45], v[156:159], v[164:167], v[42:45]
	v_mfma_f32_16x16x32_bf16 v[38:41], v[148:151], v[172:175], v[38:41]
	s_waitcnt lgkmcnt(3)
	v_mfma_f32_16x16x32_bf16 v[34:37], v[156:159], v[172:175], v[34:37]
	v_mfma_f32_16x16x32_bf16 v[22:25], v[148:151], v[182:185], v[22:25]
	s_waitcnt lgkmcnt(1)
	v_mfma_f32_16x16x32_bf16 v[18:21], v[156:159], v[182:185], v[18:21]
	v_mfma_f32_16x16x32_bf16 v[6:9], v[148:151], v[190:193], v[6:9]
	v_mfma_f32_16x16x32_bf16 v[2:5], v[156:159], v[190:193], v[2:5]
	v_mfma_f32_16x16x32_bf16 v[46:49], v[152:155], v[168:171], v[46:49]
	v_mfma_f32_16x16x32_bf16 v[42:45], v[160:163], v[168:171], v[42:45]
	v_mfma_f32_16x16x32_bf16 v[38:41], v[152:155], v[178:181], v[38:41]
	v_mfma_f32_16x16x32_bf16 v[34:37], v[160:163], v[178:181], v[34:37]
	v_mfma_f32_16x16x32_bf16 v[22:25], v[152:155], v[186:189], v[22:25]
	s_waitcnt lgkmcnt(0)
	v_mfma_f32_16x16x32_bf16 v[18:21], v[160:163], v[186:189], v[18:21]
	v_mfma_f32_16x16x32_bf16 v[6:9], v[152:155], v[194:197], v[6:9]
	v_mfma_f32_16x16x32_bf16 v[2:5], v[160:163], v[194:197], v[2:5]
	s_setprio 0
	s_barrier
	s_add_u32 s64, s66, 0x4080
	s_addc_u32 s65, s67, 0
	s_add_i32 s17, s22, s38
	v_lshl_add_u64 v[148:149], s[64:65], 0, v[138:139]
	s_mov_b32 m0, s17
	s_nop 0
	global_load_lds_dwordx4 v[148:149], off
	v_lshl_add_u64 v[148:149], s[64:65], 0, v[134:135]
	s_add_i32 m0, s17, 0x2000
	s_nop 0
	global_load_lds_dwordx4 v[148:149], off
	s_waitcnt vmcnt(10)
	s_barrier
	s_setprio 1
	v_mfma_f32_16x16x32_bf16 v[30:33], v[198:201], v[164:167], v[30:33]
	v_mfma_f32_16x16x32_bf16 v[26:29], v[222:225], v[164:167], v[26:29]
	v_mfma_f32_16x16x32_bf16 v[14:17], v[198:201], v[172:175], v[14:17]
	v_mfma_f32_16x16x32_bf16 v[10:13], v[222:225], v[172:175], v[10:13]
	v_mfma_f32_16x16x32_bf16 v[62:65], v[198:201], v[182:185], v[62:65]
	v_mfma_f32_16x16x32_bf16 v[66:69], v[222:225], v[182:185], v[66:69]
	v_mfma_f32_16x16x32_bf16 v[50:53], v[198:201], v[190:193], v[50:53]
	v_mfma_f32_16x16x32_bf16 v[54:57], v[222:225], v[190:193], v[54:57]
	v_mfma_f32_16x16x32_bf16 v[30:33], v[218:221], v[168:171], v[30:33]
	v_mfma_f32_16x16x32_bf16 v[26:29], v[226:229], v[168:171], v[26:29]
	v_mfma_f32_16x16x32_bf16 v[14:17], v[218:221], v[178:181], v[14:17]
	v_mfma_f32_16x16x32_bf16 v[10:13], v[226:229], v[178:181], v[10:13]
	v_mfma_f32_16x16x32_bf16 v[62:65], v[218:221], v[186:189], v[62:65]
	v_mfma_f32_16x16x32_bf16 v[66:69], v[226:229], v[186:189], v[66:69]
	v_mfma_f32_16x16x32_bf16 v[50:53], v[218:221], v[194:197], v[50:53]
	v_mfma_f32_16x16x32_bf16 v[54:57], v[226:229], v[194:197], v[54:57]
	s_setprio 0
	s_add_i32 s11, s11, 2
	s_add_u32 s18, s18, 0x100
	s_addc_u32 s19, s19, 0
	s_add_u32 s5, s5, 0x100
	s_addc_u32 s9, s9, 0
	s_cmp_gt_u32 s11, 13
	s_barrier
	s_cbranch_scc0 .LBB0_541
	s_mul_hi_i32 s5, s16, 0x38e38e39
	s_lshr_b32 s9, s5, 31
	s_ashr_i32 s5, s5, 1
	s_add_i32 s18, s5, s9
	s_mul_i32 s5, s18, 9
	s_sub_i32 s11, s16, s5
	s_cmp_lg_u32 s11, 8
	s_cselect_b64 s[66:67], -1, 0
	s_ashr_i32 s19, s18, 31
	s_cmp_gt_i32 s4, 2
	s_mov_b64 s[68:69], -1
	s_cbranch_scc0 .LBB0_548
	s_add_i32 s5, s4, -3
	s_and_b64 vcc, exec, s[66:67]
	s_cbranch_vccz .LBB0_545
	s_lshl_b64 s[16:17], s[18:19], 21
	s_add_u32 s9, s57, s16
	s_addc_u32 s16, s58, s17
	s_lshl_b32 s17, s5, 12
	s_add_u32 s9, s9, s17
	s_addc_u32 s22, s16, 0
	s_lshl_b32 s16, s11, 8
	s_ashr_i32 s17, s16, 31
	s_lshl_b64 s[16:17], s[16:17], 1
	s_add_u32 s16, s9, s16
	s_addc_u32 s17, s22, s17
	s_mov_b64 s[68:69], 0

.LBB0_635:
	s_add_i32 s13, s12, 0x100
	s_and_b64 s[10:11], s[10:11], exec
	s_cselect_b32 s11, 0, s13
	s_cselect_b32 s10, 0, 0
	s_add_u32 s16, s74, s11
	s_addc_u32 s17, s75, s10
	s_add_u32 s18, s4, s11
	s_addc_u32 s19, s5, s10
	s_add_i32 s11, 0, 0x10000
	s_add_u32 s84, s76, s12
	s_addc_u32 s85, s77, 0
	s_add_i32 s43, s11, s33
	s_add_i32 m0, s38, 0xc000
	s_add_i32 s60, s38, 0xe000
	s_add_i32 s94, 0, 0x14000
	s_add_i32 s27, s43, 0x2000
	s_add_u32 s14, s18, 0x1000
	v_add_u32_e32 v154, s11, v140
	s_addc_u32 s15, s19, 0
	s_add_i32 s93, s94, s33
	ds_read_b128 v[142:145], v154
	ds_read_b128 v[146:149], v154 offset:1024
	ds_read_b128 v[150:153], v154 offset:2048
	ds_read_b128 v[154:157], v154 offset:3072
	s_add_i32 s96, s93, 0x2000
	s_add_i32 s92, 0, 0x18000
	s_add_u32 s12, s16, 0x10000
	s_addc_u32 s13, s17, 0
	s_add_i32 s91, s92, s33
	s_add_i32 s90, 0, 0x1c000
	s_add_i32 s89, s91, 0x2000
	s_add_u32 s10, s18, 0x1080
	s_addc_u32 s11, s19, 0
	s_add_i32 vcc_hi, s90, s33
	s_add_i32 vcc_lo, vcc_hi, 0x2000
	v_lshl_add_u64 v[174:175], s[84:85], 0, v[132:133]
	v_lshl_add_u64 v[174:175], v[174:175], 0, s[30:31]
	ds_read_b128 v[158:161], v141
	ds_read_b128 v[162:165], v141 offset:1024
	ds_read_b128 v[166:169], v141 offset:2048
	ds_read_b128 v[170:173], v141 offset:3072
	ds_read_b128 v[178:181], v141 offset:4096
	ds_read_b128 v[182:185], v141 offset:5120
	ds_read_b128 v[188:191], v141 offset:6144
	ds_read_b128 v[192:195], v141 offset:7168
	global_load_lds_dwordx4 v[174:175], off
	v_lshl_add_u64 v[174:175], s[84:85], 0, v[136:137]
	v_lshl_add_u64 v[174:175], v[174:175], 0, s[30:31]
	s_mov_b32 m0, s60
	s_nop 0
	global_load_lds_dwordx4 v[174:175], off
	s_waitcnt lgkmcnt(8)
	s_waitcnt vmcnt(10)
	s_barrier
	s_setprio 1
	s_waitcnt lgkmcnt(7)
	v_mfma_f32_16x16x32_bf16 v[126:129], v[142:145], v[158:161], v[126:129]
	s_waitcnt lgkmcnt(5)
	v_mfma_f32_16x16x32_bf16 v[122:125], v[150:153], v[158:161], v[122:125]
	v_mfma_f32_16x16x32_bf16 v[118:121], v[142:145], v[166:169], v[118:121]
	s_waitcnt lgkmcnt(3)
	v_mfma_f32_16x16x32_bf16 v[114:117], v[150:153], v[166:169], v[114:117]
	v_mfma_f32_16x16x32_bf16 v[102:105], v[142:145], v[178:181], v[102:105]
	s_waitcnt lgkmcnt(1)
	v_mfma_f32_16x16x32_bf16 v[98:101], v[150:153], v[178:181], v[98:101]
	v_mfma_f32_16x16x32_bf16 v[86:89], v[142:145], v[188:191], v[86:89]
	v_mfma_f32_16x16x32_bf16 v[82:85], v[150:153], v[188:191], v[82:85]
	v_mfma_f32_16x16x32_bf16 v[126:129], v[146:149], v[162:165], v[126:129]
	v_mfma_f32_16x16x32_bf16 v[122:125], v[154:157], v[162:165], v[122:125]
	v_mfma_f32_16x16x32_bf16 v[118:121], v[146:149], v[170:173], v[118:121]
	v_mfma_f32_16x16x32_bf16 v[114:117], v[154:157], v[170:173], v[114:117]
	v_mfma_f32_16x16x32_bf16 v[102:105], v[146:149], v[182:185], v[102:105]
	s_waitcnt lgkmcnt(0)
	v_mfma_f32_16x16x32_bf16 v[98:101], v[154:157], v[182:185], v[98:101]
	v_mfma_f32_16x16x32_bf16 v[86:89], v[146:149], v[192:195], v[86:89]
	v_mfma_f32_16x16x32_bf16 v[82:85], v[154:157], v[192:195], v[82:85]
	s_setprio 0
	s_barrier
	v_add_u32_e32 v174, s94, v140
	s_mov_b32 m0, s43
	ds_read_b128 v[196:199], v174
	ds_read_b128 v[218:221], v174 offset:1024
	ds_read_b128 v[222:225], v174 offset:2048
	ds_read_b128 v[226:229], v174 offset:3072
	v_lshl_add_u64 v[174:175], s[18:19], 0, v[130:131]
	global_load_lds_dwordx4 v[174:175], off
	v_lshl_add_u64 v[200:201], s[18:19], 0, v[134:135]
	s_mov_b32 m0, s27
	s_nop 0
	global_load_lds_dwordx4 v[200:201], off
	s_waitcnt vmcnt(10)
	s_barrier
	s_setprio 1
	s_waitcnt lgkmcnt(3)
	s_waitcnt lgkmcnt(1)
	v_mfma_f32_16x16x32_bf16 v[110:113], v[196:199], v[158:161], v[110:113]
	v_mfma_f32_16x16x32_bf16 v[106:109], v[222:225], v[158:161], v[106:109]
	v_mfma_f32_16x16x32_bf16 v[94:97], v[196:199], v[166:169], v[94:97]
	v_mfma_f32_16x16x32_bf16 v[90:93], v[222:225], v[166:169], v[90:93]
	v_mfma_f32_16x16x32_bf16 v[78:81], v[196:199], v[178:181], v[78:81]
	v_mfma_f32_16x16x32_bf16 v[74:77], v[222:225], v[178:181], v[74:77]
	v_mfma_f32_16x16x32_bf16 v[70:73], v[196:199], v[188:191], v[70:73]
	v_mfma_f32_16x16x32_bf16 v[66:69], v[222:225], v[188:191], v[66:69]
	s_waitcnt lgkmcnt(0)
	v_mfma_f32_16x16x32_bf16 v[110:113], v[218:221], v[162:165], v[110:113]
	v_mfma_f32_16x16x32_bf16 v[106:109], v[226:229], v[162:165], v[106:109]
	v_mfma_f32_16x16x32_bf16 v[94:97], v[218:221], v[170:173], v[94:97]
	v_mfma_f32_16x16x32_bf16 v[90:93], v[226:229], v[170:173], v[90:93]
	v_mfma_f32_16x16x32_bf16 v[78:81], v[218:221], v[182:185], v[78:81]
	v_mfma_f32_16x16x32_bf16 v[74:77], v[226:229], v[182:185], v[74:77]
	v_mfma_f32_16x16x32_bf16 v[70:73], v[218:221], v[192:195], v[70:73]
	v_mfma_f32_16x16x32_bf16 v[66:69], v[226:229], v[192:195], v[66:69]
	s_setprio 0
	s_mov_b32 m0, s38
	v_lshl_add_u64 v[230:231], s[16:17], 0, v[132:133]
	s_barrier
	ds_read_b128 v[158:161], v141 offset:16384
	ds_read_b128 v[162:165], v141 offset:17408
	ds_read_b128 v[166:169], v141 offset:18432
	ds_read_b128 v[170:173], v141 offset:19456
	ds_read_b128 v[178:181], v141 offset:20480
	ds_read_b128 v[182:185], v141 offset:21504
	ds_read_b128 v[188:191], v141 offset:22528
	ds_read_b128 v[192:195], v141 offset:23552
	global_load_lds_dwordx4 v[230:231], off
	v_lshl_add_u64 v[232:233], s[16:17], 0, v[136:137]
	s_mov_b32 m0, s39
	s_nop 0
	global_load_lds_dwordx4 v[232:233], off
	s_barrier
	s_setprio 1
	s_waitcnt lgkmcnt(7)
	v_mfma_f32_16x16x32_bf16 v[54:57], v[142:145], v[158:161], v[54:57]
	s_waitcnt lgkmcnt(5)
	v_mfma_f32_16x16x32_bf16 v[50:53], v[150:153], v[158:161], v[50:53]
	v_mfma_f32_16x16x32_bf16 v[38:41], v[142:145], v[166:169], v[38:41]
	s_waitcnt lgkmcnt(3)
	v_mfma_f32_16x16x32_bf16 v[34:37], v[150:153], v[166:169], v[34:37]
	v_mfma_f32_16x16x32_bf16 v[22:25], v[142:145], v[178:181], v[22:25]
	s_waitcnt lgkmcnt(1)
	v_mfma_f32_16x16x32_bf16 v[18:21], v[150:153], v[178:181], v[18:21]
	v_mfma_f32_16x16x32_bf16 v[6:9], v[142:145], v[188:191], v[6:9]
	v_mfma_f32_16x16x32_bf16 v[2:5], v[150:153], v[188:191], v[2:5]
	v_mfma_f32_16x16x32_bf16 v[54:57], v[146:149], v[162:165], v[54:57]
	v_mfma_f32_16x16x32_bf16 v[50:53], v[154:157], v[162:165], v[50:53]
	v_mfma_f32_16x16x32_bf16 v[38:41], v[146:149], v[170:173], v[38:41]
	v_mfma_f32_16x16x32_bf16 v[34:37], v[154:157], v[170:173], v[34:37]
	v_mfma_f32_16x16x32_bf16 v[22:25], v[146:149], v[182:185], v[22:25]
	s_waitcnt lgkmcnt(0)
	v_mfma_f32_16x16x32_bf16 v[18:21], v[154:157], v[182:185], v[18:21]
	v_mfma_f32_16x16x32_bf16 v[6:9], v[146:149], v[192:195], v[6:9]
	v_mfma_f32_16x16x32_bf16 v[2:5], v[154:157], v[192:195], v[2:5]
	s_setprio 0
	s_barrier
	s_mov_b32 m0, s93
	v_lshl_add_u64 v[142:143], s[14:15], 0, v[130:131]
	global_load_lds_dwordx4 v[142:143], off
	v_lshl_add_u64 v[142:143], s[14:15], 0, v[134:135]
	s_mov_b32 m0, s96
	s_nop 0
	global_load_lds_dwordx4 v[142:143], off
	s_waitcnt vmcnt(10)
	s_barrier
	s_setprio 1
	v_mfma_f32_16x16x32_bf16 v[30:33], v[196:199], v[158:161], v[30:33]
	v_mfma_f32_16x16x32_bf16 v[26:29], v[222:225], v[158:161], v[26:29]
	v_mfma_f32_16x16x32_bf16 v[14:17], v[196:199], v[166:169], v[14:17]
	v_mfma_f32_16x16x32_bf16 v[10:13], v[222:225], v[166:169], v[10:13]
	v_mfma_f32_16x16x32_bf16 v[58:61], v[196:199], v[178:181], v[58:61]
	v_mfma_f32_16x16x32_bf16 v[62:65], v[222:225], v[178:181], v[62:65]
	v_mfma_f32_16x16x32_bf16 v[42:45], v[196:199], v[188:191], v[42:45]
	v_mfma_f32_16x16x32_bf16 v[46:49], v[222:225], v[188:191], v[46:49]
	v_mfma_f32_16x16x32_bf16 v[30:33], v[218:221], v[162:165], v[30:33]
	v_mfma_f32_16x16x32_bf16 v[26:29], v[226:229], v[162:165], v[26:29]
	v_mfma_f32_16x16x32_bf16 v[14:17], v[218:221], v[170:173], v[14:17]
	v_mfma_f32_16x16x32_bf16 v[10:13], v[226:229], v[170:173], v[10:13]
	v_mfma_f32_16x16x32_bf16 v[58:61], v[218:221], v[182:185], v[58:61]
	v_mfma_f32_16x16x32_bf16 v[62:65], v[226:229], v[182:185], v[62:65]
	v_mfma_f32_16x16x32_bf16 v[42:45], v[218:221], v[192:195], v[42:45]
	v_mfma_f32_16x16x32_bf16 v[46:49], v[226:229], v[192:195], v[46:49]
	s_setprio 0
	v_add_u32_e32 v154, s92, v140
	s_barrier
	ds_read_b128 v[142:145], v154
	ds_read_b128 v[146:149], v154 offset:1024
	ds_read_b128 v[150:153], v154 offset:2048
	ds_read_b128 v[154:157], v154 offset:3072
	s_mov_b32 m0, s42
	v_lshl_add_u64 v[196:197], s[12:13], 0, v[132:133]
	ds_read_b128 v[158:161], v141 offset:32768
	ds_read_b128 v[162:165], v141 offset:33792
	ds_read_b128 v[166:169], v141 offset:34816
	ds_read_b128 v[170:173], v141 offset:35840
	ds_read_b128 v[178:181], v141 offset:36864
	ds_read_b128 v[182:185], v141 offset:37888
	ds_read_b128 v[188:191], v141 offset:38912
	ds_read_b128 v[192:195], v141 offset:39936
	global_load_lds_dwordx4 v[196:197], off
	v_lshl_add_u64 v[196:197], s[12:13], 0, v[136:137]
	s_mov_b32 m0, s64
	s_nop 0
	global_load_lds_dwordx4 v[196:197], off
	s_waitcnt lgkmcnt(8)
	s_waitcnt vmcnt(10)
	s_barrier
	s_setprio 1
	s_waitcnt lgkmcnt(7)
	v_mfma_f32_16x16x32_bf16 v[126:129], v[142:145], v[158:161], v[126:129]
	s_waitcnt lgkmcnt(5)
	v_mfma_f32_16x16x32_bf16 v[122:125], v[150:153], v[158:161], v[122:125]
	v_mfma_f32_16x16x32_bf16 v[118:121], v[142:145], v[166:169], v[118:121]
	s_waitcnt lgkmcnt(3)
	v_mfma_f32_16x16x32_bf16 v[114:117], v[150:153], v[166:169], v[114:117]
	v_mfma_f32_16x16x32_bf16 v[102:105], v[142:145], v[178:181], v[102:105]
	s_waitcnt lgkmcnt(1)
	v_mfma_f32_16x16x32_bf16 v[98:101], v[150:153], v[178:181], v[98:101]
	v_mfma_f32_16x16x32_bf16 v[86:89], v[142:145], v[188:191], v[86:89]
	v_mfma_f32_16x16x32_bf16 v[82:85], v[150:153], v[188:191], v[82:85]
	v_mfma_f32_16x16x32_bf16 v[126:129], v[146:149], v[162:165], v[126:129]
	v_mfma_f32_16x16x32_bf16 v[122:125], v[154:157], v[162:165], v[122:125]
	v_mfma_f32_16x16x32_bf16 v[118:121], v[146:149], v[170:173], v[118:121]
	v_mfma_f32_16x16x32_bf16 v[114:117], v[154:157], v[170:173], v[114:117]
	v_mfma_f32_16x16x32_bf16 v[102:105], v[146:149], v[182:185], v[102:105]
	s_waitcnt lgkmcnt(0)
	v_mfma_f32_16x16x32_bf16 v[98:101], v[154:157], v[182:185], v[98:101]
	v_mfma_f32_16x16x32_bf16 v[86:89], v[146:149], v[192:195], v[86:89]
	v_mfma_f32_16x16x32_bf16 v[82:85], v[154:157], v[192:195], v[82:85]
	s_setprio 0
	s_barrier
	s_mov_b32 m0, s91
	v_add_u32_e32 v187, s90, v140
	v_lshl_add_u64 v[174:175], v[174:175], 0, s[30:31]
	ds_read_b128 v[196:199], v187
	ds_read_b128 v[218:221], v187 offset:1024
	ds_read_b128 v[222:225], v187 offset:2048
	ds_read_b128 v[226:229], v187 offset:3072
	global_load_lds_dwordx4 v[174:175], off
	v_lshl_add_u64 v[174:175], v[200:201], 0, s[30:31]
	s_mov_b32 m0, s89
	s_nop 0
	global_load_lds_dwordx4 v[174:175], off
	s_waitcnt vmcnt(10)
	s_barrier
	s_setprio 1
	s_waitcnt lgkmcnt(3)
	s_waitcnt lgkmcnt(1)
	v_mfma_f32_16x16x32_bf16 v[110:113], v[196:199], v[158:161], v[110:113]
	v_mfma_f32_16x16x32_bf16 v[106:109], v[222:225], v[158:161], v[106:109]
	v_mfma_f32_16x16x32_bf16 v[94:97], v[196:199], v[166:169], v[94:97]
	v_mfma_f32_16x16x32_bf16 v[90:93], v[222:225], v[166:169], v[90:93]
	v_mfma_f32_16x16x32_bf16 v[78:81], v[196:199], v[178:181], v[78:81]
	v_mfma_f32_16x16x32_bf16 v[74:77], v[222:225], v[178:181], v[74:77]
	v_mfma_f32_16x16x32_bf16 v[70:73], v[196:199], v[188:191], v[70:73]
	v_mfma_f32_16x16x32_bf16 v[66:69], v[222:225], v[188:191], v[66:69]
	s_waitcnt lgkmcnt(0)
	v_mfma_f32_16x16x32_bf16 v[110:113], v[218:221], v[162:165], v[110:113]
	v_mfma_f32_16x16x32_bf16 v[106:109], v[226:229], v[162:165], v[106:109]
	v_mfma_f32_16x16x32_bf16 v[94:97], v[218:221], v[170:173], v[94:97]
	v_mfma_f32_16x16x32_bf16 v[90:93], v[226:229], v[170:173], v[90:93]
	v_mfma_f32_16x16x32_bf16 v[78:81], v[218:221], v[182:185], v[78:81]
	v_mfma_f32_16x16x32_bf16 v[74:77], v[226:229], v[182:185], v[74:77]
	v_mfma_f32_16x16x32_bf16 v[70:73], v[218:221], v[192:195], v[70:73]
	v_mfma_f32_16x16x32_bf16 v[66:69], v[226:229], v[192:195], v[66:69]
	s_setprio 0
	s_mov_b32 m0, s87
	v_lshl_add_u64 v[174:175], v[230:231], 0, s[30:31]
	s_barrier
	ds_read_b128 v[158:161], v141 offset:49152
	ds_read_b128 v[162:165], v141 offset:50176
	ds_read_b128 v[166:169], v141 offset:51200
	ds_read_b128 v[170:173], v141 offset:52224
	ds_read_b128 v[178:181], v141 offset:53248
	ds_read_b128 v[182:185], v141 offset:54272
	ds_read_b128 v[188:191], v141 offset:55296
	ds_read_b128 v[192:195], v141 offset:56320
	global_load_lds_dwordx4 v[174:175], off
	v_lshl_add_u64 v[174:175], v[232:233], 0, s[30:31]
	s_mov_b32 m0, s88
	s_nop 0
	global_load_lds_dwordx4 v[174:175], off
	s_barrier
	s_setprio 1
	s_waitcnt lgkmcnt(7)
	v_mfma_f32_16x16x32_bf16 v[54:57], v[142:145], v[158:161], v[54:57]
	s_waitcnt lgkmcnt(5)
	v_mfma_f32_16x16x32_bf16 v[50:53], v[150:153], v[158:161], v[50:53]
	v_mfma_f32_16x16x32_bf16 v[38:41], v[142:145], v[166:169], v[38:41]
	s_waitcnt lgkmcnt(3)
	v_mfma_f32_16x16x32_bf16 v[34:37], v[150:153], v[166:169], v[34:37]
	v_mfma_f32_16x16x32_bf16 v[22:25], v[142:145], v[178:181], v[22:25]
	s_waitcnt lgkmcnt(1)
	v_mfma_f32_16x16x32_bf16 v[18:21], v[150:153], v[178:181], v[18:21]
	v_mfma_f32_16x16x32_bf16 v[6:9], v[142:145], v[188:191], v[6:9]
	v_mfma_f32_16x16x32_bf16 v[2:5], v[150:153], v[188:191], v[2:5]
	v_mfma_f32_16x16x32_bf16 v[54:57], v[146:149], v[162:165], v[54:57]
	v_mfma_f32_16x16x32_bf16 v[50:53], v[154:157], v[162:165], v[50:53]
	v_mfma_f32_16x16x32_bf16 v[38:41], v[146:149], v[170:173], v[38:41]
	v_mfma_f32_16x16x32_bf16 v[34:37], v[154:157], v[170:173], v[34:37]
	v_mfma_f32_16x16x32_bf16 v[22:25], v[146:149], v[182:185], v[22:25]
	s_waitcnt lgkmcnt(0)
	v_mfma_f32_16x16x32_bf16 v[18:21], v[154:157], v[182:185], v[18:21]
	v_mfma_f32_16x16x32_bf16 v[6:9], v[146:149], v[192:195], v[6:9]
	v_mfma_f32_16x16x32_bf16 v[2:5], v[154:157], v[192:195], v[2:5]
	s_setprio 0
	s_barrier
	s_mov_b32 m0, vcc_hi
	v_lshl_add_u64 v[142:143], s[10:11], 0, v[130:131]
	global_load_lds_dwordx4 v[142:143], off
	v_lshl_add_u64 v[142:143], s[10:11], 0, v[134:135]
	s_mov_b32 m0, vcc_lo
	s_nop 0
	global_load_lds_dwordx4 v[142:143], off
	s_waitcnt vmcnt(10)
	s_barrier
	s_setprio 1
	v_mfma_f32_16x16x32_bf16 v[30:33], v[196:199], v[158:161], v[30:33]
	v_mfma_f32_16x16x32_bf16 v[26:29], v[222:225], v[158:161], v[26:29]
	v_mfma_f32_16x16x32_bf16 v[14:17], v[196:199], v[166:169], v[14:17]
	v_mfma_f32_16x16x32_bf16 v[10:13], v[222:225], v[166:169], v[10:13]
	v_mfma_f32_16x16x32_bf16 v[58:61], v[196:199], v[178:181], v[58:61]
	v_mfma_f32_16x16x32_bf16 v[62:65], v[222:225], v[178:181], v[62:65]
	v_mfma_f32_16x16x32_bf16 v[42:45], v[196:199], v[188:191], v[42:45]
	v_mfma_f32_16x16x32_bf16 v[46:49], v[222:225], v[188:191], v[46:49]
	v_mfma_f32_16x16x32_bf16 v[30:33], v[218:221], v[162:165], v[30:33]
	v_mfma_f32_16x16x32_bf16 v[26:29], v[226:229], v[162:165], v[26:29]
	v_mfma_f32_16x16x32_bf16 v[14:17], v[218:221], v[170:173], v[14:17]
	v_mfma_f32_16x16x32_bf16 v[10:13], v[226:229], v[170:173], v[10:13]
	v_mfma_f32_16x16x32_bf16 v[58:61], v[218:221], v[182:185], v[58:61]
	v_mfma_f32_16x16x32_bf16 v[62:65], v[226:229], v[182:185], v[62:65]
	v_mfma_f32_16x16x32_bf16 v[42:45], v[218:221], v[192:195], v[42:45]
	v_mfma_f32_16x16x32_bf16 v[46:49], v[226:229], v[192:195], v[46:49]
	s_setprio 0
	s_andn2_b64 vcc, exec, s[6:7]
	s_mov_b64 s[10:11], -1
	s_mov_b64 s[6:7], 0
	s_movk_i32 s12, 0x100
	s_barrier
	s_cbranch_vccz .LBB0_635
	s_mul_i32 s4, s22, 0x900
	s_add_i32 s22, s4, 0x800
	s_lshl_b32 s6, s86, 6
	s_lshl_b64 s[4:5], s[22:23], 11
	s_add_u32 s4, s68, s4
	v_lshlrev_b32_e32 v130, 10, v139
	s_addc_u32 s5, s69, s5
	v_or3_b32 v130, v130, s6, v138
	v_cvt_pk_bf16_f32 v126, v126, v127
	v_lshl_add_u64 v[132:133], v[130:131], 1, s[4:5]
	s_mov_b64 s[4:5], 0x5ed68600
	v_lshl_add_u64 v[134:135], v[132:133], 0, s[4:5]
	s_mov_b32 s4, 0x5ed68000
	v_cvt_pk_bf16_f32 v127, v128, v129
	v_cvt_pk_bf16_f32 v128, v122, v123
	v_add_co_u32_e32 v122, vcc, s4, v132
	v_cvt_pk_bf16_f32 v110, v110, v111
	s_nop 0
	v_addc_co_u32_e32 v123, vcc, 0, v133, vcc
	v_cvt_pk_bf16_f32 v111, v112, v113
	v_cvt_pk_bf16_f32 v112, v106, v107
	v_cvt_pk_bf16_f32 v113, v108, v109
	s_mov_b32 s4, 0x5ed70000
	global_store_dwordx4 v[134:135], v[110:113], off offset:16
	v_cvt_pk_bf16_f32 v94, v94, v95
	v_cvt_pk_bf16_f32 v95, v96, v97
	v_add_co_u32_e32 v110, vcc, s4, v132
	v_cvt_pk_bf16_f32 v96, v90, v91
	s_nop 0
	v_addc_co_u32_e32 v111, vcc, 0, v133, vcc
	v_cvt_pk_bf16_f32 v97, v92, v93
	s_mov_b32 s4, 0x5ed78000
	global_store_dwordx4 v[110:111], v[94:97], off offset:1552
	v_cvt_pk_bf16_f32 v78, v78, v79
	v_cvt_pk_bf16_f32 v79, v80, v81
	v_add_co_u32_e32 v94, vcc, s4, v132
	v_cvt_pk_bf16_f32 v80, v74, v75
	s_nop 0
	v_addc_co_u32_e32 v95, vcc, 0, v133, vcc
	v_cvt_pk_bf16_f32 v81, v76, v77
	s_mov_b32 s4, 0x5ed80000
	global_store_dwordx4 v[94:95], v[78:81], off offset:1552
	v_cvt_pk_bf16_f32 v54, v54, v55
	v_cvt_pk_bf16_f32 v55, v56, v57
	v_add_co_u32_e32 v78, vcc, s4, v132
	s_mov_b32 s4, 0x5eda8000
	s_nop 0
	v_addc_co_u32_e32 v79, vcc, 0, v133, vcc
	v_cvt_pk_bf16_f32 v56, v50, v51
	v_add_co_u32_e32 v50, vcc, s4, v132
	v_cvt_pk_bf16_f32 v30, v30, v31
	s_nop 0
	v_addc_co_u32_e32 v51, vcc, 0, v133, vcc
	v_cvt_pk_bf16_f32 v31, v32, v33
	v_cvt_pk_bf16_f32 v32, v26, v27
	v_cvt_pk_bf16_f32 v33, v28, v29
	s_mov_b32 s4, 0x5edb0000
	global_store_dwordx4 v[50:51], v[30:33], off offset:1552
	v_cvt_pk_bf16_f32 v14, v14, v15
	v_cvt_pk_bf16_f32 v15, v16, v17
	v_add_co_u32_e32 v30, vcc, s4, v132
	v_cvt_pk_bf16_f32 v16, v10, v11
	s_nop 0
	v_addc_co_u32_e32 v31, vcc, 0, v133, vcc
	v_cvt_pk_bf16_f32 v17, v12, v13
	s_mov_b32 s4, 0x5edb8000
	global_store_dwordx4 v[30:31], v[14:17], off offset:1552
	v_cvt_pk_bf16_f32 v10, v22, v23
	v_cvt_pk_bf16_f32 v11, v24, v25
	v_add_co_u32_e32 v14, vcc, s4, v132
	v_cvt_pk_bf16_f32 v12, v18, v19
	v_cvt_pk_bf16_f32 v13, v20, v21
	v_addc_co_u32_e32 v15, vcc, 0, v133, vcc
	global_store_dwordx4 v[14:15], v[10:13], off offset:1536
	s_mov_b32 s4, 0x5edc0000
	v_cvt_pk_bf16_f32 v129, v124, v125
	v_cvt_pk_bf16_f32 v10, v58, v59
	v_cvt_pk_bf16_f32 v11, v60, v61
	v_cvt_pk_bf16_f32 v12, v62, v63
	v_cvt_pk_bf16_f32 v13, v64, v65
	global_store_dwordx4 v[14:15], v[10:13], off offset:1552
	v_cvt_pk_bf16_f32 v106, v118, v119
	v_cvt_pk_bf16_f32 v107, v120, v121
	v_add_co_u32_e32 v10, vcc, s4, v132
	v_cvt_pk_bf16_f32 v108, v114, v115
	v_cvt_pk_bf16_f32 v109, v116, v117
	v_cvt_pk_bf16_f32 v90, v102, v103
	v_cvt_pk_bf16_f32 v91, v104, v105
	v_cvt_pk_bf16_f32 v92, v98, v99
	v_cvt_pk_bf16_f32 v93, v100, v101
	v_cvt_pk_bf16_f32 v74, v86, v87
	v_cvt_pk_bf16_f32 v75, v88, v89
	v_cvt_pk_bf16_f32 v76, v82, v83
	v_cvt_pk_bf16_f32 v77, v84, v85
	v_cvt_pk_bf16_f32 v70, v70, v71
	v_cvt_pk_bf16_f32 v71, v72, v73
	v_cvt_pk_bf16_f32 v72, v66, v67
	v_cvt_pk_bf16_f32 v73, v68, v69
	v_cvt_pk_bf16_f32 v57, v52, v53
	v_cvt_pk_bf16_f32 v26, v38, v39
	v_cvt_pk_bf16_f32 v27, v40, v41
	v_cvt_pk_bf16_f32 v28, v34, v35
	v_cvt_pk_bf16_f32 v29, v36, v37
	v_cvt_pk_bf16_f32 v6, v6, v7
	v_cvt_pk_bf16_f32 v7, v8, v9
	v_cvt_pk_bf16_f32 v8, v2, v3
	v_cvt_pk_bf16_f32 v9, v4, v5
	v_addc_co_u32_e32 v11, vcc, 0, v133, vcc
	v_cvt_pk_bf16_f32 v2, v42, v43
	v_cvt_pk_bf16_f32 v3, v44, v45
	v_cvt_pk_bf16_f32 v4, v46, v47
	v_cvt_pk_bf16_f32 v5, v48, v49
	global_store_dwordx4 v[122:123], v[126:129], off offset:1536
	global_store_dwordx4 v[110:111], v[106:109], off offset:1536
	global_store_dwordx4 v[94:95], v[90:93], off offset:1536
	global_store_dwordx4 v[78:79], v[74:77], off offset:1536
	global_store_dwordx4 v[78:79], v[70:73], off offset:1552
	global_store_dwordx4 v[50:51], v[54:57], off offset:1536
	global_store_dwordx4 v[30:31], v[26:29], off offset:1536
	global_store_dwordx4 v[10:11], v[6:9], off offset:1536
	global_store_dwordx4 v[10:11], v[2:5], off offset:1552
	s_waitcnt vmcnt(0)
	s_cmpk_lt_u32 s1, 0x100
	s_cbranch_scc0 .LBB0_638
	s_barrier

.LBB0_684:
	s_add_u32 s12, s10, 0xc8f58080
	s_addc_u32 s13, s11, -1
	s_cmp_lg_u32 s84, 28
	s_cselect_b32 s12, s12, 0
	s_cselect_b32 s13, s13, 0
	s_add_u32 s14, s4, s12
	s_addc_u32 s15, s5, s13
	s_add_u32 s12, s6, s12
	s_addc_u32 s13, s7, s13
	s_add_i32 s27, 0, 0x10000
	v_add_u32_e32 v158, s27, v144
	ds_read_b128 v[146:149], v158
	ds_read_b128 v[150:153], v158 offset:1024
	ds_read_b128 v[154:157], v158 offset:2048
	ds_read_b128 v[158:161], v158 offset:3072
	v_lshl_add_u64 v[174:175], v[138:139], 0, s[10:11]
	s_add_i32 m0, s18, 0xc000
	ds_read_b128 v[162:165], v145
	ds_read_b128 v[166:169], v145 offset:1024
	ds_read_b128 v[170:173], v145 offset:2048
	ds_read_b128 v[178:181], v145 offset:3072
	ds_read_b128 v[182:185], v145 offset:4096
	ds_read_b128 v[188:191], v145 offset:5120
	ds_read_b128 v[192:195], v145 offset:6144
	ds_read_b128 v[196:199], v145 offset:7168
	global_load_lds_dwordx4 v[174:175], off
	v_lshl_add_u64 v[174:175], v[140:141], 0, s[10:11]
	s_add_i32 m0, s18, 0xe000
	s_nop 0
	global_load_lds_dwordx4 v[174:175], off
	s_waitcnt lgkmcnt(8)
	s_waitcnt vmcnt(10)
	s_barrier
	s_setprio 1
	s_waitcnt lgkmcnt(7)
	v_mfma_f32_16x16x32_bf16 v[126:129], v[146:149], v[162:165], v[126:129]
	s_waitcnt lgkmcnt(5)
	v_mfma_f32_16x16x32_bf16 v[122:125], v[154:157], v[162:165], v[122:125]
	v_mfma_f32_16x16x32_bf16 v[118:121], v[146:149], v[170:173], v[118:121]
	s_waitcnt lgkmcnt(3)
	v_mfma_f32_16x16x32_bf16 v[114:117], v[154:157], v[170:173], v[114:117]
	v_mfma_f32_16x16x32_bf16 v[102:105], v[146:149], v[182:185], v[102:105]
	s_waitcnt lgkmcnt(1)
	v_mfma_f32_16x16x32_bf16 v[98:101], v[154:157], v[182:185], v[98:101]
	v_mfma_f32_16x16x32_bf16 v[86:89], v[146:149], v[192:195], v[86:89]
	v_mfma_f32_16x16x32_bf16 v[82:85], v[154:157], v[192:195], v[82:85]
	v_mfma_f32_16x16x32_bf16 v[126:129], v[150:153], v[166:169], v[126:129]
	v_mfma_f32_16x16x32_bf16 v[122:125], v[158:161], v[166:169], v[122:125]
	v_mfma_f32_16x16x32_bf16 v[118:121], v[150:153], v[178:181], v[118:121]
	v_mfma_f32_16x16x32_bf16 v[114:117], v[158:161], v[178:181], v[114:117]
	v_mfma_f32_16x16x32_bf16 v[102:105], v[150:153], v[188:191], v[102:105]
	s_waitcnt lgkmcnt(0)
	v_mfma_f32_16x16x32_bf16 v[98:101], v[158:161], v[188:191], v[98:101]
	v_mfma_f32_16x16x32_bf16 v[86:89], v[150:153], v[196:199], v[86:89]
	v_mfma_f32_16x16x32_bf16 v[82:85], v[158:161], v[196:199], v[82:85]
	s_setprio 0
	s_barrier
	s_add_i32 s43, 0, 0x14000
	v_add_u32_e32 v174, s43, v144
	s_add_i32 s27, s27, s17
	ds_read_b128 v[218:221], v174
	ds_read_b128 v[222:225], v174 offset:1024
	ds_read_b128 v[226:229], v174 offset:2048
	ds_read_b128 v[230:233], v174 offset:3072
	v_lshl_add_u64 v[174:175], s[12:13], 0, v[130:131]
	s_mov_b32 m0, s27
	v_lshl_add_u64 v[200:201], s[12:13], 0, v[134:135]
	global_load_lds_dwordx4 v[174:175], off
	s_add_i32 m0, s27, 0x2000
	s_nop 0
	global_load_lds_dwordx4 v[200:201], off
	s_waitcnt vmcnt(10)
	s_barrier
	s_setprio 1
	s_waitcnt lgkmcnt(3)
	s_waitcnt lgkmcnt(1)
	v_mfma_f32_16x16x32_bf16 v[110:113], v[218:221], v[162:165], v[110:113]
	v_mfma_f32_16x16x32_bf16 v[106:109], v[226:229], v[162:165], v[106:109]
	v_mfma_f32_16x16x32_bf16 v[94:97], v[218:221], v[170:173], v[94:97]
	v_mfma_f32_16x16x32_bf16 v[90:93], v[226:229], v[170:173], v[90:93]
	v_mfma_f32_16x16x32_bf16 v[78:81], v[218:221], v[182:185], v[78:81]
	v_mfma_f32_16x16x32_bf16 v[74:77], v[226:229], v[182:185], v[74:77]
	v_mfma_f32_16x16x32_bf16 v[70:73], v[218:221], v[192:195], v[70:73]
	v_mfma_f32_16x16x32_bf16 v[66:69], v[226:229], v[192:195], v[66:69]
	s_waitcnt lgkmcnt(0)
	v_mfma_f32_16x16x32_bf16 v[110:113], v[222:225], v[166:169], v[110:113]
	v_mfma_f32_16x16x32_bf16 v[106:109], v[230:233], v[166:169], v[106:109]
	v_mfma_f32_16x16x32_bf16 v[94:97], v[222:225], v[178:181], v[94:97]
	v_mfma_f32_16x16x32_bf16 v[90:93], v[230:233], v[178:181], v[90:93]
	v_mfma_f32_16x16x32_bf16 v[78:81], v[222:225], v[188:191], v[78:81]
	v_mfma_f32_16x16x32_bf16 v[74:77], v[230:233], v[188:191], v[74:77]
	v_mfma_f32_16x16x32_bf16 v[70:73], v[222:225], v[196:199], v[70:73]
	v_mfma_f32_16x16x32_bf16 v[66:69], v[230:233], v[196:199], v[66:69]
	s_setprio 0
	s_mov_b32 m0, s18
	v_lshl_add_u64 v[234:235], s[14:15], 0, v[132:133]
	s_barrier
	ds_read_b128 v[162:165], v145 offset:16384
	ds_read_b128 v[166:169], v145 offset:17408
	ds_read_b128 v[170:173], v145 offset:18432
	ds_read_b128 v[178:181], v145 offset:19456
	ds_read_b128 v[182:185], v145 offset:20480
	ds_read_b128 v[188:191], v145 offset:21504
	ds_read_b128 v[192:195], v145 offset:22528
	ds_read_b128 v[196:199], v145 offset:23552
	global_load_lds_dwordx4 v[234:235], off
	v_lshl_add_u64 v[236:237], s[14:15], 0, v[136:137]
	s_mov_b32 m0, s19
	s_nop 0
	global_load_lds_dwordx4 v[236:237], off
	s_barrier
	s_setprio 1
	s_waitcnt lgkmcnt(7)
	v_mfma_f32_16x16x32_bf16 v[54:57], v[146:149], v[162:165], v[54:57]
	s_waitcnt lgkmcnt(5)
	v_mfma_f32_16x16x32_bf16 v[50:53], v[154:157], v[162:165], v[50:53]
	v_mfma_f32_16x16x32_bf16 v[38:41], v[146:149], v[170:173], v[38:41]
	s_waitcnt lgkmcnt(3)
	v_mfma_f32_16x16x32_bf16 v[34:37], v[154:157], v[170:173], v[34:37]
	v_mfma_f32_16x16x32_bf16 v[22:25], v[146:149], v[182:185], v[22:25]
	s_waitcnt lgkmcnt(1)
	v_mfma_f32_16x16x32_bf16 v[18:21], v[154:157], v[182:185], v[18:21]
	v_mfma_f32_16x16x32_bf16 v[6:9], v[146:149], v[192:195], v[6:9]
	v_mfma_f32_16x16x32_bf16 v[2:5], v[154:157], v[192:195], v[2:5]
	v_mfma_f32_16x16x32_bf16 v[54:57], v[150:153], v[166:169], v[54:57]
	v_mfma_f32_16x16x32_bf16 v[50:53], v[158:161], v[166:169], v[50:53]
	v_mfma_f32_16x16x32_bf16 v[38:41], v[150:153], v[178:181], v[38:41]
	v_mfma_f32_16x16x32_bf16 v[34:37], v[158:161], v[178:181], v[34:37]
	v_mfma_f32_16x16x32_bf16 v[22:25], v[150:153], v[188:191], v[22:25]
	s_waitcnt lgkmcnt(0)
	v_mfma_f32_16x16x32_bf16 v[18:21], v[158:161], v[188:191], v[18:21]
	v_mfma_f32_16x16x32_bf16 v[6:9], v[150:153], v[196:199], v[6:9]
	v_mfma_f32_16x16x32_bf16 v[2:5], v[158:161], v[196:199], v[2:5]
	s_setprio 0
	s_barrier
	s_add_u32 s60, s12, 0x8000
	s_addc_u32 s61, s13, 0
	s_add_i32 s27, s43, s17
	v_lshl_add_u64 v[146:147], s[60:61], 0, v[130:131]
	s_mov_b32 m0, s27
	s_nop 0
	global_load_lds_dwordx4 v[146:147], off
	v_lshl_add_u64 v[146:147], s[60:61], 0, v[134:135]
	s_add_i32 m0, s27, 0x2000
	s_nop 0
	global_load_lds_dwordx4 v[146:147], off
	s_waitcnt vmcnt(10)
	s_barrier
	s_setprio 1
	v_mfma_f32_16x16x32_bf16 v[30:33], v[218:221], v[162:165], v[30:33]
	v_mfma_f32_16x16x32_bf16 v[26:29], v[226:229], v[162:165], v[26:29]
	v_mfma_f32_16x16x32_bf16 v[14:17], v[218:221], v[170:173], v[14:17]
	v_mfma_f32_16x16x32_bf16 v[10:13], v[226:229], v[170:173], v[10:13]
	v_mfma_f32_16x16x32_bf16 v[58:61], v[218:221], v[182:185], v[58:61]
	v_mfma_f32_16x16x32_bf16 v[62:65], v[226:229], v[182:185], v[62:65]
	v_mfma_f32_16x16x32_bf16 v[42:45], v[218:221], v[192:195], v[42:45]
	v_mfma_f32_16x16x32_bf16 v[46:49], v[226:229], v[192:195], v[46:49]
	v_mfma_f32_16x16x32_bf16 v[30:33], v[222:225], v[166:169], v[30:33]
	v_mfma_f32_16x16x32_bf16 v[26:29], v[230:233], v[166:169], v[26:29]
	v_mfma_f32_16x16x32_bf16 v[14:17], v[222:225], v[178:181], v[14:17]
	v_mfma_f32_16x16x32_bf16 v[10:13], v[230:233], v[178:181], v[10:13]
	v_mfma_f32_16x16x32_bf16 v[58:61], v[222:225], v[188:191], v[58:61]
	v_mfma_f32_16x16x32_bf16 v[62:65], v[230:233], v[188:191], v[62:65]
	v_mfma_f32_16x16x32_bf16 v[42:45], v[222:225], v[196:199], v[42:45]
	v_mfma_f32_16x16x32_bf16 v[46:49], v[230:233], v[196:199], v[46:49]
	s_setprio 0
	s_add_i32 s27, 0, 0x18000
	v_add_u32_e32 v158, s27, v144
	s_barrier
	ds_read_b128 v[146:149], v158
	ds_read_b128 v[150:153], v158 offset:1024
	ds_read_b128 v[154:157], v158 offset:2048
	ds_read_b128 v[158:161], v158 offset:3072
	s_add_u32 s14, s14, 0x80000
	s_addc_u32 s15, s15, 0
	s_mov_b32 m0, s33
	v_lshl_add_u64 v[218:219], s[14:15], 0, v[132:133]
	ds_read_b128 v[162:165], v145 offset:32768
	ds_read_b128 v[166:169], v145 offset:33792
	ds_read_b128 v[170:173], v145 offset:34816
	ds_read_b128 v[178:181], v145 offset:35840
	ds_read_b128 v[182:185], v145 offset:36864
	ds_read_b128 v[188:191], v145 offset:37888
	ds_read_b128 v[192:195], v145 offset:38912
	ds_read_b128 v[196:199], v145 offset:39936
	global_load_lds_dwordx4 v[218:219], off
	v_lshl_add_u64 v[218:219], s[14:15], 0, v[136:137]
	s_mov_b32 m0, s38
	s_nop 0
	global_load_lds_dwordx4 v[218:219], off
	s_waitcnt lgkmcnt(8)
	s_waitcnt vmcnt(10)
	s_barrier
	s_setprio 1
	s_waitcnt lgkmcnt(7)
	v_mfma_f32_16x16x32_bf16 v[126:129], v[146:149], v[162:165], v[126:129]
	s_waitcnt lgkmcnt(5)
	v_mfma_f32_16x16x32_bf16 v[122:125], v[154:157], v[162:165], v[122:125]
	v_mfma_f32_16x16x32_bf16 v[118:121], v[146:149], v[170:173], v[118:121]
	s_waitcnt lgkmcnt(3)
	v_mfma_f32_16x16x32_bf16 v[114:117], v[154:157], v[170:173], v[114:117]
	v_mfma_f32_16x16x32_bf16 v[102:105], v[146:149], v[182:185], v[102:105]
	s_waitcnt lgkmcnt(1)
	v_mfma_f32_16x16x32_bf16 v[98:101], v[154:157], v[182:185], v[98:101]
	v_mfma_f32_16x16x32_bf16 v[86:89], v[146:149], v[192:195], v[86:89]
	v_mfma_f32_16x16x32_bf16 v[82:85], v[154:157], v[192:195], v[82:85]
	v_mfma_f32_16x16x32_bf16 v[126:129], v[150:153], v[166:169], v[126:129]
	v_mfma_f32_16x16x32_bf16 v[122:125], v[158:161], v[166:169], v[122:125]
	v_mfma_f32_16x16x32_bf16 v[118:121], v[150:153], v[178:181], v[118:121]
	v_mfma_f32_16x16x32_bf16 v[114:117], v[158:161], v[178:181], v[114:117]
	v_mfma_f32_16x16x32_bf16 v[102:105], v[150:153], v[188:191], v[102:105]
	s_waitcnt lgkmcnt(0)
	v_mfma_f32_16x16x32_bf16 v[98:101], v[158:161], v[188:191], v[98:101]
	v_mfma_f32_16x16x32_bf16 v[86:89], v[150:153], v[196:199], v[86:89]
	v_mfma_f32_16x16x32_bf16 v[82:85], v[158:161], v[196:199], v[82:85]
	s_setprio 0
	s_barrier
	s_add_i32 s14, 0, 0x1c000
	s_add_i32 s15, s27, s17
	v_add_u32_e32 v187, s14, v144
	v_lshl_add_u64 v[174:175], v[174:175], 0, s[30:31]
	s_mov_b32 m0, s15
	ds_read_b128 v[218:221], v187
	ds_read_b128 v[222:225], v187 offset:1024
	ds_read_b128 v[226:229], v187 offset:2048
	ds_read_b128 v[230:233], v187 offset:3072
	global_load_lds_dwordx4 v[174:175], off
	v_lshl_add_u64 v[174:175], v[200:201], 0, s[30:31]
	s_add_i32 m0, s15, 0x2000
	s_nop 0
	global_load_lds_dwordx4 v[174:175], off
	s_waitcnt vmcnt(10)
	s_barrier
	s_setprio 1
	s_waitcnt lgkmcnt(3)
	s_waitcnt lgkmcnt(1)
	v_mfma_f32_16x16x32_bf16 v[110:113], v[218:221], v[162:165], v[110:113]
	v_mfma_f32_16x16x32_bf16 v[106:109], v[226:229], v[162:165], v[106:109]
	v_mfma_f32_16x16x32_bf16 v[94:97], v[218:221], v[170:173], v[94:97]
	v_mfma_f32_16x16x32_bf16 v[90:93], v[226:229], v[170:173], v[90:93]
	v_mfma_f32_16x16x32_bf16 v[78:81], v[218:221], v[182:185], v[78:81]
	v_mfma_f32_16x16x32_bf16 v[74:77], v[226:229], v[182:185], v[74:77]
	v_mfma_f32_16x16x32_bf16 v[70:73], v[218:221], v[192:195], v[70:73]
	v_mfma_f32_16x16x32_bf16 v[66:69], v[226:229], v[192:195], v[66:69]
	s_waitcnt lgkmcnt(0)
	v_mfma_f32_16x16x32_bf16 v[110:113], v[222:225], v[166:169], v[110:113]
	v_mfma_f32_16x16x32_bf16 v[106:109], v[230:233], v[166:169], v[106:109]
	v_mfma_f32_16x16x32_bf16 v[94:97], v[222:225], v[178:181], v[94:97]
	v_mfma_f32_16x16x32_bf16 v[90:93], v[230:233], v[178:181], v[90:93]
	v_mfma_f32_16x16x32_bf16 v[78:81], v[222:225], v[188:191], v[78:81]
	v_mfma_f32_16x16x32_bf16 v[74:77], v[230:233], v[188:191], v[74:77]
	v_mfma_f32_16x16x32_bf16 v[70:73], v[222:225], v[196:199], v[70:73]
	v_mfma_f32_16x16x32_bf16 v[66:69], v[230:233], v[196:199], v[66:69]
	s_setprio 0
	s_mov_b32 m0, s42
	v_lshl_add_u64 v[174:175], v[234:235], 0, s[30:31]
	s_barrier
	ds_read_b128 v[162:165], v145 offset:49152
	ds_read_b128 v[166:169], v145 offset:50176
	ds_read_b128 v[170:173], v145 offset:51200
	ds_read_b128 v[178:181], v145 offset:52224
	ds_read_b128 v[182:185], v145 offset:53248
	ds_read_b128 v[188:191], v145 offset:54272
	ds_read_b128 v[192:195], v145 offset:55296
	ds_read_b128 v[196:199], v145 offset:56320
	global_load_lds_dwordx4 v[174:175], off
	v_lshl_add_u64 v[174:175], v[236:237], 0, s[30:31]
	s_mov_b32 m0, s64
	s_nop 0
	global_load_lds_dwordx4 v[174:175], off
	s_barrier
	s_setprio 1
	s_waitcnt lgkmcnt(7)
	v_mfma_f32_16x16x32_bf16 v[54:57], v[146:149], v[162:165], v[54:57]
	s_waitcnt lgkmcnt(5)
	v_mfma_f32_16x16x32_bf16 v[50:53], v[154:157], v[162:165], v[50:53]
	v_mfma_f32_16x16x32_bf16 v[38:41], v[146:149], v[170:173], v[38:41]
	s_waitcnt lgkmcnt(3)
	v_mfma_f32_16x16x32_bf16 v[34:37], v[154:157], v[170:173], v[34:37]
	v_mfma_f32_16x16x32_bf16 v[22:25], v[146:149], v[182:185], v[22:25]
	s_waitcnt lgkmcnt(1)
	v_mfma_f32_16x16x32_bf16 v[18:21], v[154:157], v[182:185], v[18:21]
	v_mfma_f32_16x16x32_bf16 v[6:9], v[146:149], v[192:195], v[6:9]
	v_mfma_f32_16x16x32_bf16 v[2:5], v[154:157], v[192:195], v[2:5]
	v_mfma_f32_16x16x32_bf16 v[54:57], v[150:153], v[166:169], v[54:57]
	v_mfma_f32_16x16x32_bf16 v[50:53], v[158:161], v[166:169], v[50:53]
	v_mfma_f32_16x16x32_bf16 v[38:41], v[150:153], v[178:181], v[38:41]
	v_mfma_f32_16x16x32_bf16 v[34:37], v[158:161], v[178:181], v[34:37]
	v_mfma_f32_16x16x32_bf16 v[22:25], v[150:153], v[188:191], v[22:25]
	s_waitcnt lgkmcnt(0)
	v_mfma_f32_16x16x32_bf16 v[18:21], v[158:161], v[188:191], v[18:21]
	v_mfma_f32_16x16x32_bf16 v[6:9], v[150:153], v[196:199], v[6:9]
	v_mfma_f32_16x16x32_bf16 v[2:5], v[158:161], v[196:199], v[2:5]
	s_setprio 0
	s_barrier
	s_add_u32 s12, s12, 0x8080
	s_addc_u32 s13, s13, 0
	s_add_i32 s14, s14, s17
	v_lshl_add_u64 v[146:147], s[12:13], 0, v[130:131]
	s_mov_b32 m0, s14
	s_nop 0
	global_load_lds_dwordx4 v[146:147], off
	v_lshl_add_u64 v[146:147], s[12:13], 0, v[134:135]
	s_add_i32 m0, s14, 0x2000
	s_nop 0
	global_load_lds_dwordx4 v[146:147], off
	s_waitcnt vmcnt(10)
	s_barrier
	s_setprio 1
	v_mfma_f32_16x16x32_bf16 v[30:33], v[218:221], v[162:165], v[30:33]
	v_mfma_f32_16x16x32_bf16 v[26:29], v[226:229], v[162:165], v[26:29]
	v_mfma_f32_16x16x32_bf16 v[14:17], v[218:221], v[170:173], v[14:17]
	v_mfma_f32_16x16x32_bf16 v[10:13], v[226:229], v[170:173], v[10:13]
	v_mfma_f32_16x16x32_bf16 v[58:61], v[218:221], v[182:185], v[58:61]
	v_mfma_f32_16x16x32_bf16 v[62:65], v[226:229], v[182:185], v[62:65]
	v_mfma_f32_16x16x32_bf16 v[42:45], v[218:221], v[192:195], v[42:45]
	v_mfma_f32_16x16x32_bf16 v[46:49], v[226:229], v[192:195], v[46:49]
	v_mfma_f32_16x16x32_bf16 v[30:33], v[222:225], v[166:169], v[30:33]
	v_mfma_f32_16x16x32_bf16 v[26:29], v[230:233], v[166:169], v[26:29]
	v_mfma_f32_16x16x32_bf16 v[14:17], v[222:225], v[178:181], v[14:17]
	v_mfma_f32_16x16x32_bf16 v[10:13], v[230:233], v[178:181], v[10:13]
	v_mfma_f32_16x16x32_bf16 v[58:61], v[222:225], v[188:191], v[58:61]
	v_mfma_f32_16x16x32_bf16 v[62:65], v[230:233], v[188:191], v[62:65]
	v_mfma_f32_16x16x32_bf16 v[42:45], v[222:225], v[196:199], v[42:45]
	v_mfma_f32_16x16x32_bf16 v[46:49], v[230:233], v[196:199], v[46:49]
	s_setprio 0
	s_add_i32 s84, s84, 2
	s_add_u32 s10, s10, 0x100
	s_addc_u32 s11, s11, 0
	s_cmp_gt_u32 s84, 29
	s_barrier
	s_cbranch_scc0 .LBB0_684
	s_mul_i32 s4, s22, 0x900
	s_lshl_b32 s5, s16, 8
	s_add_i32 s22, s4, s5
	s_lshl_b32 s6, s39, 6
	s_lshl_b64 s[4:5], s[22:23], 11
	s_add_u32 s4, s68, s4
	v_lshlrev_b32_e32 v130, 10, v143
	s_addc_u32 s5, s69, s5
	v_or3_b32 v130, v130, s6, v142
	v_cvt_pk_bf16_f32 v126, v126, v127
	v_lshl_add_u64 v[132:133], v[130:131], 1, s[4:5]
	s_mov_b64 s[4:5], 0x5ed68600
	v_lshl_add_u64 v[134:135], v[132:133], 0, s[4:5]
	s_mov_b32 s4, 0x5ed68000
	v_cvt_pk_bf16_f32 v127, v128, v129
	v_cvt_pk_bf16_f32 v128, v122, v123
	v_add_co_u32_e32 v122, vcc, s4, v132
	v_cvt_pk_bf16_f32 v110, v110, v111
	s_nop 0
	v_addc_co_u32_e32 v123, vcc, 0, v133, vcc
	v_cvt_pk_bf16_f32 v111, v112, v113
	v_cvt_pk_bf16_f32 v112, v106, v107
	v_cvt_pk_bf16_f32 v113, v108, v109
	s_mov_b32 s4, 0x5ed70000
	global_store_dwordx4 v[134:135], v[110:113], off offset:16
	v_cvt_pk_bf16_f32 v94, v94, v95
	v_cvt_pk_bf16_f32 v95, v96, v97
	v_add_co_u32_e32 v110, vcc, s4, v132
	v_cvt_pk_bf16_f32 v96, v90, v91
	s_nop 0
	v_addc_co_u32_e32 v111, vcc, 0, v133, vcc
	v_cvt_pk_bf16_f32 v97, v92, v93
	s_mov_b32 s4, 0x5ed78000
	global_store_dwordx4 v[110:111], v[94:97], off offset:1552
	v_cvt_pk_bf16_f32 v78, v78, v79
	v_cvt_pk_bf16_f32 v79, v80, v81
	v_add_co_u32_e32 v94, vcc, s4, v132
	v_cvt_pk_bf16_f32 v80, v74, v75
	s_nop 0
	v_addc_co_u32_e32 v95, vcc, 0, v133, vcc
	v_cvt_pk_bf16_f32 v81, v76, v77
	s_mov_b32 s4, 0x5ed80000
	global_store_dwordx4 v[94:95], v[78:81], off offset:1552
	v_cvt_pk_bf16_f32 v54, v54, v55
	v_cvt_pk_bf16_f32 v55, v56, v57
	v_add_co_u32_e32 v78, vcc, s4, v132
	s_mov_b32 s4, 0x5eda8000
	s_nop 0
	v_addc_co_u32_e32 v79, vcc, 0, v133, vcc
	v_cvt_pk_bf16_f32 v56, v50, v51
	v_add_co_u32_e32 v50, vcc, s4, v132
	v_cvt_pk_bf16_f32 v30, v30, v31
	s_nop 0
	v_addc_co_u32_e32 v51, vcc, 0, v133, vcc
	v_cvt_pk_bf16_f32 v31, v32, v33
	v_cvt_pk_bf16_f32 v32, v26, v27
	v_cvt_pk_bf16_f32 v33, v28, v29
	s_mov_b32 s4, 0x5edb0000
	global_store_dwordx4 v[50:51], v[30:33], off offset:1552
	v_cvt_pk_bf16_f32 v14, v14, v15
	v_cvt_pk_bf16_f32 v15, v16, v17
	v_add_co_u32_e32 v30, vcc, s4, v132
	v_cvt_pk_bf16_f32 v16, v10, v11
	s_nop 0
	v_addc_co_u32_e32 v31, vcc, 0, v133, vcc
	v_cvt_pk_bf16_f32 v17, v12, v13
	s_mov_b32 s4, 0x5edb8000
	global_store_dwordx4 v[30:31], v[14:17], off offset:1552
	v_cvt_pk_bf16_f32 v10, v22, v23
	v_cvt_pk_bf16_f32 v11, v24, v25
	v_add_co_u32_e32 v14, vcc, s4, v132
	v_cvt_pk_bf16_f32 v12, v18, v19
	v_cvt_pk_bf16_f32 v13, v20, v21
	v_addc_co_u32_e32 v15, vcc, 0, v133, vcc
	global_store_dwordx4 v[14:15], v[10:13], off offset:1536
	s_mov_b32 s4, 0x5edc0000
	v_cvt_pk_bf16_f32 v129, v124, v125
	v_cvt_pk_bf16_f32 v10, v58, v59
	v_cvt_pk_bf16_f32 v11, v60, v61
	v_cvt_pk_bf16_f32 v12, v62, v63
	v_cvt_pk_bf16_f32 v13, v64, v65
	global_store_dwordx4 v[14:15], v[10:13], off offset:1552
	v_cvt_pk_bf16_f32 v106, v118, v119
	v_cvt_pk_bf16_f32 v107, v120, v121
	v_add_co_u32_e32 v10, vcc, s4, v132
	v_cvt_pk_bf16_f32 v108, v114, v115
	v_cvt_pk_bf16_f32 v109, v116, v117
	v_cvt_pk_bf16_f32 v90, v102, v103
	v_cvt_pk_bf16_f32 v91, v104, v105
	v_cvt_pk_bf16_f32 v92, v98, v99
	v_cvt_pk_bf16_f32 v93, v100, v101
	v_cvt_pk_bf16_f32 v74, v86, v87
	v_cvt_pk_bf16_f32 v75, v88, v89
	v_cvt_pk_bf16_f32 v76, v82, v83
	v_cvt_pk_bf16_f32 v77, v84, v85
	v_cvt_pk_bf16_f32 v70, v70, v71
	v_cvt_pk_bf16_f32 v71, v72, v73
	v_cvt_pk_bf16_f32 v72, v66, v67
	v_cvt_pk_bf16_f32 v73, v68, v69
	v_cvt_pk_bf16_f32 v57, v52, v53
	v_cvt_pk_bf16_f32 v26, v38, v39
	v_cvt_pk_bf16_f32 v27, v40, v41
	v_cvt_pk_bf16_f32 v28, v34, v35
	v_cvt_pk_bf16_f32 v29, v36, v37
	v_cvt_pk_bf16_f32 v6, v6, v7
	v_cvt_pk_bf16_f32 v7, v8, v9
	v_cvt_pk_bf16_f32 v8, v2, v3
	v_cvt_pk_bf16_f32 v9, v4, v5
	v_addc_co_u32_e32 v11, vcc, 0, v133, vcc
	v_cvt_pk_bf16_f32 v2, v42, v43
	v_cvt_pk_bf16_f32 v3, v44, v45
	v_cvt_pk_bf16_f32 v4, v46, v47
	v_cvt_pk_bf16_f32 v5, v48, v49
	global_store_dwordx4 v[122:123], v[126:129], off offset:1536
	global_store_dwordx4 v[110:111], v[106:109], off offset:1536
	global_store_dwordx4 v[94:95], v[90:93], off offset:1536
	global_store_dwordx4 v[78:79], v[74:77], off offset:1536
	global_store_dwordx4 v[78:79], v[70:73], off offset:1552
	global_store_dwordx4 v[50:51], v[54:57], off offset:1536
	global_store_dwordx4 v[30:31], v[26:29], off offset:1536
	global_store_dwordx4 v[10:11], v[6:9], off offset:1536
	global_store_dwordx4 v[10:11], v[2:5], off offset:1552
	s_waitcnt vmcnt(0)
	s_cmpk_lt_u32 s1, 0x100
	s_cbranch_scc0 .LBB0_687
	s_barrier

.LBB0_869:
	s_add_u32 s58, s14, s64
	s_addc_u32 s59, s15, s65
	s_add_u32 s58, s58, 0x100
	s_addc_u32 s59, s59, 0
	s_add_u32 s60, s9, s64
	s_addc_u32 s61, s53, s65
	s_cmpk_eq_i32 s64, 0x700
	s_cselect_b32 s69, s11, s59
	s_cselect_b32 s68, s10, s58
	s_cselect_b32 s67, s13, s61
	s_cselect_b32 s66, s12, s60
	s_add_i32 s58, 0, 0x10000
	v_add_u32_e32 v130, s58, v182
	ds_read_b128 v[132:135], v130
	ds_read_b128 v[136:139], v130 offset:1024
	ds_read_b128 v[140:143], v130 offset:2048
	ds_read_b128 v[144:147], v130 offset:3072
	v_lshl_add_u64 v[218:219], v[178:179], 0, s[64:65]
	s_add_i32 m0, s36, 0xc000
	ds_read_b128 v[148:151], v185
	ds_read_b128 v[152:155], v185 offset:1024
	ds_read_b128 v[156:159], v185 offset:2048
	ds_read_b128 v[160:163], v185 offset:3072
	ds_read_b128 v[186:189], v185 offset:4096
	ds_read_b128 v[190:193], v185 offset:5120
	ds_read_b128 v[194:197], v185 offset:6144
	ds_read_b128 v[198:201], v185 offset:7168
	global_load_lds_dwordx4 v[218:219], off
	v_lshl_add_u64 v[218:219], v[180:181], 0, s[64:65]
	s_add_i32 m0, s36, 0xe000
	s_nop 0
	global_load_lds_dwordx4 v[218:219], off
	s_waitcnt lgkmcnt(8)
	s_waitcnt vmcnt(10)
	s_barrier
	s_setprio 1
	s_waitcnt lgkmcnt(7)
	v_mfma_f32_16x16x32_bf16 v[126:129], v[132:135], v[148:151], v[126:129]
	s_waitcnt lgkmcnt(5)
	v_mfma_f32_16x16x32_bf16 v[122:125], v[140:143], v[148:151], v[122:125]
	v_mfma_f32_16x16x32_bf16 v[110:113], v[132:135], v[156:159], v[110:113]
	s_waitcnt lgkmcnt(3)
	v_mfma_f32_16x16x32_bf16 v[106:109], v[140:143], v[156:159], v[106:109]
	v_mfma_f32_16x16x32_bf16 v[94:97], v[132:135], v[186:189], v[94:97]
	s_waitcnt lgkmcnt(1)
	v_mfma_f32_16x16x32_bf16 v[90:93], v[140:143], v[186:189], v[90:93]
	v_mfma_f32_16x16x32_bf16 v[78:81], v[132:135], v[194:197], v[78:81]
	v_mfma_f32_16x16x32_bf16 v[74:77], v[140:143], v[194:197], v[74:77]
	v_mfma_f32_16x16x32_bf16 v[126:129], v[136:139], v[152:155], v[126:129]
	v_mfma_f32_16x16x32_bf16 v[122:125], v[144:147], v[152:155], v[122:125]
	v_mfma_f32_16x16x32_bf16 v[110:113], v[136:139], v[160:163], v[110:113]
	v_mfma_f32_16x16x32_bf16 v[106:109], v[144:147], v[160:163], v[106:109]
	v_mfma_f32_16x16x32_bf16 v[94:97], v[136:139], v[190:193], v[94:97]
	s_waitcnt lgkmcnt(0)
	v_mfma_f32_16x16x32_bf16 v[90:93], v[144:147], v[190:193], v[90:93]
	v_mfma_f32_16x16x32_bf16 v[78:81], v[136:139], v[198:201], v[78:81]
	v_mfma_f32_16x16x32_bf16 v[74:77], v[144:147], v[198:201], v[74:77]
	s_setprio 0
	s_barrier
	s_add_i32 s60, 0, 0x14000
	s_add_i32 s58, s58, s35
	v_add_u32_e32 v130, s60, v182
	v_lshl_add_u64 v[234:235], s[66:67], 0, v[164:165]
	s_mov_b32 m0, s58
	ds_read_b128 v[218:221], v130
	ds_read_b128 v[222:225], v130 offset:1024
	ds_read_b128 v[226:229], v130 offset:2048
	ds_read_b128 v[230:233], v130 offset:3072
	global_load_lds_dwordx4 v[234:235], off
	v_lshl_add_u64 v[236:237], s[66:67], 0, v[168:169]
	s_add_i32 m0, s58, 0x2000
	s_nop 0
	global_load_lds_dwordx4 v[236:237], off
	s_waitcnt vmcnt(10)
	s_barrier
	s_setprio 1
	s_waitcnt lgkmcnt(3)
	s_waitcnt lgkmcnt(1)
	v_mfma_f32_16x16x32_bf16 v[118:121], v[218:221], v[148:151], v[118:121]
	v_mfma_f32_16x16x32_bf16 v[114:117], v[226:229], v[148:151], v[114:117]
	v_mfma_f32_16x16x32_bf16 v[102:105], v[218:221], v[156:159], v[102:105]
	v_mfma_f32_16x16x32_bf16 v[98:101], v[226:229], v[156:159], v[98:101]
	v_mfma_f32_16x16x32_bf16 v[86:89], v[218:221], v[186:189], v[86:89]
	v_mfma_f32_16x16x32_bf16 v[82:85], v[226:229], v[186:189], v[82:85]
	v_mfma_f32_16x16x32_bf16 v[70:73], v[218:221], v[194:197], v[70:73]
	v_mfma_f32_16x16x32_bf16 v[66:69], v[226:229], v[194:197], v[66:69]
	s_waitcnt lgkmcnt(0)
	v_mfma_f32_16x16x32_bf16 v[118:121], v[222:225], v[152:155], v[118:121]
	v_mfma_f32_16x16x32_bf16 v[114:117], v[230:233], v[152:155], v[114:117]
	v_mfma_f32_16x16x32_bf16 v[102:105], v[222:225], v[160:163], v[102:105]
	v_mfma_f32_16x16x32_bf16 v[98:101], v[230:233], v[160:163], v[98:101]
	v_mfma_f32_16x16x32_bf16 v[86:89], v[222:225], v[190:193], v[86:89]
	v_mfma_f32_16x16x32_bf16 v[82:85], v[230:233], v[190:193], v[82:85]
	v_mfma_f32_16x16x32_bf16 v[70:73], v[222:225], v[198:201], v[70:73]
	v_mfma_f32_16x16x32_bf16 v[66:69], v[230:233], v[198:201], v[66:69]
	s_setprio 0
	s_mov_b32 m0, s36
	v_lshl_add_u64 v[238:239], s[68:69], 0, v[166:167]
	s_barrier
	ds_read_b128 v[148:151], v185 offset:16384
	ds_read_b128 v[152:155], v185 offset:17408
	ds_read_b128 v[156:159], v185 offset:18432
	ds_read_b128 v[160:163], v185 offset:19456
	ds_read_b128 v[186:189], v185 offset:20480
	ds_read_b128 v[190:193], v185 offset:21504
	ds_read_b128 v[194:197], v185 offset:22528
	ds_read_b128 v[198:201], v185 offset:23552
	global_load_lds_dwordx4 v[238:239], off
	v_lshl_add_u64 v[240:241], s[68:69], 0, v[170:171]
	s_mov_b32 m0, s37
	s_nop 0
	global_load_lds_dwordx4 v[240:241], off
	s_barrier
	s_setprio 1
	s_waitcnt lgkmcnt(7)
	v_mfma_f32_16x16x32_bf16 v[62:65], v[132:135], v[148:151], v[62:65]
	s_waitcnt lgkmcnt(5)
	v_mfma_f32_16x16x32_bf16 v[58:61], v[140:143], v[148:151], v[58:61]
	v_mfma_f32_16x16x32_bf16 v[46:49], v[132:135], v[156:159], v[46:49]
	s_waitcnt lgkmcnt(3)
	v_mfma_f32_16x16x32_bf16 v[42:45], v[140:143], v[156:159], v[42:45]
	v_mfma_f32_16x16x32_bf16 v[30:33], v[132:135], v[186:189], v[30:33]
	s_waitcnt lgkmcnt(1)
	v_mfma_f32_16x16x32_bf16 v[26:29], v[140:143], v[186:189], v[26:29]
	v_mfma_f32_16x16x32_bf16 v[14:17], v[132:135], v[194:197], v[14:17]
	v_mfma_f32_16x16x32_bf16 v[10:13], v[140:143], v[194:197], v[10:13]
	v_mfma_f32_16x16x32_bf16 v[62:65], v[136:139], v[152:155], v[62:65]
	v_mfma_f32_16x16x32_bf16 v[58:61], v[144:147], v[152:155], v[58:61]
	v_mfma_f32_16x16x32_bf16 v[46:49], v[136:139], v[160:163], v[46:49]
	v_mfma_f32_16x16x32_bf16 v[42:45], v[144:147], v[160:163], v[42:45]
	v_mfma_f32_16x16x32_bf16 v[30:33], v[136:139], v[190:193], v[30:33]
	s_waitcnt lgkmcnt(0)
	v_mfma_f32_16x16x32_bf16 v[26:29], v[144:147], v[190:193], v[26:29]
	v_mfma_f32_16x16x32_bf16 v[14:17], v[136:139], v[198:201], v[14:17]
	v_mfma_f32_16x16x32_bf16 v[10:13], v[144:147], v[198:201], v[10:13]
	s_setprio 0
	s_barrier
	s_add_u32 s58, s66, 0x4000
	s_addc_u32 s59, s67, 0
	s_add_i32 s60, s60, s35
	v_lshl_add_u64 v[132:133], s[58:59], 0, v[164:165]
	s_mov_b32 m0, s60
	s_nop 0
	global_load_lds_dwordx4 v[132:133], off
	v_lshl_add_u64 v[132:133], s[58:59], 0, v[168:169]
	s_add_i32 m0, s60, 0x2000
	s_nop 0
	global_load_lds_dwordx4 v[132:133], off
	s_waitcnt vmcnt(10)
	s_barrier
	s_setprio 1
	v_mfma_f32_16x16x32_bf16 v[54:57], v[218:221], v[148:151], v[54:57]
	v_mfma_f32_16x16x32_bf16 v[50:53], v[226:229], v[148:151], v[50:53]
	v_mfma_f32_16x16x32_bf16 v[38:41], v[218:221], v[156:159], v[38:41]
	v_mfma_f32_16x16x32_bf16 v[34:37], v[226:229], v[156:159], v[34:37]
	v_mfma_f32_16x16x32_bf16 v[22:25], v[218:221], v[186:189], v[22:25]
	v_mfma_f32_16x16x32_bf16 v[18:21], v[226:229], v[186:189], v[18:21]
	v_mfma_f32_16x16x32_bf16 v[6:9], v[218:221], v[194:197], v[6:9]
	v_mfma_f32_16x16x32_bf16 v[2:5], v[226:229], v[194:197], v[2:5]
	v_mfma_f32_16x16x32_bf16 v[54:57], v[222:225], v[152:155], v[54:57]
	v_mfma_f32_16x16x32_bf16 v[50:53], v[230:233], v[152:155], v[50:53]
	v_mfma_f32_16x16x32_bf16 v[38:41], v[222:225], v[160:163], v[38:41]
	v_mfma_f32_16x16x32_bf16 v[34:37], v[230:233], v[160:163], v[34:37]
	v_mfma_f32_16x16x32_bf16 v[22:25], v[222:225], v[190:193], v[22:25]
	v_mfma_f32_16x16x32_bf16 v[18:21], v[230:233], v[190:193], v[18:21]
	v_mfma_f32_16x16x32_bf16 v[6:9], v[222:225], v[198:201], v[6:9]
	v_mfma_f32_16x16x32_bf16 v[2:5], v[230:233], v[198:201], v[2:5]
	s_setprio 0
	s_add_i32 s60, 0, 0x18000
	v_add_u32_e32 v130, s60, v182
	s_barrier
	ds_read_b128 v[132:135], v130
	ds_read_b128 v[136:139], v130 offset:1024
	ds_read_b128 v[140:143], v130 offset:2048
	ds_read_b128 v[144:147], v130 offset:3072
	s_add_u32 s58, s68, 0x40000
	s_addc_u32 s59, s69, 0
	s_mov_b32 m0, s38
	v_lshl_add_u64 v[218:219], s[58:59], 0, v[166:167]
	ds_read_b128 v[148:151], v185 offset:32768
	ds_read_b128 v[152:155], v185 offset:33792
	ds_read_b128 v[156:159], v185 offset:34816
	ds_read_b128 v[160:163], v185 offset:35840
	ds_read_b128 v[186:189], v185 offset:36864
	ds_read_b128 v[190:193], v185 offset:37888
	ds_read_b128 v[194:197], v185 offset:38912
	ds_read_b128 v[198:201], v185 offset:39936
	global_load_lds_dwordx4 v[218:219], off
	v_lshl_add_u64 v[218:219], s[58:59], 0, v[170:171]
	s_mov_b32 m0, s39
	s_nop 0
	global_load_lds_dwordx4 v[218:219], off
	s_waitcnt lgkmcnt(8)
	s_waitcnt vmcnt(10)
	s_barrier
	s_setprio 1
	s_waitcnt lgkmcnt(7)
	v_mfma_f32_16x16x32_bf16 v[126:129], v[132:135], v[148:151], v[126:129]
	s_waitcnt lgkmcnt(5)
	v_mfma_f32_16x16x32_bf16 v[122:125], v[140:143], v[148:151], v[122:125]
	v_mfma_f32_16x16x32_bf16 v[110:113], v[132:135], v[156:159], v[110:113]
	s_waitcnt lgkmcnt(3)
	v_mfma_f32_16x16x32_bf16 v[106:109], v[140:143], v[156:159], v[106:109]
	v_mfma_f32_16x16x32_bf16 v[94:97], v[132:135], v[186:189], v[94:97]
	s_waitcnt lgkmcnt(1)
	v_mfma_f32_16x16x32_bf16 v[90:93], v[140:143], v[186:189], v[90:93]
	v_mfma_f32_16x16x32_bf16 v[78:81], v[132:135], v[194:197], v[78:81]
	v_mfma_f32_16x16x32_bf16 v[74:77], v[140:143], v[194:197], v[74:77]
	v_mfma_f32_16x16x32_bf16 v[126:129], v[136:139], v[152:155], v[126:129]
	v_mfma_f32_16x16x32_bf16 v[122:125], v[144:147], v[152:155], v[122:125]
	v_mfma_f32_16x16x32_bf16 v[110:113], v[136:139], v[160:163], v[110:113]
	v_mfma_f32_16x16x32_bf16 v[106:109], v[144:147], v[160:163], v[106:109]
	v_mfma_f32_16x16x32_bf16 v[94:97], v[136:139], v[190:193], v[94:97]
	s_waitcnt lgkmcnt(0)
	v_mfma_f32_16x16x32_bf16 v[90:93], v[144:147], v[190:193], v[90:93]
	v_mfma_f32_16x16x32_bf16 v[78:81], v[136:139], v[198:201], v[78:81]
	v_mfma_f32_16x16x32_bf16 v[74:77], v[144:147], v[198:201], v[74:77]
	s_setprio 0
	s_barrier
	s_add_i32 s61, 0, 0x1c000
	s_add_i32 s58, s60, s35
	v_add_u32_e32 v130, s61, v182
	v_lshl_add_u64 v[234:235], v[234:235], 0, s[30:31]
	s_mov_b32 m0, s58
	ds_read_b128 v[218:221], v130
	ds_read_b128 v[222:225], v130 offset:1024
	ds_read_b128 v[226:229], v130 offset:2048
	ds_read_b128 v[230:233], v130 offset:3072
	global_load_lds_dwordx4 v[234:235], off
	v_lshl_add_u64 v[234:235], v[236:237], 0, s[30:31]
	s_add_i32 m0, s58, 0x2000
	s_nop 0
	global_load_lds_dwordx4 v[234:235], off
	s_waitcnt vmcnt(10)
	s_barrier
	s_setprio 1
	s_waitcnt lgkmcnt(3)
	s_waitcnt lgkmcnt(1)
	v_mfma_f32_16x16x32_bf16 v[118:121], v[218:221], v[148:151], v[118:121]
	v_mfma_f32_16x16x32_bf16 v[114:117], v[226:229], v[148:151], v[114:117]
	v_mfma_f32_16x16x32_bf16 v[102:105], v[218:221], v[156:159], v[102:105]
	v_mfma_f32_16x16x32_bf16 v[98:101], v[226:229], v[156:159], v[98:101]
	v_mfma_f32_16x16x32_bf16 v[86:89], v[218:221], v[186:189], v[86:89]
	v_mfma_f32_16x16x32_bf16 v[82:85], v[226:229], v[186:189], v[82:85]
	v_mfma_f32_16x16x32_bf16 v[70:73], v[218:221], v[194:197], v[70:73]
	v_mfma_f32_16x16x32_bf16 v[66:69], v[226:229], v[194:197], v[66:69]
	s_waitcnt lgkmcnt(0)
	v_mfma_f32_16x16x32_bf16 v[118:121], v[222:225], v[152:155], v[118:121]
	v_mfma_f32_16x16x32_bf16 v[114:117], v[230:233], v[152:155], v[114:117]
	v_mfma_f32_16x16x32_bf16 v[102:105], v[222:225], v[160:163], v[102:105]
	v_mfma_f32_16x16x32_bf16 v[98:101], v[230:233], v[160:163], v[98:101]
	v_mfma_f32_16x16x32_bf16 v[86:89], v[222:225], v[190:193], v[86:89]
	v_mfma_f32_16x16x32_bf16 v[82:85], v[230:233], v[190:193], v[82:85]
	v_mfma_f32_16x16x32_bf16 v[70:73], v[222:225], v[198:201], v[70:73]
	v_mfma_f32_16x16x32_bf16 v[66:69], v[230:233], v[198:201], v[66:69]
	s_setprio 0
	s_mov_b32 m0, s46
	v_lshl_add_u64 v[234:235], v[238:239], 0, s[30:31]
	s_barrier
	ds_read_b128 v[148:151], v185 offset:49152
	ds_read_b128 v[152:155], v185 offset:50176
	ds_read_b128 v[156:159], v185 offset:51200
	ds_read_b128 v[160:163], v185 offset:52224
	ds_read_b128 v[186:189], v185 offset:53248
	ds_read_b128 v[190:193], v185 offset:54272
	ds_read_b128 v[194:197], v185 offset:55296
	ds_read_b128 v[198:201], v185 offset:56320
	global_load_lds_dwordx4 v[234:235], off
	v_lshl_add_u64 v[234:235], v[240:241], 0, s[30:31]
	s_mov_b32 m0, s47
	s_nop 0
	global_load_lds_dwordx4 v[234:235], off
	s_barrier
	s_setprio 1
	s_waitcnt lgkmcnt(7)
	v_mfma_f32_16x16x32_bf16 v[62:65], v[132:135], v[148:151], v[62:65]
	s_waitcnt lgkmcnt(5)
	v_mfma_f32_16x16x32_bf16 v[58:61], v[140:143], v[148:151], v[58:61]
	v_mfma_f32_16x16x32_bf16 v[46:49], v[132:135], v[156:159], v[46:49]
	s_waitcnt lgkmcnt(3)
	v_mfma_f32_16x16x32_bf16 v[42:45], v[140:143], v[156:159], v[42:45]
	v_mfma_f32_16x16x32_bf16 v[30:33], v[132:135], v[186:189], v[30:33]
	s_waitcnt lgkmcnt(1)
	v_mfma_f32_16x16x32_bf16 v[26:29], v[140:143], v[186:189], v[26:29]
	v_mfma_f32_16x16x32_bf16 v[14:17], v[132:135], v[194:197], v[14:17]
	v_mfma_f32_16x16x32_bf16 v[10:13], v[140:143], v[194:197], v[10:13]
	v_mfma_f32_16x16x32_bf16 v[62:65], v[136:139], v[152:155], v[62:65]
	v_mfma_f32_16x16x32_bf16 v[58:61], v[144:147], v[152:155], v[58:61]
	v_mfma_f32_16x16x32_bf16 v[46:49], v[136:139], v[160:163], v[46:49]
	v_mfma_f32_16x16x32_bf16 v[42:45], v[144:147], v[160:163], v[42:45]
	v_mfma_f32_16x16x32_bf16 v[30:33], v[136:139], v[190:193], v[30:33]
	s_waitcnt lgkmcnt(0)
	v_mfma_f32_16x16x32_bf16 v[26:29], v[144:147], v[190:193], v[26:29]
	v_mfma_f32_16x16x32_bf16 v[14:17], v[136:139], v[198:201], v[14:17]
	v_mfma_f32_16x16x32_bf16 v[10:13], v[144:147], v[198:201], v[10:13]
	s_setprio 0
	s_barrier
	s_add_u32 s58, s66, 0x4080
	s_addc_u32 s59, s67, 0
	s_add_i32 s60, s61, s35
	v_lshl_add_u64 v[132:133], s[58:59], 0, v[164:165]
	s_mov_b32 m0, s60
	s_nop 0
	global_load_lds_dwordx4 v[132:133], off
	v_lshl_add_u64 v[132:133], s[58:59], 0, v[168:169]
	s_add_i32 m0, s60, 0x2000
	s_nop 0
	global_load_lds_dwordx4 v[132:133], off
	s_waitcnt vmcnt(10)
	s_barrier
	s_setprio 1
	v_mfma_f32_16x16x32_bf16 v[54:57], v[218:221], v[148:151], v[54:57]
	v_mfma_f32_16x16x32_bf16 v[50:53], v[226:229], v[148:151], v[50:53]
	v_mfma_f32_16x16x32_bf16 v[38:41], v[218:221], v[156:159], v[38:41]
	v_mfma_f32_16x16x32_bf16 v[34:37], v[226:229], v[156:159], v[34:37]
	v_mfma_f32_16x16x32_bf16 v[22:25], v[218:221], v[186:189], v[22:25]
	v_mfma_f32_16x16x32_bf16 v[18:21], v[226:229], v[186:189], v[18:21]
	v_mfma_f32_16x16x32_bf16 v[6:9], v[218:221], v[194:197], v[6:9]
	v_mfma_f32_16x16x32_bf16 v[2:5], v[226:229], v[194:197], v[2:5]
	v_mfma_f32_16x16x32_bf16 v[54:57], v[222:225], v[152:155], v[54:57]
	v_mfma_f32_16x16x32_bf16 v[50:53], v[230:233], v[152:155], v[50:53]
	v_mfma_f32_16x16x32_bf16 v[38:41], v[222:225], v[160:163], v[38:41]
	v_mfma_f32_16x16x32_bf16 v[34:37], v[230:233], v[160:163], v[34:37]
	v_mfma_f32_16x16x32_bf16 v[22:25], v[222:225], v[190:193], v[22:25]
	v_mfma_f32_16x16x32_bf16 v[18:21], v[230:233], v[190:193], v[18:21]
	v_mfma_f32_16x16x32_bf16 v[6:9], v[222:225], v[198:201], v[6:9]
	v_mfma_f32_16x16x32_bf16 v[2:5], v[230:233], v[198:201], v[2:5]
	s_setprio 0
	s_add_u32 s64, s64, 0x100
	s_addc_u32 s65, s65, 0
	s_cmp_gt_u32 s57, 13
	s_barrier
	s_cbranch_scc1 .LBB0_861

.LBB0_956:
	s_add_u32 s18, s16, 0xfffc0080
	s_addc_u32 s19, s17, -1
	s_cmp_eq_u32 s51, 12
	s_cselect_b32 s63, s11, s19
	s_cselect_b32 s62, s10, s18
	s_cselect_b32 s19, s15, s50
	s_cselect_b32 s18, s14, s9
	s_add_i32 s53, 0, 0x10000
	v_add_u32_e32 v130, s53, v144
	ds_read_b128 v[148:151], v130
	ds_read_b128 v[152:155], v130 offset:1024
	ds_read_b128 v[156:159], v130 offset:2048
	ds_read_b128 v[160:163], v130 offset:3072
	v_lshl_add_u64 v[198:199], s[16:17], 0, v[140:141]
	s_add_i32 m0, s7, 0xc000
	ds_read_b128 v[164:167], v146
	ds_read_b128 v[168:171], v146 offset:1024
	ds_read_b128 v[172:175], v146 offset:2048
	ds_read_b128 v[178:181], v146 offset:3072
	ds_read_b128 v[182:185], v146 offset:4096
	ds_read_b128 v[186:189], v146 offset:5120
	ds_read_b128 v[190:193], v146 offset:6144
	ds_read_b128 v[194:197], v146 offset:7168
	global_load_lds_dwordx4 v[198:199], off
	v_lshl_add_u64 v[198:199], s[16:17], 0, v[142:143]
	s_add_i32 m0, s7, 0xe000
	s_nop 0
	global_load_lds_dwordx4 v[198:199], off
	s_waitcnt lgkmcnt(8)
	s_waitcnt vmcnt(10)
	s_barrier
	s_setprio 1
	s_waitcnt lgkmcnt(7)
	v_mfma_f32_16x16x32_bf16 v[126:129], v[148:151], v[164:167], v[126:129]
	s_waitcnt lgkmcnt(5)
	v_mfma_f32_16x16x32_bf16 v[122:125], v[156:159], v[164:167], v[122:125]
	v_mfma_f32_16x16x32_bf16 v[118:121], v[148:151], v[172:175], v[118:121]
	s_waitcnt lgkmcnt(3)
	v_mfma_f32_16x16x32_bf16 v[114:117], v[156:159], v[172:175], v[114:117]
	v_mfma_f32_16x16x32_bf16 v[102:105], v[148:151], v[182:185], v[102:105]
	s_waitcnt lgkmcnt(1)
	v_mfma_f32_16x16x32_bf16 v[98:101], v[156:159], v[182:185], v[98:101]
	v_mfma_f32_16x16x32_bf16 v[86:89], v[148:151], v[190:193], v[86:89]
	v_mfma_f32_16x16x32_bf16 v[82:85], v[156:159], v[190:193], v[82:85]
	v_mfma_f32_16x16x32_bf16 v[126:129], v[152:155], v[168:171], v[126:129]
	v_mfma_f32_16x16x32_bf16 v[122:125], v[160:163], v[168:171], v[122:125]
	v_mfma_f32_16x16x32_bf16 v[118:121], v[152:155], v[178:181], v[118:121]
	v_mfma_f32_16x16x32_bf16 v[114:117], v[160:163], v[178:181], v[114:117]
	v_mfma_f32_16x16x32_bf16 v[102:105], v[152:155], v[186:189], v[102:105]
	s_waitcnt lgkmcnt(0)
	v_mfma_f32_16x16x32_bf16 v[98:101], v[160:163], v[186:189], v[98:101]
	v_mfma_f32_16x16x32_bf16 v[86:89], v[152:155], v[194:197], v[86:89]
	v_mfma_f32_16x16x32_bf16 v[82:85], v[160:163], v[194:197], v[82:85]
	s_setprio 0
	s_barrier
	s_add_i32 s57, 0, 0x14000
	s_add_i32 s53, s53, s35
	v_add_u32_e32 v130, s57, v144
	v_lshl_add_u64 v[230:231], s[18:19], 0, v[138:139]
	s_mov_b32 m0, s53
	ds_read_b128 v[198:201], v130
	ds_read_b128 v[218:221], v130 offset:1024
	ds_read_b128 v[222:225], v130 offset:2048
	ds_read_b128 v[226:229], v130 offset:3072
	global_load_lds_dwordx4 v[230:231], off
	v_lshl_add_u64 v[232:233], s[18:19], 0, v[134:135]
	s_add_i32 m0, s53, 0x2000
	s_nop 0
	global_load_lds_dwordx4 v[232:233], off
	s_waitcnt vmcnt(10)
	s_barrier
	s_setprio 1
	s_waitcnt lgkmcnt(3)
	s_waitcnt lgkmcnt(1)
	v_mfma_f32_16x16x32_bf16 v[110:113], v[198:201], v[164:167], v[110:113]
	v_mfma_f32_16x16x32_bf16 v[106:109], v[222:225], v[164:167], v[106:109]
	v_mfma_f32_16x16x32_bf16 v[94:97], v[198:201], v[172:175], v[94:97]
	v_mfma_f32_16x16x32_bf16 v[90:93], v[222:225], v[172:175], v[90:93]
	v_mfma_f32_16x16x32_bf16 v[78:81], v[198:201], v[182:185], v[78:81]
	v_mfma_f32_16x16x32_bf16 v[74:77], v[222:225], v[182:185], v[74:77]
	v_mfma_f32_16x16x32_bf16 v[70:73], v[198:201], v[190:193], v[70:73]
	v_mfma_f32_16x16x32_bf16 v[66:69], v[222:225], v[190:193], v[66:69]
	s_waitcnt lgkmcnt(0)
	v_mfma_f32_16x16x32_bf16 v[110:113], v[218:221], v[168:171], v[110:113]
	v_mfma_f32_16x16x32_bf16 v[106:109], v[226:229], v[168:171], v[106:109]
	v_mfma_f32_16x16x32_bf16 v[94:97], v[218:221], v[178:181], v[94:97]
	v_mfma_f32_16x16x32_bf16 v[90:93], v[226:229], v[178:181], v[90:93]
	v_mfma_f32_16x16x32_bf16 v[78:81], v[218:221], v[186:189], v[78:81]
	v_mfma_f32_16x16x32_bf16 v[74:77], v[226:229], v[186:189], v[74:77]
	v_mfma_f32_16x16x32_bf16 v[70:73], v[218:221], v[194:197], v[70:73]
	v_mfma_f32_16x16x32_bf16 v[66:69], v[226:229], v[194:197], v[66:69]
	s_setprio 0
	s_mov_b32 m0, s7
	v_lshl_add_u64 v[234:235], s[62:63], 0, v[136:137]
	s_barrier
	ds_read_b128 v[164:167], v146 offset:16384
	ds_read_b128 v[168:171], v146 offset:17408
	ds_read_b128 v[172:175], v146 offset:18432
	ds_read_b128 v[178:181], v146 offset:19456
	ds_read_b128 v[182:185], v146 offset:20480
	ds_read_b128 v[186:189], v146 offset:21504
	ds_read_b128 v[190:193], v146 offset:22528
	ds_read_b128 v[194:197], v146 offset:23552
	global_load_lds_dwordx4 v[234:235], off
	v_lshl_add_u64 v[236:237], s[62:63], 0, v[132:133]
	s_mov_b32 m0, s36
	s_nop 0
	global_load_lds_dwordx4 v[236:237], off
	s_barrier
	s_setprio 1
	s_waitcnt lgkmcnt(7)
	v_mfma_f32_16x16x32_bf16 v[54:57], v[148:151], v[164:167], v[54:57]
	s_waitcnt lgkmcnt(5)
	v_mfma_f32_16x16x32_bf16 v[50:53], v[156:159], v[164:167], v[50:53]
	v_mfma_f32_16x16x32_bf16 v[38:41], v[148:151], v[172:175], v[38:41]
	s_waitcnt lgkmcnt(3)
	v_mfma_f32_16x16x32_bf16 v[34:37], v[156:159], v[172:175], v[34:37]
	v_mfma_f32_16x16x32_bf16 v[22:25], v[148:151], v[182:185], v[22:25]
	s_waitcnt lgkmcnt(1)
	v_mfma_f32_16x16x32_bf16 v[18:21], v[156:159], v[182:185], v[18:21]
	v_mfma_f32_16x16x32_bf16 v[6:9], v[148:151], v[190:193], v[6:9]
	v_mfma_f32_16x16x32_bf16 v[2:5], v[156:159], v[190:193], v[2:5]
	v_mfma_f32_16x16x32_bf16 v[54:57], v[152:155], v[168:171], v[54:57]
	v_mfma_f32_16x16x32_bf16 v[50:53], v[160:163], v[168:171], v[50:53]
	v_mfma_f32_16x16x32_bf16 v[38:41], v[152:155], v[178:181], v[38:41]
	v_mfma_f32_16x16x32_bf16 v[34:37], v[160:163], v[178:181], v[34:37]
	v_mfma_f32_16x16x32_bf16 v[22:25], v[152:155], v[186:189], v[22:25]
	s_waitcnt lgkmcnt(0)
	v_mfma_f32_16x16x32_bf16 v[18:21], v[160:163], v[186:189], v[18:21]
	v_mfma_f32_16x16x32_bf16 v[6:9], v[152:155], v[194:197], v[6:9]
	v_mfma_f32_16x16x32_bf16 v[2:5], v[160:163], v[194:197], v[2:5]
	s_setprio 0
	s_barrier
	s_add_u32 s58, s18, 0x4000
	s_addc_u32 s59, s19, 0
	s_add_i32 s53, s57, s35
	v_lshl_add_u64 v[148:149], s[58:59], 0, v[138:139]
	s_mov_b32 m0, s53
	s_nop 0
	global_load_lds_dwordx4 v[148:149], off
	v_lshl_add_u64 v[148:149], s[58:59], 0, v[134:135]
	s_add_i32 m0, s53, 0x2000
	s_nop 0
	global_load_lds_dwordx4 v[148:149], off
	s_waitcnt vmcnt(10)
	s_barrier
	s_setprio 1
	v_mfma_f32_16x16x32_bf16 v[30:33], v[198:201], v[164:167], v[30:33]
	v_mfma_f32_16x16x32_bf16 v[26:29], v[222:225], v[164:167], v[26:29]
	v_mfma_f32_16x16x32_bf16 v[14:17], v[198:201], v[172:175], v[14:17]
	v_mfma_f32_16x16x32_bf16 v[10:13], v[222:225], v[172:175], v[10:13]
	v_mfma_f32_16x16x32_bf16 v[58:61], v[198:201], v[182:185], v[58:61]
	v_mfma_f32_16x16x32_bf16 v[62:65], v[222:225], v[182:185], v[62:65]
	v_mfma_f32_16x16x32_bf16 v[42:45], v[198:201], v[190:193], v[42:45]
	v_mfma_f32_16x16x32_bf16 v[46:49], v[222:225], v[190:193], v[46:49]
	v_mfma_f32_16x16x32_bf16 v[30:33], v[218:221], v[168:171], v[30:33]
	v_mfma_f32_16x16x32_bf16 v[26:29], v[226:229], v[168:171], v[26:29]
	v_mfma_f32_16x16x32_bf16 v[14:17], v[218:221], v[178:181], v[14:17]
	v_mfma_f32_16x16x32_bf16 v[10:13], v[226:229], v[178:181], v[10:13]
	v_mfma_f32_16x16x32_bf16 v[58:61], v[218:221], v[186:189], v[58:61]
	v_mfma_f32_16x16x32_bf16 v[62:65], v[226:229], v[186:189], v[62:65]
	v_mfma_f32_16x16x32_bf16 v[42:45], v[218:221], v[194:197], v[42:45]
	v_mfma_f32_16x16x32_bf16 v[46:49], v[226:229], v[194:197], v[46:49]
	s_setprio 0
	s_add_i32 s53, 0, 0x18000
	v_add_u32_e32 v130, s53, v144
	s_barrier
	ds_read_b128 v[148:151], v130
	ds_read_b128 v[152:155], v130 offset:1024
	ds_read_b128 v[156:159], v130 offset:2048
	ds_read_b128 v[160:163], v130 offset:3072
	s_add_u32 s58, s62, 0x40000
	s_addc_u32 s59, s63, 0
	s_mov_b32 m0, s37
	v_lshl_add_u64 v[198:199], s[58:59], 0, v[136:137]
	ds_read_b128 v[164:167], v146 offset:32768
	ds_read_b128 v[168:171], v146 offset:33792
	ds_read_b128 v[172:175], v146 offset:34816
	ds_read_b128 v[178:181], v146 offset:35840
	ds_read_b128 v[182:185], v146 offset:36864
	ds_read_b128 v[186:189], v146 offset:37888
	ds_read_b128 v[190:193], v146 offset:38912
	ds_read_b128 v[194:197], v146 offset:39936
	global_load_lds_dwordx4 v[198:199], off
	v_lshl_add_u64 v[198:199], s[58:59], 0, v[132:133]
	s_mov_b32 m0, s38
	s_nop 0
	global_load_lds_dwordx4 v[198:199], off
	s_waitcnt lgkmcnt(8)
	s_waitcnt vmcnt(10)
	s_barrier
	s_setprio 1
	s_waitcnt lgkmcnt(7)
	v_mfma_f32_16x16x32_bf16 v[126:129], v[148:151], v[164:167], v[126:129]
	s_waitcnt lgkmcnt(5)
	v_mfma_f32_16x16x32_bf16 v[122:125], v[156:159], v[164:167], v[122:125]
	v_mfma_f32_16x16x32_bf16 v[118:121], v[148:151], v[172:175], v[118:121]
	s_waitcnt lgkmcnt(3)
	v_mfma_f32_16x16x32_bf16 v[114:117], v[156:159], v[172:175], v[114:117]
	v_mfma_f32_16x16x32_bf16 v[102:105], v[148:151], v[182:185], v[102:105]
	s_waitcnt lgkmcnt(1)
	v_mfma_f32_16x16x32_bf16 v[98:101], v[156:159], v[182:185], v[98:101]
	v_mfma_f32_16x16x32_bf16 v[86:89], v[148:151], v[190:193], v[86:89]
	v_mfma_f32_16x16x32_bf16 v[82:85], v[156:159], v[190:193], v[82:85]
	v_mfma_f32_16x16x32_bf16 v[126:129], v[152:155], v[168:171], v[126:129]
	v_mfma_f32_16x16x32_bf16 v[122:125], v[160:163], v[168:171], v[122:125]
	v_mfma_f32_16x16x32_bf16 v[118:121], v[152:155], v[178:181], v[118:121]
	v_mfma_f32_16x16x32_bf16 v[114:117], v[160:163], v[178:181], v[114:117]
	v_mfma_f32_16x16x32_bf16 v[102:105], v[152:155], v[186:189], v[102:105]
	s_waitcnt lgkmcnt(0)
	v_mfma_f32_16x16x32_bf16 v[98:101], v[160:163], v[186:189], v[98:101]
	v_mfma_f32_16x16x32_bf16 v[86:89], v[152:155], v[194:197], v[86:89]
	v_mfma_f32_16x16x32_bf16 v[82:85], v[160:163], v[194:197], v[82:85]
	s_setprio 0
	s_barrier
	s_add_i32 s57, 0, 0x1c000
	s_add_i32 s53, s53, s35
	v_add_u32_e32 v130, s57, v144
	v_lshl_add_u64 v[230:231], v[230:231], 0, s[30:31]
	s_mov_b32 m0, s53
	ds_read_b128 v[198:201], v130
	ds_read_b128 v[218:221], v130 offset:1024
	ds_read_b128 v[222:225], v130 offset:2048
	ds_read_b128 v[226:229], v130 offset:3072
	global_load_lds_dwordx4 v[230:231], off
	v_lshl_add_u64 v[230:231], v[232:233], 0, s[30:31]
	s_add_i32 m0, s53, 0x2000
	s_nop 0
	global_load_lds_dwordx4 v[230:231], off
	s_waitcnt vmcnt(10)
	s_barrier
	s_setprio 1
	s_waitcnt lgkmcnt(3)
	s_waitcnt lgkmcnt(1)
	v_mfma_f32_16x16x32_bf16 v[110:113], v[198:201], v[164:167], v[110:113]
	v_mfma_f32_16x16x32_bf16 v[106:109], v[222:225], v[164:167], v[106:109]
	v_mfma_f32_16x16x32_bf16 v[94:97], v[198:201], v[172:175], v[94:97]
	v_mfma_f32_16x16x32_bf16 v[90:93], v[222:225], v[172:175], v[90:93]
	v_mfma_f32_16x16x32_bf16 v[78:81], v[198:201], v[182:185], v[78:81]
	v_mfma_f32_16x16x32_bf16 v[74:77], v[222:225], v[182:185], v[74:77]
	v_mfma_f32_16x16x32_bf16 v[70:73], v[198:201], v[190:193], v[70:73]
	v_mfma_f32_16x16x32_bf16 v[66:69], v[222:225], v[190:193], v[66:69]
	s_waitcnt lgkmcnt(0)
	v_mfma_f32_16x16x32_bf16 v[110:113], v[218:221], v[168:171], v[110:113]
	v_mfma_f32_16x16x32_bf16 v[106:109], v[226:229], v[168:171], v[106:109]
	v_mfma_f32_16x16x32_bf16 v[94:97], v[218:221], v[178:181], v[94:97]
	v_mfma_f32_16x16x32_bf16 v[90:93], v[226:229], v[178:181], v[90:93]
	v_mfma_f32_16x16x32_bf16 v[78:81], v[218:221], v[186:189], v[78:81]
	v_mfma_f32_16x16x32_bf16 v[74:77], v[226:229], v[186:189], v[74:77]
	v_mfma_f32_16x16x32_bf16 v[70:73], v[218:221], v[194:197], v[70:73]
	v_mfma_f32_16x16x32_bf16 v[66:69], v[226:229], v[194:197], v[66:69]
	s_setprio 0
	s_mov_b32 m0, s43
	v_lshl_add_u64 v[230:231], v[234:235], 0, s[30:31]
	s_barrier
	ds_read_b128 v[164:167], v146 offset:49152
	ds_read_b128 v[168:171], v146 offset:50176
	ds_read_b128 v[172:175], v146 offset:51200
	ds_read_b128 v[178:181], v146 offset:52224
	ds_read_b128 v[182:185], v146 offset:53248
	ds_read_b128 v[186:189], v146 offset:54272
	ds_read_b128 v[190:193], v146 offset:55296
	ds_read_b128 v[194:197], v146 offset:56320
	global_load_lds_dwordx4 v[230:231], off
	v_lshl_add_u64 v[230:231], v[236:237], 0, s[30:31]
	s_mov_b32 m0, s44
	s_nop 0
	global_load_lds_dwordx4 v[230:231], off
	s_barrier
	s_setprio 1
	s_waitcnt lgkmcnt(7)
	v_mfma_f32_16x16x32_bf16 v[54:57], v[148:151], v[164:167], v[54:57]
	s_waitcnt lgkmcnt(5)
	v_mfma_f32_16x16x32_bf16 v[50:53], v[156:159], v[164:167], v[50:53]
	v_mfma_f32_16x16x32_bf16 v[38:41], v[148:151], v[172:175], v[38:41]
	s_waitcnt lgkmcnt(3)
	v_mfma_f32_16x16x32_bf16 v[34:37], v[156:159], v[172:175], v[34:37]
	v_mfma_f32_16x16x32_bf16 v[22:25], v[148:151], v[182:185], v[22:25]
	s_waitcnt lgkmcnt(1)
	v_mfma_f32_16x16x32_bf16 v[18:21], v[156:159], v[182:185], v[18:21]
	v_mfma_f32_16x16x32_bf16 v[6:9], v[148:151], v[190:193], v[6:9]
	v_mfma_f32_16x16x32_bf16 v[2:5], v[156:159], v[190:193], v[2:5]
	v_mfma_f32_16x16x32_bf16 v[54:57], v[152:155], v[168:171], v[54:57]
	v_mfma_f32_16x16x32_bf16 v[50:53], v[160:163], v[168:171], v[50:53]
	v_mfma_f32_16x16x32_bf16 v[38:41], v[152:155], v[178:181], v[38:41]
	v_mfma_f32_16x16x32_bf16 v[34:37], v[160:163], v[178:181], v[34:37]
	v_mfma_f32_16x16x32_bf16 v[22:25], v[152:155], v[186:189], v[22:25]
	s_waitcnt lgkmcnt(0)
	v_mfma_f32_16x16x32_bf16 v[18:21], v[160:163], v[186:189], v[18:21]
	v_mfma_f32_16x16x32_bf16 v[6:9], v[152:155], v[194:197], v[6:9]
	v_mfma_f32_16x16x32_bf16 v[2:5], v[160:163], v[194:197], v[2:5]
	s_setprio 0
	s_barrier
	s_add_u32 s18, s18, 0x4080
	s_addc_u32 s19, s19, 0
	s_add_i32 s53, s57, s35
	v_lshl_add_u64 v[148:149], s[18:19], 0, v[138:139]
	s_mov_b32 m0, s53
	s_nop 0
	global_load_lds_dwordx4 v[148:149], off
	v_lshl_add_u64 v[148:149], s[18:19], 0, v[134:135]
	s_add_i32 m0, s53, 0x2000
	s_nop 0
	global_load_lds_dwordx4 v[148:149], off
	s_waitcnt vmcnt(10)
	s_barrier
	s_setprio 1
	v_mfma_f32_16x16x32_bf16 v[30:33], v[198:201], v[164:167], v[30:33]
	v_mfma_f32_16x16x32_bf16 v[26:29], v[222:225], v[164:167], v[26:29]
	v_mfma_f32_16x16x32_bf16 v[14:17], v[198:201], v[172:175], v[14:17]
	v_mfma_f32_16x16x32_bf16 v[10:13], v[222:225], v[172:175], v[10:13]
	v_mfma_f32_16x16x32_bf16 v[58:61], v[198:201], v[182:185], v[58:61]
	v_mfma_f32_16x16x32_bf16 v[62:65], v[222:225], v[182:185], v[62:65]
	v_mfma_f32_16x16x32_bf16 v[42:45], v[198:201], v[190:193], v[42:45]
	v_mfma_f32_16x16x32_bf16 v[46:49], v[222:225], v[190:193], v[46:49]
	v_mfma_f32_16x16x32_bf16 v[30:33], v[218:221], v[168:171], v[30:33]
	v_mfma_f32_16x16x32_bf16 v[26:29], v[226:229], v[168:171], v[26:29]
	v_mfma_f32_16x16x32_bf16 v[14:17], v[218:221], v[178:181], v[14:17]
	v_mfma_f32_16x16x32_bf16 v[10:13], v[226:229], v[178:181], v[10:13]
	v_mfma_f32_16x16x32_bf16 v[58:61], v[218:221], v[186:189], v[58:61]
	v_mfma_f32_16x16x32_bf16 v[62:65], v[226:229], v[186:189], v[62:65]
	v_mfma_f32_16x16x32_bf16 v[42:45], v[218:221], v[194:197], v[42:45]
	v_mfma_f32_16x16x32_bf16 v[46:49], v[226:229], v[194:197], v[46:49]
	s_setprio 0
	s_add_i32 s51, s51, 2
	s_add_u32 s16, s16, 0x100
	s_addc_u32 s17, s17, 0
	s_add_u32 s9, s9, 0x100
	s_addc_u32 s50, s50, 0
	s_cmp_gt_u32 s51, 13
	s_barrier
	s_cbranch_scc0 .LBB0_956
	s_lshl_b32 s16, s6, 8
	s_ashr_i32 s17, s16, 31
	s_lshl_b64 s[16:17], s[16:17], 11
	s_add_u32 s6, s39, s16
	s_addc_u32 s9, s42, s17
	s_lshl_b32 s16, s47, 8
	s_ashr_i32 s17, s16, 31
	s_lshl_b64 s[16:17], s[16:17], 1
	s_add_u32 s16, s6, s16
	s_addc_u32 s17, s9, s17
	v_mov_b32_e32 v130, v145
	v_cvt_pk_bf16_f32 v110, v110, v111
	v_lshl_add_u64 v[148:149], v[130:131], 1, s[16:17]
	v_cvt_pk_bf16_f32 v111, v112, v113
	v_cvt_pk_bf16_f32 v112, v106, v107
	v_cvt_pk_bf16_f32 v113, v108, v109
	s_mov_b32 s6, 0x8000
	global_store_dwordx4 v[148:149], v[110:113], off offset:16
	v_cvt_pk_bf16_f32 v94, v94, v95
	v_cvt_pk_bf16_f32 v95, v96, v97
	v_add_co_u32_e32 v110, vcc, s6, v148
	v_cvt_pk_bf16_f32 v96, v90, v91
	s_nop 0
	v_addc_co_u32_e32 v111, vcc, 0, v149, vcc
	v_cvt_pk_bf16_f32 v97, v92, v93
	s_mov_b32 s6, 0x10000
	global_store_dwordx4 v[110:111], v[94:97], off offset:16
	v_cvt_pk_bf16_f32 v78, v78, v79
	v_cvt_pk_bf16_f32 v79, v80, v81
	v_add_co_u32_e32 v94, vcc, s6, v148
	v_cvt_pk_bf16_f32 v80, v74, v75
	s_nop 0
	v_addc_co_u32_e32 v95, vcc, 0, v149, vcc
	v_cvt_pk_bf16_f32 v81, v76, v77
	s_mov_b32 s6, 0x18000
	global_store_dwordx4 v[94:95], v[78:81], off offset:16
	v_cvt_pk_bf16_f32 v54, v54, v55
	v_cvt_pk_bf16_f32 v55, v56, v57
	v_add_co_u32_e32 v78, vcc, s6, v148
	s_mov_b32 s6, 0x40000
	s_nop 0
	v_addc_co_u32_e32 v79, vcc, 0, v149, vcc
	v_cvt_pk_bf16_f32 v56, v50, v51
	v_add_co_u32_e32 v50, vcc, s6, v148
	v_cvt_pk_bf16_f32 v30, v30, v31
	s_nop 0
	v_addc_co_u32_e32 v51, vcc, 0, v149, vcc
	v_cvt_pk_bf16_f32 v31, v32, v33
	v_cvt_pk_bf16_f32 v32, v26, v27
	v_cvt_pk_bf16_f32 v33, v28, v29
	s_mov_b32 s6, 0x48000
	global_store_dwordx4 v[50:51], v[30:33], off offset:16
	v_cvt_pk_bf16_f32 v14, v14, v15
	v_cvt_pk_bf16_f32 v15, v16, v17
	v_add_co_u32_e32 v30, vcc, s6, v148
	v_cvt_pk_bf16_f32 v16, v10, v11
	s_nop 0
	v_addc_co_u32_e32 v31, vcc, 0, v149, vcc
	v_cvt_pk_bf16_f32 v17, v12, v13
	s_mov_b32 s6, 0x50000
	global_store_dwordx4 v[30:31], v[14:17], off offset:16
	v_cvt_pk_bf16_f32 v10, v22, v23
	v_cvt_pk_bf16_f32 v11, v24, v25
	v_add_co_u32_e32 v14, vcc, s6, v148
	v_cvt_pk_bf16_f32 v12, v18, v19
	v_cvt_pk_bf16_f32 v13, v20, v21
	v_addc_co_u32_e32 v15, vcc, 0, v149, vcc
	global_store_dwordx4 v[14:15], v[10:13], off
	s_mov_b32 s6, 0x58000
	v_cvt_pk_bf16_f32 v126, v126, v127
	v_cvt_pk_bf16_f32 v10, v58, v59
	v_cvt_pk_bf16_f32 v11, v60, v61
	v_cvt_pk_bf16_f32 v12, v62, v63
	v_cvt_pk_bf16_f32 v13, v64, v65
	global_store_dwordx4 v[14:15], v[10:13], off offset:16
	v_cvt_pk_bf16_f32 v127, v128, v129
	v_cvt_pk_bf16_f32 v128, v122, v123
	v_add_co_u32_e32 v10, vcc, s6, v148
	v_cvt_pk_bf16_f32 v129, v124, v125
	s_nop 0
	v_addc_co_u32_e32 v11, vcc, 0, v149, vcc
	v_cvt_pk_bf16_f32 v106, v118, v119
	v_cvt_pk_bf16_f32 v107, v120, v121
	v_cvt_pk_bf16_f32 v108, v114, v115
	v_cvt_pk_bf16_f32 v109, v116, v117
	v_cvt_pk_bf16_f32 v90, v102, v103
	v_cvt_pk_bf16_f32 v91, v104, v105
	v_cvt_pk_bf16_f32 v92, v98, v99
	v_cvt_pk_bf16_f32 v93, v100, v101
	v_cvt_pk_bf16_f32 v74, v86, v87
	v_cvt_pk_bf16_f32 v75, v88, v89
	v_cvt_pk_bf16_f32 v76, v82, v83
	v_cvt_pk_bf16_f32 v77, v84, v85
	v_cvt_pk_bf16_f32 v70, v70, v71
	v_cvt_pk_bf16_f32 v71, v72, v73
	v_cvt_pk_bf16_f32 v72, v66, v67
	v_cvt_pk_bf16_f32 v73, v68, v69
	v_cvt_pk_bf16_f32 v57, v52, v53
	v_cvt_pk_bf16_f32 v26, v38, v39
	v_cvt_pk_bf16_f32 v27, v40, v41
	v_cvt_pk_bf16_f32 v28, v34, v35
	v_cvt_pk_bf16_f32 v29, v36, v37
	v_cvt_pk_bf16_f32 v6, v6, v7
	v_cvt_pk_bf16_f32 v7, v8, v9
	v_cvt_pk_bf16_f32 v8, v2, v3
	v_cvt_pk_bf16_f32 v9, v4, v5
	v_cvt_pk_bf16_f32 v2, v42, v43
	v_cvt_pk_bf16_f32 v3, v44, v45
	v_cvt_pk_bf16_f32 v4, v46, v47
	v_cvt_pk_bf16_f32 v5, v48, v49
	s_and_b64 vcc, exec, s[12:13]
	s_mov_b32 s6, s8
	s_mov_b32 s47, s46
	s_mov_b64 s[18:19], s[14:15]
	s_mov_b64 s[16:17], s[10:11]
	global_store_dwordx4 v[148:149], v[126:129], off
	global_store_dwordx4 v[110:111], v[106:109], off
	global_store_dwordx4 v[94:95], v[90:93], off
	global_store_dwordx4 v[78:79], v[74:77], off
	global_store_dwordx4 v[78:79], v[70:73], off offset:16
	global_store_dwordx4 v[50:51], v[54:57], off
	global_store_dwordx4 v[30:31], v[26:29], off
	global_store_dwordx4 v[10:11], v[6:9], off
	global_store_dwordx4 v[10:11], v[2:5], off offset:16
	s_cbranch_vccz .LBB0_953
	s_waitcnt vmcnt(0)
	v_readlane_b32 s44, v254, 28
	s_cmpk_gt_u32 s2, 0xff
	s_movk_i32 s47, 0x900
	s_mov_b64 s[42:43], 0x4000
	v_readlane_b32 s45, v254, 29
	s_cbranch_scc1 .LBB0_960
	s_barrier

.LBB0_1028:
	s_add_u32 s16, s14, 0xfffc0080
	s_addc_u32 s17, s15, -1
	s_cmp_eq_u32 s51, 12
	s_cselect_b32 s19, s11, s17
	s_cselect_b32 s18, s10, s16
	s_cselect_b32 s17, s13, s50
	s_cselect_b32 s16, s12, s9
	s_add_i32 s53, 0, 0x10000
	v_add_u32_e32 v130, s53, v144
	ds_read_b128 v[148:151], v130
	ds_read_b128 v[152:155], v130 offset:1024
	ds_read_b128 v[156:159], v130 offset:2048
	ds_read_b128 v[160:163], v130 offset:3072
	v_lshl_add_u64 v[198:199], s[14:15], 0, v[140:141]
	s_add_i32 m0, s5, 0xc000
	ds_read_b128 v[164:167], v146
	ds_read_b128 v[168:171], v146 offset:1024
	ds_read_b128 v[172:175], v146 offset:2048
	ds_read_b128 v[178:181], v146 offset:3072
	ds_read_b128 v[182:185], v146 offset:4096
	ds_read_b128 v[186:189], v146 offset:5120
	ds_read_b128 v[190:193], v146 offset:6144
	ds_read_b128 v[194:197], v146 offset:7168
	global_load_lds_dwordx4 v[198:199], off
	v_lshl_add_u64 v[198:199], s[14:15], 0, v[142:143]
	s_add_i32 m0, s5, 0xe000
	s_nop 0
	global_load_lds_dwordx4 v[198:199], off
	s_waitcnt lgkmcnt(8)
	s_waitcnt vmcnt(10)
	s_barrier
	s_setprio 1
	s_waitcnt lgkmcnt(7)
	v_mfma_f32_16x16x32_bf16 v[126:129], v[148:151], v[164:167], v[126:129]
	s_waitcnt lgkmcnt(5)
	v_mfma_f32_16x16x32_bf16 v[122:125], v[156:159], v[164:167], v[122:125]
	v_mfma_f32_16x16x32_bf16 v[118:121], v[148:151], v[172:175], v[118:121]
	s_waitcnt lgkmcnt(3)
	v_mfma_f32_16x16x32_bf16 v[114:117], v[156:159], v[172:175], v[114:117]
	v_mfma_f32_16x16x32_bf16 v[102:105], v[148:151], v[182:185], v[102:105]
	s_waitcnt lgkmcnt(1)
	v_mfma_f32_16x16x32_bf16 v[98:101], v[156:159], v[182:185], v[98:101]
	v_mfma_f32_16x16x32_bf16 v[86:89], v[148:151], v[190:193], v[86:89]
	v_mfma_f32_16x16x32_bf16 v[82:85], v[156:159], v[190:193], v[82:85]
	v_mfma_f32_16x16x32_bf16 v[126:129], v[152:155], v[168:171], v[126:129]
	v_mfma_f32_16x16x32_bf16 v[122:125], v[160:163], v[168:171], v[122:125]
	v_mfma_f32_16x16x32_bf16 v[118:121], v[152:155], v[178:181], v[118:121]
	v_mfma_f32_16x16x32_bf16 v[114:117], v[160:163], v[178:181], v[114:117]
	v_mfma_f32_16x16x32_bf16 v[102:105], v[152:155], v[186:189], v[102:105]
	s_waitcnt lgkmcnt(0)
	v_mfma_f32_16x16x32_bf16 v[98:101], v[160:163], v[186:189], v[98:101]
	v_mfma_f32_16x16x32_bf16 v[86:89], v[152:155], v[194:197], v[86:89]
	v_mfma_f32_16x16x32_bf16 v[82:85], v[160:163], v[194:197], v[82:85]
	s_setprio 0
	s_barrier
	s_add_i32 s57, 0, 0x14000
	s_add_i32 s53, s53, s35
	v_add_u32_e32 v130, s57, v144
	v_lshl_add_u64 v[230:231], s[16:17], 0, v[132:133]
	s_mov_b32 m0, s53
	ds_read_b128 v[198:201], v130
	ds_read_b128 v[218:221], v130 offset:1024
	ds_read_b128 v[222:225], v130 offset:2048
	ds_read_b128 v[226:229], v130 offset:3072
	global_load_lds_dwordx4 v[230:231], off
	v_lshl_add_u64 v[232:233], s[16:17], 0, v[136:137]
	s_add_i32 m0, s53, 0x2000
	s_nop 0
	global_load_lds_dwordx4 v[232:233], off
	s_waitcnt vmcnt(10)
	s_barrier
	s_setprio 1
	s_waitcnt lgkmcnt(3)
	s_waitcnt lgkmcnt(1)
	v_mfma_f32_16x16x32_bf16 v[110:113], v[198:201], v[164:167], v[110:113]
	v_mfma_f32_16x16x32_bf16 v[106:109], v[222:225], v[164:167], v[106:109]
	v_mfma_f32_16x16x32_bf16 v[94:97], v[198:201], v[172:175], v[94:97]
	v_mfma_f32_16x16x32_bf16 v[90:93], v[222:225], v[172:175], v[90:93]
	v_mfma_f32_16x16x32_bf16 v[78:81], v[198:201], v[182:185], v[78:81]
	v_mfma_f32_16x16x32_bf16 v[74:77], v[222:225], v[182:185], v[74:77]
	v_mfma_f32_16x16x32_bf16 v[70:73], v[198:201], v[190:193], v[70:73]
	v_mfma_f32_16x16x32_bf16 v[66:69], v[222:225], v[190:193], v[66:69]
	s_waitcnt lgkmcnt(0)
	v_mfma_f32_16x16x32_bf16 v[110:113], v[218:221], v[168:171], v[110:113]
	v_mfma_f32_16x16x32_bf16 v[106:109], v[226:229], v[168:171], v[106:109]
	v_mfma_f32_16x16x32_bf16 v[94:97], v[218:221], v[178:181], v[94:97]
	v_mfma_f32_16x16x32_bf16 v[90:93], v[226:229], v[178:181], v[90:93]
	v_mfma_f32_16x16x32_bf16 v[78:81], v[218:221], v[186:189], v[78:81]
	v_mfma_f32_16x16x32_bf16 v[74:77], v[226:229], v[186:189], v[74:77]
	v_mfma_f32_16x16x32_bf16 v[70:73], v[218:221], v[194:197], v[70:73]
	v_mfma_f32_16x16x32_bf16 v[66:69], v[226:229], v[194:197], v[66:69]
	s_setprio 0
	s_mov_b32 m0, s5
	v_lshl_add_u64 v[234:235], s[18:19], 0, v[134:135]
	s_barrier
	ds_read_b128 v[164:167], v146 offset:16384
	ds_read_b128 v[168:171], v146 offset:17408
	ds_read_b128 v[172:175], v146 offset:18432
	ds_read_b128 v[178:181], v146 offset:19456
	ds_read_b128 v[182:185], v146 offset:20480
	ds_read_b128 v[186:189], v146 offset:21504
	ds_read_b128 v[190:193], v146 offset:22528
	ds_read_b128 v[194:197], v146 offset:23552
	global_load_lds_dwordx4 v[234:235], off
	v_lshl_add_u64 v[236:237], s[18:19], 0, v[138:139]
	s_mov_b32 m0, s36
	s_nop 0
	global_load_lds_dwordx4 v[236:237], off
	s_barrier
	s_setprio 1
	s_waitcnt lgkmcnt(7)
	v_mfma_f32_16x16x32_bf16 v[54:57], v[148:151], v[164:167], v[54:57]
	s_waitcnt lgkmcnt(5)
	v_mfma_f32_16x16x32_bf16 v[50:53], v[156:159], v[164:167], v[50:53]
	v_mfma_f32_16x16x32_bf16 v[38:41], v[148:151], v[172:175], v[38:41]
	s_waitcnt lgkmcnt(3)
	v_mfma_f32_16x16x32_bf16 v[34:37], v[156:159], v[172:175], v[34:37]
	v_mfma_f32_16x16x32_bf16 v[22:25], v[148:151], v[182:185], v[22:25]
	s_waitcnt lgkmcnt(1)
	v_mfma_f32_16x16x32_bf16 v[18:21], v[156:159], v[182:185], v[18:21]
	v_mfma_f32_16x16x32_bf16 v[6:9], v[148:151], v[190:193], v[6:9]
	v_mfma_f32_16x16x32_bf16 v[2:5], v[156:159], v[190:193], v[2:5]
	v_mfma_f32_16x16x32_bf16 v[54:57], v[152:155], v[168:171], v[54:57]
	v_mfma_f32_16x16x32_bf16 v[50:53], v[160:163], v[168:171], v[50:53]
	v_mfma_f32_16x16x32_bf16 v[38:41], v[152:155], v[178:181], v[38:41]
	v_mfma_f32_16x16x32_bf16 v[34:37], v[160:163], v[178:181], v[34:37]
	v_mfma_f32_16x16x32_bf16 v[22:25], v[152:155], v[186:189], v[22:25]
	s_waitcnt lgkmcnt(0)
	v_mfma_f32_16x16x32_bf16 v[18:21], v[160:163], v[186:189], v[18:21]
	v_mfma_f32_16x16x32_bf16 v[6:9], v[152:155], v[194:197], v[6:9]
	v_mfma_f32_16x16x32_bf16 v[2:5], v[160:163], v[194:197], v[2:5]
	s_setprio 0
	s_barrier
	s_add_u32 s58, s16, 0x4000
	s_addc_u32 s59, s17, 0
	s_add_i32 s53, s57, s35
	v_lshl_add_u64 v[148:149], s[58:59], 0, v[132:133]
	s_mov_b32 m0, s53
	s_nop 0
	global_load_lds_dwordx4 v[148:149], off
	v_lshl_add_u64 v[148:149], s[58:59], 0, v[136:137]
	s_add_i32 m0, s53, 0x2000
	s_nop 0
	global_load_lds_dwordx4 v[148:149], off
	s_waitcnt vmcnt(10)
	s_barrier
	s_setprio 1
	v_mfma_f32_16x16x32_bf16 v[30:33], v[198:201], v[164:167], v[30:33]
	v_mfma_f32_16x16x32_bf16 v[26:29], v[222:225], v[164:167], v[26:29]
	v_mfma_f32_16x16x32_bf16 v[14:17], v[198:201], v[172:175], v[14:17]
	v_mfma_f32_16x16x32_bf16 v[10:13], v[222:225], v[172:175], v[10:13]
	v_mfma_f32_16x16x32_bf16 v[58:61], v[198:201], v[182:185], v[58:61]
	v_mfma_f32_16x16x32_bf16 v[62:65], v[222:225], v[182:185], v[62:65]
	v_mfma_f32_16x16x32_bf16 v[42:45], v[198:201], v[190:193], v[42:45]
	v_mfma_f32_16x16x32_bf16 v[46:49], v[222:225], v[190:193], v[46:49]
	v_mfma_f32_16x16x32_bf16 v[30:33], v[218:221], v[168:171], v[30:33]
	v_mfma_f32_16x16x32_bf16 v[26:29], v[226:229], v[168:171], v[26:29]
	v_mfma_f32_16x16x32_bf16 v[14:17], v[218:221], v[178:181], v[14:17]
	v_mfma_f32_16x16x32_bf16 v[10:13], v[226:229], v[178:181], v[10:13]
	v_mfma_f32_16x16x32_bf16 v[58:61], v[218:221], v[186:189], v[58:61]
	v_mfma_f32_16x16x32_bf16 v[62:65], v[226:229], v[186:189], v[62:65]
	v_mfma_f32_16x16x32_bf16 v[42:45], v[218:221], v[194:197], v[42:45]
	v_mfma_f32_16x16x32_bf16 v[46:49], v[226:229], v[194:197], v[46:49]
	s_setprio 0
	s_add_i32 s53, 0, 0x18000
	v_add_u32_e32 v130, s53, v144
	s_barrier
	ds_read_b128 v[148:151], v130
	ds_read_b128 v[152:155], v130 offset:1024
	ds_read_b128 v[156:159], v130 offset:2048
	ds_read_b128 v[160:163], v130 offset:3072
	s_add_u32 s18, s18, 0x40000
	s_addc_u32 s19, s19, 0
	s_mov_b32 m0, s37
	v_lshl_add_u64 v[198:199], s[18:19], 0, v[134:135]
	ds_read_b128 v[164:167], v146 offset:32768
	ds_read_b128 v[168:171], v146 offset:33792
	ds_read_b128 v[172:175], v146 offset:34816
	ds_read_b128 v[178:181], v146 offset:35840
	ds_read_b128 v[182:185], v146 offset:36864
	ds_read_b128 v[186:189], v146 offset:37888
	ds_read_b128 v[190:193], v146 offset:38912
	ds_read_b128 v[194:197], v146 offset:39936
	global_load_lds_dwordx4 v[198:199], off
	v_lshl_add_u64 v[198:199], s[18:19], 0, v[138:139]
	s_mov_b32 m0, s38
	s_nop 0
	global_load_lds_dwordx4 v[198:199], off
	s_waitcnt lgkmcnt(8)
	s_waitcnt vmcnt(10)
	s_barrier
	s_setprio 1
	s_waitcnt lgkmcnt(7)
	v_mfma_f32_16x16x32_bf16 v[126:129], v[148:151], v[164:167], v[126:129]
	s_waitcnt lgkmcnt(5)
	v_mfma_f32_16x16x32_bf16 v[122:125], v[156:159], v[164:167], v[122:125]
	v_mfma_f32_16x16x32_bf16 v[118:121], v[148:151], v[172:175], v[118:121]
	s_waitcnt lgkmcnt(3)
	v_mfma_f32_16x16x32_bf16 v[114:117], v[156:159], v[172:175], v[114:117]
	v_mfma_f32_16x16x32_bf16 v[102:105], v[148:151], v[182:185], v[102:105]
	s_waitcnt lgkmcnt(1)
	v_mfma_f32_16x16x32_bf16 v[98:101], v[156:159], v[182:185], v[98:101]
	v_mfma_f32_16x16x32_bf16 v[86:89], v[148:151], v[190:193], v[86:89]
	v_mfma_f32_16x16x32_bf16 v[82:85], v[156:159], v[190:193], v[82:85]
	v_mfma_f32_16x16x32_bf16 v[126:129], v[152:155], v[168:171], v[126:129]
	v_mfma_f32_16x16x32_bf16 v[122:125], v[160:163], v[168:171], v[122:125]
	v_mfma_f32_16x16x32_bf16 v[118:121], v[152:155], v[178:181], v[118:121]
	v_mfma_f32_16x16x32_bf16 v[114:117], v[160:163], v[178:181], v[114:117]
	v_mfma_f32_16x16x32_bf16 v[102:105], v[152:155], v[186:189], v[102:105]
	s_waitcnt lgkmcnt(0)
	v_mfma_f32_16x16x32_bf16 v[98:101], v[160:163], v[186:189], v[98:101]
	v_mfma_f32_16x16x32_bf16 v[86:89], v[152:155], v[194:197], v[86:89]
	v_mfma_f32_16x16x32_bf16 v[82:85], v[160:163], v[194:197], v[82:85]
	s_setprio 0
	s_barrier
	s_add_i32 s18, 0, 0x1c000
	s_add_i32 s19, s53, s35
	v_add_u32_e32 v130, s18, v144
	v_lshl_add_u64 v[230:231], v[230:231], 0, s[30:31]
	s_mov_b32 m0, s19
	ds_read_b128 v[198:201], v130
	ds_read_b128 v[218:221], v130 offset:1024
	ds_read_b128 v[222:225], v130 offset:2048
	ds_read_b128 v[226:229], v130 offset:3072
	global_load_lds_dwordx4 v[230:231], off
	v_lshl_add_u64 v[230:231], v[232:233], 0, s[30:31]
	s_add_i32 m0, s19, 0x2000
	s_nop 0
	global_load_lds_dwordx4 v[230:231], off
	s_waitcnt vmcnt(10)
	s_barrier
	s_setprio 1
	s_waitcnt lgkmcnt(3)
	s_waitcnt lgkmcnt(1)
	v_mfma_f32_16x16x32_bf16 v[110:113], v[198:201], v[164:167], v[110:113]
	v_mfma_f32_16x16x32_bf16 v[106:109], v[222:225], v[164:167], v[106:109]
	v_mfma_f32_16x16x32_bf16 v[94:97], v[198:201], v[172:175], v[94:97]
	v_mfma_f32_16x16x32_bf16 v[90:93], v[222:225], v[172:175], v[90:93]
	v_mfma_f32_16x16x32_bf16 v[78:81], v[198:201], v[182:185], v[78:81]
	v_mfma_f32_16x16x32_bf16 v[74:77], v[222:225], v[182:185], v[74:77]
	v_mfma_f32_16x16x32_bf16 v[70:73], v[198:201], v[190:193], v[70:73]
	v_mfma_f32_16x16x32_bf16 v[66:69], v[222:225], v[190:193], v[66:69]
	s_waitcnt lgkmcnt(0)
	v_mfma_f32_16x16x32_bf16 v[110:113], v[218:221], v[168:171], v[110:113]
	v_mfma_f32_16x16x32_bf16 v[106:109], v[226:229], v[168:171], v[106:109]
	v_mfma_f32_16x16x32_bf16 v[94:97], v[218:221], v[178:181], v[94:97]
	v_mfma_f32_16x16x32_bf16 v[90:93], v[226:229], v[178:181], v[90:93]
	v_mfma_f32_16x16x32_bf16 v[78:81], v[218:221], v[186:189], v[78:81]
	v_mfma_f32_16x16x32_bf16 v[74:77], v[226:229], v[186:189], v[74:77]
	v_mfma_f32_16x16x32_bf16 v[70:73], v[218:221], v[194:197], v[70:73]
	v_mfma_f32_16x16x32_bf16 v[66:69], v[226:229], v[194:197], v[66:69]
	s_setprio 0
	s_mov_b32 m0, s43
	v_lshl_add_u64 v[230:231], v[234:235], 0, s[30:31]
	s_barrier
	ds_read_b128 v[164:167], v146 offset:49152
	ds_read_b128 v[168:171], v146 offset:50176
	ds_read_b128 v[172:175], v146 offset:51200
	ds_read_b128 v[178:181], v146 offset:52224
	ds_read_b128 v[182:185], v146 offset:53248
	ds_read_b128 v[186:189], v146 offset:54272
	ds_read_b128 v[190:193], v146 offset:55296
	ds_read_b128 v[194:197], v146 offset:56320
	global_load_lds_dwordx4 v[230:231], off
	v_lshl_add_u64 v[230:231], v[236:237], 0, s[30:31]
	s_mov_b32 m0, s44
	s_nop 0
	global_load_lds_dwordx4 v[230:231], off
	s_barrier
	s_setprio 1
	s_waitcnt lgkmcnt(7)
	v_mfma_f32_16x16x32_bf16 v[54:57], v[148:151], v[164:167], v[54:57]
	s_waitcnt lgkmcnt(5)
	v_mfma_f32_16x16x32_bf16 v[50:53], v[156:159], v[164:167], v[50:53]
	v_mfma_f32_16x16x32_bf16 v[38:41], v[148:151], v[172:175], v[38:41]
	s_waitcnt lgkmcnt(3)
	v_mfma_f32_16x16x32_bf16 v[34:37], v[156:159], v[172:175], v[34:37]
	v_mfma_f32_16x16x32_bf16 v[22:25], v[148:151], v[182:185], v[22:25]
	s_waitcnt lgkmcnt(1)
	v_mfma_f32_16x16x32_bf16 v[18:21], v[156:159], v[182:185], v[18:21]
	v_mfma_f32_16x16x32_bf16 v[6:9], v[148:151], v[190:193], v[6:9]
	v_mfma_f32_16x16x32_bf16 v[2:5], v[156:159], v[190:193], v[2:5]
	v_mfma_f32_16x16x32_bf16 v[54:57], v[152:155], v[168:171], v[54:57]
	v_mfma_f32_16x16x32_bf16 v[50:53], v[160:163], v[168:171], v[50:53]
	v_mfma_f32_16x16x32_bf16 v[38:41], v[152:155], v[178:181], v[38:41]
	v_mfma_f32_16x16x32_bf16 v[34:37], v[160:163], v[178:181], v[34:37]
	v_mfma_f32_16x16x32_bf16 v[22:25], v[152:155], v[186:189], v[22:25]
	s_waitcnt lgkmcnt(0)
	v_mfma_f32_16x16x32_bf16 v[18:21], v[160:163], v[186:189], v[18:21]
	v_mfma_f32_16x16x32_bf16 v[6:9], v[152:155], v[194:197], v[6:9]
	v_mfma_f32_16x16x32_bf16 v[2:5], v[160:163], v[194:197], v[2:5]
	s_setprio 0
	s_barrier
	s_add_u32 s16, s16, 0x4080
	s_addc_u32 s17, s17, 0
	s_add_i32 s18, s18, s35
	v_lshl_add_u64 v[148:149], s[16:17], 0, v[132:133]
	s_mov_b32 m0, s18
	s_nop 0
	global_load_lds_dwordx4 v[148:149], off
	v_lshl_add_u64 v[148:149], s[16:17], 0, v[136:137]
	s_add_i32 m0, s18, 0x2000
	s_nop 0
	global_load_lds_dwordx4 v[148:149], off
	s_waitcnt vmcnt(10)
	s_barrier
	s_setprio 1
	v_mfma_f32_16x16x32_bf16 v[30:33], v[198:201], v[164:167], v[30:33]
	v_mfma_f32_16x16x32_bf16 v[26:29], v[222:225], v[164:167], v[26:29]
	v_mfma_f32_16x16x32_bf16 v[14:17], v[198:201], v[172:175], v[14:17]
	v_mfma_f32_16x16x32_bf16 v[10:13], v[222:225], v[172:175], v[10:13]
	v_mfma_f32_16x16x32_bf16 v[58:61], v[198:201], v[182:185], v[58:61]
	v_mfma_f32_16x16x32_bf16 v[62:65], v[222:225], v[182:185], v[62:65]
	v_mfma_f32_16x16x32_bf16 v[42:45], v[198:201], v[190:193], v[42:45]
	v_mfma_f32_16x16x32_bf16 v[46:49], v[222:225], v[190:193], v[46:49]
	v_mfma_f32_16x16x32_bf16 v[30:33], v[218:221], v[168:171], v[30:33]
	v_mfma_f32_16x16x32_bf16 v[26:29], v[226:229], v[168:171], v[26:29]
	v_mfma_f32_16x16x32_bf16 v[14:17], v[218:221], v[178:181], v[14:17]
	v_mfma_f32_16x16x32_bf16 v[10:13], v[226:229], v[178:181], v[10:13]
	v_mfma_f32_16x16x32_bf16 v[58:61], v[218:221], v[186:189], v[58:61]
	v_mfma_f32_16x16x32_bf16 v[62:65], v[226:229], v[186:189], v[62:65]
	v_mfma_f32_16x16x32_bf16 v[42:45], v[218:221], v[194:197], v[42:45]
	v_mfma_f32_16x16x32_bf16 v[46:49], v[226:229], v[194:197], v[46:49]
	s_setprio 0
	s_add_i32 s51, s51, 2
	s_add_u32 s14, s14, 0x100
	s_addc_u32 s15, s15, 0
	s_add_u32 s9, s9, 0x100
	s_addc_u32 s50, s50, 0
	s_cmp_gt_u32 s51, 13
	s_barrier
	s_cbranch_scc0 .LBB0_1028
	s_lshl_b32 s14, s4, 8
	s_ashr_i32 s15, s14, 31
	s_lshl_b64 s[14:15], s[14:15], 11
	s_add_u32 s4, s39, s14
	s_addc_u32 s9, s42, s15
	s_lshl_b32 s14, s47, 8
	s_ashr_i32 s15, s14, 31
	s_lshl_b64 s[14:15], s[14:15], 1
	s_add_u32 s14, s4, s14
	s_addc_u32 s15, s9, s15
	v_mov_b32_e32 v130, v145
	v_cvt_pk_bf16_f32 v110, v110, v111
	v_lshl_add_u64 v[148:149], v[130:131], 1, s[14:15]
	v_cvt_pk_bf16_f32 v111, v112, v113
	v_cvt_pk_bf16_f32 v112, v106, v107
	v_cvt_pk_bf16_f32 v113, v108, v109
	s_mov_b32 s4, 0x8000
	global_store_dwordx4 v[148:149], v[110:113], off offset:16
	v_cvt_pk_bf16_f32 v94, v94, v95
	v_cvt_pk_bf16_f32 v95, v96, v97
	v_add_co_u32_e32 v110, vcc, s4, v148
	v_cvt_pk_bf16_f32 v96, v90, v91
	s_nop 0
	v_addc_co_u32_e32 v111, vcc, 0, v149, vcc
	v_cvt_pk_bf16_f32 v97, v92, v93
	s_mov_b32 s4, 0x10000
	global_store_dwordx4 v[110:111], v[94:97], off offset:16
	v_cvt_pk_bf16_f32 v78, v78, v79
	v_cvt_pk_bf16_f32 v79, v80, v81
	v_add_co_u32_e32 v94, vcc, s4, v148
	v_cvt_pk_bf16_f32 v80, v74, v75
	s_nop 0
	v_addc_co_u32_e32 v95, vcc, 0, v149, vcc
	v_cvt_pk_bf16_f32 v81, v76, v77
	s_mov_b32 s4, 0x18000
	global_store_dwordx4 v[94:95], v[78:81], off offset:16
	v_cvt_pk_bf16_f32 v54, v54, v55
	v_cvt_pk_bf16_f32 v55, v56, v57
	v_add_co_u32_e32 v78, vcc, s4, v148
	s_mov_b32 s4, 0x40000
	s_nop 0
	v_addc_co_u32_e32 v79, vcc, 0, v149, vcc
	v_cvt_pk_bf16_f32 v56, v50, v51
	v_add_co_u32_e32 v50, vcc, s4, v148
	v_cvt_pk_bf16_f32 v30, v30, v31
	s_nop 0
	v_addc_co_u32_e32 v51, vcc, 0, v149, vcc
	v_cvt_pk_bf16_f32 v31, v32, v33
	v_cvt_pk_bf16_f32 v32, v26, v27
	v_cvt_pk_bf16_f32 v33, v28, v29
	s_mov_b32 s4, 0x48000
	global_store_dwordx4 v[50:51], v[30:33], off offset:16
	v_cvt_pk_bf16_f32 v14, v14, v15
	v_cvt_pk_bf16_f32 v15, v16, v17
	v_add_co_u32_e32 v30, vcc, s4, v148
	v_cvt_pk_bf16_f32 v16, v10, v11
	s_nop 0
	v_addc_co_u32_e32 v31, vcc, 0, v149, vcc
	v_cvt_pk_bf16_f32 v17, v12, v13
	s_mov_b32 s4, 0x50000
	global_store_dwordx4 v[30:31], v[14:17], off offset:16
	v_cvt_pk_bf16_f32 v10, v22, v23
	v_cvt_pk_bf16_f32 v11, v24, v25
	v_add_co_u32_e32 v14, vcc, s4, v148
	v_cvt_pk_bf16_f32 v12, v18, v19
	v_cvt_pk_bf16_f32 v13, v20, v21
	v_addc_co_u32_e32 v15, vcc, 0, v149, vcc
	global_store_dwordx4 v[14:15], v[10:13], off
	s_mov_b32 s4, 0x58000
	v_cvt_pk_bf16_f32 v126, v126, v127
	v_cvt_pk_bf16_f32 v10, v58, v59
	v_cvt_pk_bf16_f32 v11, v60, v61
	v_cvt_pk_bf16_f32 v12, v62, v63
	v_cvt_pk_bf16_f32 v13, v64, v65
	global_store_dwordx4 v[14:15], v[10:13], off offset:16
	v_cvt_pk_bf16_f32 v127, v128, v129
	v_cvt_pk_bf16_f32 v128, v122, v123
	v_add_co_u32_e32 v10, vcc, s4, v148
	v_cvt_pk_bf16_f32 v129, v124, v125
	s_nop 0
	v_addc_co_u32_e32 v11, vcc, 0, v149, vcc
	v_cvt_pk_bf16_f32 v106, v118, v119
	v_cvt_pk_bf16_f32 v107, v120, v121
	v_cvt_pk_bf16_f32 v108, v114, v115
	v_cvt_pk_bf16_f32 v109, v116, v117
	v_cvt_pk_bf16_f32 v90, v102, v103
	v_cvt_pk_bf16_f32 v91, v104, v105
	v_cvt_pk_bf16_f32 v92, v98, v99
	v_cvt_pk_bf16_f32 v93, v100, v101
	v_cvt_pk_bf16_f32 v74, v86, v87
	v_cvt_pk_bf16_f32 v75, v88, v89
	v_cvt_pk_bf16_f32 v76, v82, v83
	v_cvt_pk_bf16_f32 v77, v84, v85
	v_cvt_pk_bf16_f32 v70, v70, v71
	v_cvt_pk_bf16_f32 v71, v72, v73
	v_cvt_pk_bf16_f32 v72, v66, v67
	v_cvt_pk_bf16_f32 v73, v68, v69
	v_cvt_pk_bf16_f32 v57, v52, v53
	v_cvt_pk_bf16_f32 v26, v38, v39
	v_cvt_pk_bf16_f32 v27, v40, v41
	v_cvt_pk_bf16_f32 v28, v34, v35
	v_cvt_pk_bf16_f32 v29, v36, v37
	v_cvt_pk_bf16_f32 v6, v6, v7
	v_cvt_pk_bf16_f32 v7, v8, v9
	v_cvt_pk_bf16_f32 v8, v2, v3
	v_cvt_pk_bf16_f32 v9, v4, v5
	v_cvt_pk_bf16_f32 v2, v42, v43
	v_cvt_pk_bf16_f32 v3, v44, v45
	v_cvt_pk_bf16_f32 v4, v46, v47
	v_cvt_pk_bf16_f32 v5, v48, v49
	s_and_b64 vcc, exec, s[6:7]
	s_mov_b32 s4, s8
	s_mov_b32 s47, s46
	s_mov_b64 s[16:17], s[12:13]
	s_mov_b64 s[14:15], s[10:11]
	s_mov_b32 s53, 0x42b17218
	global_store_dwordx4 v[148:149], v[126:129], off
	global_store_dwordx4 v[110:111], v[106:109], off
	global_store_dwordx4 v[94:95], v[90:93], off
	global_store_dwordx4 v[78:79], v[74:77], off
	global_store_dwordx4 v[78:79], v[70:73], off offset:16
	global_store_dwordx4 v[50:51], v[54:57], off
	global_store_dwordx4 v[30:31], v[26:29], off
	global_store_dwordx4 v[10:11], v[6:9], off
	global_store_dwordx4 v[10:11], v[2:5], off offset:16
	s_cbranch_vccz .LBB0_1021
	s_waitcnt vmcnt(0)
	s_cmpk_gt_u32 s22, 0xff
	s_cbranch_scc1 .LBB0_1032
	s_barrier

.LBB0_1103:
	s_add_u32 s58, s12, s62
	s_addc_u32 s59, s13, s63
	s_add_u32 s58, s58, 0x100
	s_addc_u32 s59, s59, 0
	s_add_u32 s60, s7, s62
	s_addc_u32 s61, s53, s63
	s_cmpk_eq_i32 s62, 0x700
	s_cselect_b32 s67, s9, s59
	s_cselect_b32 s66, s8, s58
	s_cselect_b32 s65, s11, s61
	s_cselect_b32 s64, s10, s60
	s_add_i32 s58, 0, 0x10000
	v_add_u32_e32 v130, s58, v182
	ds_read_b128 v[132:135], v130
	ds_read_b128 v[136:139], v130 offset:1024
	ds_read_b128 v[140:143], v130 offset:2048
	ds_read_b128 v[144:147], v130 offset:3072
	v_lshl_add_u64 v[218:219], v[178:179], 0, s[62:63]
	s_add_i32 m0, s36, 0xc000
	ds_read_b128 v[148:151], v185
	ds_read_b128 v[152:155], v185 offset:1024
	ds_read_b128 v[156:159], v185 offset:2048
	ds_read_b128 v[160:163], v185 offset:3072
	ds_read_b128 v[186:189], v185 offset:4096
	ds_read_b128 v[190:193], v185 offset:5120
	ds_read_b128 v[194:197], v185 offset:6144
	ds_read_b128 v[198:201], v185 offset:7168
	global_load_lds_dwordx4 v[218:219], off
	v_lshl_add_u64 v[218:219], v[180:181], 0, s[62:63]
	s_add_i32 m0, s36, 0xe000
	s_nop 0
	global_load_lds_dwordx4 v[218:219], off
	s_waitcnt lgkmcnt(8)
	s_waitcnt vmcnt(10)
	s_barrier
	s_setprio 1
	s_waitcnt lgkmcnt(7)
	v_mfma_f32_16x16x32_bf16 v[126:129], v[132:135], v[148:151], v[126:129]
	s_waitcnt lgkmcnt(5)
	v_mfma_f32_16x16x32_bf16 v[122:125], v[140:143], v[148:151], v[122:125]
	v_mfma_f32_16x16x32_bf16 v[110:113], v[132:135], v[156:159], v[110:113]
	s_waitcnt lgkmcnt(3)
	v_mfma_f32_16x16x32_bf16 v[106:109], v[140:143], v[156:159], v[106:109]
	v_mfma_f32_16x16x32_bf16 v[94:97], v[132:135], v[186:189], v[94:97]
	s_waitcnt lgkmcnt(1)
	v_mfma_f32_16x16x32_bf16 v[90:93], v[140:143], v[186:189], v[90:93]
	v_mfma_f32_16x16x32_bf16 v[78:81], v[132:135], v[194:197], v[78:81]
	v_mfma_f32_16x16x32_bf16 v[74:77], v[140:143], v[194:197], v[74:77]
	v_mfma_f32_16x16x32_bf16 v[126:129], v[136:139], v[152:155], v[126:129]
	v_mfma_f32_16x16x32_bf16 v[122:125], v[144:147], v[152:155], v[122:125]
	v_mfma_f32_16x16x32_bf16 v[110:113], v[136:139], v[160:163], v[110:113]
	v_mfma_f32_16x16x32_bf16 v[106:109], v[144:147], v[160:163], v[106:109]
	v_mfma_f32_16x16x32_bf16 v[94:97], v[136:139], v[190:193], v[94:97]
	s_waitcnt lgkmcnt(0)
	v_mfma_f32_16x16x32_bf16 v[90:93], v[144:147], v[190:193], v[90:93]
	v_mfma_f32_16x16x32_bf16 v[78:81], v[136:139], v[198:201], v[78:81]
	v_mfma_f32_16x16x32_bf16 v[74:77], v[144:147], v[198:201], v[74:77]
	s_setprio 0
	s_barrier
	s_add_i32 s60, 0, 0x14000
	s_add_i32 s58, s58, s35
	v_add_u32_e32 v130, s60, v182
	v_lshl_add_u64 v[234:235], s[64:65], 0, v[164:165]
	s_mov_b32 m0, s58
	ds_read_b128 v[218:221], v130
	ds_read_b128 v[222:225], v130 offset:1024
	ds_read_b128 v[226:229], v130 offset:2048
	ds_read_b128 v[230:233], v130 offset:3072
	global_load_lds_dwordx4 v[234:235], off
	v_lshl_add_u64 v[236:237], s[64:65], 0, v[168:169]
	s_add_i32 m0, s58, 0x2000
	s_nop 0
	global_load_lds_dwordx4 v[236:237], off
	s_waitcnt vmcnt(10)
	s_barrier
	s_setprio 1
	s_waitcnt lgkmcnt(3)
	s_waitcnt lgkmcnt(1)
	v_mfma_f32_16x16x32_bf16 v[118:121], v[218:221], v[148:151], v[118:121]
	v_mfma_f32_16x16x32_bf16 v[114:117], v[226:229], v[148:151], v[114:117]
	v_mfma_f32_16x16x32_bf16 v[102:105], v[218:221], v[156:159], v[102:105]
	v_mfma_f32_16x16x32_bf16 v[98:101], v[226:229], v[156:159], v[98:101]
	v_mfma_f32_16x16x32_bf16 v[86:89], v[218:221], v[186:189], v[86:89]
	v_mfma_f32_16x16x32_bf16 v[82:85], v[226:229], v[186:189], v[82:85]
	v_mfma_f32_16x16x32_bf16 v[70:73], v[218:221], v[194:197], v[70:73]
	v_mfma_f32_16x16x32_bf16 v[66:69], v[226:229], v[194:197], v[66:69]
	s_waitcnt lgkmcnt(0)
	v_mfma_f32_16x16x32_bf16 v[118:121], v[222:225], v[152:155], v[118:121]
	v_mfma_f32_16x16x32_bf16 v[114:117], v[230:233], v[152:155], v[114:117]
	v_mfma_f32_16x16x32_bf16 v[102:105], v[222:225], v[160:163], v[102:105]
	v_mfma_f32_16x16x32_bf16 v[98:101], v[230:233], v[160:163], v[98:101]
	v_mfma_f32_16x16x32_bf16 v[86:89], v[222:225], v[190:193], v[86:89]
	v_mfma_f32_16x16x32_bf16 v[82:85], v[230:233], v[190:193], v[82:85]
	v_mfma_f32_16x16x32_bf16 v[70:73], v[222:225], v[198:201], v[70:73]
	v_mfma_f32_16x16x32_bf16 v[66:69], v[230:233], v[198:201], v[66:69]
	s_setprio 0
	s_mov_b32 m0, s36
	v_lshl_add_u64 v[238:239], s[66:67], 0, v[166:167]
	s_barrier
	ds_read_b128 v[148:151], v185 offset:16384
	ds_read_b128 v[152:155], v185 offset:17408
	ds_read_b128 v[156:159], v185 offset:18432
	ds_read_b128 v[160:163], v185 offset:19456
	ds_read_b128 v[186:189], v185 offset:20480
	ds_read_b128 v[190:193], v185 offset:21504
	ds_read_b128 v[194:197], v185 offset:22528
	ds_read_b128 v[198:201], v185 offset:23552
	global_load_lds_dwordx4 v[238:239], off
	v_lshl_add_u64 v[240:241], s[66:67], 0, v[170:171]
	s_mov_b32 m0, s37
	s_nop 0
	global_load_lds_dwordx4 v[240:241], off
	s_barrier
	s_setprio 1
	s_waitcnt lgkmcnt(7)
	v_mfma_f32_16x16x32_bf16 v[62:65], v[132:135], v[148:151], v[62:65]
	s_waitcnt lgkmcnt(5)
	v_mfma_f32_16x16x32_bf16 v[58:61], v[140:143], v[148:151], v[58:61]
	v_mfma_f32_16x16x32_bf16 v[46:49], v[132:135], v[156:159], v[46:49]
	s_waitcnt lgkmcnt(3)
	v_mfma_f32_16x16x32_bf16 v[42:45], v[140:143], v[156:159], v[42:45]
	v_mfma_f32_16x16x32_bf16 v[30:33], v[132:135], v[186:189], v[30:33]
	s_waitcnt lgkmcnt(1)
	v_mfma_f32_16x16x32_bf16 v[26:29], v[140:143], v[186:189], v[26:29]
	v_mfma_f32_16x16x32_bf16 v[14:17], v[132:135], v[194:197], v[14:17]
	v_mfma_f32_16x16x32_bf16 v[10:13], v[140:143], v[194:197], v[10:13]
	v_mfma_f32_16x16x32_bf16 v[62:65], v[136:139], v[152:155], v[62:65]
	v_mfma_f32_16x16x32_bf16 v[58:61], v[144:147], v[152:155], v[58:61]
	v_mfma_f32_16x16x32_bf16 v[46:49], v[136:139], v[160:163], v[46:49]
	v_mfma_f32_16x16x32_bf16 v[42:45], v[144:147], v[160:163], v[42:45]
	v_mfma_f32_16x16x32_bf16 v[30:33], v[136:139], v[190:193], v[30:33]
	s_waitcnt lgkmcnt(0)
	v_mfma_f32_16x16x32_bf16 v[26:29], v[144:147], v[190:193], v[26:29]
	v_mfma_f32_16x16x32_bf16 v[14:17], v[136:139], v[198:201], v[14:17]
	v_mfma_f32_16x16x32_bf16 v[10:13], v[144:147], v[198:201], v[10:13]
	s_setprio 0
	s_barrier
	s_add_u32 s58, s64, 0x4000
	s_addc_u32 s59, s65, 0
	s_add_i32 s60, s60, s35
	v_lshl_add_u64 v[132:133], s[58:59], 0, v[164:165]
	s_mov_b32 m0, s60
	s_nop 0
	global_load_lds_dwordx4 v[132:133], off
	v_lshl_add_u64 v[132:133], s[58:59], 0, v[168:169]
	s_add_i32 m0, s60, 0x2000
	s_nop 0
	global_load_lds_dwordx4 v[132:133], off
	s_waitcnt vmcnt(10)
	s_barrier
	s_setprio 1
	v_mfma_f32_16x16x32_bf16 v[54:57], v[218:221], v[148:151], v[54:57]
	v_mfma_f32_16x16x32_bf16 v[50:53], v[226:229], v[148:151], v[50:53]
	v_mfma_f32_16x16x32_bf16 v[38:41], v[218:221], v[156:159], v[38:41]
	v_mfma_f32_16x16x32_bf16 v[34:37], v[226:229], v[156:159], v[34:37]
	v_mfma_f32_16x16x32_bf16 v[22:25], v[218:221], v[186:189], v[22:25]
	v_mfma_f32_16x16x32_bf16 v[18:21], v[226:229], v[186:189], v[18:21]
	v_mfma_f32_16x16x32_bf16 v[6:9], v[218:221], v[194:197], v[6:9]
	v_mfma_f32_16x16x32_bf16 v[2:5], v[226:229], v[194:197], v[2:5]
	v_mfma_f32_16x16x32_bf16 v[54:57], v[222:225], v[152:155], v[54:57]
	v_mfma_f32_16x16x32_bf16 v[50:53], v[230:233], v[152:155], v[50:53]
	v_mfma_f32_16x16x32_bf16 v[38:41], v[222:225], v[160:163], v[38:41]
	v_mfma_f32_16x16x32_bf16 v[34:37], v[230:233], v[160:163], v[34:37]
	v_mfma_f32_16x16x32_bf16 v[22:25], v[222:225], v[190:193], v[22:25]
	v_mfma_f32_16x16x32_bf16 v[18:21], v[230:233], v[190:193], v[18:21]
	v_mfma_f32_16x16x32_bf16 v[6:9], v[222:225], v[198:201], v[6:9]
	v_mfma_f32_16x16x32_bf16 v[2:5], v[230:233], v[198:201], v[2:5]
	s_setprio 0
	s_add_i32 s60, 0, 0x18000
	v_add_u32_e32 v130, s60, v182
	s_barrier
	ds_read_b128 v[132:135], v130
	ds_read_b128 v[136:139], v130 offset:1024
	ds_read_b128 v[140:143], v130 offset:2048
	ds_read_b128 v[144:147], v130 offset:3072
	s_add_u32 s58, s66, 0x40000
	s_addc_u32 s59, s67, 0
	s_mov_b32 m0, s38
	v_lshl_add_u64 v[218:219], s[58:59], 0, v[166:167]
	ds_read_b128 v[148:151], v185 offset:32768
	ds_read_b128 v[152:155], v185 offset:33792
	ds_read_b128 v[156:159], v185 offset:34816
	ds_read_b128 v[160:163], v185 offset:35840
	ds_read_b128 v[186:189], v185 offset:36864
	ds_read_b128 v[190:193], v185 offset:37888
	ds_read_b128 v[194:197], v185 offset:38912
	ds_read_b128 v[198:201], v185 offset:39936
	global_load_lds_dwordx4 v[218:219], off
	v_lshl_add_u64 v[218:219], s[58:59], 0, v[170:171]
	s_mov_b32 m0, s39
	s_nop 0
	global_load_lds_dwordx4 v[218:219], off
	s_waitcnt lgkmcnt(8)
	s_waitcnt vmcnt(10)
	s_barrier
	s_setprio 1
	s_waitcnt lgkmcnt(7)
	v_mfma_f32_16x16x32_bf16 v[126:129], v[132:135], v[148:151], v[126:129]
	s_waitcnt lgkmcnt(5)
	v_mfma_f32_16x16x32_bf16 v[122:125], v[140:143], v[148:151], v[122:125]
	v_mfma_f32_16x16x32_bf16 v[110:113], v[132:135], v[156:159], v[110:113]
	s_waitcnt lgkmcnt(3)
	v_mfma_f32_16x16x32_bf16 v[106:109], v[140:143], v[156:159], v[106:109]
	v_mfma_f32_16x16x32_bf16 v[94:97], v[132:135], v[186:189], v[94:97]
	s_waitcnt lgkmcnt(1)
	v_mfma_f32_16x16x32_bf16 v[90:93], v[140:143], v[186:189], v[90:93]
	v_mfma_f32_16x16x32_bf16 v[78:81], v[132:135], v[194:197], v[78:81]
	v_mfma_f32_16x16x32_bf16 v[74:77], v[140:143], v[194:197], v[74:77]
	v_mfma_f32_16x16x32_bf16 v[126:129], v[136:139], v[152:155], v[126:129]
	v_mfma_f32_16x16x32_bf16 v[122:125], v[144:147], v[152:155], v[122:125]
	v_mfma_f32_16x16x32_bf16 v[110:113], v[136:139], v[160:163], v[110:113]
	v_mfma_f32_16x16x32_bf16 v[106:109], v[144:147], v[160:163], v[106:109]
	v_mfma_f32_16x16x32_bf16 v[94:97], v[136:139], v[190:193], v[94:97]
	s_waitcnt lgkmcnt(0)
	v_mfma_f32_16x16x32_bf16 v[90:93], v[144:147], v[190:193], v[90:93]
	v_mfma_f32_16x16x32_bf16 v[78:81], v[136:139], v[198:201], v[78:81]
	v_mfma_f32_16x16x32_bf16 v[74:77], v[144:147], v[198:201], v[74:77]
	s_setprio 0
	s_barrier
	s_add_i32 s61, 0, 0x1c000
	s_add_i32 s58, s60, s35
	v_add_u32_e32 v130, s61, v182
	v_lshl_add_u64 v[234:235], v[234:235], 0, s[30:31]
	s_mov_b32 m0, s58
	ds_read_b128 v[218:221], v130
	ds_read_b128 v[222:225], v130 offset:1024
	ds_read_b128 v[226:229], v130 offset:2048
	ds_read_b128 v[230:233], v130 offset:3072
	global_load_lds_dwordx4 v[234:235], off
	v_lshl_add_u64 v[234:235], v[236:237], 0, s[30:31]
	s_add_i32 m0, s58, 0x2000
	s_nop 0
	global_load_lds_dwordx4 v[234:235], off
	s_waitcnt vmcnt(10)
	s_barrier
	s_setprio 1
	s_waitcnt lgkmcnt(3)
	s_waitcnt lgkmcnt(1)
	v_mfma_f32_16x16x32_bf16 v[118:121], v[218:221], v[148:151], v[118:121]
	v_mfma_f32_16x16x32_bf16 v[114:117], v[226:229], v[148:151], v[114:117]
	v_mfma_f32_16x16x32_bf16 v[102:105], v[218:221], v[156:159], v[102:105]
	v_mfma_f32_16x16x32_bf16 v[98:101], v[226:229], v[156:159], v[98:101]
	v_mfma_f32_16x16x32_bf16 v[86:89], v[218:221], v[186:189], v[86:89]
	v_mfma_f32_16x16x32_bf16 v[82:85], v[226:229], v[186:189], v[82:85]
	v_mfma_f32_16x16x32_bf16 v[70:73], v[218:221], v[194:197], v[70:73]
	v_mfma_f32_16x16x32_bf16 v[66:69], v[226:229], v[194:197], v[66:69]
	s_waitcnt lgkmcnt(0)
	v_mfma_f32_16x16x32_bf16 v[118:121], v[222:225], v[152:155], v[118:121]
	v_mfma_f32_16x16x32_bf16 v[114:117], v[230:233], v[152:155], v[114:117]
	v_mfma_f32_16x16x32_bf16 v[102:105], v[222:225], v[160:163], v[102:105]
	v_mfma_f32_16x16x32_bf16 v[98:101], v[230:233], v[160:163], v[98:101]
	v_mfma_f32_16x16x32_bf16 v[86:89], v[222:225], v[190:193], v[86:89]
	v_mfma_f32_16x16x32_bf16 v[82:85], v[230:233], v[190:193], v[82:85]
	v_mfma_f32_16x16x32_bf16 v[70:73], v[222:225], v[198:201], v[70:73]
	v_mfma_f32_16x16x32_bf16 v[66:69], v[230:233], v[198:201], v[66:69]
	s_setprio 0
	s_mov_b32 m0, s46
	v_lshl_add_u64 v[234:235], v[238:239], 0, s[30:31]
	s_barrier
	ds_read_b128 v[148:151], v185 offset:49152
	ds_read_b128 v[152:155], v185 offset:50176
	ds_read_b128 v[156:159], v185 offset:51200
	ds_read_b128 v[160:163], v185 offset:52224
	ds_read_b128 v[186:189], v185 offset:53248
	ds_read_b128 v[190:193], v185 offset:54272
	ds_read_b128 v[194:197], v185 offset:55296
	ds_read_b128 v[198:201], v185 offset:56320
	global_load_lds_dwordx4 v[234:235], off
	v_lshl_add_u64 v[234:235], v[240:241], 0, s[30:31]
	s_mov_b32 m0, s47
	s_nop 0
	global_load_lds_dwordx4 v[234:235], off
	s_barrier
	s_setprio 1
	s_waitcnt lgkmcnt(7)
	v_mfma_f32_16x16x32_bf16 v[62:65], v[132:135], v[148:151], v[62:65]
	s_waitcnt lgkmcnt(5)
	v_mfma_f32_16x16x32_bf16 v[58:61], v[140:143], v[148:151], v[58:61]
	v_mfma_f32_16x16x32_bf16 v[46:49], v[132:135], v[156:159], v[46:49]
	s_waitcnt lgkmcnt(3)
	v_mfma_f32_16x16x32_bf16 v[42:45], v[140:143], v[156:159], v[42:45]
	v_mfma_f32_16x16x32_bf16 v[30:33], v[132:135], v[186:189], v[30:33]
	s_waitcnt lgkmcnt(1)
	v_mfma_f32_16x16x32_bf16 v[26:29], v[140:143], v[186:189], v[26:29]
	v_mfma_f32_16x16x32_bf16 v[14:17], v[132:135], v[194:197], v[14:17]
	v_mfma_f32_16x16x32_bf16 v[10:13], v[140:143], v[194:197], v[10:13]
	v_mfma_f32_16x16x32_bf16 v[62:65], v[136:139], v[152:155], v[62:65]
	v_mfma_f32_16x16x32_bf16 v[58:61], v[144:147], v[152:155], v[58:61]
	v_mfma_f32_16x16x32_bf16 v[46:49], v[136:139], v[160:163], v[46:49]
	v_mfma_f32_16x16x32_bf16 v[42:45], v[144:147], v[160:163], v[42:45]
	v_mfma_f32_16x16x32_bf16 v[30:33], v[136:139], v[190:193], v[30:33]
	s_waitcnt lgkmcnt(0)
	v_mfma_f32_16x16x32_bf16 v[26:29], v[144:147], v[190:193], v[26:29]
	v_mfma_f32_16x16x32_bf16 v[14:17], v[136:139], v[198:201], v[14:17]
	v_mfma_f32_16x16x32_bf16 v[10:13], v[144:147], v[198:201], v[10:13]
	s_setprio 0
	s_barrier
	s_add_u32 s58, s64, 0x4080
	s_addc_u32 s59, s65, 0
	s_add_i32 s60, s61, s35
	v_lshl_add_u64 v[132:133], s[58:59], 0, v[164:165]
	s_mov_b32 m0, s60
	s_nop 0
	global_load_lds_dwordx4 v[132:133], off
	v_lshl_add_u64 v[132:133], s[58:59], 0, v[168:169]
	s_add_i32 m0, s60, 0x2000
	s_nop 0
	global_load_lds_dwordx4 v[132:133], off
	s_waitcnt vmcnt(10)
	s_barrier
	s_setprio 1
	v_mfma_f32_16x16x32_bf16 v[54:57], v[218:221], v[148:151], v[54:57]
	v_mfma_f32_16x16x32_bf16 v[50:53], v[226:229], v[148:151], v[50:53]
	v_mfma_f32_16x16x32_bf16 v[38:41], v[218:221], v[156:159], v[38:41]
	v_mfma_f32_16x16x32_bf16 v[34:37], v[226:229], v[156:159], v[34:37]
	v_mfma_f32_16x16x32_bf16 v[22:25], v[218:221], v[186:189], v[22:25]
	v_mfma_f32_16x16x32_bf16 v[18:21], v[226:229], v[186:189], v[18:21]
	v_mfma_f32_16x16x32_bf16 v[6:9], v[218:221], v[194:197], v[6:9]
	v_mfma_f32_16x16x32_bf16 v[2:5], v[226:229], v[194:197], v[2:5]
	v_mfma_f32_16x16x32_bf16 v[54:57], v[222:225], v[152:155], v[54:57]
	v_mfma_f32_16x16x32_bf16 v[50:53], v[230:233], v[152:155], v[50:53]
	v_mfma_f32_16x16x32_bf16 v[38:41], v[222:225], v[160:163], v[38:41]
	v_mfma_f32_16x16x32_bf16 v[34:37], v[230:233], v[160:163], v[34:37]
	v_mfma_f32_16x16x32_bf16 v[22:25], v[222:225], v[190:193], v[22:25]
	v_mfma_f32_16x16x32_bf16 v[18:21], v[230:233], v[190:193], v[18:21]
	v_mfma_f32_16x16x32_bf16 v[6:9], v[222:225], v[198:201], v[6:9]
	v_mfma_f32_16x16x32_bf16 v[2:5], v[230:233], v[198:201], v[2:5]
	s_setprio 0
	s_add_u32 s62, s62, 0x100
	s_addc_u32 s63, s63, 0
	s_cmp_gt_u32 s57, 13
	s_barrier
	s_cbranch_scc1 .LBB0_1095

.LBB0_1418:
	s_add_i32 s65, 0, 0x10000
	v_add_u32_e32 v130, s65, v168
	ds_read_b128 v[2:5], v130
	ds_read_b128 v[6:9], v130 offset:1024
	ds_read_b128 v[10:13], v130 offset:2048
	ds_read_b128 v[14:17], v130 offset:3072
	s_add_u32 s62, s18, 0x20080
	s_addc_u32 s63, s19, 0
	s_add_i32 s13, s43, 0xc000
	v_lshl_add_u64 v[50:51], s[62:63], 0, v[152:153]
	s_mov_b32 m0, s13
	s_add_i32 s64, s43, 0xe000
	ds_read_b128 v[18:21], v170
	ds_read_b128 v[22:25], v170 offset:1024
	ds_read_b128 v[26:29], v170 offset:2048
	ds_read_b128 v[30:33], v170 offset:3072
	ds_read_b128 v[34:37], v170 offset:4096
	ds_read_b128 v[38:41], v170 offset:5120
	ds_read_b128 v[42:45], v170 offset:6144
	ds_read_b128 v[46:49], v170 offset:7168
	global_load_lds_dwordx4 v[50:51], off
	v_lshl_add_u64 v[50:51], s[62:63], 0, v[148:149]
	s_mov_b32 m0, s64
	s_nop 0
	global_load_lds_dwordx4 v[50:51], off
	s_waitcnt lgkmcnt(8)
	s_waitcnt vmcnt(10)
	s_barrier
	s_setprio 1
	s_waitcnt lgkmcnt(6)
	v_mfma_scale_f32_16x16x128_f8f6f4 v[140:143], v[2:9], v[18:25], 0, v205, v205 op_sel_hi:[0,0,0]
	v_mfma_scale_f32_16x16x128_f8f6f4 v[132:135], v[10:17], v[18:25], 0, v205, v205 op_sel_hi:[0,0,0]
	s_waitcnt lgkmcnt(4)
	v_mfma_scale_f32_16x16x128_f8f6f4 v[122:125], v[2:9], v[26:33], 0, v205, v205 op_sel_hi:[0,0,0]
	v_mfma_scale_f32_16x16x128_f8f6f4 v[114:117], v[10:17], v[26:33], 0, v205, v205 op_sel_hi:[0,0,0]
	s_waitcnt lgkmcnt(2)
	v_mfma_scale_f32_16x16x128_f8f6f4 v[106:109], v[2:9], v[34:41], 0, v205, v205 op_sel_hi:[0,0,0]
	v_mfma_scale_f32_16x16x128_f8f6f4 v[98:101], v[10:17], v[34:41], 0, v205, v205 op_sel_hi:[0,0,0]
	s_waitcnt lgkmcnt(0)
	v_mfma_scale_f32_16x16x128_f8f6f4 v[90:93], v[2:9], v[42:49], 0, v205, v205 op_sel_hi:[0,0,0]
	v_mfma_scale_f32_16x16x128_f8f6f4 v[78:81], v[10:17], v[42:49], 0, v205, v205 op_sel_hi:[0,0,0]
	s_setprio 0
	s_barrier
	s_add_i32 s67, 0, 0x14000
	v_lshl_add_u64 v[164:165], s[60:61], 0, v[154:155]
	s_mov_b64 s[62:63], 0x100
	s_add_i32 s65, s65, s38
	v_add_u32_e32 v171, s67, v168
	v_lshl_add_u64 v[50:51], v[164:165], 0, s[62:63]
	s_mov_b32 m0, s65
	v_lshl_add_u64 v[166:167], s[60:61], 0, v[150:151]
	s_add_i32 s66, s65, 0x2000
	ds_read_b128 v[178:181], v171
	ds_read_b128 v[182:185], v171 offset:1024
	ds_read_b128 v[186:189], v171 offset:2048
	ds_read_b128 v[190:193], v171 offset:3072
	global_load_lds_dwordx4 v[50:51], off
	v_lshl_add_u64 v[50:51], v[166:167], 0, s[62:63]
	s_mov_b32 m0, s66
	s_nop 0
	global_load_lds_dwordx4 v[50:51], off
	s_waitcnt vmcnt(10)
	s_barrier
	s_setprio 1
	s_waitcnt lgkmcnt(2)
	v_mfma_scale_f32_16x16x128_f8f6f4 v[144:147], v[178:185], v[18:25], 0, v205, v205 op_sel_hi:[0,0,0]
	s_waitcnt lgkmcnt(0)
	v_mfma_scale_f32_16x16x128_f8f6f4 v[136:139], v[186:193], v[18:25], 0, v205, v205 op_sel_hi:[0,0,0]
	v_mfma_scale_f32_16x16x128_f8f6f4 v[126:129], v[178:185], v[26:33], 0, v205, v205 op_sel_hi:[0,0,0]
	v_mfma_scale_f32_16x16x128_f8f6f4 v[118:121], v[186:193], v[26:33], 0, v205, v205 op_sel_hi:[0,0,0]
	v_mfma_scale_f32_16x16x128_f8f6f4 v[110:113], v[178:185], v[34:41], 0, v205, v205 op_sel_hi:[0,0,0]
	v_mfma_scale_f32_16x16x128_f8f6f4 v[102:105], v[186:193], v[34:41], 0, v205, v205 op_sel_hi:[0,0,0]
	v_mfma_scale_f32_16x16x128_f8f6f4 v[94:97], v[178:185], v[42:49], 0, v205, v205 op_sel_hi:[0,0,0]
	v_mfma_scale_f32_16x16x128_f8f6f4 v[86:89], v[186:193], v[42:49], 0, v205, v205 op_sel_hi:[0,0,0]
	s_setprio 0
	v_lshl_add_u64 v[160:161], s[18:19], 0, v[152:153]
	s_mov_b32 m0, s43
	v_lshl_add_u64 v[18:19], v[160:161], 0, s[62:63]
	v_lshl_add_u64 v[162:163], s[18:19], 0, v[148:149]
	s_barrier
	ds_read_b128 v[194:197], v170 offset:16384
	ds_read_b128 v[198:201], v170 offset:17408
	ds_read_b128 v[218:221], v170 offset:18432
	ds_read_b128 v[222:225], v170 offset:19456
	ds_read_b128 v[226:229], v170 offset:20480
	ds_read_b128 v[230:233], v170 offset:21504
	ds_read_b128 v[234:237], v170 offset:22528
	ds_read_b128 v[238:241], v170 offset:23552
	global_load_lds_dwordx4 v[18:19], off
	v_lshl_add_u64 v[18:19], v[162:163], 0, s[62:63]
	s_mov_b32 m0, s44
	s_nop 0
	global_load_lds_dwordx4 v[18:19], off
	s_barrier
	s_setprio 1
	s_waitcnt lgkmcnt(6)
	v_mfma_scale_f32_16x16x128_f8f6f4 v[74:77], v[2:9], v[194:201], 0, v205, v205 op_sel_hi:[0,0,0]
	v_mfma_scale_f32_16x16x128_f8f6f4 v[66:69], v[10:17], v[194:201], 0, v205, v205 op_sel_hi:[0,0,0]
	s_waitcnt lgkmcnt(4)
	v_mfma_scale_f32_16x16x128_f8f6f4 v[58:61], v[2:9], v[218:225], 0, v205, v205 op_sel_hi:[0,0,0]
	v_mfma_scale_f32_16x16x128_f8f6f4 v[50:53], v[10:17], v[218:225], 0, v205, v205 op_sel_hi:[0,0,0]
	s_waitcnt lgkmcnt(2)
	v_mfma_scale_f32_16x16x128_f8f6f4 v[42:45], v[2:9], v[226:233], 0, v205, v205 op_sel_hi:[0,0,0]
	v_mfma_scale_f32_16x16x128_f8f6f4 v[34:37], v[10:17], v[226:233], 0, v205, v205 op_sel_hi:[0,0,0]
	s_waitcnt lgkmcnt(0)
	v_mfma_scale_f32_16x16x128_f8f6f4 v[26:29], v[2:9], v[234:241], 0, v205, v205 op_sel_hi:[0,0,0]
	v_mfma_scale_f32_16x16x128_f8f6f4 v[18:21], v[10:17], v[234:241], 0, v205, v205 op_sel_hi:[0,0,0]
	s_setprio 0
	s_barrier
	s_add_u32 s62, s60, 0x2100
	s_addc_u32 s63, s61, 0
	s_add_i32 s67, s67, s38
	v_lshl_add_u64 v[2:3], s[62:63], 0, v[154:155]
	s_mov_b32 m0, s67
	s_add_i32 s68, s67, 0x2000
	global_load_lds_dwordx4 v[2:3], off
	v_lshl_add_u64 v[2:3], s[62:63], 0, v[150:151]
	s_mov_b32 m0, s68
	s_nop 0
	global_load_lds_dwordx4 v[2:3], off
	s_waitcnt vmcnt(10)
	s_barrier
	s_setprio 1
	v_mfma_scale_f32_16x16x128_f8f6f4 v[82:85], v[178:185], v[194:201], 0, v205, v205 op_sel_hi:[0,0,0]
	v_mfma_scale_f32_16x16x128_f8f6f4 v[70:73], v[186:193], v[194:201], 0, v205, v205 op_sel_hi:[0,0,0]
	v_mfma_scale_f32_16x16x128_f8f6f4 v[62:65], v[178:185], v[218:225], 0, v205, v205 op_sel_hi:[0,0,0]
	v_mfma_scale_f32_16x16x128_f8f6f4 v[54:57], v[186:193], v[218:225], 0, v205, v205 op_sel_hi:[0,0,0]
	v_mfma_scale_f32_16x16x128_f8f6f4 v[46:49], v[178:185], v[226:233], 0, v205, v205 op_sel_hi:[0,0,0]
	v_mfma_scale_f32_16x16x128_f8f6f4 v[38:41], v[186:193], v[226:233], 0, v205, v205 op_sel_hi:[0,0,0]
	v_mfma_scale_f32_16x16x128_f8f6f4 v[30:33], v[178:185], v[234:241], 0, v205, v205 op_sel_hi:[0,0,0]
	v_mfma_scale_f32_16x16x128_f8f6f4 v[22:25], v[186:193], v[234:241], 0, v205, v205 op_sel_hi:[0,0,0]
	s_setprio 0
	s_add_i32 s69, 0, 0x18000
	v_add_u32_e32 v172, s69, v168
	s_barrier
	ds_read_b128 v[10:13], v172
	ds_read_b128 v[14:17], v172 offset:1024
	ds_read_b128 v[2:5], v172 offset:2048
	ds_read_b128 v[6:9], v172 offset:3072
	s_add_u32 s62, s18, 0x20100
	s_addc_u32 s63, s19, 0
	s_mov_b32 m0, s45
	v_lshl_add_u64 v[174:175], s[62:63], 0, v[152:153]
	ds_read_b128 v[178:181], v170 offset:32768
	ds_read_b128 v[182:185], v170 offset:33792
	ds_read_b128 v[186:189], v170 offset:34816
	ds_read_b128 v[190:193], v170 offset:35840
	ds_read_b128 v[194:197], v170 offset:36864
	ds_read_b128 v[198:201], v170 offset:37888
	ds_read_b128 v[218:221], v170 offset:38912
	ds_read_b128 v[222:225], v170 offset:39936
	global_load_lds_dwordx4 v[174:175], off
	v_lshl_add_u64 v[174:175], s[62:63], 0, v[148:149]
	s_mov_b32 m0, s46
	s_nop 0
	global_load_lds_dwordx4 v[174:175], off
	s_waitcnt lgkmcnt(8)
	s_waitcnt vmcnt(10)
	s_barrier
	s_setprio 1
	s_waitcnt lgkmcnt(6)
	v_mfma_scale_f32_16x16x128_f8f6f4 v[140:143], v[10:17], v[178:185], v[140:143], v205, v205 op_sel_hi:[0,0,0]
	v_mfma_scale_f32_16x16x128_f8f6f4 v[132:135], v[2:9], v[178:185], v[132:135], v205, v205 op_sel_hi:[0,0,0]
	s_waitcnt lgkmcnt(4)
	v_mfma_scale_f32_16x16x128_f8f6f4 v[122:125], v[10:17], v[186:193], v[122:125], v205, v205 op_sel_hi:[0,0,0]
	v_mfma_scale_f32_16x16x128_f8f6f4 v[114:117], v[2:9], v[186:193], v[114:117], v205, v205 op_sel_hi:[0,0,0]
	s_waitcnt lgkmcnt(2)
	v_mfma_scale_f32_16x16x128_f8f6f4 v[106:109], v[10:17], v[194:201], v[106:109], v205, v205 op_sel_hi:[0,0,0]
	v_mfma_scale_f32_16x16x128_f8f6f4 v[98:101], v[2:9], v[194:201], v[98:101], v205, v205 op_sel_hi:[0,0,0]
	s_waitcnt lgkmcnt(0)
	v_mfma_scale_f32_16x16x128_f8f6f4 v[90:93], v[10:17], v[218:225], v[90:93], v205, v205 op_sel_hi:[0,0,0]
	v_mfma_scale_f32_16x16x128_f8f6f4 v[78:81], v[2:9], v[218:225], v[78:81], v205, v205 op_sel_hi:[0,0,0]
	s_setprio 0
	s_barrier
	s_add_i32 s71, 0, 0x1c000
	s_mov_b64 s[62:63], 0x180
	s_add_i32 s69, s69, s38
	v_add_u32_e32 v173, s71, v168
	v_lshl_add_u64 v[164:165], v[164:165], 0, s[62:63]
	s_mov_b32 m0, s69
	s_add_i32 s70, s69, 0x2000
	ds_read_b128 v[226:229], v173
	ds_read_b128 v[230:233], v173 offset:1024
	ds_read_b128 v[234:237], v173 offset:2048
	ds_read_b128 v[238:241], v173 offset:3072
	global_load_lds_dwordx4 v[164:165], off
	v_lshl_add_u64 v[164:165], v[166:167], 0, s[62:63]
	s_mov_b32 m0, s70
	s_nop 0
	global_load_lds_dwordx4 v[164:165], off
	s_waitcnt vmcnt(10)
	s_barrier
	s_setprio 1
	s_waitcnt lgkmcnt(2)
	v_mfma_scale_f32_16x16x128_f8f6f4 v[144:147], v[226:233], v[178:185], v[144:147], v205, v205 op_sel_hi:[0,0,0]
	s_waitcnt lgkmcnt(0)
	v_mfma_scale_f32_16x16x128_f8f6f4 v[136:139], v[234:241], v[178:185], v[136:139], v205, v205 op_sel_hi:[0,0,0]
	v_mfma_scale_f32_16x16x128_f8f6f4 v[126:129], v[226:233], v[186:193], v[126:129], v205, v205 op_sel_hi:[0,0,0]
	v_mfma_scale_f32_16x16x128_f8f6f4 v[118:121], v[234:241], v[186:193], v[118:121], v205, v205 op_sel_hi:[0,0,0]
	v_mfma_scale_f32_16x16x128_f8f6f4 v[110:113], v[226:233], v[194:201], v[110:113], v205, v205 op_sel_hi:[0,0,0]
	v_mfma_scale_f32_16x16x128_f8f6f4 v[102:105], v[234:241], v[194:201], v[102:105], v205, v205 op_sel_hi:[0,0,0]
	v_mfma_scale_f32_16x16x128_f8f6f4 v[94:97], v[226:233], v[218:225], v[94:97], v205, v205 op_sel_hi:[0,0,0]
	v_mfma_scale_f32_16x16x128_f8f6f4 v[86:89], v[234:241], v[218:225], v[86:89], v205, v205 op_sel_hi:[0,0,0]
	s_setprio 0
	s_mov_b32 m0, s51
	v_lshl_add_u64 v[160:161], v[160:161], 0, s[62:63]
	s_barrier
	ds_read_b128 v[178:181], v170 offset:49152
	ds_read_b128 v[182:185], v170 offset:50176
	ds_read_b128 v[186:189], v170 offset:51200
	ds_read_b128 v[190:193], v170 offset:52224
	ds_read_b128 v[194:197], v170 offset:53248
	ds_read_b128 v[198:201], v170 offset:54272
	ds_read_b128 v[218:221], v170 offset:55296
	ds_read_b128 v[222:225], v170 offset:56320
	global_load_lds_dwordx4 v[160:161], off
	v_lshl_add_u64 v[160:161], v[162:163], 0, s[62:63]
	s_mov_b32 m0, s53
	s_nop 0
	global_load_lds_dwordx4 v[160:161], off
	s_barrier
	s_setprio 1
	s_waitcnt lgkmcnt(6)
	v_mfma_scale_f32_16x16x128_f8f6f4 v[74:77], v[10:17], v[178:185], v[74:77], v205, v205 op_sel_hi:[0,0,0]
	v_mfma_scale_f32_16x16x128_f8f6f4 v[66:69], v[2:9], v[178:185], v[66:69], v205, v205 op_sel_hi:[0,0,0]
	s_waitcnt lgkmcnt(4)
	v_mfma_scale_f32_16x16x128_f8f6f4 v[58:61], v[10:17], v[186:193], v[58:61], v205, v205 op_sel_hi:[0,0,0]
	v_mfma_scale_f32_16x16x128_f8f6f4 v[50:53], v[2:9], v[186:193], v[50:53], v205, v205 op_sel_hi:[0,0,0]
	s_waitcnt lgkmcnt(2)
	v_mfma_scale_f32_16x16x128_f8f6f4 v[42:45], v[10:17], v[194:201], v[42:45], v205, v205 op_sel_hi:[0,0,0]
	v_mfma_scale_f32_16x16x128_f8f6f4 v[34:37], v[2:9], v[194:201], v[34:37], v205, v205 op_sel_hi:[0,0,0]
	s_waitcnt lgkmcnt(0)
	v_mfma_scale_f32_16x16x128_f8f6f4 v[26:29], v[10:17], v[218:225], v[26:29], v205, v205 op_sel_hi:[0,0,0]
	v_mfma_scale_f32_16x16x128_f8f6f4 v[18:21], v[2:9], v[218:225], v[18:21], v205, v205 op_sel_hi:[0,0,0]
	s_setprio 0
	s_barrier
	s_add_u32 s62, s60, 0x2180
	s_addc_u32 s63, s61, 0
	s_add_i32 s71, s71, s38
	v_lshl_add_u64 v[2:3], s[62:63], 0, v[154:155]
	s_mov_b32 m0, s71
	s_add_i32 s72, s71, 0x2000
	global_load_lds_dwordx4 v[2:3], off
	v_lshl_add_u64 v[2:3], s[62:63], 0, v[150:151]
	s_mov_b32 m0, s72
	s_nop 0
	global_load_lds_dwordx4 v[2:3], off
	s_waitcnt vmcnt(10)
	s_barrier
	s_setprio 1
	v_mfma_scale_f32_16x16x128_f8f6f4 v[82:85], v[226:233], v[178:185], v[82:85], v205, v205 op_sel_hi:[0,0,0]
	v_mfma_scale_f32_16x16x128_f8f6f4 v[70:73], v[234:241], v[178:185], v[70:73], v205, v205 op_sel_hi:[0,0,0]
	v_mfma_scale_f32_16x16x128_f8f6f4 v[62:65], v[226:233], v[186:193], v[62:65], v205, v205 op_sel_hi:[0,0,0]
	v_mfma_scale_f32_16x16x128_f8f6f4 v[54:57], v[234:241], v[186:193], v[54:57], v205, v205 op_sel_hi:[0,0,0]
	v_mfma_scale_f32_16x16x128_f8f6f4 v[46:49], v[226:233], v[194:201], v[46:49], v205, v205 op_sel_hi:[0,0,0]
	v_mfma_scale_f32_16x16x128_f8f6f4 v[38:41], v[234:241], v[194:201], v[38:41], v205, v205 op_sel_hi:[0,0,0]
	v_mfma_scale_f32_16x16x128_f8f6f4 v[30:33], v[226:233], v[218:225], v[30:33], v205, v205 op_sel_hi:[0,0,0]
	v_mfma_scale_f32_16x16x128_f8f6f4 v[22:25], v[234:241], v[218:225], v[22:25], v205, v205 op_sel_hi:[0,0,0]
	s_setprio 0
	s_add_u32 s18, s18, 0x20180
	s_addc_u32 s19, s19, 0
	s_add_u32 s73, s60, 0x200
	s_addc_u32 s74, s61, 0
	s_mov_b32 s75, 0
	s_barrier
.LBB0_1419:
	ds_read_b128 v[10:13], v130
	ds_read_b128 v[14:17], v130 offset:1024
	ds_read_b128 v[160:163], v130 offset:2048
	ds_read_b128 v[164:167], v130 offset:3072
	s_add_u32 s60, s18, 0xfffe0080
	s_addc_u32 s61, s19, -1
	s_cmp_eq_u32 s75, 4
	s_cselect_b32 s63, s15, s61
	s_cselect_b32 s62, s14, s60
	s_cselect_b32 s61, s17, s74
	s_cselect_b32 s60, s16, s73
	s_mov_b32 m0, s13
	v_lshl_add_u64 v[2:3], s[18:19], 0, v[156:157]
	ds_read_b128 v[178:181], v170
	ds_read_b128 v[182:185], v170 offset:1024
	ds_read_b128 v[186:189], v170 offset:2048
	ds_read_b128 v[190:193], v170 offset:3072
	ds_read_b128 v[194:197], v170 offset:4096
	ds_read_b128 v[198:201], v170 offset:5120
	ds_read_b128 v[218:221], v170 offset:6144
	ds_read_b128 v[222:225], v170 offset:7168
	global_load_lds_dwordx4 v[2:3], off
	v_lshl_add_u64 v[2:3], s[18:19], 0, v[158:159]
	s_mov_b32 m0, s64
	s_nop 0
	global_load_lds_dwordx4 v[2:3], off
	s_waitcnt lgkmcnt(8)
	s_waitcnt vmcnt(10)
	s_barrier
	s_setprio 1
	s_waitcnt lgkmcnt(6)
	v_mfma_scale_f32_16x16x128_f8f6f4 v[140:143], v[10:17], v[178:185], v[140:143], v205, v205 op_sel_hi:[0,0,0]
	v_mfma_scale_f32_16x16x128_f8f6f4 v[132:135], v[160:167], v[178:185], v[132:135], v205, v205 op_sel_hi:[0,0,0]
	s_waitcnt lgkmcnt(4)
	v_mfma_scale_f32_16x16x128_f8f6f4 v[122:125], v[10:17], v[186:193], v[122:125], v205, v205 op_sel_hi:[0,0,0]
	v_mfma_scale_f32_16x16x128_f8f6f4 v[114:117], v[160:167], v[186:193], v[114:117], v205, v205 op_sel_hi:[0,0,0]
	s_waitcnt lgkmcnt(2)
	v_mfma_scale_f32_16x16x128_f8f6f4 v[106:109], v[10:17], v[194:201], v[106:109], v205, v205 op_sel_hi:[0,0,0]
	v_mfma_scale_f32_16x16x128_f8f6f4 v[98:101], v[160:167], v[194:201], v[98:101], v205, v205 op_sel_hi:[0,0,0]
	s_waitcnt lgkmcnt(0)
	v_mfma_scale_f32_16x16x128_f8f6f4 v[90:93], v[10:17], v[218:225], v[90:93], v205, v205 op_sel_hi:[0,0,0]
	v_mfma_scale_f32_16x16x128_f8f6f4 v[78:81], v[160:167], v[218:225], v[78:81], v205, v205 op_sel_hi:[0,0,0]
	s_setprio 0
	s_barrier
	s_mov_b32 m0, s65
	v_lshl_add_u64 v[6:7], s[60:61], 0, v[154:155]
	ds_read_b128 v[226:229], v171
	ds_read_b128 v[230:233], v171 offset:1024
	ds_read_b128 v[234:237], v171 offset:2048
	ds_read_b128 v[238:241], v171 offset:3072
	global_load_lds_dwordx4 v[6:7], off
	v_lshl_add_u64 v[8:9], s[60:61], 0, v[150:151]
	s_mov_b32 m0, s66
	s_nop 0
	global_load_lds_dwordx4 v[8:9], off
	s_waitcnt vmcnt(10)
	s_barrier
	s_setprio 1
	s_waitcnt lgkmcnt(2)
	v_mfma_scale_f32_16x16x128_f8f6f4 v[144:147], v[226:233], v[178:185], v[144:147], v205, v205 op_sel_hi:[0,0,0]
	s_waitcnt lgkmcnt(0)
	v_mfma_scale_f32_16x16x128_f8f6f4 v[136:139], v[234:241], v[178:185], v[136:139], v205, v205 op_sel_hi:[0,0,0]
	v_mfma_scale_f32_16x16x128_f8f6f4 v[126:129], v[226:233], v[186:193], v[126:129], v205, v205 op_sel_hi:[0,0,0]
	v_mfma_scale_f32_16x16x128_f8f6f4 v[118:121], v[234:241], v[186:193], v[118:121], v205, v205 op_sel_hi:[0,0,0]
	v_mfma_scale_f32_16x16x128_f8f6f4 v[110:113], v[226:233], v[194:201], v[110:113], v205, v205 op_sel_hi:[0,0,0]
	v_mfma_scale_f32_16x16x128_f8f6f4 v[102:105], v[234:241], v[194:201], v[102:105], v205, v205 op_sel_hi:[0,0,0]
	v_mfma_scale_f32_16x16x128_f8f6f4 v[94:97], v[226:233], v[218:225], v[94:97], v205, v205 op_sel_hi:[0,0,0]
	v_mfma_scale_f32_16x16x128_f8f6f4 v[86:89], v[234:241], v[218:225], v[86:89], v205, v205 op_sel_hi:[0,0,0]
	s_setprio 0
	s_mov_b32 m0, s43
	v_lshl_add_u64 v[2:3], s[62:63], 0, v[152:153]
	s_barrier
	ds_read_b128 v[178:181], v170 offset:16384
	ds_read_b128 v[182:185], v170 offset:17408
	ds_read_b128 v[186:189], v170 offset:18432
	ds_read_b128 v[190:193], v170 offset:19456
	ds_read_b128 v[194:197], v170 offset:20480
	ds_read_b128 v[198:201], v170 offset:21504
	ds_read_b128 v[218:221], v170 offset:22528
	ds_read_b128 v[222:225], v170 offset:23552
	global_load_lds_dwordx4 v[2:3], off
	v_lshl_add_u64 v[4:5], s[62:63], 0, v[148:149]
	s_mov_b32 m0, s44
	s_nop 0
	global_load_lds_dwordx4 v[4:5], off
	s_barrier
	s_setprio 1
	s_waitcnt lgkmcnt(6)
	v_mfma_scale_f32_16x16x128_f8f6f4 v[74:77], v[10:17], v[178:185], v[74:77], v205, v205 op_sel_hi:[0,0,0]
	v_mfma_scale_f32_16x16x128_f8f6f4 v[66:69], v[160:167], v[178:185], v[66:69], v205, v205 op_sel_hi:[0,0,0]
	s_waitcnt lgkmcnt(4)
	v_mfma_scale_f32_16x16x128_f8f6f4 v[58:61], v[10:17], v[186:193], v[58:61], v205, v205 op_sel_hi:[0,0,0]
	v_mfma_scale_f32_16x16x128_f8f6f4 v[50:53], v[160:167], v[186:193], v[50:53], v205, v205 op_sel_hi:[0,0,0]
	s_waitcnt lgkmcnt(2)
	v_mfma_scale_f32_16x16x128_f8f6f4 v[42:45], v[10:17], v[194:201], v[42:45], v205, v205 op_sel_hi:[0,0,0]
	v_mfma_scale_f32_16x16x128_f8f6f4 v[34:37], v[160:167], v[194:201], v[34:37], v205, v205 op_sel_hi:[0,0,0]
	s_waitcnt lgkmcnt(0)
	v_mfma_scale_f32_16x16x128_f8f6f4 v[26:29], v[10:17], v[218:225], v[26:29], v205, v205 op_sel_hi:[0,0,0]
	v_mfma_scale_f32_16x16x128_f8f6f4 v[18:21], v[160:167], v[218:225], v[18:21], v205, v205 op_sel_hi:[0,0,0]
	s_setprio 0
	s_barrier
	s_add_u32 s76, s60, 0x2000
	s_addc_u32 s77, s61, 0
	s_mov_b32 m0, s67
	v_lshl_add_u64 v[10:11], s[76:77], 0, v[154:155]
	global_load_lds_dwordx4 v[10:11], off
	v_lshl_add_u64 v[10:11], s[76:77], 0, v[150:151]
	s_mov_b32 m0, s68
	s_nop 0
	global_load_lds_dwordx4 v[10:11], off
	s_waitcnt vmcnt(10)
	s_barrier
	s_setprio 1
	v_mfma_scale_f32_16x16x128_f8f6f4 v[82:85], v[226:233], v[178:185], v[82:85], v205, v205 op_sel_hi:[0,0,0]
	v_mfma_scale_f32_16x16x128_f8f6f4 v[70:73], v[234:241], v[178:185], v[70:73], v205, v205 op_sel_hi:[0,0,0]
	v_mfma_scale_f32_16x16x128_f8f6f4 v[62:65], v[226:233], v[186:193], v[62:65], v205, v205 op_sel_hi:[0,0,0]
	v_mfma_scale_f32_16x16x128_f8f6f4 v[54:57], v[234:241], v[186:193], v[54:57], v205, v205 op_sel_hi:[0,0,0]
	v_mfma_scale_f32_16x16x128_f8f6f4 v[46:49], v[226:233], v[194:201], v[46:49], v205, v205 op_sel_hi:[0,0,0]
	v_mfma_scale_f32_16x16x128_f8f6f4 v[38:41], v[234:241], v[194:201], v[38:41], v205, v205 op_sel_hi:[0,0,0]
	v_mfma_scale_f32_16x16x128_f8f6f4 v[30:33], v[226:233], v[218:225], v[30:33], v205, v205 op_sel_hi:[0,0,0]
	v_mfma_scale_f32_16x16x128_f8f6f4 v[22:25], v[234:241], v[218:225], v[22:25], v205, v205 op_sel_hi:[0,0,0]
	s_setprio 0
	s_barrier
	ds_read_b128 v[10:13], v172
	ds_read_b128 v[14:17], v172 offset:1024
	ds_read_b128 v[160:163], v172 offset:2048
	ds_read_b128 v[164:167], v172 offset:3072
	s_add_u32 s62, s62, 0x20000
	s_addc_u32 s63, s63, 0
	s_mov_b32 m0, s45
	v_lshl_add_u64 v[174:175], s[62:63], 0, v[152:153]
	ds_read_b128 v[178:181], v170 offset:32768
	ds_read_b128 v[182:185], v170 offset:33792
	ds_read_b128 v[186:189], v170 offset:34816
	ds_read_b128 v[190:193], v170 offset:35840
	ds_read_b128 v[194:197], v170 offset:36864
	ds_read_b128 v[198:201], v170 offset:37888
	ds_read_b128 v[218:221], v170 offset:38912
	ds_read_b128 v[222:225], v170 offset:39936
	global_load_lds_dwordx4 v[174:175], off
	v_lshl_add_u64 v[174:175], s[62:63], 0, v[148:149]
	s_mov_b32 m0, s46
	s_nop 0
	global_load_lds_dwordx4 v[174:175], off
	s_waitcnt lgkmcnt(8)
	s_waitcnt vmcnt(10)
	s_barrier
	s_setprio 1
	s_waitcnt lgkmcnt(6)
	v_mfma_scale_f32_16x16x128_f8f6f4 v[140:143], v[10:17], v[178:185], v[140:143], v205, v205 op_sel_hi:[0,0,0]
	v_mfma_scale_f32_16x16x128_f8f6f4 v[132:135], v[160:167], v[178:185], v[132:135], v205, v205 op_sel_hi:[0,0,0]
	s_waitcnt lgkmcnt(4)
	v_mfma_scale_f32_16x16x128_f8f6f4 v[122:125], v[10:17], v[186:193], v[122:125], v205, v205 op_sel_hi:[0,0,0]
	v_mfma_scale_f32_16x16x128_f8f6f4 v[114:117], v[160:167], v[186:193], v[114:117], v205, v205 op_sel_hi:[0,0,0]
	s_waitcnt lgkmcnt(2)
	v_mfma_scale_f32_16x16x128_f8f6f4 v[106:109], v[10:17], v[194:201], v[106:109], v205, v205 op_sel_hi:[0,0,0]
	v_mfma_scale_f32_16x16x128_f8f6f4 v[98:101], v[160:167], v[194:201], v[98:101], v205, v205 op_sel_hi:[0,0,0]
	s_waitcnt lgkmcnt(0)
	v_mfma_scale_f32_16x16x128_f8f6f4 v[90:93], v[10:17], v[218:225], v[90:93], v205, v205 op_sel_hi:[0,0,0]
	v_mfma_scale_f32_16x16x128_f8f6f4 v[78:81], v[160:167], v[218:225], v[78:81], v205, v205 op_sel_hi:[0,0,0]
	s_setprio 0
	s_barrier
	s_mov_b32 m0, s69
	v_lshl_add_u64 v[6:7], v[6:7], 0, s[30:31]
	ds_read_b128 v[226:229], v173
	ds_read_b128 v[230:233], v173 offset:1024
	ds_read_b128 v[234:237], v173 offset:2048
	ds_read_b128 v[238:241], v173 offset:3072
	global_load_lds_dwordx4 v[6:7], off
	v_lshl_add_u64 v[6:7], v[8:9], 0, s[30:31]
	s_mov_b32 m0, s70
	s_nop 0
	global_load_lds_dwordx4 v[6:7], off
	s_waitcnt vmcnt(10)
	s_barrier
	s_setprio 1
	s_waitcnt lgkmcnt(2)
	v_mfma_scale_f32_16x16x128_f8f6f4 v[144:147], v[226:233], v[178:185], v[144:147], v205, v205 op_sel_hi:[0,0,0]
	s_waitcnt lgkmcnt(0)
	v_mfma_scale_f32_16x16x128_f8f6f4 v[136:139], v[234:241], v[178:185], v[136:139], v205, v205 op_sel_hi:[0,0,0]
	v_mfma_scale_f32_16x16x128_f8f6f4 v[126:129], v[226:233], v[186:193], v[126:129], v205, v205 op_sel_hi:[0,0,0]
	v_mfma_scale_f32_16x16x128_f8f6f4 v[118:121], v[234:241], v[186:193], v[118:121], v205, v205 op_sel_hi:[0,0,0]
	v_mfma_scale_f32_16x16x128_f8f6f4 v[110:113], v[226:233], v[194:201], v[110:113], v205, v205 op_sel_hi:[0,0,0]
	v_mfma_scale_f32_16x16x128_f8f6f4 v[102:105], v[234:241], v[194:201], v[102:105], v205, v205 op_sel_hi:[0,0,0]
	v_mfma_scale_f32_16x16x128_f8f6f4 v[94:97], v[226:233], v[218:225], v[94:97], v205, v205 op_sel_hi:[0,0,0]
	v_mfma_scale_f32_16x16x128_f8f6f4 v[86:89], v[234:241], v[218:225], v[86:89], v205, v205 op_sel_hi:[0,0,0]
	s_setprio 0
	s_mov_b32 m0, s51
	v_lshl_add_u64 v[2:3], v[2:3], 0, s[30:31]
	s_barrier
	ds_read_b128 v[178:181], v170 offset:49152
	ds_read_b128 v[182:185], v170 offset:50176
	ds_read_b128 v[186:189], v170 offset:51200
	ds_read_b128 v[190:193], v170 offset:52224
	ds_read_b128 v[194:197], v170 offset:53248
	ds_read_b128 v[198:201], v170 offset:54272
	ds_read_b128 v[218:221], v170 offset:55296
	ds_read_b128 v[222:225], v170 offset:56320
	global_load_lds_dwordx4 v[2:3], off
	v_lshl_add_u64 v[2:3], v[4:5], 0, s[30:31]
	s_mov_b32 m0, s53
	s_nop 0
	global_load_lds_dwordx4 v[2:3], off
	s_barrier
	s_setprio 1
	s_waitcnt lgkmcnt(6)
	v_mfma_scale_f32_16x16x128_f8f6f4 v[74:77], v[10:17], v[178:185], v[74:77], v205, v205 op_sel_hi:[0,0,0]
	v_mfma_scale_f32_16x16x128_f8f6f4 v[66:69], v[160:167], v[178:185], v[66:69], v205, v205 op_sel_hi:[0,0,0]
	s_waitcnt lgkmcnt(4)
	v_mfma_scale_f32_16x16x128_f8f6f4 v[58:61], v[10:17], v[186:193], v[58:61], v205, v205 op_sel_hi:[0,0,0]
	v_mfma_scale_f32_16x16x128_f8f6f4 v[50:53], v[160:167], v[186:193], v[50:53], v205, v205 op_sel_hi:[0,0,0]
	s_waitcnt lgkmcnt(2)
	v_mfma_scale_f32_16x16x128_f8f6f4 v[42:45], v[10:17], v[194:201], v[42:45], v205, v205 op_sel_hi:[0,0,0]
	v_mfma_scale_f32_16x16x128_f8f6f4 v[34:37], v[160:167], v[194:201], v[34:37], v205, v205 op_sel_hi:[0,0,0]
	s_waitcnt lgkmcnt(0)
	v_mfma_scale_f32_16x16x128_f8f6f4 v[26:29], v[10:17], v[218:225], v[26:29], v205, v205 op_sel_hi:[0,0,0]
	v_mfma_scale_f32_16x16x128_f8f6f4 v[18:21], v[160:167], v[218:225], v[18:21], v205, v205 op_sel_hi:[0,0,0]
	s_setprio 0
	s_barrier
	s_add_u32 s60, s60, 0x2080
	s_addc_u32 s61, s61, 0
	s_mov_b32 m0, s71
	v_lshl_add_u64 v[2:3], s[60:61], 0, v[154:155]
	global_load_lds_dwordx4 v[2:3], off
	v_lshl_add_u64 v[2:3], s[60:61], 0, v[150:151]
	s_mov_b32 m0, s72
	s_nop 0
	global_load_lds_dwordx4 v[2:3], off
	s_waitcnt vmcnt(10)
	s_barrier
	s_setprio 1
	v_mfma_scale_f32_16x16x128_f8f6f4 v[82:85], v[226:233], v[178:185], v[82:85], v205, v205 op_sel_hi:[0,0,0]
	v_mfma_scale_f32_16x16x128_f8f6f4 v[70:73], v[234:241], v[178:185], v[70:73], v205, v205 op_sel_hi:[0,0,0]
	v_mfma_scale_f32_16x16x128_f8f6f4 v[62:65], v[226:233], v[186:193], v[62:65], v205, v205 op_sel_hi:[0,0,0]
	v_mfma_scale_f32_16x16x128_f8f6f4 v[54:57], v[234:241], v[186:193], v[54:57], v205, v205 op_sel_hi:[0,0,0]
	v_mfma_scale_f32_16x16x128_f8f6f4 v[46:49], v[226:233], v[194:201], v[46:49], v205, v205 op_sel_hi:[0,0,0]
	v_mfma_scale_f32_16x16x128_f8f6f4 v[38:41], v[234:241], v[194:201], v[38:41], v205, v205 op_sel_hi:[0,0,0]
	v_mfma_scale_f32_16x16x128_f8f6f4 v[30:33], v[226:233], v[218:225], v[30:33], v205, v205 op_sel_hi:[0,0,0]
	v_mfma_scale_f32_16x16x128_f8f6f4 v[22:25], v[234:241], v[218:225], v[22:25], v205, v205 op_sel_hi:[0,0,0]
	s_setprio 0
	s_add_i32 s75, s75, 2
	s_add_u32 s18, s18, 0x100
	s_addc_u32 s19, s19, 0
	s_add_u32 s73, s73, 0x100
	s_addc_u32 s74, s74, 0
	s_cmp_gt_u32 s75, 5
	s_barrier
	s_cbranch_scc0 .LBB0_1419
	v_mul_f32_e32 v5, 0xbcb8aa3b, v140
	v_exp_f32_e32 v5, v5
	v_mul_f32_e32 v6, 0xbcb8aa3b, v141
	v_exp_f32_e32 v6, v6
	v_mul_f32_e32 v7, 0xbcb8aa3b, v142
	v_add_f32_e32 v5, 1.0, v5
	v_exp_f32_e32 v7, v7
	v_rcp_f32_e32 v5, v5
	v_mul_f32_e32 v8, 0xbcb8aa3b, v143
	v_add_f32_e32 v6, 1.0, v6
	v_exp_f32_e32 v8, v8
	v_mul_f32_e32 v4, v140, v144
	v_rcp_f32_e32 v6, v6
	v_mul_f32_e32 v4, 0x3b000000, v4
	v_add_f32_e32 v7, 1.0, v7
	v_mul_f32_e32 v4, v5, v4
	v_mul_f32_e32 v5, v141, v145
	v_rcp_f32_e32 v7, v7
	v_mul_f32_e32 v5, 0x3b000000, v5
	v_add_f32_e32 v8, 1.0, v8
	v_mul_f32_e32 v5, v6, v5
	v_mul_f32_e32 v6, v142, v146
	v_rcp_f32_e32 v8, v8
	v_mul_f32_e32 v6, 0x3b000000, v6
	v_mul_f32_e32 v6, v7, v6
	v_mul_f32_e32 v7, v143, v147
	v_mul_f32_e32 v7, 0x3b000000, v7
	v_mul_f32_e32 v7, v8, v7
	v_med3_f32 v8, v4, s26, v209
	v_med3_f32 v5, v5, s26, v209
	v_mov_b32_e32 v4, v131
	v_cvt_pk_fp8_f32 v4, v8, v5
	v_med3_f32 v5, v6, s26, v209
	v_med3_f32 v6, v7, s26, v209
	v_mul_f32_e32 v7, 0xbcb8aa3b, v133
	v_cvt_pk_fp8_f32 v4, v5, v6 op_sel:[0,0,1]
	v_mul_f32_e32 v6, 0xbcb8aa3b, v132
	v_exp_f32_e32 v6, v6
	v_exp_f32_e32 v7, v7
	v_mul_f32_e32 v8, 0xbcb8aa3b, v134
	v_exp_f32_e32 v8, v8
	v_add_f32_e32 v6, 1.0, v6
	v_rcp_f32_e32 v6, v6
	v_mul_f32_e32 v9, 0xbcb8aa3b, v135
	v_add_f32_e32 v7, 1.0, v7
	v_exp_f32_e32 v9, v9
	v_mul_f32_e32 v5, v132, v136
	v_rcp_f32_e32 v7, v7
	v_mul_f32_e32 v5, 0x3b000000, v5
	v_add_f32_e32 v8, 1.0, v8
	v_mul_f32_e32 v5, v6, v5
	v_mul_f32_e32 v6, v133, v137
	v_rcp_f32_e32 v8, v8
	v_mul_f32_e32 v6, 0x3b000000, v6
	v_add_f32_e32 v9, 1.0, v9
	v_mul_f32_e32 v6, v7, v6
	v_mul_f32_e32 v7, v134, v138
	v_rcp_f32_e32 v9, v9
	v_mul_f32_e32 v7, 0x3b000000, v7
	v_mul_f32_e32 v7, v8, v7
	v_mul_f32_e32 v8, v135, v139
	v_mul_f32_e32 v8, 0x3b000000, v8
	v_mul_f32_e32 v8, v9, v8
	v_med3_f32 v9, v5, s26, v209
	v_med3_f32 v6, v6, s26, v209
	v_mov_b32_e32 v5, v131
	v_cvt_pk_fp8_f32 v5, v9, v6
	s_ashr_i32 s13, s12, 31
	s_lshl_b64 s[12:13], s[12:13], 11
	v_med3_f32 v6, v7, s26, v209
	v_med3_f32 v7, v8, s26, v209
	s_add_u32 s12, s47, s12
	v_cvt_pk_fp8_f32 v5, v6, v7 op_sel:[0,0,1]
	s_addc_u32 s13, s50, s13
	s_ashr_i32 s14, s59, 31
	s_add_u32 s12, s12, s59
	s_addc_u32 s13, s13, s14
	v_mov_b32_e32 v130, v169
	s_nop 15
	s_nop 15
	global_store_dwordx2 v130, v[4:5], s[12:13]
	v_mul_f32_e32 v5, 0xbcb8aa3b, v122
	v_exp_f32_e32 v5, v5
	v_mul_f32_e32 v6, 0xbcb8aa3b, v123
	v_exp_f32_e32 v6, v6
	v_mul_f32_e32 v7, 0xbcb8aa3b, v124
	v_add_f32_e32 v5, 1.0, v5
	v_exp_f32_e32 v7, v7
	v_rcp_f32_e32 v5, v5
	v_mul_f32_e32 v8, 0xbcb8aa3b, v125
	v_add_f32_e32 v6, 1.0, v6
	v_exp_f32_e32 v8, v8
	v_mul_f32_e32 v4, v122, v126
	v_rcp_f32_e32 v6, v6
	v_mul_f32_e32 v4, 0x3b000000, v4
	v_add_f32_e32 v7, 1.0, v7
	v_mul_f32_e32 v4, v5, v4
	v_mul_f32_e32 v5, v123, v127
	v_rcp_f32_e32 v7, v7
	v_mul_f32_e32 v5, 0x3b000000, v5
	v_add_f32_e32 v8, 1.0, v8
	v_mul_f32_e32 v5, v6, v5
	v_mul_f32_e32 v6, v124, v128
	v_rcp_f32_e32 v8, v8
	v_mul_f32_e32 v6, 0x3b000000, v6
	v_mul_f32_e32 v6, v7, v6
	v_mul_f32_e32 v7, v125, v129
	v_mul_f32_e32 v7, 0x3b000000, v7
	v_mul_f32_e32 v7, v8, v7
	v_med3_f32 v8, v4, s26, v209
	v_med3_f32 v5, v5, s26, v209
	v_mov_b32_e32 v4, v131
	v_cvt_pk_fp8_f32 v4, v8, v5
	v_med3_f32 v5, v6, s26, v209
	v_med3_f32 v6, v7, s26, v209
	v_mul_f32_e32 v7, 0xbcb8aa3b, v115
	v_cvt_pk_fp8_f32 v4, v5, v6 op_sel:[0,0,1]
	v_mul_f32_e32 v6, 0xbcb8aa3b, v114
	v_exp_f32_e32 v6, v6
	v_exp_f32_e32 v7, v7
	v_mul_f32_e32 v8, 0xbcb8aa3b, v116
	v_exp_f32_e32 v8, v8
	v_add_f32_e32 v6, 1.0, v6
	v_rcp_f32_e32 v6, v6
	v_mul_f32_e32 v9, 0xbcb8aa3b, v117
	v_add_f32_e32 v7, 1.0, v7
	v_exp_f32_e32 v9, v9
	v_mul_f32_e32 v5, v114, v118
	v_rcp_f32_e32 v7, v7
	v_mul_f32_e32 v5, 0x3b000000, v5
	v_add_f32_e32 v8, 1.0, v8
	v_mul_f32_e32 v5, v6, v5
	v_mul_f32_e32 v6, v115, v119
	v_rcp_f32_e32 v8, v8
	v_mul_f32_e32 v6, 0x3b000000, v6
	v_add_f32_e32 v9, 1.0, v9
	v_mul_f32_e32 v6, v7, v6
	v_mul_f32_e32 v7, v116, v120
	v_rcp_f32_e32 v9, v9
	v_mul_f32_e32 v7, 0x3b000000, v7
	v_mul_f32_e32 v7, v8, v7
	v_mul_f32_e32 v8, v117, v121
	v_mul_f32_e32 v8, 0x3b000000, v8
	v_mul_f32_e32 v8, v9, v8
	v_med3_f32 v9, v5, s26, v209
	v_med3_f32 v6, v6, s26, v209
	v_mov_b32_e32 v5, v131
	v_cvt_pk_fp8_f32 v5, v9, v6
	v_med3_f32 v6, v7, s26, v209
	v_med3_f32 v7, v8, s26, v209
	v_lshl_add_u64 v[2:3], s[12:13], 0, v[130:131]
	v_cvt_pk_fp8_f32 v5, v6, v7 op_sel:[0,0,1]
	s_mov_b32 s12, 0x8000
	v_add_co_u32_e32 v6, vcc, s12, v2
	v_mul_f32_e32 v8, 0xbcb8aa3b, v109
	s_nop 0
	v_addc_co_u32_e32 v7, vcc, 0, v3, vcc
	global_store_dwordx2 v[6:7], v[4:5], off
	v_mul_f32_e32 v5, 0xbcb8aa3b, v106
	v_exp_f32_e32 v5, v5
	v_mul_f32_e32 v6, 0xbcb8aa3b, v107
	v_exp_f32_e32 v6, v6
	v_mul_f32_e32 v7, 0xbcb8aa3b, v108
	v_add_f32_e32 v5, 1.0, v5
	v_exp_f32_e32 v7, v7
	v_rcp_f32_e32 v5, v5
	v_add_f32_e32 v6, 1.0, v6
	v_exp_f32_e32 v8, v8
	v_mul_f32_e32 v4, v106, v110
	v_rcp_f32_e32 v6, v6
	v_mul_f32_e32 v4, 0x3b000000, v4
	v_add_f32_e32 v7, 1.0, v7
	v_mul_f32_e32 v4, v5, v4
	v_mul_f32_e32 v5, v107, v111
	v_rcp_f32_e32 v7, v7
	v_mul_f32_e32 v5, 0x3b000000, v5
	v_add_f32_e32 v8, 1.0, v8
	v_mul_f32_e32 v5, v6, v5
	v_mul_f32_e32 v6, v108, v112
	v_rcp_f32_e32 v8, v8
	v_mul_f32_e32 v6, 0x3b000000, v6
	v_mul_f32_e32 v6, v7, v6
	v_mul_f32_e32 v7, v109, v113
	v_mul_f32_e32 v7, 0x3b000000, v7
	v_mul_f32_e32 v7, v8, v7
	v_med3_f32 v8, v4, s26, v209
	v_med3_f32 v5, v5, s26, v209
	v_mov_b32_e32 v4, v131
	v_cvt_pk_fp8_f32 v4, v8, v5
	v_med3_f32 v5, v6, s26, v209
	v_med3_f32 v6, v7, s26, v209
	v_mul_f32_e32 v7, 0xbcb8aa3b, v99
	v_cvt_pk_fp8_f32 v4, v5, v6 op_sel:[0,0,1]
	v_mul_f32_e32 v6, 0xbcb8aa3b, v98
	v_exp_f32_e32 v6, v6
	v_exp_f32_e32 v7, v7
	v_mul_f32_e32 v8, 0xbcb8aa3b, v100
	v_exp_f32_e32 v8, v8
	v_add_f32_e32 v6, 1.0, v6
	v_rcp_f32_e32 v6, v6
	v_mul_f32_e32 v9, 0xbcb8aa3b, v101
	v_add_f32_e32 v7, 1.0, v7
	v_exp_f32_e32 v9, v9
	v_mul_f32_e32 v5, v98, v102
	v_rcp_f32_e32 v7, v7
	v_mul_f32_e32 v5, 0x3b000000, v5
	v_add_f32_e32 v8, 1.0, v8
	v_mul_f32_e32 v5, v6, v5
	v_mul_f32_e32 v6, v99, v103
	v_rcp_f32_e32 v8, v8
	v_mul_f32_e32 v6, 0x3b000000, v6
	v_add_f32_e32 v9, 1.0, v9
	v_mul_f32_e32 v6, v7, v6
	v_mul_f32_e32 v7, v100, v104
	v_rcp_f32_e32 v9, v9
	v_mul_f32_e32 v7, 0x3b000000, v7
	v_mul_f32_e32 v7, v8, v7
	v_mul_f32_e32 v8, v101, v105
	v_mul_f32_e32 v8, 0x3b000000, v8
	v_mul_f32_e32 v8, v9, v8
	v_med3_f32 v9, v5, s26, v209
	v_med3_f32 v6, v6, s26, v209
	v_mov_b32_e32 v5, v131
	v_cvt_pk_fp8_f32 v5, v9, v6
	v_med3_f32 v6, v7, s26, v209
	v_med3_f32 v7, v8, s26, v209
	s_mov_b32 s12, 0x10000
	v_cvt_pk_fp8_f32 v5, v6, v7 op_sel:[0,0,1]
	v_add_co_u32_e32 v6, vcc, s12, v2
	v_mul_f32_e32 v8, 0xbcb8aa3b, v93
	s_nop 0
	v_addc_co_u32_e32 v7, vcc, 0, v3, vcc
	global_store_dwordx2 v[6:7], v[4:5], off
	v_mul_f32_e32 v5, 0xbcb8aa3b, v90
	v_exp_f32_e32 v5, v5
	v_mul_f32_e32 v6, 0xbcb8aa3b, v91
	v_exp_f32_e32 v6, v6
	v_mul_f32_e32 v7, 0xbcb8aa3b, v92
	v_add_f32_e32 v5, 1.0, v5
	v_exp_f32_e32 v7, v7
	v_rcp_f32_e32 v5, v5
	v_add_f32_e32 v6, 1.0, v6
	v_exp_f32_e32 v8, v8
	v_mul_f32_e32 v4, v90, v94
	v_rcp_f32_e32 v6, v6
	v_mul_f32_e32 v4, 0x3b000000, v4
	v_add_f32_e32 v7, 1.0, v7
	v_mul_f32_e32 v4, v5, v4
	v_mul_f32_e32 v5, v91, v95
	v_rcp_f32_e32 v7, v7
	v_mul_f32_e32 v5, 0x3b000000, v5
	v_add_f32_e32 v8, 1.0, v8
	v_mul_f32_e32 v5, v6, v5
	v_mul_f32_e32 v6, v92, v96
	v_rcp_f32_e32 v8, v8
	v_mul_f32_e32 v6, 0x3b000000, v6
	v_mul_f32_e32 v6, v7, v6
	v_mul_f32_e32 v7, v93, v97
	v_mul_f32_e32 v7, 0x3b000000, v7
	v_mul_f32_e32 v7, v8, v7
	v_med3_f32 v8, v4, s26, v209
	v_med3_f32 v5, v5, s26, v209
	v_mov_b32_e32 v4, v131
	v_cvt_pk_fp8_f32 v4, v8, v5
	v_med3_f32 v5, v6, s26, v209
	v_med3_f32 v6, v7, s26, v209
	v_mul_f32_e32 v7, 0xbcb8aa3b, v79
	v_cvt_pk_fp8_f32 v4, v5, v6 op_sel:[0,0,1]
	v_mul_f32_e32 v6, 0xbcb8aa3b, v78
	v_exp_f32_e32 v6, v6
	v_exp_f32_e32 v7, v7
	v_mul_f32_e32 v8, 0xbcb8aa3b, v80
	v_exp_f32_e32 v8, v8
	v_add_f32_e32 v6, 1.0, v6
	v_rcp_f32_e32 v6, v6
	v_mul_f32_e32 v9, 0xbcb8aa3b, v81
	v_add_f32_e32 v7, 1.0, v7
	v_exp_f32_e32 v9, v9
	v_mul_f32_e32 v5, v78, v86
	v_rcp_f32_e32 v7, v7
	v_mul_f32_e32 v5, 0x3b000000, v5
	v_add_f32_e32 v8, 1.0, v8
	v_mul_f32_e32 v5, v6, v5
	v_mul_f32_e32 v6, v79, v87
	v_rcp_f32_e32 v8, v8
	v_mul_f32_e32 v6, 0x3b000000, v6
	v_add_f32_e32 v9, 1.0, v9
	v_mul_f32_e32 v6, v7, v6
	v_mul_f32_e32 v7, v80, v88
	v_rcp_f32_e32 v9, v9
	v_mul_f32_e32 v7, 0x3b000000, v7
	v_mul_f32_e32 v7, v8, v7
	v_mul_f32_e32 v8, v81, v89
	v_mul_f32_e32 v8, 0x3b000000, v8
	v_mul_f32_e32 v8, v9, v8
	v_med3_f32 v9, v5, s26, v209
	v_med3_f32 v6, v6, s26, v209
	v_mov_b32_e32 v5, v131
	v_cvt_pk_fp8_f32 v5, v9, v6
	v_med3_f32 v6, v7, s26, v209
	v_med3_f32 v7, v8, s26, v209
	s_mov_b32 s12, 0x18000
	v_cvt_pk_fp8_f32 v5, v6, v7 op_sel:[0,0,1]
	v_add_co_u32_e32 v6, vcc, s12, v2
	v_mul_f32_e32 v8, 0xbcb8aa3b, v77
	s_nop 0
	v_addc_co_u32_e32 v7, vcc, 0, v3, vcc
	global_store_dwordx2 v[6:7], v[4:5], off
	v_mul_f32_e32 v5, 0xbcb8aa3b, v74
	v_exp_f32_e32 v5, v5
	v_mul_f32_e32 v6, 0xbcb8aa3b, v75
	v_exp_f32_e32 v6, v6
	v_mul_f32_e32 v7, 0xbcb8aa3b, v76
	v_add_f32_e32 v5, 1.0, v5
	v_exp_f32_e32 v7, v7
	v_rcp_f32_e32 v5, v5
	v_add_f32_e32 v6, 1.0, v6
	v_exp_f32_e32 v8, v8
	v_mul_f32_e32 v4, v74, v82
	v_rcp_f32_e32 v6, v6
	v_mul_f32_e32 v4, 0x3b000000, v4
	v_add_f32_e32 v7, 1.0, v7
	v_mul_f32_e32 v4, v5, v4
	v_mul_f32_e32 v5, v75, v83
	v_rcp_f32_e32 v7, v7
	v_mul_f32_e32 v5, 0x3b000000, v5
	v_add_f32_e32 v8, 1.0, v8
	v_mul_f32_e32 v5, v6, v5
	v_mul_f32_e32 v6, v76, v84
	v_rcp_f32_e32 v8, v8
	v_mul_f32_e32 v6, 0x3b000000, v6
	v_mul_f32_e32 v6, v7, v6
	v_mul_f32_e32 v7, v77, v85
	v_mul_f32_e32 v7, 0x3b000000, v7
	v_mul_f32_e32 v7, v8, v7
	v_med3_f32 v8, v4, s26, v209
	v_med3_f32 v5, v5, s26, v209
	v_mov_b32_e32 v4, v131
	v_cvt_pk_fp8_f32 v4, v8, v5
	v_med3_f32 v5, v6, s26, v209
	v_med3_f32 v6, v7, s26, v209
	v_mul_f32_e32 v7, 0xbcb8aa3b, v67
	v_cvt_pk_fp8_f32 v4, v5, v6 op_sel:[0,0,1]
	v_mul_f32_e32 v6, 0xbcb8aa3b, v66
	v_exp_f32_e32 v6, v6
	v_exp_f32_e32 v7, v7
	v_mul_f32_e32 v8, 0xbcb8aa3b, v68
	v_exp_f32_e32 v8, v8
	v_add_f32_e32 v6, 1.0, v6
	v_rcp_f32_e32 v6, v6
	v_mul_f32_e32 v9, 0xbcb8aa3b, v69
	v_add_f32_e32 v7, 1.0, v7
	v_exp_f32_e32 v9, v9
	v_mul_f32_e32 v5, v66, v70
	v_rcp_f32_e32 v7, v7
	v_mul_f32_e32 v5, 0x3b000000, v5
	v_add_f32_e32 v8, 1.0, v8
	v_mul_f32_e32 v5, v6, v5
	v_mul_f32_e32 v6, v67, v71
	v_rcp_f32_e32 v8, v8
	v_mul_f32_e32 v6, 0x3b000000, v6
	v_add_f32_e32 v9, 1.0, v9
	v_mul_f32_e32 v6, v7, v6
	v_mul_f32_e32 v7, v68, v72
	v_rcp_f32_e32 v9, v9
	v_mul_f32_e32 v7, 0x3b000000, v7
	v_mul_f32_e32 v7, v8, v7
	v_mul_f32_e32 v8, v69, v73
	v_mul_f32_e32 v8, 0x3b000000, v8
	v_mul_f32_e32 v8, v9, v8
	v_med3_f32 v9, v5, s26, v209
	v_med3_f32 v6, v6, s26, v209
	v_mov_b32_e32 v5, v131
	v_cvt_pk_fp8_f32 v5, v9, v6
	v_med3_f32 v6, v7, s26, v209
	v_med3_f32 v7, v8, s26, v209
	s_mov_b32 s12, 0x40000
	v_cvt_pk_fp8_f32 v5, v6, v7 op_sel:[0,0,1]
	v_add_co_u32_e32 v6, vcc, s12, v2
	v_mul_f32_e32 v8, 0xbcb8aa3b, v61
	s_nop 0
	v_addc_co_u32_e32 v7, vcc, 0, v3, vcc
	global_store_dwordx2 v[6:7], v[4:5], off
	v_mul_f32_e32 v5, 0xbcb8aa3b, v58
	v_exp_f32_e32 v5, v5
	v_mul_f32_e32 v6, 0xbcb8aa3b, v59
	v_exp_f32_e32 v6, v6
	v_mul_f32_e32 v7, 0xbcb8aa3b, v60
	v_add_f32_e32 v5, 1.0, v5
	v_exp_f32_e32 v7, v7
	v_rcp_f32_e32 v5, v5
	v_add_f32_e32 v6, 1.0, v6
	v_exp_f32_e32 v8, v8
	v_mul_f32_e32 v4, v58, v62
	v_rcp_f32_e32 v6, v6
	v_mul_f32_e32 v4, 0x3b000000, v4
	v_add_f32_e32 v7, 1.0, v7
	v_mul_f32_e32 v4, v5, v4
	v_mul_f32_e32 v5, v59, v63
	v_rcp_f32_e32 v7, v7
	v_mul_f32_e32 v5, 0x3b000000, v5
	v_add_f32_e32 v8, 1.0, v8
	v_mul_f32_e32 v5, v6, v5
	v_mul_f32_e32 v6, v60, v64
	v_rcp_f32_e32 v8, v8
	v_mul_f32_e32 v6, 0x3b000000, v6
	v_mul_f32_e32 v6, v7, v6
	v_mul_f32_e32 v7, v61, v65
	v_mul_f32_e32 v7, 0x3b000000, v7
	v_mul_f32_e32 v7, v8, v7
	v_med3_f32 v8, v4, s26, v209
	v_med3_f32 v5, v5, s26, v209
	v_mov_b32_e32 v4, v131
	v_cvt_pk_fp8_f32 v4, v8, v5
	v_med3_f32 v5, v6, s26, v209
	v_med3_f32 v6, v7, s26, v209
	v_mul_f32_e32 v7, 0xbcb8aa3b, v51
	v_cvt_pk_fp8_f32 v4, v5, v6 op_sel:[0,0,1]
	v_mul_f32_e32 v6, 0xbcb8aa3b, v50
	v_exp_f32_e32 v6, v6
	v_exp_f32_e32 v7, v7
	v_mul_f32_e32 v8, 0xbcb8aa3b, v52
	v_exp_f32_e32 v8, v8
	v_add_f32_e32 v6, 1.0, v6
	v_rcp_f32_e32 v6, v6
	v_mul_f32_e32 v9, 0xbcb8aa3b, v53
	v_add_f32_e32 v7, 1.0, v7
	v_exp_f32_e32 v9, v9
	v_mul_f32_e32 v5, v50, v54
	v_rcp_f32_e32 v7, v7
	v_mul_f32_e32 v5, 0x3b000000, v5
	v_add_f32_e32 v8, 1.0, v8
	v_mul_f32_e32 v5, v6, v5
	v_mul_f32_e32 v6, v51, v55
	v_rcp_f32_e32 v8, v8
	v_mul_f32_e32 v6, 0x3b000000, v6
	v_add_f32_e32 v9, 1.0, v9
	v_mul_f32_e32 v6, v7, v6
	v_mul_f32_e32 v7, v52, v56
	v_rcp_f32_e32 v9, v9
	v_mul_f32_e32 v7, 0x3b000000, v7
	v_mul_f32_e32 v7, v8, v7
	v_mul_f32_e32 v8, v53, v57
	v_mul_f32_e32 v8, 0x3b000000, v8
	v_mul_f32_e32 v8, v9, v8
	v_med3_f32 v9, v5, s26, v209
	v_med3_f32 v6, v6, s26, v209
	v_mov_b32_e32 v5, v131
	v_cvt_pk_fp8_f32 v5, v9, v6
	v_med3_f32 v6, v7, s26, v209
	v_med3_f32 v7, v8, s26, v209
	s_mov_b32 s12, 0x48000
	v_cvt_pk_fp8_f32 v5, v6, v7 op_sel:[0,0,1]
	v_add_co_u32_e32 v6, vcc, s12, v2
	v_mul_f32_e32 v8, 0xbcb8aa3b, v45
	s_nop 0
	v_addc_co_u32_e32 v7, vcc, 0, v3, vcc
	global_store_dwordx2 v[6:7], v[4:5], off
	v_mul_f32_e32 v5, 0xbcb8aa3b, v42
	v_exp_f32_e32 v5, v5
	v_mul_f32_e32 v6, 0xbcb8aa3b, v43
	v_exp_f32_e32 v6, v6
	v_mul_f32_e32 v7, 0xbcb8aa3b, v44
	v_add_f32_e32 v5, 1.0, v5
	v_exp_f32_e32 v7, v7
	v_rcp_f32_e32 v5, v5
	v_add_f32_e32 v6, 1.0, v6
	v_exp_f32_e32 v8, v8
	v_mul_f32_e32 v4, v42, v46
	v_rcp_f32_e32 v6, v6
	v_mul_f32_e32 v4, 0x3b000000, v4
	v_add_f32_e32 v7, 1.0, v7
	v_mul_f32_e32 v4, v5, v4
	v_mul_f32_e32 v5, v43, v47
	v_rcp_f32_e32 v7, v7
	v_mul_f32_e32 v5, 0x3b000000, v5
	v_add_f32_e32 v8, 1.0, v8
	v_mul_f32_e32 v5, v6, v5
	v_mul_f32_e32 v6, v44, v48
	v_rcp_f32_e32 v8, v8
	v_mul_f32_e32 v6, 0x3b000000, v6
	v_mul_f32_e32 v6, v7, v6
	v_mul_f32_e32 v7, v45, v49
	v_mul_f32_e32 v7, 0x3b000000, v7
	v_mul_f32_e32 v7, v8, v7
	v_med3_f32 v8, v4, s26, v209
	v_med3_f32 v5, v5, s26, v209
	v_mov_b32_e32 v4, v131
	v_cvt_pk_fp8_f32 v4, v8, v5
	v_med3_f32 v5, v6, s26, v209
	v_med3_f32 v6, v7, s26, v209
	v_mul_f32_e32 v7, 0xbcb8aa3b, v35
	v_cvt_pk_fp8_f32 v4, v5, v6 op_sel:[0,0,1]
	v_mul_f32_e32 v6, 0xbcb8aa3b, v34
	v_exp_f32_e32 v6, v6
	v_exp_f32_e32 v7, v7
	v_mul_f32_e32 v8, 0xbcb8aa3b, v36
	v_exp_f32_e32 v8, v8
	v_add_f32_e32 v6, 1.0, v6
	v_rcp_f32_e32 v6, v6
	v_mul_f32_e32 v9, 0xbcb8aa3b, v37
	v_add_f32_e32 v7, 1.0, v7
	v_exp_f32_e32 v9, v9
	v_mul_f32_e32 v5, v34, v38
	v_rcp_f32_e32 v7, v7
	v_mul_f32_e32 v5, 0x3b000000, v5
	v_add_f32_e32 v8, 1.0, v8
	v_mul_f32_e32 v5, v6, v5
	v_mul_f32_e32 v6, v35, v39
	v_rcp_f32_e32 v8, v8
	v_mul_f32_e32 v6, 0x3b000000, v6
	v_add_f32_e32 v9, 1.0, v9
	v_mul_f32_e32 v6, v7, v6
	v_mul_f32_e32 v7, v36, v40
	v_rcp_f32_e32 v9, v9
	v_mul_f32_e32 v7, 0x3b000000, v7
	v_mul_f32_e32 v7, v8, v7
	v_mul_f32_e32 v8, v37, v41
	v_mul_f32_e32 v8, 0x3b000000, v8
	v_mul_f32_e32 v8, v9, v8
	v_med3_f32 v9, v5, s26, v209
	v_med3_f32 v6, v6, s26, v209
	v_mov_b32_e32 v5, v131
	v_cvt_pk_fp8_f32 v5, v9, v6
	v_med3_f32 v6, v7, s26, v209
	v_med3_f32 v7, v8, s26, v209
	s_mov_b32 s12, 0x50000
	v_cvt_pk_fp8_f32 v5, v6, v7 op_sel:[0,0,1]
	v_add_co_u32_e32 v6, vcc, s12, v2
	v_mul_f32_e32 v8, 0xbcb8aa3b, v29
	s_nop 0
	v_addc_co_u32_e32 v7, vcc, 0, v3, vcc
	global_store_dwordx2 v[6:7], v[4:5], off
	v_mul_f32_e32 v5, 0xbcb8aa3b, v26
	v_exp_f32_e32 v5, v5
	v_mul_f32_e32 v6, 0xbcb8aa3b, v27
	v_exp_f32_e32 v6, v6
	v_mul_f32_e32 v7, 0xbcb8aa3b, v28
	v_add_f32_e32 v5, 1.0, v5
	v_exp_f32_e32 v7, v7
	v_rcp_f32_e32 v5, v5
	v_add_f32_e32 v6, 1.0, v6
	v_exp_f32_e32 v8, v8
	v_mul_f32_e32 v4, v26, v30
	v_rcp_f32_e32 v6, v6
	v_mul_f32_e32 v4, 0x3b000000, v4
	v_add_f32_e32 v7, 1.0, v7
	v_mul_f32_e32 v4, v5, v4
	v_mul_f32_e32 v5, v27, v31
	v_rcp_f32_e32 v7, v7
	v_mul_f32_e32 v5, 0x3b000000, v5
	v_add_f32_e32 v8, 1.0, v8
	v_mul_f32_e32 v5, v6, v5
	v_mul_f32_e32 v6, v28, v32
	v_rcp_f32_e32 v8, v8
	v_mul_f32_e32 v6, 0x3b000000, v6
	v_mul_f32_e32 v6, v7, v6
	v_mul_f32_e32 v7, v29, v33
	v_mul_f32_e32 v7, 0x3b000000, v7
	v_mul_f32_e32 v7, v8, v7
	v_med3_f32 v8, v4, s26, v209
	v_med3_f32 v5, v5, s26, v209
	v_mov_b32_e32 v4, v131
	v_cvt_pk_fp8_f32 v4, v8, v5
	v_med3_f32 v5, v6, s26, v209
	v_med3_f32 v6, v7, s26, v209
	v_mul_f32_e32 v7, 0xbcb8aa3b, v19
	v_cvt_pk_fp8_f32 v4, v5, v6 op_sel:[0,0,1]
	v_mul_f32_e32 v6, 0xbcb8aa3b, v18
	v_exp_f32_e32 v6, v6
	v_exp_f32_e32 v7, v7
	v_mul_f32_e32 v8, 0xbcb8aa3b, v20
	v_exp_f32_e32 v8, v8
	v_add_f32_e32 v6, 1.0, v6
	v_rcp_f32_e32 v6, v6
	v_mul_f32_e32 v9, 0xbcb8aa3b, v21
	v_add_f32_e32 v7, 1.0, v7
	v_exp_f32_e32 v9, v9
	v_mul_f32_e32 v5, v18, v22
	v_rcp_f32_e32 v7, v7
	v_mul_f32_e32 v5, 0x3b000000, v5
	v_add_f32_e32 v8, 1.0, v8
	v_mul_f32_e32 v5, v6, v5
	v_mul_f32_e32 v6, v19, v23
	v_rcp_f32_e32 v8, v8
	v_mul_f32_e32 v6, 0x3b000000, v6
	v_add_f32_e32 v9, 1.0, v9
	v_mul_f32_e32 v6, v7, v6
	v_mul_f32_e32 v7, v20, v24
	v_rcp_f32_e32 v9, v9
	v_mul_f32_e32 v7, 0x3b000000, v7
	v_mul_f32_e32 v7, v8, v7
	v_mul_f32_e32 v8, v21, v25
	v_mul_f32_e32 v8, 0x3b000000, v8
	v_mul_f32_e32 v8, v9, v8
	v_med3_f32 v9, v5, s26, v209
	v_med3_f32 v6, v6, s26, v209
	v_mov_b32_e32 v5, v131
	v_cvt_pk_fp8_f32 v5, v9, v6
	v_med3_f32 v6, v7, s26, v209
	v_med3_f32 v7, v8, s26, v209
	v_add_co_u32_e32 v2, vcc, 0x58000, v2
	v_cvt_pk_fp8_f32 v5, v6, v7 op_sel:[0,0,1]
	s_nop 0
	v_addc_co_u32_e32 v3, vcc, 0, v3, vcc
	s_and_b64 vcc, exec, s[4:5]
	s_mov_b32 s12, s6
	s_mov_b32 s59, s7
	s_mov_b64 s[60:61], s[8:9]
	s_mov_b64 s[18:19], s[10:11]
	global_store_dwordx2 v[2:3], v[4:5], off
	s_cbranch_vccz .LBB0_1416
	s_waitcnt vmcnt(0)
	s_cmpk_gt_u32 s27, 0xff
	s_movk_i32 s47, 0x900
	s_cbranch_scc1 .LBB0_1423
	s_barrier

.LBB0_1482:
	s_add_i32 s15, 0, 0x10000
	v_add_u32_e32 v130, s15, v168
	ds_read_b128 v[2:5], v130
	ds_read_b128 v[6:9], v130 offset:1024
	ds_read_b128 v[10:13], v130 offset:2048
	ds_read_b128 v[14:17], v130 offset:3072
	s_add_u32 s58, s62, 0x40080
	s_addc_u32 s59, s63, 0
	s_add_i32 s7, s17, 0xc000
	v_lshl_add_u64 v[50:51], s[58:59], 0, v[152:153]
	s_mov_b32 m0, s7
	s_add_i32 s9, s17, 0xe000
	ds_read_b128 v[18:21], v170
	ds_read_b128 v[22:25], v170 offset:1024
	ds_read_b128 v[26:29], v170 offset:2048
	ds_read_b128 v[30:33], v170 offset:3072
	ds_read_b128 v[34:37], v170 offset:4096
	ds_read_b128 v[38:41], v170 offset:5120
	ds_read_b128 v[42:45], v170 offset:6144
	ds_read_b128 v[46:49], v170 offset:7168
	global_load_lds_dwordx4 v[50:51], off
	v_lshl_add_u64 v[50:51], s[58:59], 0, v[148:149]
	s_mov_b32 m0, s9
	s_nop 0
	global_load_lds_dwordx4 v[50:51], off
	s_waitcnt lgkmcnt(8)
	s_waitcnt vmcnt(10)
	s_barrier
	s_setprio 1
	s_waitcnt lgkmcnt(6)
	v_mfma_scale_f32_16x16x128_f8f6f4 v[132:135], v[2:9], v[18:25], 0, v205, v205 op_sel_hi:[0,0,0]
	v_mfma_scale_f32_16x16x128_f8f6f4 v[136:139], v[10:17], v[18:25], 0, v205, v205 op_sel_hi:[0,0,0]
	s_waitcnt lgkmcnt(4)
	v_mfma_scale_f32_16x16x128_f8f6f4 v[118:121], v[2:9], v[26:33], 0, v205, v205 op_sel_hi:[0,0,0]
	v_mfma_scale_f32_16x16x128_f8f6f4 v[114:117], v[10:17], v[26:33], 0, v205, v205 op_sel_hi:[0,0,0]
	s_waitcnt lgkmcnt(2)
	v_mfma_scale_f32_16x16x128_f8f6f4 v[102:105], v[2:9], v[34:41], 0, v205, v205 op_sel_hi:[0,0,0]
	v_mfma_scale_f32_16x16x128_f8f6f4 v[98:101], v[10:17], v[34:41], 0, v205, v205 op_sel_hi:[0,0,0]
	s_waitcnt lgkmcnt(0)
	v_mfma_scale_f32_16x16x128_f8f6f4 v[70:73], v[2:9], v[42:49], 0, v205, v205 op_sel_hi:[0,0,0]
	v_mfma_scale_f32_16x16x128_f8f6f4 v[66:69], v[10:17], v[42:49], 0, v205, v205 op_sel_hi:[0,0,0]
	s_setprio 0
	s_barrier
	s_add_i32 s58, 0, 0x14000
	v_lshl_add_u64 v[164:165], s[64:65], 0, v[154:155]
	s_mov_b64 s[66:67], 0x100
	s_add_i32 s15, s15, s38
	v_add_u32_e32 v171, s58, v168
	v_lshl_add_u64 v[50:51], v[164:165], 0, s[66:67]
	s_mov_b32 m0, s15
	v_lshl_add_u64 v[166:167], s[64:65], 0, v[150:151]
	s_add_i32 s57, s15, 0x2000
	ds_read_b128 v[178:181], v171
	ds_read_b128 v[182:185], v171 offset:1024
	ds_read_b128 v[186:189], v171 offset:2048
	ds_read_b128 v[190:193], v171 offset:3072
	global_load_lds_dwordx4 v[50:51], off
	v_lshl_add_u64 v[50:51], v[166:167], 0, s[66:67]
	s_mov_b32 m0, s57
	s_nop 0
	global_load_lds_dwordx4 v[50:51], off
	s_waitcnt vmcnt(10)
	s_barrier
	s_setprio 1
	s_waitcnt lgkmcnt(2)
	v_mfma_scale_f32_16x16x128_f8f6f4 v[140:143], v[178:185], v[18:25], 0, v205, v205 op_sel_hi:[0,0,0]
	s_waitcnt lgkmcnt(0)
	v_mfma_scale_f32_16x16x128_f8f6f4 v[144:147], v[186:193], v[18:25], 0, v205, v205 op_sel_hi:[0,0,0]
	v_mfma_scale_f32_16x16x128_f8f6f4 v[126:129], v[178:185], v[26:33], 0, v205, v205 op_sel_hi:[0,0,0]
	v_mfma_scale_f32_16x16x128_f8f6f4 v[122:125], v[186:193], v[26:33], 0, v205, v205 op_sel_hi:[0,0,0]
	v_mfma_scale_f32_16x16x128_f8f6f4 v[110:113], v[178:185], v[34:41], 0, v205, v205 op_sel_hi:[0,0,0]
	v_mfma_scale_f32_16x16x128_f8f6f4 v[106:109], v[186:193], v[34:41], 0, v205, v205 op_sel_hi:[0,0,0]
	v_mfma_scale_f32_16x16x128_f8f6f4 v[86:89], v[178:185], v[42:49], 0, v205, v205 op_sel_hi:[0,0,0]
	v_mfma_scale_f32_16x16x128_f8f6f4 v[82:85], v[186:193], v[42:49], 0, v205, v205 op_sel_hi:[0,0,0]
	s_setprio 0
	v_lshl_add_u64 v[160:161], s[62:63], 0, v[152:153]
	s_mov_b32 m0, s17
	v_lshl_add_u64 v[26:27], v[160:161], 0, s[66:67]
	v_lshl_add_u64 v[162:163], s[62:63], 0, v[148:149]
	s_barrier
	ds_read_b128 v[18:21], v170 offset:16384
	ds_read_b128 v[22:25], v170 offset:17408
	ds_read_b128 v[42:45], v170 offset:18432
	ds_read_b128 v[46:49], v170 offset:19456
	ds_read_b128 v[194:197], v170 offset:20480
	ds_read_b128 v[198:201], v170 offset:21504
	ds_read_b128 v[218:221], v170 offset:22528
	ds_read_b128 v[222:225], v170 offset:23552
	global_load_lds_dwordx4 v[26:27], off
	v_lshl_add_u64 v[26:27], v[162:163], 0, s[66:67]
	s_mov_b32 m0, s43
	s_nop 0
	global_load_lds_dwordx4 v[26:27], off
	s_barrier
	s_setprio 1
	s_waitcnt lgkmcnt(6)
	v_mfma_scale_f32_16x16x128_f8f6f4 v[78:81], v[2:9], v[18:25], 0, v205, v205 op_sel_hi:[0,0,0]
	v_mfma_scale_f32_16x16x128_f8f6f4 v[74:77], v[10:17], v[18:25], 0, v205, v205 op_sel_hi:[0,0,0]
	s_waitcnt lgkmcnt(4)
	v_mfma_scale_f32_16x16x128_f8f6f4 v[54:57], v[2:9], v[42:49], 0, v205, v205 op_sel_hi:[0,0,0]
	v_mfma_scale_f32_16x16x128_f8f6f4 v[50:53], v[10:17], v[42:49], 0, v205, v205 op_sel_hi:[0,0,0]
	s_waitcnt lgkmcnt(2)
	v_mfma_scale_f32_16x16x128_f8f6f4 v[38:41], v[2:9], v[194:201], 0, v205, v205 op_sel_hi:[0,0,0]
	v_mfma_scale_f32_16x16x128_f8f6f4 v[34:37], v[10:17], v[194:201], 0, v205, v205 op_sel_hi:[0,0,0]
	s_waitcnt lgkmcnt(0)
	v_mfma_scale_f32_16x16x128_f8f6f4 v[30:33], v[2:9], v[218:225], 0, v205, v205 op_sel_hi:[0,0,0]
	v_mfma_scale_f32_16x16x128_f8f6f4 v[26:29], v[10:17], v[218:225], 0, v205, v205 op_sel_hi:[0,0,0]
	s_setprio 0
	s_barrier
	s_add_u32 s66, s64, 0x4100
	s_addc_u32 s67, s65, 0
	s_add_i32 s58, s58, s38
	v_lshl_add_u64 v[2:3], s[66:67], 0, v[154:155]
	s_mov_b32 m0, s58
	s_add_i32 s59, s58, 0x2000
	global_load_lds_dwordx4 v[2:3], off
	v_lshl_add_u64 v[2:3], s[66:67], 0, v[150:151]
	s_mov_b32 m0, s59
	s_nop 0
	global_load_lds_dwordx4 v[2:3], off
	s_waitcnt vmcnt(10)
	s_barrier
	s_setprio 1
	v_mfma_scale_f32_16x16x128_f8f6f4 v[94:97], v[178:185], v[18:25], 0, v205, v205 op_sel_hi:[0,0,0]
	v_mfma_scale_f32_16x16x128_f8f6f4 v[90:93], v[186:193], v[18:25], 0, v205, v205 op_sel_hi:[0,0,0]
	v_mfma_scale_f32_16x16x128_f8f6f4 v[62:65], v[178:185], v[42:49], 0, v205, v205 op_sel_hi:[0,0,0]
	v_mfma_scale_f32_16x16x128_f8f6f4 v[58:61], v[186:193], v[42:49], 0, v205, v205 op_sel_hi:[0,0,0]
	v_mfma_scale_f32_16x16x128_f8f6f4 v[46:49], v[178:185], v[194:201], 0, v205, v205 op_sel_hi:[0,0,0]
	v_mfma_scale_f32_16x16x128_f8f6f4 v[42:45], v[186:193], v[194:201], 0, v205, v205 op_sel_hi:[0,0,0]
	v_mfma_scale_f32_16x16x128_f8f6f4 v[22:25], v[178:185], v[218:225], 0, v205, v205 op_sel_hi:[0,0,0]
	v_mfma_scale_f32_16x16x128_f8f6f4 v[18:21], v[186:193], v[218:225], 0, v205, v205 op_sel_hi:[0,0,0]
	s_setprio 0
	s_add_i32 s68, 0, 0x18000
	v_add_u32_e32 v172, s68, v168
	s_barrier
	ds_read_b128 v[10:13], v172
	ds_read_b128 v[14:17], v172 offset:1024
	ds_read_b128 v[2:5], v172 offset:2048
	ds_read_b128 v[6:9], v172 offset:3072
	s_add_u32 s66, s62, 0x40100
	s_addc_u32 s67, s63, 0
	s_mov_b32 m0, s44
	v_lshl_add_u64 v[174:175], s[66:67], 0, v[152:153]
	ds_read_b128 v[178:181], v170 offset:32768
	ds_read_b128 v[182:185], v170 offset:33792
	ds_read_b128 v[186:189], v170 offset:34816
	ds_read_b128 v[190:193], v170 offset:35840
	ds_read_b128 v[194:197], v170 offset:36864
	ds_read_b128 v[198:201], v170 offset:37888
	ds_read_b128 v[218:221], v170 offset:38912
	ds_read_b128 v[222:225], v170 offset:39936
	global_load_lds_dwordx4 v[174:175], off
	v_lshl_add_u64 v[174:175], s[66:67], 0, v[148:149]
	s_mov_b32 m0, s45
	s_nop 0
	global_load_lds_dwordx4 v[174:175], off
	s_waitcnt lgkmcnt(8)
	s_waitcnt vmcnt(10)
	s_barrier
	s_setprio 1
	s_waitcnt lgkmcnt(6)
	v_mfma_scale_f32_16x16x128_f8f6f4 v[132:135], v[10:17], v[178:185], v[132:135], v205, v205 op_sel_hi:[0,0,0]
	v_mfma_scale_f32_16x16x128_f8f6f4 v[136:139], v[2:9], v[178:185], v[136:139], v205, v205 op_sel_hi:[0,0,0]
	s_waitcnt lgkmcnt(4)
	v_mfma_scale_f32_16x16x128_f8f6f4 v[118:121], v[10:17], v[186:193], v[118:121], v205, v205 op_sel_hi:[0,0,0]
	v_mfma_scale_f32_16x16x128_f8f6f4 v[114:117], v[2:9], v[186:193], v[114:117], v205, v205 op_sel_hi:[0,0,0]
	s_waitcnt lgkmcnt(2)
	v_mfma_scale_f32_16x16x128_f8f6f4 v[102:105], v[10:17], v[194:201], v[102:105], v205, v205 op_sel_hi:[0,0,0]
	v_mfma_scale_f32_16x16x128_f8f6f4 v[98:101], v[2:9], v[194:201], v[98:101], v205, v205 op_sel_hi:[0,0,0]
	s_waitcnt lgkmcnt(0)
	v_mfma_scale_f32_16x16x128_f8f6f4 v[70:73], v[10:17], v[218:225], v[70:73], v205, v205 op_sel_hi:[0,0,0]
	v_mfma_scale_f32_16x16x128_f8f6f4 v[66:69], v[2:9], v[218:225], v[66:69], v205, v205 op_sel_hi:[0,0,0]
	s_setprio 0
	s_barrier
	s_add_i32 s70, 0, 0x1c000
	s_mov_b64 s[66:67], 0x180
	s_add_i32 s68, s68, s38
	v_add_u32_e32 v173, s70, v168
	v_lshl_add_u64 v[164:165], v[164:165], 0, s[66:67]
	s_mov_b32 m0, s68
	s_add_i32 s69, s68, 0x2000
	ds_read_b128 v[226:229], v173
	ds_read_b128 v[230:233], v173 offset:1024
	ds_read_b128 v[234:237], v173 offset:2048
	ds_read_b128 v[238:241], v173 offset:3072
	global_load_lds_dwordx4 v[164:165], off
	v_lshl_add_u64 v[164:165], v[166:167], 0, s[66:67]
	s_mov_b32 m0, s69
	s_nop 0
	global_load_lds_dwordx4 v[164:165], off
	s_waitcnt vmcnt(10)
	s_barrier
	s_setprio 1
	s_waitcnt lgkmcnt(2)
	v_mfma_scale_f32_16x16x128_f8f6f4 v[140:143], v[226:233], v[178:185], v[140:143], v205, v205 op_sel_hi:[0,0,0]
	s_waitcnt lgkmcnt(0)
	v_mfma_scale_f32_16x16x128_f8f6f4 v[144:147], v[234:241], v[178:185], v[144:147], v205, v205 op_sel_hi:[0,0,0]
	v_mfma_scale_f32_16x16x128_f8f6f4 v[126:129], v[226:233], v[186:193], v[126:129], v205, v205 op_sel_hi:[0,0,0]
	v_mfma_scale_f32_16x16x128_f8f6f4 v[122:125], v[234:241], v[186:193], v[122:125], v205, v205 op_sel_hi:[0,0,0]
	v_mfma_scale_f32_16x16x128_f8f6f4 v[110:113], v[226:233], v[194:201], v[110:113], v205, v205 op_sel_hi:[0,0,0]
	v_mfma_scale_f32_16x16x128_f8f6f4 v[106:109], v[234:241], v[194:201], v[106:109], v205, v205 op_sel_hi:[0,0,0]
	v_mfma_scale_f32_16x16x128_f8f6f4 v[86:89], v[226:233], v[218:225], v[86:89], v205, v205 op_sel_hi:[0,0,0]
	v_mfma_scale_f32_16x16x128_f8f6f4 v[82:85], v[234:241], v[218:225], v[82:85], v205, v205 op_sel_hi:[0,0,0]
	s_setprio 0
	s_mov_b32 m0, s50
	v_lshl_add_u64 v[160:161], v[160:161], 0, s[66:67]
	s_barrier
	ds_read_b128 v[178:181], v170 offset:49152
	ds_read_b128 v[182:185], v170 offset:50176
	ds_read_b128 v[186:189], v170 offset:51200
	ds_read_b128 v[190:193], v170 offset:52224
	ds_read_b128 v[194:197], v170 offset:53248
	ds_read_b128 v[198:201], v170 offset:54272
	ds_read_b128 v[218:221], v170 offset:55296
	ds_read_b128 v[222:225], v170 offset:56320
	global_load_lds_dwordx4 v[160:161], off
	v_lshl_add_u64 v[160:161], v[162:163], 0, s[66:67]
	s_mov_b32 m0, s51
	s_nop 0
	global_load_lds_dwordx4 v[160:161], off
	s_barrier
	s_setprio 1
	s_waitcnt lgkmcnt(6)
	v_mfma_scale_f32_16x16x128_f8f6f4 v[78:81], v[10:17], v[178:185], v[78:81], v205, v205 op_sel_hi:[0,0,0]
	v_mfma_scale_f32_16x16x128_f8f6f4 v[74:77], v[2:9], v[178:185], v[74:77], v205, v205 op_sel_hi:[0,0,0]
	s_waitcnt lgkmcnt(4)
	v_mfma_scale_f32_16x16x128_f8f6f4 v[54:57], v[10:17], v[186:193], v[54:57], v205, v205 op_sel_hi:[0,0,0]
	v_mfma_scale_f32_16x16x128_f8f6f4 v[50:53], v[2:9], v[186:193], v[50:53], v205, v205 op_sel_hi:[0,0,0]
	s_waitcnt lgkmcnt(2)
	v_mfma_scale_f32_16x16x128_f8f6f4 v[38:41], v[10:17], v[194:201], v[38:41], v205, v205 op_sel_hi:[0,0,0]
	v_mfma_scale_f32_16x16x128_f8f6f4 v[34:37], v[2:9], v[194:201], v[34:37], v205, v205 op_sel_hi:[0,0,0]
	s_waitcnt lgkmcnt(0)
	v_mfma_scale_f32_16x16x128_f8f6f4 v[30:33], v[10:17], v[218:225], v[30:33], v205, v205 op_sel_hi:[0,0,0]
	v_mfma_scale_f32_16x16x128_f8f6f4 v[26:29], v[2:9], v[218:225], v[26:29], v205, v205 op_sel_hi:[0,0,0]
	s_setprio 0
	s_barrier
	s_add_u32 s66, s64, 0x4180
	s_addc_u32 s67, s65, 0
	s_add_i32 s70, s70, s38
	v_lshl_add_u64 v[2:3], s[66:67], 0, v[154:155]
	s_mov_b32 m0, s70
	s_add_i32 s71, s70, 0x2000
	global_load_lds_dwordx4 v[2:3], off
	v_lshl_add_u64 v[2:3], s[66:67], 0, v[150:151]
	s_mov_b32 m0, s71
	s_nop 0
	global_load_lds_dwordx4 v[2:3], off
	s_waitcnt vmcnt(10)
	s_barrier
	s_setprio 1
	v_mfma_scale_f32_16x16x128_f8f6f4 v[94:97], v[226:233], v[178:185], v[94:97], v205, v205 op_sel_hi:[0,0,0]
	v_mfma_scale_f32_16x16x128_f8f6f4 v[90:93], v[234:241], v[178:185], v[90:93], v205, v205 op_sel_hi:[0,0,0]
	v_mfma_scale_f32_16x16x128_f8f6f4 v[62:65], v[226:233], v[186:193], v[62:65], v205, v205 op_sel_hi:[0,0,0]
	v_mfma_scale_f32_16x16x128_f8f6f4 v[58:61], v[234:241], v[186:193], v[58:61], v205, v205 op_sel_hi:[0,0,0]
	v_mfma_scale_f32_16x16x128_f8f6f4 v[46:49], v[226:233], v[194:201], v[46:49], v205, v205 op_sel_hi:[0,0,0]
	v_mfma_scale_f32_16x16x128_f8f6f4 v[42:45], v[234:241], v[194:201], v[42:45], v205, v205 op_sel_hi:[0,0,0]
	v_mfma_scale_f32_16x16x128_f8f6f4 v[22:25], v[226:233], v[218:225], v[22:25], v205, v205 op_sel_hi:[0,0,0]
	v_mfma_scale_f32_16x16x128_f8f6f4 v[18:21], v[234:241], v[218:225], v[18:21], v205, v205 op_sel_hi:[0,0,0]
	s_setprio 0
	s_add_u32 s62, s62, 0x40180
	s_addc_u32 s63, s63, 0
	s_add_u32 s72, s64, 0x200
	s_addc_u32 s73, s65, 0
	s_mov_b32 s74, 0
	s_barrier
.LBB0_1483:
	ds_read_b128 v[10:13], v130
	ds_read_b128 v[14:17], v130 offset:1024
	ds_read_b128 v[160:163], v130 offset:2048
	ds_read_b128 v[164:167], v130 offset:3072
	s_add_u32 s64, s62, 0xfffc0080
	s_addc_u32 s65, s63, -1
	s_cmp_eq_u32 s74, 12
	s_cselect_b32 s67, s19, s65
	s_cselect_b32 s66, s18, s64
	s_cselect_b32 s65, s61, s73
	s_cselect_b32 s64, s60, s72
	s_mov_b32 m0, s7
	v_lshl_add_u64 v[2:3], s[62:63], 0, v[156:157]
	ds_read_b128 v[178:181], v170
	ds_read_b128 v[182:185], v170 offset:1024
	ds_read_b128 v[186:189], v170 offset:2048
	ds_read_b128 v[190:193], v170 offset:3072
	ds_read_b128 v[194:197], v170 offset:4096
	ds_read_b128 v[198:201], v170 offset:5120
	ds_read_b128 v[218:221], v170 offset:6144
	ds_read_b128 v[222:225], v170 offset:7168
	global_load_lds_dwordx4 v[2:3], off
	v_lshl_add_u64 v[2:3], s[62:63], 0, v[158:159]
	s_mov_b32 m0, s9
	s_nop 0
	global_load_lds_dwordx4 v[2:3], off
	s_waitcnt lgkmcnt(8)
	s_waitcnt vmcnt(10)
	s_barrier
	s_setprio 1
	s_waitcnt lgkmcnt(6)
	v_mfma_scale_f32_16x16x128_f8f6f4 v[132:135], v[10:17], v[178:185], v[132:135], v205, v205 op_sel_hi:[0,0,0]
	v_mfma_scale_f32_16x16x128_f8f6f4 v[136:139], v[160:167], v[178:185], v[136:139], v205, v205 op_sel_hi:[0,0,0]
	s_waitcnt lgkmcnt(4)
	v_mfma_scale_f32_16x16x128_f8f6f4 v[118:121], v[10:17], v[186:193], v[118:121], v205, v205 op_sel_hi:[0,0,0]
	v_mfma_scale_f32_16x16x128_f8f6f4 v[114:117], v[160:167], v[186:193], v[114:117], v205, v205 op_sel_hi:[0,0,0]
	s_waitcnt lgkmcnt(2)
	v_mfma_scale_f32_16x16x128_f8f6f4 v[102:105], v[10:17], v[194:201], v[102:105], v205, v205 op_sel_hi:[0,0,0]
	v_mfma_scale_f32_16x16x128_f8f6f4 v[98:101], v[160:167], v[194:201], v[98:101], v205, v205 op_sel_hi:[0,0,0]
	s_waitcnt lgkmcnt(0)
	v_mfma_scale_f32_16x16x128_f8f6f4 v[70:73], v[10:17], v[218:225], v[70:73], v205, v205 op_sel_hi:[0,0,0]
	v_mfma_scale_f32_16x16x128_f8f6f4 v[66:69], v[160:167], v[218:225], v[66:69], v205, v205 op_sel_hi:[0,0,0]
	s_setprio 0
	s_barrier
	s_mov_b32 m0, s15
	v_lshl_add_u64 v[6:7], s[64:65], 0, v[154:155]
	ds_read_b128 v[226:229], v171
	ds_read_b128 v[230:233], v171 offset:1024
	ds_read_b128 v[234:237], v171 offset:2048
	ds_read_b128 v[238:241], v171 offset:3072
	global_load_lds_dwordx4 v[6:7], off
	v_lshl_add_u64 v[8:9], s[64:65], 0, v[150:151]
	s_mov_b32 m0, s57
	s_nop 0
	global_load_lds_dwordx4 v[8:9], off
	s_waitcnt vmcnt(10)
	s_barrier
	s_setprio 1
	s_waitcnt lgkmcnt(2)
	v_mfma_scale_f32_16x16x128_f8f6f4 v[140:143], v[226:233], v[178:185], v[140:143], v205, v205 op_sel_hi:[0,0,0]
	s_waitcnt lgkmcnt(0)
	v_mfma_scale_f32_16x16x128_f8f6f4 v[144:147], v[234:241], v[178:185], v[144:147], v205, v205 op_sel_hi:[0,0,0]
	v_mfma_scale_f32_16x16x128_f8f6f4 v[126:129], v[226:233], v[186:193], v[126:129], v205, v205 op_sel_hi:[0,0,0]
	v_mfma_scale_f32_16x16x128_f8f6f4 v[122:125], v[234:241], v[186:193], v[122:125], v205, v205 op_sel_hi:[0,0,0]
	v_mfma_scale_f32_16x16x128_f8f6f4 v[110:113], v[226:233], v[194:201], v[110:113], v205, v205 op_sel_hi:[0,0,0]
	v_mfma_scale_f32_16x16x128_f8f6f4 v[106:109], v[234:241], v[194:201], v[106:109], v205, v205 op_sel_hi:[0,0,0]
	v_mfma_scale_f32_16x16x128_f8f6f4 v[86:89], v[226:233], v[218:225], v[86:89], v205, v205 op_sel_hi:[0,0,0]
	v_mfma_scale_f32_16x16x128_f8f6f4 v[82:85], v[234:241], v[218:225], v[82:85], v205, v205 op_sel_hi:[0,0,0]
	s_setprio 0
	s_mov_b32 m0, s17
	v_lshl_add_u64 v[2:3], s[66:67], 0, v[152:153]
	s_barrier
	ds_read_b128 v[178:181], v170 offset:16384
	ds_read_b128 v[182:185], v170 offset:17408
	ds_read_b128 v[186:189], v170 offset:18432
	ds_read_b128 v[190:193], v170 offset:19456
	ds_read_b128 v[194:197], v170 offset:20480
	ds_read_b128 v[198:201], v170 offset:21504
	ds_read_b128 v[218:221], v170 offset:22528
	ds_read_b128 v[222:225], v170 offset:23552
	global_load_lds_dwordx4 v[2:3], off
	v_lshl_add_u64 v[4:5], s[66:67], 0, v[148:149]
	s_mov_b32 m0, s43
	s_nop 0
	global_load_lds_dwordx4 v[4:5], off
	s_barrier
	s_setprio 1
	s_waitcnt lgkmcnt(6)
	v_mfma_scale_f32_16x16x128_f8f6f4 v[78:81], v[10:17], v[178:185], v[78:81], v205, v205 op_sel_hi:[0,0,0]
	v_mfma_scale_f32_16x16x128_f8f6f4 v[74:77], v[160:167], v[178:185], v[74:77], v205, v205 op_sel_hi:[0,0,0]
	s_waitcnt lgkmcnt(4)
	v_mfma_scale_f32_16x16x128_f8f6f4 v[54:57], v[10:17], v[186:193], v[54:57], v205, v205 op_sel_hi:[0,0,0]
	v_mfma_scale_f32_16x16x128_f8f6f4 v[50:53], v[160:167], v[186:193], v[50:53], v205, v205 op_sel_hi:[0,0,0]
	s_waitcnt lgkmcnt(2)
	v_mfma_scale_f32_16x16x128_f8f6f4 v[38:41], v[10:17], v[194:201], v[38:41], v205, v205 op_sel_hi:[0,0,0]
	v_mfma_scale_f32_16x16x128_f8f6f4 v[34:37], v[160:167], v[194:201], v[34:37], v205, v205 op_sel_hi:[0,0,0]
	s_waitcnt lgkmcnt(0)
	v_mfma_scale_f32_16x16x128_f8f6f4 v[30:33], v[10:17], v[218:225], v[30:33], v205, v205 op_sel_hi:[0,0,0]
	v_mfma_scale_f32_16x16x128_f8f6f4 v[26:29], v[160:167], v[218:225], v[26:29], v205, v205 op_sel_hi:[0,0,0]
	s_setprio 0
	s_barrier
	s_add_u32 s76, s64, 0x4000
	s_addc_u32 s77, s65, 0
	s_mov_b32 m0, s58
	v_lshl_add_u64 v[10:11], s[76:77], 0, v[154:155]
	global_load_lds_dwordx4 v[10:11], off
	v_lshl_add_u64 v[10:11], s[76:77], 0, v[150:151]
	s_mov_b32 m0, s59
	s_nop 0
	global_load_lds_dwordx4 v[10:11], off
	s_waitcnt vmcnt(10)
	s_barrier
	s_setprio 1
	v_mfma_scale_f32_16x16x128_f8f6f4 v[94:97], v[226:233], v[178:185], v[94:97], v205, v205 op_sel_hi:[0,0,0]
	v_mfma_scale_f32_16x16x128_f8f6f4 v[90:93], v[234:241], v[178:185], v[90:93], v205, v205 op_sel_hi:[0,0,0]
	v_mfma_scale_f32_16x16x128_f8f6f4 v[62:65], v[226:233], v[186:193], v[62:65], v205, v205 op_sel_hi:[0,0,0]
	v_mfma_scale_f32_16x16x128_f8f6f4 v[58:61], v[234:241], v[186:193], v[58:61], v205, v205 op_sel_hi:[0,0,0]
	v_mfma_scale_f32_16x16x128_f8f6f4 v[46:49], v[226:233], v[194:201], v[46:49], v205, v205 op_sel_hi:[0,0,0]
	v_mfma_scale_f32_16x16x128_f8f6f4 v[42:45], v[234:241], v[194:201], v[42:45], v205, v205 op_sel_hi:[0,0,0]
	v_mfma_scale_f32_16x16x128_f8f6f4 v[22:25], v[226:233], v[218:225], v[22:25], v205, v205 op_sel_hi:[0,0,0]
	v_mfma_scale_f32_16x16x128_f8f6f4 v[18:21], v[234:241], v[218:225], v[18:21], v205, v205 op_sel_hi:[0,0,0]
	s_setprio 0
	s_barrier
	ds_read_b128 v[10:13], v172
	ds_read_b128 v[14:17], v172 offset:1024
	ds_read_b128 v[160:163], v172 offset:2048
	ds_read_b128 v[164:167], v172 offset:3072
	s_add_u32 s66, s66, 0x40000
	s_addc_u32 s67, s67, 0
	s_mov_b32 m0, s44
	v_lshl_add_u64 v[174:175], s[66:67], 0, v[152:153]
	ds_read_b128 v[178:181], v170 offset:32768
	ds_read_b128 v[182:185], v170 offset:33792
	ds_read_b128 v[186:189], v170 offset:34816
	ds_read_b128 v[190:193], v170 offset:35840
	ds_read_b128 v[194:197], v170 offset:36864
	ds_read_b128 v[198:201], v170 offset:37888
	ds_read_b128 v[218:221], v170 offset:38912
	ds_read_b128 v[222:225], v170 offset:39936
	global_load_lds_dwordx4 v[174:175], off
	v_lshl_add_u64 v[174:175], s[66:67], 0, v[148:149]
	s_mov_b32 m0, s45
	s_nop 0
	global_load_lds_dwordx4 v[174:175], off
	s_waitcnt lgkmcnt(8)
	s_waitcnt vmcnt(10)
	s_barrier
	s_setprio 1
	s_waitcnt lgkmcnt(6)
	v_mfma_scale_f32_16x16x128_f8f6f4 v[132:135], v[10:17], v[178:185], v[132:135], v205, v205 op_sel_hi:[0,0,0]
	v_mfma_scale_f32_16x16x128_f8f6f4 v[136:139], v[160:167], v[178:185], v[136:139], v205, v205 op_sel_hi:[0,0,0]
	s_waitcnt lgkmcnt(4)
	v_mfma_scale_f32_16x16x128_f8f6f4 v[118:121], v[10:17], v[186:193], v[118:121], v205, v205 op_sel_hi:[0,0,0]
	v_mfma_scale_f32_16x16x128_f8f6f4 v[114:117], v[160:167], v[186:193], v[114:117], v205, v205 op_sel_hi:[0,0,0]
	s_waitcnt lgkmcnt(2)
	v_mfma_scale_f32_16x16x128_f8f6f4 v[102:105], v[10:17], v[194:201], v[102:105], v205, v205 op_sel_hi:[0,0,0]
	v_mfma_scale_f32_16x16x128_f8f6f4 v[98:101], v[160:167], v[194:201], v[98:101], v205, v205 op_sel_hi:[0,0,0]
	s_waitcnt lgkmcnt(0)
	v_mfma_scale_f32_16x16x128_f8f6f4 v[70:73], v[10:17], v[218:225], v[70:73], v205, v205 op_sel_hi:[0,0,0]
	v_mfma_scale_f32_16x16x128_f8f6f4 v[66:69], v[160:167], v[218:225], v[66:69], v205, v205 op_sel_hi:[0,0,0]
	s_setprio 0
	s_barrier
	s_mov_b32 m0, s68
	v_lshl_add_u64 v[6:7], v[6:7], 0, s[30:31]
	ds_read_b128 v[226:229], v173
	ds_read_b128 v[230:233], v173 offset:1024
	ds_read_b128 v[234:237], v173 offset:2048
	ds_read_b128 v[238:241], v173 offset:3072
	global_load_lds_dwordx4 v[6:7], off
	v_lshl_add_u64 v[6:7], v[8:9], 0, s[30:31]
	s_mov_b32 m0, s69
	s_nop 0
	global_load_lds_dwordx4 v[6:7], off
	s_waitcnt vmcnt(10)
	s_barrier
	s_setprio 1
	s_waitcnt lgkmcnt(2)
	v_mfma_scale_f32_16x16x128_f8f6f4 v[140:143], v[226:233], v[178:185], v[140:143], v205, v205 op_sel_hi:[0,0,0]
	s_waitcnt lgkmcnt(0)
	v_mfma_scale_f32_16x16x128_f8f6f4 v[144:147], v[234:241], v[178:185], v[144:147], v205, v205 op_sel_hi:[0,0,0]
	v_mfma_scale_f32_16x16x128_f8f6f4 v[126:129], v[226:233], v[186:193], v[126:129], v205, v205 op_sel_hi:[0,0,0]
	v_mfma_scale_f32_16x16x128_f8f6f4 v[122:125], v[234:241], v[186:193], v[122:125], v205, v205 op_sel_hi:[0,0,0]
	v_mfma_scale_f32_16x16x128_f8f6f4 v[110:113], v[226:233], v[194:201], v[110:113], v205, v205 op_sel_hi:[0,0,0]
	v_mfma_scale_f32_16x16x128_f8f6f4 v[106:109], v[234:241], v[194:201], v[106:109], v205, v205 op_sel_hi:[0,0,0]
	v_mfma_scale_f32_16x16x128_f8f6f4 v[86:89], v[226:233], v[218:225], v[86:89], v205, v205 op_sel_hi:[0,0,0]
	v_mfma_scale_f32_16x16x128_f8f6f4 v[82:85], v[234:241], v[218:225], v[82:85], v205, v205 op_sel_hi:[0,0,0]
	s_setprio 0
	s_mov_b32 m0, s50
	v_lshl_add_u64 v[2:3], v[2:3], 0, s[30:31]
	s_barrier
	ds_read_b128 v[178:181], v170 offset:49152
	ds_read_b128 v[182:185], v170 offset:50176
	ds_read_b128 v[186:189], v170 offset:51200
	ds_read_b128 v[190:193], v170 offset:52224
	ds_read_b128 v[194:197], v170 offset:53248
	ds_read_b128 v[198:201], v170 offset:54272
	ds_read_b128 v[218:221], v170 offset:55296
	ds_read_b128 v[222:225], v170 offset:56320
	global_load_lds_dwordx4 v[2:3], off
	v_lshl_add_u64 v[2:3], v[4:5], 0, s[30:31]
	s_mov_b32 m0, s51
	s_nop 0
	global_load_lds_dwordx4 v[2:3], off
	s_barrier
	s_setprio 1
	s_waitcnt lgkmcnt(6)
	v_mfma_scale_f32_16x16x128_f8f6f4 v[78:81], v[10:17], v[178:185], v[78:81], v205, v205 op_sel_hi:[0,0,0]
	v_mfma_scale_f32_16x16x128_f8f6f4 v[74:77], v[160:167], v[178:185], v[74:77], v205, v205 op_sel_hi:[0,0,0]
	s_waitcnt lgkmcnt(4)
	v_mfma_scale_f32_16x16x128_f8f6f4 v[54:57], v[10:17], v[186:193], v[54:57], v205, v205 op_sel_hi:[0,0,0]
	v_mfma_scale_f32_16x16x128_f8f6f4 v[50:53], v[160:167], v[186:193], v[50:53], v205, v205 op_sel_hi:[0,0,0]
	s_waitcnt lgkmcnt(2)
	v_mfma_scale_f32_16x16x128_f8f6f4 v[38:41], v[10:17], v[194:201], v[38:41], v205, v205 op_sel_hi:[0,0,0]
	v_mfma_scale_f32_16x16x128_f8f6f4 v[34:37], v[160:167], v[194:201], v[34:37], v205, v205 op_sel_hi:[0,0,0]
	s_waitcnt lgkmcnt(0)
	v_mfma_scale_f32_16x16x128_f8f6f4 v[30:33], v[10:17], v[218:225], v[30:33], v205, v205 op_sel_hi:[0,0,0]
	v_mfma_scale_f32_16x16x128_f8f6f4 v[26:29], v[160:167], v[218:225], v[26:29], v205, v205 op_sel_hi:[0,0,0]
	s_setprio 0
	s_barrier
	s_add_u32 s64, s64, 0x4080
	s_addc_u32 s65, s65, 0
	s_mov_b32 m0, s70
	v_lshl_add_u64 v[2:3], s[64:65], 0, v[154:155]
	global_load_lds_dwordx4 v[2:3], off
	v_lshl_add_u64 v[2:3], s[64:65], 0, v[150:151]
	s_mov_b32 m0, s71
	s_nop 0
	global_load_lds_dwordx4 v[2:3], off
	s_waitcnt vmcnt(10)
	s_barrier
	s_setprio 1
	v_mfma_scale_f32_16x16x128_f8f6f4 v[94:97], v[226:233], v[178:185], v[94:97], v205, v205 op_sel_hi:[0,0,0]
	v_mfma_scale_f32_16x16x128_f8f6f4 v[90:93], v[234:241], v[178:185], v[90:93], v205, v205 op_sel_hi:[0,0,0]
	v_mfma_scale_f32_16x16x128_f8f6f4 v[62:65], v[226:233], v[186:193], v[62:65], v205, v205 op_sel_hi:[0,0,0]
	v_mfma_scale_f32_16x16x128_f8f6f4 v[58:61], v[234:241], v[186:193], v[58:61], v205, v205 op_sel_hi:[0,0,0]
	v_mfma_scale_f32_16x16x128_f8f6f4 v[46:49], v[226:233], v[194:201], v[46:49], v205, v205 op_sel_hi:[0,0,0]
	v_mfma_scale_f32_16x16x128_f8f6f4 v[42:45], v[234:241], v[194:201], v[42:45], v205, v205 op_sel_hi:[0,0,0]
	v_mfma_scale_f32_16x16x128_f8f6f4 v[22:25], v[226:233], v[218:225], v[22:25], v205, v205 op_sel_hi:[0,0,0]
	v_mfma_scale_f32_16x16x128_f8f6f4 v[18:21], v[234:241], v[218:225], v[18:21], v205, v205 op_sel_hi:[0,0,0]
	s_setprio 0
	s_add_i32 s74, s74, 2
	s_add_u32 s62, s62, 0x100
	s_addc_u32 s63, s63, 0
	s_add_u32 s72, s72, 0x100
	s_addc_u32 s73, s73, 0
	s_cmp_gt_u32 s74, 13
	s_barrier
	s_cbranch_scc0 .LBB0_1483
	v_pk_mul_f32 v[4:5], v[132:133], s[56:57] op_sel_hi:[1,0]
	v_pk_mul_f32 v[6:7], v[134:135], s[56:57] op_sel_hi:[1,0]
	v_med3_f32 v12, v4, s26, v209
	v_med3_f32 v5, v5, s26, v209
	v_mov_b32_e32 v4, v131
	v_cvt_pk_fp8_f32 v4, v12, v5
	v_pk_mul_f32 v[10:11], v[136:137], s[56:57] op_sel_hi:[1,0]
	v_med3_f32 v5, v6, s26, v209
	v_med3_f32 v6, v7, s26, v209
	v_cvt_pk_fp8_f32 v4, v5, v6 op_sel:[0,0,1]
	v_med3_f32 v6, v10, s26, v209
	v_med3_f32 v7, v11, s26, v209
	v_mov_b32_e32 v5, v131
	v_cvt_pk_fp8_f32 v5, v6, v7
	v_pk_mul_f32 v[8:9], v[138:139], s[56:57] op_sel_hi:[1,0]
	v_pk_mul_f32 v[12:13], v[144:145], s[56:57] op_sel_hi:[1,0]
	v_med3_f32 v6, v8, s26, v209
	v_med3_f32 v7, v9, s26, v209
	v_cvt_pk_fp8_f32 v5, v6, v7 op_sel:[0,0,1]
	v_pk_mul_f32 v[6:7], v[140:141], s[56:57] op_sel_hi:[1,0]
	v_pk_mul_f32 v[8:9], v[142:143], s[56:57] op_sel_hi:[1,0]
	v_med3_f32 v14, v6, s26, v209
	v_med3_f32 v7, v7, s26, v209
	v_mov_b32_e32 v6, v131
	v_cvt_pk_fp8_f32 v6, v14, v7
	v_med3_f32 v7, v8, s26, v209
	v_med3_f32 v8, v9, s26, v209
	v_med3_f32 v9, v13, s26, v209
	v_cvt_pk_fp8_f32 v6, v7, v8 op_sel:[0,0,1]
	v_med3_f32 v8, v12, s26, v209
	v_mov_b32_e32 v7, v131
	v_cvt_pk_fp8_f32 v7, v8, v9
	s_ashr_i32 s15, s14, 31
	v_pk_mul_f32 v[10:11], v[146:147], s[56:57] op_sel_hi:[1,0]
	s_lshl_b64 s[14:15], s[14:15], 10
	v_med3_f32 v8, v10, s26, v209
	v_med3_f32 v9, v11, s26, v209
	s_add_u32 s7, s46, s14
	v_cvt_pk_fp8_f32 v7, v8, v9 op_sel:[0,0,1]
	s_addc_u32 s9, s47, s15
	s_ashr_i32 s15, s16, 31
	s_add_u32 s14, s7, s16
	s_addc_u32 s15, s9, s15
	v_mov_b32_e32 v130, v169
	s_nop 15
	s_nop 15
	global_store_dwordx4 v130, v[4:7], s[14:15]
	v_pk_mul_f32 v[10:11], v[114:115], s[56:57] op_sel_hi:[1,0]
	v_pk_mul_f32 v[8:9], v[116:117], s[56:57] op_sel_hi:[1,0]
	v_pk_mul_f32 v[4:5], v[118:119], s[56:57] op_sel_hi:[1,0]
	v_pk_mul_f32 v[6:7], v[120:121], s[56:57] op_sel_hi:[1,0]
	v_med3_f32 v12, v4, s26, v209
	v_med3_f32 v5, v5, s26, v209
	v_mov_b32_e32 v4, v131
	v_cvt_pk_fp8_f32 v4, v12, v5
	v_med3_f32 v5, v6, s26, v209
	v_med3_f32 v6, v7, s26, v209
	v_med3_f32 v7, v11, s26, v209
	v_cvt_pk_fp8_f32 v4, v5, v6 op_sel:[0,0,1]
	v_med3_f32 v6, v10, s26, v209
	v_mov_b32_e32 v5, v131
	v_cvt_pk_fp8_f32 v5, v6, v7
	v_med3_f32 v6, v8, s26, v209
	v_med3_f32 v7, v9, s26, v209
	v_pk_mul_f32 v[8:9], v[128:129], s[56:57] op_sel_hi:[1,0]
	v_cvt_pk_fp8_f32 v5, v6, v7 op_sel:[0,0,1]
	v_pk_mul_f32 v[6:7], v[126:127], s[56:57] op_sel_hi:[1,0]
	v_pk_mul_f32 v[12:13], v[122:123], s[56:57] op_sel_hi:[1,0]
	v_med3_f32 v14, v6, s26, v209
	v_med3_f32 v7, v7, s26, v209
	v_mov_b32_e32 v6, v131
	v_cvt_pk_fp8_f32 v6, v14, v7
	v_med3_f32 v7, v8, s26, v209
	v_med3_f32 v8, v9, s26, v209
	v_med3_f32 v9, v13, s26, v209
	v_cvt_pk_fp8_f32 v6, v7, v8 op_sel:[0,0,1]
	v_med3_f32 v8, v12, s26, v209
	v_mov_b32_e32 v7, v131
	v_cvt_pk_fp8_f32 v7, v8, v9
	v_pk_mul_f32 v[10:11], v[124:125], s[56:57] op_sel_hi:[1,0]
	v_lshl_add_u64 v[2:3], s[14:15], 0, v[130:131]
	v_med3_f32 v8, v10, s26, v209
	v_med3_f32 v9, v11, s26, v209
	v_cvt_pk_fp8_f32 v7, v8, v9 op_sel:[0,0,1]
	v_add_co_u32_e32 v8, vcc, s90, v2
	v_pk_mul_f32 v[10:11], v[98:99], s[56:57] op_sel_hi:[1,0]
	s_nop 0
	v_addc_co_u32_e32 v9, vcc, 0, v3, vcc
	global_store_dwordx4 v[8:9], v[4:7], off
	v_pk_mul_f32 v[8:9], v[100:101], s[56:57] op_sel_hi:[1,0]
	s_mov_b32 s7, 0x8000
	v_pk_mul_f32 v[4:5], v[102:103], s[56:57] op_sel_hi:[1,0]
	v_pk_mul_f32 v[6:7], v[104:105], s[56:57] op_sel_hi:[1,0]
	v_med3_f32 v12, v4, s26, v209
	v_med3_f32 v5, v5, s26, v209
	v_mov_b32_e32 v4, v131
	v_cvt_pk_fp8_f32 v4, v12, v5
	v_med3_f32 v5, v6, s26, v209
	v_med3_f32 v6, v7, s26, v209
	v_med3_f32 v7, v11, s26, v209
	v_cvt_pk_fp8_f32 v4, v5, v6 op_sel:[0,0,1]
	v_med3_f32 v6, v10, s26, v209
	v_mov_b32_e32 v5, v131
	v_cvt_pk_fp8_f32 v5, v6, v7
	v_med3_f32 v6, v8, s26, v209
	v_med3_f32 v7, v9, s26, v209
	v_pk_mul_f32 v[8:9], v[112:113], s[56:57] op_sel_hi:[1,0]
	v_cvt_pk_fp8_f32 v5, v6, v7 op_sel:[0,0,1]
	v_pk_mul_f32 v[6:7], v[110:111], s[56:57] op_sel_hi:[1,0]
	v_pk_mul_f32 v[12:13], v[106:107], s[56:57] op_sel_hi:[1,0]
	v_med3_f32 v14, v6, s26, v209
	v_med3_f32 v7, v7, s26, v209
	v_mov_b32_e32 v6, v131
	v_cvt_pk_fp8_f32 v6, v14, v7
	v_med3_f32 v7, v8, s26, v209
	v_med3_f32 v8, v9, s26, v209
	v_med3_f32 v9, v13, s26, v209
	v_cvt_pk_fp8_f32 v6, v7, v8 op_sel:[0,0,1]
	v_med3_f32 v8, v12, s26, v209
	v_mov_b32_e32 v7, v131
	v_cvt_pk_fp8_f32 v7, v8, v9
	v_pk_mul_f32 v[10:11], v[108:109], s[56:57] op_sel_hi:[1,0]
	s_mov_b32 s14, s6
	v_med3_f32 v8, v10, s26, v209
	v_med3_f32 v9, v11, s26, v209
	v_cvt_pk_fp8_f32 v7, v8, v9 op_sel:[0,0,1]
	v_add_co_u32_e32 v8, vcc, s7, v2
	v_pk_mul_f32 v[10:11], v[66:67], s[56:57] op_sel_hi:[1,0]
	s_nop 0
	v_addc_co_u32_e32 v9, vcc, 0, v3, vcc
	global_store_dwordx4 v[8:9], v[4:7], off
	v_pk_mul_f32 v[8:9], v[68:69], s[56:57] op_sel_hi:[1,0]
	s_mov_b32 s7, 0xc000
	v_pk_mul_f32 v[4:5], v[70:71], s[56:57] op_sel_hi:[1,0]
	v_pk_mul_f32 v[6:7], v[72:73], s[56:57] op_sel_hi:[1,0]
	v_med3_f32 v12, v4, s26, v209
	v_med3_f32 v5, v5, s26, v209
	v_mov_b32_e32 v4, v131
	v_cvt_pk_fp8_f32 v4, v12, v5
	v_med3_f32 v5, v6, s26, v209
	v_med3_f32 v6, v7, s26, v209
	v_med3_f32 v7, v11, s26, v209
	v_cvt_pk_fp8_f32 v4, v5, v6 op_sel:[0,0,1]
	v_med3_f32 v6, v10, s26, v209
	v_mov_b32_e32 v5, v131
	v_cvt_pk_fp8_f32 v5, v6, v7
	v_med3_f32 v6, v8, s26, v209
	v_med3_f32 v7, v9, s26, v209
	v_pk_mul_f32 v[8:9], v[88:89], s[56:57] op_sel_hi:[1,0]
	v_cvt_pk_fp8_f32 v5, v6, v7 op_sel:[0,0,1]
	v_pk_mul_f32 v[6:7], v[86:87], s[56:57] op_sel_hi:[1,0]
	v_pk_mul_f32 v[12:13], v[82:83], s[56:57] op_sel_hi:[1,0]
	v_med3_f32 v14, v6, s26, v209
	v_med3_f32 v7, v7, s26, v209
	v_mov_b32_e32 v6, v131
	v_cvt_pk_fp8_f32 v6, v14, v7
	v_med3_f32 v7, v8, s26, v209
	v_med3_f32 v8, v9, s26, v209
	v_med3_f32 v9, v13, s26, v209
	v_cvt_pk_fp8_f32 v6, v7, v8 op_sel:[0,0,1]
	v_med3_f32 v8, v12, s26, v209
	v_mov_b32_e32 v7, v131
	v_cvt_pk_fp8_f32 v7, v8, v9
	v_pk_mul_f32 v[10:11], v[84:85], s[56:57] op_sel_hi:[1,0]
	s_mov_b32 s16, s8
	v_med3_f32 v8, v10, s26, v209
	v_med3_f32 v9, v11, s26, v209
	v_cvt_pk_fp8_f32 v7, v8, v9 op_sel:[0,0,1]
	v_add_co_u32_e32 v8, vcc, s7, v2
	v_pk_mul_f32 v[10:11], v[74:75], s[56:57] op_sel_hi:[1,0]
	s_nop 0
	v_addc_co_u32_e32 v9, vcc, 0, v3, vcc
	global_store_dwordx4 v[8:9], v[4:7], off
	v_pk_mul_f32 v[8:9], v[76:77], s[56:57] op_sel_hi:[1,0]
	s_mov_b32 s7, 0x20000
	v_pk_mul_f32 v[4:5], v[78:79], s[56:57] op_sel_hi:[1,0]
	v_pk_mul_f32 v[6:7], v[80:81], s[56:57] op_sel_hi:[1,0]
	v_med3_f32 v12, v4, s26, v209
	v_med3_f32 v5, v5, s26, v209
	v_mov_b32_e32 v4, v131
	v_cvt_pk_fp8_f32 v4, v12, v5
	v_med3_f32 v5, v6, s26, v209
	v_med3_f32 v6, v7, s26, v209
	v_med3_f32 v7, v11, s26, v209
	v_cvt_pk_fp8_f32 v4, v5, v6 op_sel:[0,0,1]
	v_med3_f32 v6, v10, s26, v209
	v_mov_b32_e32 v5, v131
	v_cvt_pk_fp8_f32 v5, v6, v7
	v_med3_f32 v6, v8, s26, v209
	v_med3_f32 v7, v9, s26, v209
	v_pk_mul_f32 v[8:9], v[96:97], s[56:57] op_sel_hi:[1,0]
	v_cvt_pk_fp8_f32 v5, v6, v7 op_sel:[0,0,1]
	v_pk_mul_f32 v[6:7], v[94:95], s[56:57] op_sel_hi:[1,0]
	v_pk_mul_f32 v[12:13], v[90:91], s[56:57] op_sel_hi:[1,0]
	v_med3_f32 v14, v6, s26, v209
	v_med3_f32 v7, v7, s26, v209
	v_mov_b32_e32 v6, v131
	v_cvt_pk_fp8_f32 v6, v14, v7
	v_med3_f32 v7, v8, s26, v209
	v_med3_f32 v8, v9, s26, v209
	v_med3_f32 v9, v13, s26, v209
	v_cvt_pk_fp8_f32 v6, v7, v8 op_sel:[0,0,1]
	v_med3_f32 v8, v12, s26, v209
	v_mov_b32_e32 v7, v131
	v_cvt_pk_fp8_f32 v7, v8, v9
	v_pk_mul_f32 v[10:11], v[92:93], s[56:57] op_sel_hi:[1,0]
	s_mov_b64 s[64:65], s[10:11]
	v_med3_f32 v8, v10, s26, v209
	v_med3_f32 v9, v11, s26, v209
	v_cvt_pk_fp8_f32 v7, v8, v9 op_sel:[0,0,1]
	v_add_co_u32_e32 v8, vcc, s7, v2
	v_pk_mul_f32 v[10:11], v[50:51], s[56:57] op_sel_hi:[1,0]
	s_nop 0
	v_addc_co_u32_e32 v9, vcc, 0, v3, vcc
	global_store_dwordx4 v[8:9], v[4:7], off
	v_pk_mul_f32 v[8:9], v[52:53], s[56:57] op_sel_hi:[1,0]
	s_mov_b32 s7, 0x24000
	v_pk_mul_f32 v[4:5], v[54:55], s[56:57] op_sel_hi:[1,0]
	v_pk_mul_f32 v[6:7], v[56:57], s[56:57] op_sel_hi:[1,0]
	v_med3_f32 v12, v4, s26, v209
	v_med3_f32 v5, v5, s26, v209
	v_mov_b32_e32 v4, v131
	v_cvt_pk_fp8_f32 v4, v12, v5
	v_med3_f32 v5, v6, s26, v209
	v_med3_f32 v6, v7, s26, v209
	v_med3_f32 v7, v11, s26, v209
	v_cvt_pk_fp8_f32 v4, v5, v6 op_sel:[0,0,1]
	v_med3_f32 v6, v10, s26, v209
	v_mov_b32_e32 v5, v131
	v_cvt_pk_fp8_f32 v5, v6, v7
	v_med3_f32 v6, v8, s26, v209
	v_med3_f32 v7, v9, s26, v209
	v_pk_mul_f32 v[8:9], v[64:65], s[56:57] op_sel_hi:[1,0]
	v_cvt_pk_fp8_f32 v5, v6, v7 op_sel:[0,0,1]
	v_pk_mul_f32 v[6:7], v[62:63], s[56:57] op_sel_hi:[1,0]
	v_pk_mul_f32 v[12:13], v[58:59], s[56:57] op_sel_hi:[1,0]
	v_med3_f32 v14, v6, s26, v209
	v_med3_f32 v7, v7, s26, v209
	v_mov_b32_e32 v6, v131
	v_cvt_pk_fp8_f32 v6, v14, v7
	v_med3_f32 v7, v8, s26, v209
	v_med3_f32 v8, v9, s26, v209
	v_med3_f32 v9, v13, s26, v209
	v_cvt_pk_fp8_f32 v6, v7, v8 op_sel:[0,0,1]
	v_med3_f32 v8, v12, s26, v209
	v_mov_b32_e32 v7, v131
	v_cvt_pk_fp8_f32 v7, v8, v9
	v_pk_mul_f32 v[10:11], v[60:61], s[56:57] op_sel_hi:[1,0]
	s_mov_b64 s[62:63], s[12:13]
	v_med3_f32 v8, v10, s26, v209
	v_med3_f32 v9, v11, s26, v209
	v_cvt_pk_fp8_f32 v7, v8, v9 op_sel:[0,0,1]
	v_add_co_u32_e32 v8, vcc, s7, v2
	v_pk_mul_f32 v[10:11], v[34:35], s[56:57] op_sel_hi:[1,0]
	s_nop 0
	v_addc_co_u32_e32 v9, vcc, 0, v3, vcc
	global_store_dwordx4 v[8:9], v[4:7], off
	v_pk_mul_f32 v[8:9], v[36:37], s[56:57] op_sel_hi:[1,0]
	s_mov_b32 s7, 0x28000
	v_pk_mul_f32 v[4:5], v[38:39], s[56:57] op_sel_hi:[1,0]
	v_pk_mul_f32 v[6:7], v[40:41], s[56:57] op_sel_hi:[1,0]
	v_med3_f32 v12, v4, s26, v209
	v_med3_f32 v5, v5, s26, v209
	v_mov_b32_e32 v4, v131
	v_cvt_pk_fp8_f32 v4, v12, v5
	v_med3_f32 v5, v6, s26, v209
	v_med3_f32 v6, v7, s26, v209
	v_med3_f32 v7, v11, s26, v209
	v_cvt_pk_fp8_f32 v4, v5, v6 op_sel:[0,0,1]
	v_med3_f32 v6, v10, s26, v209
	v_mov_b32_e32 v5, v131
	v_cvt_pk_fp8_f32 v5, v6, v7
	v_med3_f32 v6, v8, s26, v209
	v_med3_f32 v7, v9, s26, v209
	v_pk_mul_f32 v[8:9], v[48:49], s[56:57] op_sel_hi:[1,0]
	v_cvt_pk_fp8_f32 v5, v6, v7 op_sel:[0,0,1]
	v_pk_mul_f32 v[6:7], v[46:47], s[56:57] op_sel_hi:[1,0]
	v_pk_mul_f32 v[12:13], v[42:43], s[56:57] op_sel_hi:[1,0]
	v_med3_f32 v14, v6, s26, v209
	v_med3_f32 v7, v7, s26, v209
	v_mov_b32_e32 v6, v131
	v_cvt_pk_fp8_f32 v6, v14, v7
	v_med3_f32 v7, v8, s26, v209
	v_med3_f32 v8, v9, s26, v209
	v_med3_f32 v9, v13, s26, v209
	v_cvt_pk_fp8_f32 v6, v7, v8 op_sel:[0,0,1]
	v_med3_f32 v8, v12, s26, v209
	v_mov_b32_e32 v7, v131
	v_cvt_pk_fp8_f32 v7, v8, v9
	v_pk_mul_f32 v[10:11], v[44:45], s[56:57] op_sel_hi:[1,0]
	s_nop 0
	v_med3_f32 v8, v10, s26, v209
	v_med3_f32 v9, v11, s26, v209
	v_cvt_pk_fp8_f32 v7, v8, v9 op_sel:[0,0,1]
	v_add_co_u32_e32 v8, vcc, s7, v2
	v_pk_mul_f32 v[10:11], v[26:27], s[56:57] op_sel_hi:[1,0]
	s_nop 0
	v_addc_co_u32_e32 v9, vcc, 0, v3, vcc
	global_store_dwordx4 v[8:9], v[4:7], off
	v_pk_mul_f32 v[8:9], v[28:29], s[56:57] op_sel_hi:[1,0]
	v_add_co_u32_e32 v2, vcc, 0x2c000, v2
	v_pk_mul_f32 v[4:5], v[30:31], s[56:57] op_sel_hi:[1,0]
	v_pk_mul_f32 v[6:7], v[32:33], s[56:57] op_sel_hi:[1,0]
	v_med3_f32 v12, v4, s26, v209
	v_med3_f32 v5, v5, s26, v209
	v_mov_b32_e32 v4, v131
	v_cvt_pk_fp8_f32 v4, v12, v5
	v_med3_f32 v5, v6, s26, v209
	v_med3_f32 v6, v7, s26, v209
	v_med3_f32 v7, v11, s26, v209
	v_cvt_pk_fp8_f32 v4, v5, v6 op_sel:[0,0,1]
	v_med3_f32 v6, v10, s26, v209
	v_mov_b32_e32 v5, v131
	v_cvt_pk_fp8_f32 v5, v6, v7
	v_med3_f32 v6, v8, s26, v209
	v_med3_f32 v7, v9, s26, v209
	v_pk_mul_f32 v[8:9], v[24:25], s[56:57] op_sel_hi:[1,0]
	v_cvt_pk_fp8_f32 v5, v6, v7 op_sel:[0,0,1]
	v_pk_mul_f32 v[6:7], v[22:23], s[56:57] op_sel_hi:[1,0]
	v_pk_mul_f32 v[12:13], v[18:19], s[56:57] op_sel_hi:[1,0]
	v_med3_f32 v14, v6, s26, v209
	v_med3_f32 v7, v7, s26, v209
	v_mov_b32_e32 v6, v131
	v_cvt_pk_fp8_f32 v6, v14, v7
	v_med3_f32 v7, v8, s26, v209
	v_med3_f32 v8, v9, s26, v209
	v_med3_f32 v9, v13, s26, v209
	v_cvt_pk_fp8_f32 v6, v7, v8 op_sel:[0,0,1]
	v_med3_f32 v8, v12, s26, v209
	v_mov_b32_e32 v7, v131
	v_cvt_pk_fp8_f32 v7, v8, v9
	v_pk_mul_f32 v[10:11], v[20:21], s[56:57] op_sel_hi:[1,0]
	v_addc_co_u32_e32 v3, vcc, 0, v3, vcc
	v_med3_f32 v8, v10, s26, v209
	v_med3_f32 v9, v11, s26, v209
	v_cvt_pk_fp8_f32 v7, v8, v9 op_sel:[0,0,1]
	s_and_b64 vcc, exec, s[4:5]
	global_store_dwordx4 v[2:3], v[4:7], off
	s_cbranch_vccz .LBB0_1480
	s_waitcnt vmcnt(0)
	s_cmpk_gt_u32 s27, 0xff
	s_movk_i32 s47, 0x900
	s_cbranch_scc1 .LBB0_1487
	s_barrier
